# v50 + packed f32 VALU unpacked into scalar f32 ops in every phase (GEMM epilogues, LRU, router, combine), bit-exact
# baseline (speedup 1.0000x reference)
.LBB0_1024:
	s_lshl_b32 s10, s93, 8
	v_mbcnt_lo_u32_b32 v128, -1, 0
	v_mbcnt_hi_u32_b32 v128, -1, v128
	s_add_i32 s10, s10, s73
	v_and_or_b32 v140, v128, 15, s10
	s_lshl_b32 s10, s92, 8
	v_ashrrev_i32_e32 v128, 1, v128
	s_or_b32 s10, s10, s74
	v_and_b32_e32 v128, -8, v128
	v_add_u32_e32 v130, s10, v128
	v_readlane_b32 s10, v254, 14
	v_readlane_b32 s11, v254, 15
	v_ashrrev_i32_e32 v131, 31, v130
	v_lshlrev_b64 v[130:131], 1, v[130:131]
	v_mov_b64_e32 v[128:129], s[10:11]
	v_mad_i64_i32 v[136:137], s[10:11], v140, s87, v[128:129]
	v_lshl_add_u64 v[136:137], v[136:137], 0, v[130:131]
	v_mul_f32_e32 v126, s30, v126
	v_mul_f32_e32 v127, s30, v127
	v_mul_f32_e32 v124, s30, v124
	v_mul_f32_e32 v125, s30, v125
	v_mul_f32_e32 v138, s30, v122
	v_mul_f32_e32 v139, s30, v123
	v_mul_f32_e32 v122, s30, v120
	v_mul_f32_e32 v123, s30, v121
	v_cvt_pk_bf16_f32 v120, v124, v125
	v_cvt_pk_bf16_f32 v121, v126, v127
	v_mul_f32_e32 v116, s30, v116
	v_mul_f32_e32 v117, s30, v117
	v_cvt_pk_bf16_f32 v122, v122, v123
	v_cvt_pk_bf16_f32 v123, v138, v139
	global_store_dwordx4 v[136:137], v[120:123], off
	v_mul_f32_e32 v118, s30, v118
	v_mul_f32_e32 v119, s30, v119
	v_mul_f32_e32 v112, s30, v112
	v_mul_f32_e32 v113, s30, v113
	v_mul_f32_e32 v120, s30, v110
	v_mul_f32_e32 v121, s30, v111
	v_mul_f32_e32 v110, s30, v108
	v_mul_f32_e32 v111, s30, v109
	v_cvt_pk_bf16_f32 v108, v116, v117
	v_cvt_pk_bf16_f32 v109, v118, v119
	v_mul_f32_e32 v100, s30, v100
	v_mul_f32_e32 v101, s30, v101
	v_cvt_pk_bf16_f32 v110, v110, v111
	v_cvt_pk_bf16_f32 v111, v120, v121
	global_store_dwordx4 v[136:137], v[108:111], off offset:256
	v_mul_f32_e32 v102, s30, v102
	v_mul_f32_e32 v103, s30, v103
	v_mul_f32_e32 v96, s30, v96
	v_mul_f32_e32 v97, s30, v97
	v_or_b32_e32 v108, 16, v140
	v_mad_i64_i32 v[108:109], s[10:11], v108, s87, v[128:129]
	v_lshl_add_u64 v[108:109], v[108:109], 0, v[130:131]
	v_mul_f32_e32 v110, s30, v114
	v_mul_f32_e32 v111, s30, v115
	v_mul_f32_e32 v114, s30, v106
	v_mul_f32_e32 v115, s30, v107
	v_mul_f32_e32 v106, s30, v104
	v_mul_f32_e32 v107, s30, v105
	v_cvt_pk_bf16_f32 v104, v112, v113
	v_cvt_pk_bf16_f32 v105, v110, v111
	v_mul_f32_e32 v84, s30, v84
	v_mul_f32_e32 v85, s30, v85
	v_cvt_pk_bf16_f32 v106, v106, v107
	v_cvt_pk_bf16_f32 v107, v114, v115
	global_store_dwordx4 v[108:109], v[104:107], off
	v_mul_f32_e32 v86, s30, v86
	v_mul_f32_e32 v87, s30, v87
	v_mul_f32_e32 v80, s30, v80
	v_mul_f32_e32 v81, s30, v81
	v_mul_f32_e32 v104, s30, v94
	v_mul_f32_e32 v105, s30, v95
	v_mul_f32_e32 v94, s30, v92
	v_mul_f32_e32 v95, s30, v93
	v_cvt_pk_bf16_f32 v92, v100, v101
	v_cvt_pk_bf16_f32 v93, v102, v103
	v_mul_f32_e32 v68, s30, v68
	v_mul_f32_e32 v69, s30, v69
	v_cvt_pk_bf16_f32 v94, v94, v95
	v_cvt_pk_bf16_f32 v95, v104, v105
	global_store_dwordx4 v[108:109], v[92:95], off offset:256
	v_mul_f32_e32 v70, s30, v70
	v_mul_f32_e32 v71, s30, v71
	v_mul_f32_e32 v62, s30, v62
	v_mul_f32_e32 v63, s30, v63
	v_or_b32_e32 v92, 32, v140
	v_mad_i64_i32 v[92:93], s[10:11], v92, s87, v[128:129]
	v_lshl_add_u64 v[92:93], v[92:93], 0, v[130:131]
	v_mul_f32_e32 v94, s30, v98
	v_mul_f32_e32 v95, s30, v99
	v_mul_f32_e32 v98, s30, v90
	v_mul_f32_e32 v99, s30, v91
	v_mul_f32_e32 v90, s30, v88
	v_mul_f32_e32 v91, s30, v89
	v_cvt_pk_bf16_f32 v88, v96, v97
	v_cvt_pk_bf16_f32 v89, v94, v95
	v_mul_f32_e32 v60, s30, v60
	v_mul_f32_e32 v61, s30, v61
	v_cvt_pk_bf16_f32 v90, v90, v91
	v_cvt_pk_bf16_f32 v91, v98, v99
	global_store_dwordx4 v[92:93], v[88:91], off
	v_mul_f32_e32 v52, s30, v52
	v_mul_f32_e32 v53, s30, v53
	v_mul_f32_e32 v54, s30, v54
	v_mul_f32_e32 v55, s30, v55
	v_mul_f32_e32 v88, s30, v78
	v_mul_f32_e32 v89, s30, v79
	v_mul_f32_e32 v78, s30, v76
	v_mul_f32_e32 v79, s30, v77
	v_cvt_pk_bf16_f32 v76, v84, v85
	v_cvt_pk_bf16_f32 v77, v86, v87
	v_mul_f32_e32 v48, s30, v48
	v_mul_f32_e32 v49, s30, v49
	v_cvt_pk_bf16_f32 v78, v78, v79
	v_cvt_pk_bf16_f32 v79, v88, v89
	global_store_dwordx4 v[92:93], v[76:79], off offset:256
	v_mul_f32_e32 v36, s30, v36
	v_mul_f32_e32 v37, s30, v37
	v_mul_f32_e32 v38, s30, v38
	v_mul_f32_e32 v39, s30, v39
	v_or_b32_e32 v76, 48, v140
	v_mad_i64_i32 v[76:77], s[10:11], v76, s87, v[128:129]
	v_lshl_add_u64 v[76:77], v[76:77], 0, v[130:131]
	v_mul_f32_e32 v78, s30, v82
	v_mul_f32_e32 v79, s30, v83
	v_mul_f32_e32 v82, s30, v74
	v_mul_f32_e32 v83, s30, v75
	v_mul_f32_e32 v74, s30, v72
	v_mul_f32_e32 v75, s30, v73
	v_cvt_pk_bf16_f32 v72, v80, v81
	v_cvt_pk_bf16_f32 v73, v78, v79
	v_mul_f32_e32 v32, s30, v32
	v_mul_f32_e32 v33, s30, v33
	v_cvt_pk_bf16_f32 v74, v74, v75
	v_cvt_pk_bf16_f32 v75, v82, v83
	global_store_dwordx4 v[76:77], v[72:75], off
	v_mul_f32_e32 v20, s30, v20
	v_mul_f32_e32 v21, s30, v21
	v_mul_f32_e32 v22, s30, v22
	v_mul_f32_e32 v23, s30, v23
	v_mul_f32_e32 v72, s30, v66
	v_mul_f32_e32 v73, s30, v67
	v_mul_f32_e32 v66, s30, v64
	v_mul_f32_e32 v67, s30, v65
	v_cvt_pk_bf16_f32 v64, v68, v69
	v_cvt_pk_bf16_f32 v65, v70, v71
	v_mul_f32_e32 v16, s30, v16
	v_mul_f32_e32 v17, s30, v17
	v_cvt_pk_bf16_f32 v66, v66, v67
	v_cvt_pk_bf16_f32 v67, v72, v73
	global_store_dwordx4 v[76:77], v[64:67], off offset:256
	s_andn2_b64 vcc, exec, s[34:35]
	v_readlane_b32 s96, v254, 10
	v_add_u32_e32 v64, 0x80, v140
	v_mad_i64_i32 v[64:65], s[10:11], v64, s87, v[128:129]
	v_lshl_add_u64 v[64:65], v[64:65], 0, v[130:131]
	v_mul_f32_e32 v66, s30, v58
	v_mul_f32_e32 v67, s30, v59
	v_mul_f32_e32 v58, s30, v56
	v_mul_f32_e32 v59, s30, v57
	v_cvt_pk_bf16_f32 v56, v60, v61
	v_cvt_pk_bf16_f32 v57, v62, v63
	v_mul_f32_e32 v6, s30, v6
	v_mul_f32_e32 v7, s30, v7
	v_cvt_pk_bf16_f32 v58, v58, v59
	v_cvt_pk_bf16_f32 v59, v66, v67
	global_store_dwordx4 v[64:65], v[56:59], off
	v_mul_f32_e32 v4, s30, v4
	v_mul_f32_e32 v5, s30, v5
	v_readlane_b32 s97, v254, 11
	v_mul_f32_e32 v56, s30, v46
	v_mul_f32_e32 v57, s30, v47
	v_mul_f32_e32 v46, s30, v44
	v_mul_f32_e32 v47, s30, v45
	v_cvt_pk_bf16_f32 v44, v52, v53
	v_cvt_pk_bf16_f32 v45, v54, v55
	s_nop 0
	v_cvt_pk_bf16_f32 v46, v46, v47
	v_cvt_pk_bf16_f32 v47, v56, v57
	global_store_dwordx4 v[64:65], v[44:47], off offset:256
	s_nop 1
	v_add_u32_e32 v44, 0x90, v140
	v_mad_i64_i32 v[44:45], s[10:11], v44, s87, v[128:129]
	v_lshl_add_u64 v[44:45], v[44:45], 0, v[130:131]
	v_mul_f32_e32 v46, s30, v50
	v_mul_f32_e32 v47, s30, v51
	v_mul_f32_e32 v50, s30, v42
	v_mul_f32_e32 v51, s30, v43
	v_mul_f32_e32 v42, s30, v40
	v_mul_f32_e32 v43, s30, v41
	v_cvt_pk_bf16_f32 v40, v48, v49
	v_cvt_pk_bf16_f32 v41, v46, v47
	s_nop 0
	v_cvt_pk_bf16_f32 v42, v42, v43
	v_cvt_pk_bf16_f32 v43, v50, v51
	global_store_dwordx4 v[44:45], v[40:43], off
	s_nop 1
	v_mul_f32_e32 v40, s30, v30
	v_mul_f32_e32 v41, s30, v31
	v_mul_f32_e32 v30, s30, v28
	v_mul_f32_e32 v31, s30, v29
	v_cvt_pk_bf16_f32 v28, v36, v37
	v_cvt_pk_bf16_f32 v29, v38, v39
	s_nop 0
	v_cvt_pk_bf16_f32 v30, v30, v31
	v_cvt_pk_bf16_f32 v31, v40, v41
	global_store_dwordx4 v[44:45], v[28:31], off offset:256
	s_nop 1
	v_add_u32_e32 v28, 0xa0, v140
	v_mad_i64_i32 v[28:29], s[10:11], v28, s87, v[128:129]
	v_lshl_add_u64 v[28:29], v[28:29], 0, v[130:131]
	v_mul_f32_e32 v30, s30, v34
	v_mul_f32_e32 v31, s30, v35
	v_mul_f32_e32 v34, s30, v26
	v_mul_f32_e32 v35, s30, v27
	v_mul_f32_e32 v26, s30, v24
	v_mul_f32_e32 v27, s30, v25
	v_cvt_pk_bf16_f32 v24, v32, v33
	v_cvt_pk_bf16_f32 v25, v30, v31
	s_nop 0
	v_cvt_pk_bf16_f32 v26, v26, v27
	v_cvt_pk_bf16_f32 v27, v34, v35
	global_store_dwordx4 v[28:29], v[24:27], off
	s_nop 1
	v_mul_f32_e32 v24, s30, v14
	v_mul_f32_e32 v25, s30, v15
	v_mul_f32_e32 v14, s30, v12
	v_mul_f32_e32 v15, s30, v13
	v_cvt_pk_bf16_f32 v12, v20, v21
	v_cvt_pk_bf16_f32 v13, v22, v23
	s_nop 0
	v_cvt_pk_bf16_f32 v14, v14, v15
	v_cvt_pk_bf16_f32 v15, v24, v25
	global_store_dwordx4 v[28:29], v[12:15], off offset:256
	s_nop 1
	v_add_u32_e32 v12, 0xb0, v140
	v_mad_i64_i32 v[12:13], s[10:11], v12, s87, v[128:129]
	v_lshl_add_u64 v[12:13], v[12:13], 0, v[130:131]
	v_mul_f32_e32 v14, s30, v18
	v_mul_f32_e32 v15, s30, v19
	v_mul_f32_e32 v18, s30, v10
	v_mul_f32_e32 v19, s30, v11
	v_mul_f32_e32 v10, s30, v8
	v_mul_f32_e32 v11, s30, v9
	v_cvt_pk_bf16_f32 v8, v16, v17
	v_cvt_pk_bf16_f32 v9, v14, v15
	s_mov_b64 s[10:11], -1
	v_cvt_pk_bf16_f32 v10, v10, v11
	v_cvt_pk_bf16_f32 v11, v18, v19
	global_store_dwordx4 v[12:13], v[8:11], off
	s_nop 1
	v_mul_f32_e32 v8, s30, v2
	v_mul_f32_e32 v9, s30, v3
	v_mul_f32_e32 v2, s30, v0
	v_mul_f32_e32 v3, s30, v1
	v_cvt_pk_bf16_f32 v0, v4, v5
	v_cvt_pk_bf16_f32 v1, v6, v7
	s_nop 0
	v_cvt_pk_bf16_f32 v2, v2, v3
	v_cvt_pk_bf16_f32 v3, v8, v9
	global_store_dwordx4 v[12:13], v[0:3], off offset:256
	s_cbranch_vccnz .LBB0_980
	s_andn2_b64 vcc, exec, s[0:1]
	s_cbranch_vccnz .LBB0_979
	s_barrier
	s_branch .LBB0_979

.LBB0_1427:
	s_lshl_b32 s10, s21, 8
	s_add_i32 s21, s10, s59
	s_lshl_b32 s10, s20, 8
	v_mbcnt_lo_u32_b32 v78, -1, 0
	v_mbcnt_hi_u32_b32 v78, -1, v78
	s_ashr_i32 s11, s10, 31
	v_ashrrev_i32_e32 v76, 1, v78
	v_and_b32_e32 v76, -8, v76
	s_lshl_b64 s[10:11], s[10:11], 2
	v_add_u32_e32 v76, s60, v76
	s_add_u32 s10, s48, s10
	s_addc_u32 s11, s49, s11
	v_ashrrev_i32_e32 v77, 31, v76
	v_lshl_add_u64 v[80:81], v[76:77], 2, s[10:11]
	global_load_dwordx4 v[96:99], v[80:81], off
	global_load_dwordx4 v[92:95], v[80:81], off offset:16
	v_and_or_b32 v78, v78, 15, s21
	v_ashrrev_i32_e32 v79, 31, v78
	v_lshlrev_b64 v[148:149], 9, v[78:79]
	v_lshlrev_b64 v[150:151], 1, v[76:77]
	global_load_dwordx4 v[76:79], v[80:81], off offset:528
	s_nop 0
	global_load_dwordx4 v[80:83], v[80:81], off offset:512
	s_ashr_i32 s21, s20, 31
	s_lshl_b64 s[10:11], s[20:21], 21
	v_lshl_add_u64 v[152:153], v[148:149], 0, s[10:11]
	v_lshl_add_u64 v[148:149], s[2:3], 0, v[152:153]
	v_lshl_add_u64 v[148:149], v[148:149], 0, v[150:151]
	s_waitcnt vmcnt(3)
	v_add_f32_e32 v146, v146, v98
	v_add_f32_e32 v147, v147, v99
	v_add_f32_e32 v144, v144, v96
	v_add_f32_e32 v145, v145, v97
	s_waitcnt vmcnt(2)
	v_add_f32_e32 v154, v142, v94
	v_add_f32_e32 v155, v143, v95
	v_add_f32_e32 v142, v140, v92
	v_add_f32_e32 v143, v141, v93
	v_mul_f32_e32 v140, 0x3d372713, v144
	v_mul_f32_e32 v141, 0x3d372713, v145
	v_mul_f32_e32 v156, 0x3d372713, v146
	v_mul_f32_e32 v157, 0x3d372713, v147
	v_mul_f32_e32 v140, v144, v140
	v_mul_f32_e32 v141, v145, v141
	v_mul_f32_e32 v156, v146, v156
	v_mul_f32_e32 v157, v147, v157
	v_fma_f32 v140, v144, v140, v144
	v_fma_f32 v141, v145, v141, v145
	v_fma_f32 v156, v146, v156, v146
	v_fma_f32 v157, v147, v157, v147
	v_mul_f32_e32 v140, 0x3f4c422a, v140
	v_mul_f32_e32 v141, 0x3f4c422a, v141
	v_mul_f32_e32 v156, 0x3f4c422a, v156
	v_mul_f32_e32 v157, 0x3f4c422a, v157
	v_add_f32_e32 v140, v140, v140
	v_add_f32_e32 v141, v141, v141
	v_add_f32_e32 v156, v156, v156
	v_add_f32_e32 v157, v157, v157
	v_mul_f32_e32 v158, 0x3d372713, v142
	v_mul_f32_e32 v159, 0x3d372713, v143
	v_mul_f32_e32 v140, 0xbfb8aa3b, v140
	v_mul_f32_e32 v141, 0xbfb8aa3b, v141
	v_mul_f32_e32 v156, 0xbfb8aa3b, v156
	v_mul_f32_e32 v157, 0xbfb8aa3b, v157
	v_mul_f32_e32 v160, 0x3d372713, v154
	v_mul_f32_e32 v158, v142, v158
	v_mul_f32_e32 v159, v143, v159
	v_exp_f32_e32 v140, v140
	v_exp_f32_e32 v141, v141
	v_exp_f32_e32 v156, v156
	v_exp_f32_e32 v157, v157
	v_mul_f32_e32 v161, 0x3d372713, v155
	v_mul_f32_e32 v160, v154, v160
	v_fma_f32 v158, v142, v158, v142
	v_fma_f32 v159, v143, v159, v143
	v_mul_f32_e32 v161, v155, v161
	v_fma_f32 v160, v154, v160, v154
	v_mul_f32_e32 v158, 0x3f4c422a, v158
	v_mul_f32_e32 v159, 0x3f4c422a, v159
	v_fma_f32 v161, v155, v161, v155
	v_mul_f32_e32 v160, 0x3f4c422a, v160
	v_add_f32_e32 v158, v158, v158
	v_add_f32_e32 v159, v159, v159
	v_mul_f32_e32 v161, 0x3f4c422a, v161
	v_add_f32_e32 v160, v160, v160
	v_mul_f32_e32 v158, 0xbfb8aa3b, v158
	v_mul_f32_e32 v159, 0xbfb8aa3b, v159
	v_add_f32_e32 v140, 1.0, v140
	v_add_f32_e32 v141, 1.0, v141
	v_add_f32_e32 v156, 1.0, v156
	v_add_f32_e32 v157, 1.0, v157
	v_add_f32_e32 v161, v161, v161
	v_mul_f32_e32 v160, 0xbfb8aa3b, v160
	v_exp_f32_e32 v158, v158
	v_exp_f32_e32 v159, v159
	v_rcp_f32_e32 v140, v140
	v_rcp_f32_e32 v141, v141
	v_rcp_f32_e32 v156, v156
	v_rcp_f32_e32 v157, v157
	v_mul_f32_e32 v161, 0xbfb8aa3b, v161
	v_exp_f32_e32 v160, v160
	v_exp_f32_e32 v161, v161
	v_add_f32_e32 v158, 1.0, v158
	v_add_f32_e32 v159, 1.0, v159
	v_mul_f32_e32 v140, v144, v140
	v_mul_f32_e32 v141, v145, v141
	v_mul_f32_e32 v144, v146, v156
	v_mul_f32_e32 v145, v147, v157
	v_rcp_f32_e32 v158, v158
	v_cvt_pk_bf16_f32 v140, v140, v141
	v_cvt_pk_bf16_f32 v141, v144, v145
	v_rcp_f32_e32 v144, v159
	v_add_f32_e32 v145, 1.0, v160
	v_rcp_f32_e32 v145, v145
	v_add_f32_e32 v146, 1.0, v161
	v_rcp_f32_e32 v146, v146
	v_mul_f32_e32 v142, v142, v158
	v_mul_f32_e32 v143, v143, v144
	v_cvt_pk_bf16_f32 v142, v142, v143
	v_mul_f32_e32 v143, v154, v145
	s_waitcnt vmcnt(0)
	v_add_f32_e32 v136, v136, v80
	v_add_f32_e32 v137, v137, v81
	v_mul_f32_e32 v144, v155, v146
	v_cvt_pk_bf16_f32 v143, v143, v144
	global_store_dwordx4 v[148:149], v[140:143], off
	v_add_f32_e32 v138, v138, v82
	v_add_f32_e32 v139, v139, v83
	v_add_f32_e32 v128, v128, v96
	v_add_f32_e32 v129, v129, v97
	v_add_f32_e32 v140, v134, v78
	v_add_f32_e32 v141, v135, v79
	v_mul_f32_e32 v134, 0x3d372713, v136
	v_mul_f32_e32 v134, v136, v134
	v_fma_f32 v134, v136, v134, v136
	v_mul_f32_e32 v134, 0x3f4c422a, v134
	v_add_f32_e32 v134, v134, v134
	v_mul_f32_e32 v134, 0xbfb8aa3b, v134
	v_exp_f32_e32 v142, v134
	v_mul_f32_e32 v134, 0x3d372713, v137
	v_mul_f32_e32 v134, v137, v134
	v_fma_f32 v134, v137, v134, v137
	v_mul_f32_e32 v134, 0x3f4c422a, v134
	v_add_f32_e32 v134, v134, v134
	v_mul_f32_e32 v134, 0xbfb8aa3b, v134
	v_exp_f32_e32 v143, v134
	v_add_f32_e32 v134, v132, v76
	v_add_f32_e32 v135, v133, v77
	v_add_f32_e32 v132, 1.0, v142
	v_mul_f32_e32 v142, 0x3d372713, v138
	v_mul_f32_e32 v142, v138, v142
	v_fma_f32 v142, v138, v142, v138
	v_mul_f32_e32 v142, 0x3f4c422a, v142
	v_add_f32_e32 v133, 1.0, v143
	v_add_f32_e32 v142, v142, v142
	v_rcp_f32_e32 v132, v132
	v_rcp_f32_e32 v133, v133
	v_mul_f32_e32 v142, 0xbfb8aa3b, v142
	v_exp_f32_e32 v142, v142
	v_mul_f32_e32 v132, v136, v132
	v_mul_f32_e32 v133, v137, v133
	v_mul_f32_e32 v136, 0x3d372713, v139
	v_mul_f32_e32 v137, 0x3d372713, v134
	v_cvt_pk_bf16_f32 v132, v132, v133
	v_add_f32_e32 v133, 1.0, v142
	v_mul_f32_e32 v136, v139, v136
	v_mul_f32_e32 v137, v134, v137
	v_rcp_f32_e32 v133, v133
	v_fma_f32 v136, v139, v136, v139
	v_fma_f32 v137, v134, v137, v134
	v_mul_f32_e32 v136, 0x3f4c422a, v136
	v_mul_f32_e32 v137, 0x3f4c422a, v137
	v_add_f32_e32 v136, v136, v136
	v_add_f32_e32 v137, v137, v137
	v_mul_f32_e32 v136, 0xbfb8aa3b, v136
	v_mul_f32_e32 v137, 0xbfb8aa3b, v137
	v_exp_f32_e32 v136, v136
	v_exp_f32_e32 v137, v137
	v_mul_f32_e32 v133, v138, v133
	v_mul_f32_e32 v138, 0x3d372713, v135
	v_mul_f32_e32 v138, v135, v138
	v_fma_f32 v138, v135, v138, v135
	v_mul_f32_e32 v138, 0x3f4c422a, v138
	v_add_f32_e32 v136, 1.0, v136
	v_add_f32_e32 v137, 1.0, v137
	v_add_f32_e32 v138, v138, v138
	v_rcp_f32_e32 v136, v136
	v_rcp_f32_e32 v137, v137
	v_mul_f32_e32 v138, 0xbfb8aa3b, v138
	v_exp_f32_e32 v138, v138
	v_mul_f32_e32 v136, v139, v136
	v_mul_f32_e32 v134, v134, v137
	v_mul_f32_e32 v137, 0x3d372713, v140
	v_cvt_pk_bf16_f32 v133, v133, v136
	v_add_f32_e32 v136, 1.0, v138
	v_mul_f32_e32 v137, v140, v137
	v_mul_f32_e32 v138, 0x3d372713, v141
	v_fma_f32 v137, v140, v137, v140
	v_mul_f32_e32 v138, v141, v138
	v_mul_f32_e32 v137, 0x3f4c422a, v137
	v_fma_f32 v138, v141, v138, v141
	v_add_f32_e32 v137, v137, v137
	v_mul_f32_e32 v138, 0x3f4c422a, v138
	v_mul_f32_e32 v137, 0xbfb8aa3b, v137
	v_add_f32_e32 v138, v138, v138
	v_exp_f32_e32 v137, v137
	v_mul_f32_e32 v138, 0xbfb8aa3b, v138
	v_exp_f32_e32 v138, v138
	v_rcp_f32_e32 v136, v136
	v_add_f32_e32 v137, 1.0, v137
	v_rcp_f32_e32 v137, v137
	v_add_f32_e32 v138, 1.0, v138
	v_rcp_f32_e32 v138, v138
	v_mul_f32_e32 v135, v135, v136
	v_cvt_pk_bf16_f32 v134, v134, v135
	v_mul_f32_e32 v135, v140, v137
	v_mul_f32_e32 v136, v141, v138
	v_cvt_pk_bf16_f32 v135, v135, v136
	global_store_dwordx4 v[148:149], v[132:135], off offset:256
	v_add_f32_e32 v130, v130, v98
	v_add_f32_e32 v131, v131, v99
	v_add_f32_e32 v120, v120, v80
	v_add_f32_e32 v121, v121, v81
	v_add_f32_e32 v134, v126, v94
	v_add_f32_e32 v135, v127, v95
	v_mul_f32_e32 v126, 0x3d372713, v128
	v_mul_f32_e32 v126, v128, v126
	v_fma_f32 v126, v128, v126, v128
	v_mul_f32_e32 v126, 0x3f4c422a, v126
	v_add_f32_e32 v126, v126, v126
	v_mul_f32_e32 v126, 0xbfb8aa3b, v126
	v_exp_f32_e32 v136, v126
	v_mul_f32_e32 v126, 0x3d372713, v129
	v_mul_f32_e32 v126, v129, v126
	v_fma_f32 v126, v129, v126, v129
	v_mul_f32_e32 v126, 0x3f4c422a, v126
	v_add_f32_e32 v126, v126, v126
	v_mul_f32_e32 v126, 0xbfb8aa3b, v126
	v_exp_f32_e32 v137, v126
	v_add_f32_e32 v126, v124, v92
	v_add_f32_e32 v127, v125, v93
	v_add_f32_e32 v124, 1.0, v136
	v_mul_f32_e32 v136, 0x3d372713, v130
	v_mul_f32_e32 v136, v130, v136
	v_fma_f32 v136, v130, v136, v130
	v_mul_f32_e32 v136, 0x3f4c422a, v136
	v_add_f32_e32 v125, 1.0, v137
	v_add_f32_e32 v136, v136, v136
	v_rcp_f32_e32 v124, v124
	v_rcp_f32_e32 v125, v125
	v_mul_f32_e32 v136, 0xbfb8aa3b, v136
	v_exp_f32_e32 v136, v136
	v_mul_f32_e32 v124, v128, v124
	v_mul_f32_e32 v125, v129, v125
	v_mul_f32_e32 v128, 0x3d372713, v131
	v_mul_f32_e32 v129, 0x3d372713, v126
	v_cvt_pk_bf16_f32 v124, v124, v125
	v_add_f32_e32 v125, 1.0, v136
	v_mul_f32_e32 v128, v131, v128
	v_mul_f32_e32 v129, v126, v129
	v_rcp_f32_e32 v125, v125
	v_fma_f32 v128, v131, v128, v131
	v_fma_f32 v129, v126, v129, v126
	v_mul_f32_e32 v128, 0x3f4c422a, v128
	v_mul_f32_e32 v129, 0x3f4c422a, v129
	v_add_f32_e32 v128, v128, v128
	v_add_f32_e32 v129, v129, v129
	v_mul_f32_e32 v128, 0xbfb8aa3b, v128
	v_mul_f32_e32 v129, 0xbfb8aa3b, v129
	v_exp_f32_e32 v128, v128
	v_exp_f32_e32 v129, v129
	v_mul_f32_e32 v125, v130, v125
	v_mul_f32_e32 v130, 0x3d372713, v127
	v_mul_f32_e32 v130, v127, v130
	v_fma_f32 v130, v127, v130, v127
	v_mul_f32_e32 v130, 0x3f4c422a, v130
	v_add_f32_e32 v128, 1.0, v128
	v_add_f32_e32 v129, 1.0, v129
	v_add_f32_e32 v130, v130, v130
	v_rcp_f32_e32 v128, v128
	v_rcp_f32_e32 v129, v129
	v_mul_f32_e32 v130, 0xbfb8aa3b, v130
	v_exp_f32_e32 v130, v130
	v_mul_f32_e32 v128, v131, v128
	v_mul_f32_e32 v126, v126, v129
	v_mul_f32_e32 v129, 0x3d372713, v134
	v_cvt_pk_bf16_f32 v125, v125, v128
	v_add_f32_e32 v128, 1.0, v130
	v_mul_f32_e32 v129, v134, v129
	v_mul_f32_e32 v130, 0x3d372713, v135
	v_fma_f32 v129, v134, v129, v134
	v_mul_f32_e32 v130, v135, v130
	v_mul_f32_e32 v129, 0x3f4c422a, v129
	v_fma_f32 v130, v135, v130, v135
	v_add_f32_e32 v129, v129, v129
	v_mul_f32_e32 v130, 0x3f4c422a, v130
	v_mul_f32_e32 v129, 0xbfb8aa3b, v129
	v_add_f32_e32 v130, v130, v130
	v_exp_f32_e32 v129, v129
	v_mul_f32_e32 v130, 0xbfb8aa3b, v130
	v_exp_f32_e32 v130, v130
	v_rcp_f32_e32 v128, v128
	v_add_f32_e32 v129, 1.0, v129
	v_rcp_f32_e32 v129, v129
	v_add_f32_e32 v130, 1.0, v130
	v_rcp_f32_e32 v130, v130
	v_or_b32_e32 v132, 0x2000, v152
	v_mov_b32_e32 v133, v153
	v_lshl_add_u64 v[132:133], s[2:3], 0, v[132:133]
	v_mul_f32_e32 v127, v127, v128
	v_lshl_add_u64 v[132:133], v[132:133], 0, v[150:151]
	v_cvt_pk_bf16_f32 v126, v126, v127
	v_mul_f32_e32 v127, v134, v129
	v_mul_f32_e32 v128, v135, v130
	v_cvt_pk_bf16_f32 v127, v127, v128
	global_store_dwordx4 v[132:133], v[124:127], off
	v_add_f32_e32 v122, v122, v82
	v_add_f32_e32 v123, v123, v83
	v_add_f32_e32 v112, v112, v96
	v_add_f32_e32 v113, v113, v97
	v_add_f32_e32 v124, v118, v78
	v_add_f32_e32 v125, v119, v79
	v_mul_f32_e32 v118, 0x3d372713, v120
	v_mul_f32_e32 v118, v120, v118
	v_fma_f32 v118, v120, v118, v120
	v_mul_f32_e32 v118, 0x3f4c422a, v118
	v_add_f32_e32 v118, v118, v118
	v_mul_f32_e32 v118, 0xbfb8aa3b, v118
	v_exp_f32_e32 v126, v118
	v_mul_f32_e32 v118, 0x3d372713, v121
	v_mul_f32_e32 v118, v121, v118
	v_fma_f32 v118, v121, v118, v121
	v_mul_f32_e32 v118, 0x3f4c422a, v118
	v_add_f32_e32 v118, v118, v118
	v_mul_f32_e32 v118, 0xbfb8aa3b, v118
	v_exp_f32_e32 v127, v118
	v_add_f32_e32 v118, v116, v76
	v_add_f32_e32 v119, v117, v77
	v_add_f32_e32 v116, 1.0, v126
	v_mul_f32_e32 v126, 0x3d372713, v122
	v_mul_f32_e32 v126, v122, v126
	v_fma_f32 v126, v122, v126, v122
	v_mul_f32_e32 v126, 0x3f4c422a, v126
	v_add_f32_e32 v117, 1.0, v127
	v_add_f32_e32 v126, v126, v126
	v_rcp_f32_e32 v116, v116
	v_rcp_f32_e32 v117, v117
	v_mul_f32_e32 v126, 0xbfb8aa3b, v126
	v_exp_f32_e32 v126, v126
	v_mul_f32_e32 v116, v120, v116
	v_mul_f32_e32 v117, v121, v117
	v_mul_f32_e32 v120, 0x3d372713, v123
	v_mul_f32_e32 v121, 0x3d372713, v118
	v_cvt_pk_bf16_f32 v116, v116, v117
	v_add_f32_e32 v117, 1.0, v126
	v_mul_f32_e32 v120, v123, v120
	v_mul_f32_e32 v121, v118, v121
	v_rcp_f32_e32 v117, v117
	v_fma_f32 v120, v123, v120, v123
	v_fma_f32 v121, v118, v121, v118
	v_mul_f32_e32 v120, 0x3f4c422a, v120
	v_mul_f32_e32 v121, 0x3f4c422a, v121
	v_add_f32_e32 v120, v120, v120
	v_add_f32_e32 v121, v121, v121
	v_mul_f32_e32 v120, 0xbfb8aa3b, v120
	v_mul_f32_e32 v121, 0xbfb8aa3b, v121
	v_exp_f32_e32 v120, v120
	v_exp_f32_e32 v121, v121
	v_mul_f32_e32 v117, v122, v117
	v_mul_f32_e32 v122, 0x3d372713, v119
	v_mul_f32_e32 v122, v119, v122
	v_fma_f32 v122, v119, v122, v119
	v_mul_f32_e32 v122, 0x3f4c422a, v122
	v_add_f32_e32 v120, 1.0, v120
	v_add_f32_e32 v121, 1.0, v121
	v_add_f32_e32 v122, v122, v122
	v_rcp_f32_e32 v120, v120
	v_rcp_f32_e32 v121, v121
	v_mul_f32_e32 v122, 0xbfb8aa3b, v122
	v_exp_f32_e32 v122, v122
	v_mul_f32_e32 v120, v123, v120
	v_mul_f32_e32 v118, v118, v121
	v_mul_f32_e32 v121, 0x3d372713, v124
	v_cvt_pk_bf16_f32 v117, v117, v120
	v_add_f32_e32 v120, 1.0, v122
	v_mul_f32_e32 v121, v124, v121
	v_mul_f32_e32 v122, 0x3d372713, v125
	v_fma_f32 v121, v124, v121, v124
	v_mul_f32_e32 v122, v125, v122
	v_mul_f32_e32 v121, 0x3f4c422a, v121
	v_fma_f32 v122, v125, v122, v125
	v_add_f32_e32 v121, v121, v121
	v_mul_f32_e32 v122, 0x3f4c422a, v122
	v_mul_f32_e32 v121, 0xbfb8aa3b, v121
	v_add_f32_e32 v122, v122, v122
	v_exp_f32_e32 v121, v121
	v_mul_f32_e32 v122, 0xbfb8aa3b, v122
	v_exp_f32_e32 v122, v122
	v_rcp_f32_e32 v120, v120
	v_add_f32_e32 v121, 1.0, v121
	v_rcp_f32_e32 v121, v121
	v_add_f32_e32 v122, 1.0, v122
	v_rcp_f32_e32 v122, v122
	v_mul_f32_e32 v119, v119, v120
	v_cvt_pk_bf16_f32 v118, v118, v119
	v_mul_f32_e32 v119, v124, v121
	v_mul_f32_e32 v120, v125, v122
	v_cvt_pk_bf16_f32 v119, v119, v120
	global_store_dwordx4 v[132:133], v[116:119], off offset:256
	v_add_f32_e32 v114, v114, v98
	v_add_f32_e32 v115, v115, v99
	v_add_f32_e32 v104, v104, v80
	v_add_f32_e32 v105, v105, v81
	v_add_f32_e32 v118, v110, v94
	v_add_f32_e32 v119, v111, v95
	v_mul_f32_e32 v110, 0x3d372713, v112
	v_mul_f32_e32 v110, v112, v110
	v_fma_f32 v110, v112, v110, v112
	v_mul_f32_e32 v110, 0x3f4c422a, v110
	v_add_f32_e32 v110, v110, v110
	v_mul_f32_e32 v110, 0xbfb8aa3b, v110
	v_exp_f32_e32 v120, v110
	v_mul_f32_e32 v110, 0x3d372713, v113
	v_mul_f32_e32 v110, v113, v110
	v_fma_f32 v110, v113, v110, v113
	v_mul_f32_e32 v110, 0x3f4c422a, v110
	v_add_f32_e32 v110, v110, v110
	v_mul_f32_e32 v110, 0xbfb8aa3b, v110
	v_exp_f32_e32 v121, v110
	v_add_f32_e32 v110, v108, v92
	v_add_f32_e32 v111, v109, v93
	v_add_f32_e32 v108, 1.0, v120
	v_mul_f32_e32 v120, 0x3d372713, v114
	v_mul_f32_e32 v120, v114, v120
	v_fma_f32 v120, v114, v120, v114
	v_mul_f32_e32 v120, 0x3f4c422a, v120
	v_add_f32_e32 v109, 1.0, v121
	v_add_f32_e32 v120, v120, v120
	v_rcp_f32_e32 v108, v108
	v_rcp_f32_e32 v109, v109
	v_mul_f32_e32 v120, 0xbfb8aa3b, v120
	v_exp_f32_e32 v120, v120
	v_mul_f32_e32 v108, v112, v108
	v_mul_f32_e32 v109, v113, v109
	v_mul_f32_e32 v112, 0x3d372713, v115
	v_mul_f32_e32 v113, 0x3d372713, v110
	v_cvt_pk_bf16_f32 v108, v108, v109
	v_add_f32_e32 v109, 1.0, v120
	v_mul_f32_e32 v112, v115, v112
	v_mul_f32_e32 v113, v110, v113
	v_rcp_f32_e32 v109, v109
	v_fma_f32 v112, v115, v112, v115
	v_fma_f32 v113, v110, v113, v110
	v_mul_f32_e32 v112, 0x3f4c422a, v112
	v_mul_f32_e32 v113, 0x3f4c422a, v113
	v_add_f32_e32 v112, v112, v112
	v_add_f32_e32 v113, v113, v113
	v_mul_f32_e32 v112, 0xbfb8aa3b, v112
	v_mul_f32_e32 v113, 0xbfb8aa3b, v113
	v_exp_f32_e32 v112, v112
	v_exp_f32_e32 v113, v113
	v_mul_f32_e32 v109, v114, v109
	v_mul_f32_e32 v114, 0x3d372713, v111
	v_mul_f32_e32 v114, v111, v114
	v_fma_f32 v114, v111, v114, v111
	v_mul_f32_e32 v114, 0x3f4c422a, v114
	v_add_f32_e32 v112, 1.0, v112
	v_add_f32_e32 v113, 1.0, v113
	v_add_f32_e32 v114, v114, v114
	v_rcp_f32_e32 v112, v112
	v_rcp_f32_e32 v113, v113
	v_mul_f32_e32 v114, 0xbfb8aa3b, v114
	v_exp_f32_e32 v114, v114
	v_mul_f32_e32 v112, v115, v112
	v_mul_f32_e32 v110, v110, v113
	v_mul_f32_e32 v113, 0x3d372713, v118
	v_cvt_pk_bf16_f32 v109, v109, v112
	v_add_f32_e32 v112, 1.0, v114
	v_mul_f32_e32 v113, v118, v113
	v_mul_f32_e32 v114, 0x3d372713, v119
	v_fma_f32 v113, v118, v113, v118
	v_mul_f32_e32 v114, v119, v114
	v_mul_f32_e32 v113, 0x3f4c422a, v113
	v_fma_f32 v114, v119, v114, v119
	v_add_f32_e32 v113, v113, v113
	v_mul_f32_e32 v114, 0x3f4c422a, v114
	v_mul_f32_e32 v113, 0xbfb8aa3b, v113
	v_add_f32_e32 v114, v114, v114
	v_exp_f32_e32 v113, v113
	v_mul_f32_e32 v114, 0xbfb8aa3b, v114
	v_exp_f32_e32 v114, v114
	v_rcp_f32_e32 v112, v112
	v_add_f32_e32 v113, 1.0, v113
	v_rcp_f32_e32 v113, v113
	v_add_f32_e32 v114, 1.0, v114
	v_rcp_f32_e32 v114, v114
	v_or_b32_e32 v116, 0x4000, v152
	v_mov_b32_e32 v117, v153
	v_lshl_add_u64 v[116:117], s[2:3], 0, v[116:117]
	v_mul_f32_e32 v111, v111, v112
	v_lshl_add_u64 v[116:117], v[116:117], 0, v[150:151]
	v_cvt_pk_bf16_f32 v110, v110, v111
	v_mul_f32_e32 v111, v118, v113
	v_mul_f32_e32 v112, v119, v114
	v_cvt_pk_bf16_f32 v111, v111, v112
	global_store_dwordx4 v[116:117], v[108:111], off
	v_add_f32_e32 v106, v106, v82
	v_add_f32_e32 v107, v107, v83
	v_add_f32_e32 v88, v88, v96
	v_add_f32_e32 v89, v89, v97
	v_add_f32_e32 v108, v102, v78
	v_add_f32_e32 v109, v103, v79
	v_mul_f32_e32 v102, 0x3d372713, v104
	v_mul_f32_e32 v102, v104, v102
	v_fma_f32 v102, v104, v102, v104
	v_mul_f32_e32 v102, 0x3f4c422a, v102
	v_add_f32_e32 v102, v102, v102
	v_mul_f32_e32 v102, 0xbfb8aa3b, v102
	v_exp_f32_e32 v110, v102
	v_mul_f32_e32 v102, 0x3d372713, v105
	v_mul_f32_e32 v102, v105, v102
	v_fma_f32 v102, v105, v102, v105
	v_mul_f32_e32 v102, 0x3f4c422a, v102
	v_add_f32_e32 v102, v102, v102
	v_mul_f32_e32 v102, 0xbfb8aa3b, v102
	v_exp_f32_e32 v111, v102
	v_add_f32_e32 v102, v100, v76
	v_add_f32_e32 v103, v101, v77
	v_add_f32_e32 v100, 1.0, v110
	v_mul_f32_e32 v110, 0x3d372713, v106
	v_mul_f32_e32 v110, v106, v110
	v_fma_f32 v110, v106, v110, v106
	v_mul_f32_e32 v110, 0x3f4c422a, v110
	v_add_f32_e32 v101, 1.0, v111
	v_add_f32_e32 v110, v110, v110
	v_rcp_f32_e32 v100, v100
	v_rcp_f32_e32 v101, v101
	v_mul_f32_e32 v110, 0xbfb8aa3b, v110
	v_exp_f32_e32 v110, v110
	v_mul_f32_e32 v100, v104, v100
	v_mul_f32_e32 v101, v105, v101
	v_mul_f32_e32 v104, 0x3d372713, v107
	v_mul_f32_e32 v105, 0x3d372713, v102
	v_cvt_pk_bf16_f32 v100, v100, v101
	v_add_f32_e32 v101, 1.0, v110
	v_mul_f32_e32 v104, v107, v104
	v_mul_f32_e32 v105, v102, v105
	v_rcp_f32_e32 v101, v101
	v_fma_f32 v104, v107, v104, v107
	v_fma_f32 v105, v102, v105, v102
	v_mul_f32_e32 v104, 0x3f4c422a, v104
	v_mul_f32_e32 v105, 0x3f4c422a, v105
	v_add_f32_e32 v104, v104, v104
	v_add_f32_e32 v105, v105, v105
	v_mul_f32_e32 v104, 0xbfb8aa3b, v104
	v_mul_f32_e32 v105, 0xbfb8aa3b, v105
	v_exp_f32_e32 v104, v104
	v_exp_f32_e32 v105, v105
	v_mul_f32_e32 v101, v106, v101
	v_mul_f32_e32 v106, 0x3d372713, v103
	v_mul_f32_e32 v106, v103, v106
	v_fma_f32 v106, v103, v106, v103
	v_mul_f32_e32 v106, 0x3f4c422a, v106
	v_add_f32_e32 v104, 1.0, v104
	v_add_f32_e32 v105, 1.0, v105
	v_add_f32_e32 v106, v106, v106
	v_rcp_f32_e32 v104, v104
	v_rcp_f32_e32 v105, v105
	v_mul_f32_e32 v106, 0xbfb8aa3b, v106
	v_exp_f32_e32 v106, v106
	v_mul_f32_e32 v104, v107, v104
	v_mul_f32_e32 v102, v102, v105
	v_mul_f32_e32 v105, 0x3d372713, v108
	v_cvt_pk_bf16_f32 v101, v101, v104
	v_add_f32_e32 v104, 1.0, v106
	v_mul_f32_e32 v105, v108, v105
	v_mul_f32_e32 v106, 0x3d372713, v109
	v_fma_f32 v105, v108, v105, v108
	v_mul_f32_e32 v106, v109, v106
	v_mul_f32_e32 v105, 0x3f4c422a, v105
	v_fma_f32 v106, v109, v106, v109
	v_add_f32_e32 v105, v105, v105
	v_mul_f32_e32 v106, 0x3f4c422a, v106
	v_mul_f32_e32 v105, 0xbfb8aa3b, v105
	v_add_f32_e32 v106, v106, v106
	v_exp_f32_e32 v105, v105
	v_mul_f32_e32 v106, 0xbfb8aa3b, v106
	v_exp_f32_e32 v106, v106
	v_rcp_f32_e32 v104, v104
	v_add_f32_e32 v105, 1.0, v105
	v_rcp_f32_e32 v105, v105
	v_add_f32_e32 v106, 1.0, v106
	v_rcp_f32_e32 v106, v106
	v_mul_f32_e32 v103, v103, v104
	v_cvt_pk_bf16_f32 v102, v102, v103
	v_mul_f32_e32 v103, v108, v105
	v_mul_f32_e32 v104, v109, v106
	v_cvt_pk_bf16_f32 v103, v103, v104
	global_store_dwordx4 v[116:117], v[100:103], off offset:256
	v_add_f32_e32 v90, v90, v98
	v_add_f32_e32 v91, v91, v99
	v_or_b32_e32 v152, 0x6000, v152
	v_add_f32_e32 v102, v86, v94
	v_add_f32_e32 v103, v87, v95
	v_mul_f32_e32 v86, 0x3d372713, v88
	v_mul_f32_e32 v86, v88, v86
	v_fma_f32 v86, v88, v86, v88
	v_mul_f32_e32 v86, 0x3f4c422a, v86
	v_add_f32_e32 v86, v86, v86
	v_mul_f32_e32 v86, 0xbfb8aa3b, v86
	v_exp_f32_e32 v104, v86
	v_mul_f32_e32 v86, 0x3d372713, v89
	v_mul_f32_e32 v86, v89, v86
	v_fma_f32 v86, v89, v86, v89
	v_mul_f32_e32 v86, 0x3f4c422a, v86
	v_add_f32_e32 v86, v86, v86
	v_mul_f32_e32 v86, 0xbfb8aa3b, v86
	v_exp_f32_e32 v105, v86
	v_add_f32_e32 v86, v84, v92
	v_add_f32_e32 v87, v85, v93
	v_add_f32_e32 v84, 1.0, v104
	v_mul_f32_e32 v104, 0x3d372713, v90
	v_mul_f32_e32 v104, v90, v104
	v_fma_f32 v104, v90, v104, v90
	v_mul_f32_e32 v104, 0x3f4c422a, v104
	v_add_f32_e32 v85, 1.0, v105
	v_add_f32_e32 v104, v104, v104
	v_rcp_f32_e32 v84, v84
	v_rcp_f32_e32 v85, v85
	v_mul_f32_e32 v104, 0xbfb8aa3b, v104
	v_exp_f32_e32 v104, v104
	v_mul_f32_e32 v84, v88, v84
	v_mul_f32_e32 v85, v89, v85
	v_mul_f32_e32 v88, 0x3d372713, v91
	v_mul_f32_e32 v89, 0x3d372713, v86
	v_cvt_pk_bf16_f32 v84, v84, v85
	v_add_f32_e32 v85, 1.0, v104
	v_mul_f32_e32 v88, v91, v88
	v_mul_f32_e32 v89, v86, v89
	v_rcp_f32_e32 v85, v85
	v_fma_f32 v88, v91, v88, v91
	v_fma_f32 v89, v86, v89, v86
	v_mul_f32_e32 v88, 0x3f4c422a, v88
	v_mul_f32_e32 v89, 0x3f4c422a, v89
	v_add_f32_e32 v88, v88, v88
	v_add_f32_e32 v89, v89, v89
	v_mul_f32_e32 v88, 0xbfb8aa3b, v88
	v_mul_f32_e32 v89, 0xbfb8aa3b, v89
	v_exp_f32_e32 v88, v88
	v_exp_f32_e32 v89, v89
	v_mul_f32_e32 v85, v90, v85
	v_mul_f32_e32 v90, 0x3d372713, v87
	v_mul_f32_e32 v90, v87, v90
	v_fma_f32 v90, v87, v90, v87
	v_mul_f32_e32 v90, 0x3f4c422a, v90
	v_add_f32_e32 v88, 1.0, v88
	v_add_f32_e32 v89, 1.0, v89
	v_add_f32_e32 v90, v90, v90
	v_rcp_f32_e32 v88, v88
	v_rcp_f32_e32 v89, v89
	v_mul_f32_e32 v90, 0xbfb8aa3b, v90
	v_exp_f32_e32 v90, v90
	v_mul_f32_e32 v88, v91, v88
	v_mul_f32_e32 v86, v86, v89
	v_mul_f32_e32 v89, 0x3d372713, v102
	v_cvt_pk_bf16_f32 v85, v85, v88
	v_add_f32_e32 v88, 1.0, v90
	v_mul_f32_e32 v89, v102, v89
	v_mul_f32_e32 v90, 0x3d372713, v103
	v_fma_f32 v89, v102, v89, v102
	v_mul_f32_e32 v90, v103, v90
	v_mul_f32_e32 v89, 0x3f4c422a, v89
	v_fma_f32 v90, v103, v90, v103
	v_add_f32_e32 v89, v89, v89
	v_mul_f32_e32 v90, 0x3f4c422a, v90
	v_mul_f32_e32 v89, 0xbfb8aa3b, v89
	v_add_f32_e32 v90, v90, v90
	v_exp_f32_e32 v89, v89
	v_mul_f32_e32 v90, 0xbfb8aa3b, v90
	v_exp_f32_e32 v90, v90
	v_rcp_f32_e32 v88, v88
	v_add_f32_e32 v89, 1.0, v89
	v_rcp_f32_e32 v89, v89
	v_add_f32_e32 v90, 1.0, v90
	v_rcp_f32_e32 v90, v90
	v_lshl_add_u64 v[100:101], s[2:3], 0, v[152:153]
	v_mul_f32_e32 v87, v87, v88
	v_lshl_add_u64 v[100:101], v[100:101], 0, v[150:151]
	v_cvt_pk_bf16_f32 v86, v86, v87
	v_mul_f32_e32 v87, v102, v89
	v_add_f32_e32 v72, v72, v80
	v_add_f32_e32 v73, v73, v81
	v_mul_f32_e32 v88, v103, v90
	v_cvt_pk_bf16_f32 v87, v87, v88
	global_store_dwordx4 v[100:101], v[84:87], off
	v_add_f32_e32 v74, v74, v82
	v_add_f32_e32 v75, v75, v83
	v_add_f32_e32 v64, v64, v96
	v_add_f32_e32 v65, v65, v97
	v_add_f32_e32 v84, v70, v78
	v_add_f32_e32 v85, v71, v79
	v_mul_f32_e32 v70, 0x3d372713, v72
	v_mul_f32_e32 v70, v72, v70
	v_fma_f32 v70, v72, v70, v72
	v_mul_f32_e32 v70, 0x3f4c422a, v70
	v_add_f32_e32 v70, v70, v70
	v_mul_f32_e32 v70, 0xbfb8aa3b, v70
	v_exp_f32_e32 v86, v70
	v_mul_f32_e32 v70, 0x3d372713, v73
	v_mul_f32_e32 v70, v73, v70
	v_fma_f32 v70, v73, v70, v73
	v_mul_f32_e32 v70, 0x3f4c422a, v70
	v_add_f32_e32 v70, v70, v70
	v_mul_f32_e32 v70, 0xbfb8aa3b, v70
	v_exp_f32_e32 v87, v70
	v_add_f32_e32 v70, v68, v76
	v_add_f32_e32 v71, v69, v77
	v_add_f32_e32 v68, 1.0, v86
	v_mul_f32_e32 v86, 0x3d372713, v74
	v_mul_f32_e32 v86, v74, v86
	v_fma_f32 v86, v74, v86, v74
	v_mul_f32_e32 v86, 0x3f4c422a, v86
	v_add_f32_e32 v69, 1.0, v87
	v_add_f32_e32 v86, v86, v86
	v_rcp_f32_e32 v68, v68
	v_rcp_f32_e32 v69, v69
	v_mul_f32_e32 v86, 0xbfb8aa3b, v86
	v_exp_f32_e32 v86, v86
	v_mul_f32_e32 v68, v72, v68
	v_mul_f32_e32 v69, v73, v69
	v_mul_f32_e32 v72, 0x3d372713, v75
	v_mul_f32_e32 v73, 0x3d372713, v70
	v_cvt_pk_bf16_f32 v68, v68, v69
	v_add_f32_e32 v69, 1.0, v86
	v_mul_f32_e32 v72, v75, v72
	v_mul_f32_e32 v73, v70, v73
	v_rcp_f32_e32 v69, v69
	v_fma_f32 v72, v75, v72, v75
	v_fma_f32 v73, v70, v73, v70
	v_mul_f32_e32 v72, 0x3f4c422a, v72
	v_mul_f32_e32 v73, 0x3f4c422a, v73
	v_add_f32_e32 v72, v72, v72
	v_add_f32_e32 v73, v73, v73
	v_mul_f32_e32 v72, 0xbfb8aa3b, v72
	v_mul_f32_e32 v73, 0xbfb8aa3b, v73
	v_exp_f32_e32 v72, v72
	v_exp_f32_e32 v73, v73
	v_mul_f32_e32 v69, v74, v69
	v_mul_f32_e32 v74, 0x3d372713, v71
	v_mul_f32_e32 v74, v71, v74
	v_fma_f32 v74, v71, v74, v71
	v_mul_f32_e32 v74, 0x3f4c422a, v74
	v_add_f32_e32 v72, 1.0, v72
	v_add_f32_e32 v73, 1.0, v73
	v_add_f32_e32 v74, v74, v74
	v_rcp_f32_e32 v72, v72
	v_rcp_f32_e32 v73, v73
	v_mul_f32_e32 v74, 0xbfb8aa3b, v74
	v_exp_f32_e32 v74, v74
	v_mul_f32_e32 v72, v75, v72
	v_mul_f32_e32 v70, v70, v73
	v_mul_f32_e32 v73, 0x3d372713, v84
	v_cvt_pk_bf16_f32 v69, v69, v72
	v_add_f32_e32 v72, 1.0, v74
	v_mul_f32_e32 v73, v84, v73
	v_mul_f32_e32 v74, 0x3d372713, v85
	v_fma_f32 v73, v84, v73, v84
	v_mul_f32_e32 v74, v85, v74
	v_mul_f32_e32 v73, 0x3f4c422a, v73
	v_fma_f32 v74, v85, v74, v85
	v_add_f32_e32 v73, v73, v73
	v_mul_f32_e32 v74, 0x3f4c422a, v74
	v_mul_f32_e32 v73, 0xbfb8aa3b, v73
	v_add_f32_e32 v74, v74, v74
	v_exp_f32_e32 v73, v73
	v_mul_f32_e32 v74, 0xbfb8aa3b, v74
	v_exp_f32_e32 v74, v74
	v_rcp_f32_e32 v72, v72
	v_add_f32_e32 v73, 1.0, v73
	v_rcp_f32_e32 v73, v73
	v_add_f32_e32 v74, 1.0, v74
	v_rcp_f32_e32 v74, v74
	v_mul_f32_e32 v71, v71, v72
	v_cvt_pk_bf16_f32 v70, v70, v71
	v_mul_f32_e32 v71, v84, v73
	v_mul_f32_e32 v72, v85, v74
	v_cvt_pk_bf16_f32 v71, v71, v72
	global_store_dwordx4 v[100:101], v[68:71], off offset:256
	v_add_f32_e32 v66, v66, v98
	v_add_f32_e32 v67, v67, v99
	v_add_f32_e32 v56, v56, v80
	v_add_f32_e32 v57, v57, v81
	v_add_f32_e32 v70, v62, v94
	v_add_f32_e32 v71, v63, v95
	v_mul_f32_e32 v62, 0x3d372713, v64
	v_mul_f32_e32 v62, v64, v62
	v_fma_f32 v62, v64, v62, v64
	v_mul_f32_e32 v62, 0x3f4c422a, v62
	v_add_f32_e32 v62, v62, v62
	v_mul_f32_e32 v62, 0xbfb8aa3b, v62
	v_exp_f32_e32 v72, v62
	v_mul_f32_e32 v62, 0x3d372713, v65
	v_mul_f32_e32 v62, v65, v62
	v_fma_f32 v62, v65, v62, v65
	v_mul_f32_e32 v62, 0x3f4c422a, v62
	v_add_f32_e32 v62, v62, v62
	v_mul_f32_e32 v62, 0xbfb8aa3b, v62
	v_exp_f32_e32 v73, v62
	v_add_f32_e32 v62, v60, v92
	v_add_f32_e32 v63, v61, v93
	v_add_f32_e32 v60, 1.0, v72
	v_mul_f32_e32 v72, 0x3d372713, v66
	v_mul_f32_e32 v72, v66, v72
	v_fma_f32 v72, v66, v72, v66
	v_mul_f32_e32 v72, 0x3f4c422a, v72
	v_add_f32_e32 v61, 1.0, v73
	v_add_f32_e32 v72, v72, v72
	v_rcp_f32_e32 v60, v60
	v_rcp_f32_e32 v61, v61
	v_mul_f32_e32 v72, 0xbfb8aa3b, v72
	v_exp_f32_e32 v72, v72
	v_mul_f32_e32 v60, v64, v60
	v_mul_f32_e32 v61, v65, v61
	v_mul_f32_e32 v64, 0x3d372713, v67
	v_cvt_pk_bf16_f32 v60, v60, v61
	v_add_f32_e32 v61, 1.0, v72
	v_mul_f32_e32 v64, v67, v64
	v_mul_f32_e32 v65, 0x3d372713, v62
	v_rcp_f32_e32 v61, v61
	v_fma_f32 v64, v67, v64, v67
	v_mul_f32_e32 v65, v62, v65
	v_mul_f32_e32 v64, 0x3f4c422a, v64
	v_fma_f32 v65, v62, v65, v62
	v_add_f32_e32 v64, v64, v64
	v_mul_f32_e32 v65, 0x3f4c422a, v65
	v_mul_f32_e32 v64, 0xbfb8aa3b, v64
	v_add_f32_e32 v65, v65, v65
	v_exp_f32_e32 v64, v64
	v_mul_f32_e32 v65, 0xbfb8aa3b, v65
	v_mul_f32_e32 v61, v66, v61
	v_mul_f32_e32 v66, 0x3d372713, v63
	v_exp_f32_e32 v65, v65
	v_mul_f32_e32 v66, v63, v66
	v_fma_f32 v66, v63, v66, v63
	v_mul_f32_e32 v66, 0x3f4c422a, v66
	v_add_f32_e32 v64, 1.0, v64
	v_add_f32_e32 v66, v66, v66
	v_rcp_f32_e32 v64, v64
	v_add_f32_e32 v65, 1.0, v65
	v_mul_f32_e32 v66, 0xbfb8aa3b, v66
	v_rcp_f32_e32 v65, v65
	v_exp_f32_e32 v66, v66
	v_mul_f32_e32 v64, v67, v64
	v_cvt_pk_bf16_f32 v61, v61, v64
	v_mul_f32_e32 v62, v62, v65
	v_add_f32_e32 v64, 1.0, v66
	v_mul_f32_e32 v65, 0x3d372713, v70
	v_mul_f32_e32 v66, 0x3d372713, v71
	v_mul_f32_e32 v65, v70, v65
	v_mul_f32_e32 v66, v71, v66
	v_fma_f32 v65, v70, v65, v70
	v_fma_f32 v66, v71, v66, v71
	v_mul_f32_e32 v65, 0x3f4c422a, v65
	v_mul_f32_e32 v66, 0x3f4c422a, v66
	v_add_f32_e32 v65, v65, v65
	v_add_f32_e32 v66, v66, v66
	v_mul_f32_e32 v65, 0xbfb8aa3b, v65
	v_mul_f32_e32 v66, 0xbfb8aa3b, v66
	v_exp_f32_e32 v65, v65
	v_exp_f32_e32 v66, v66
	v_rcp_f32_e32 v64, v64
	v_add_f32_e32 v58, v58, v82
	v_add_f32_e32 v59, v59, v83
	v_add_f32_e32 v65, 1.0, v65
	v_add_f32_e32 v66, 1.0, v66
	v_rcp_f32_e32 v65, v65
	v_rcp_f32_e32 v66, v66
	v_mul_f32_e32 v63, v63, v64
	v_cvt_pk_bf16_f32 v62, v62, v63
	v_mul_f32_e32 v63, v70, v65
	v_mul_f32_e32 v64, v71, v66
	v_cvt_pk_bf16_f32 v63, v63, v64
	v_add_co_u32_e32 v64, vcc, s43, v148
	v_lshl_add_u64 v[68:69], v[148:149], 0, s[12:13]
	s_nop 0
	v_addc_co_u32_e32 v65, vcc, 0, v149, vcc
	global_store_dwordx4 v[64:65], v[60:63], off
	v_add_f32_e32 v48, v48, v96
	v_add_f32_e32 v49, v49, v97
	v_add_f32_e32 v50, v50, v98
	v_add_f32_e32 v51, v51, v99
	v_add_f32_e32 v60, v54, v78
	v_add_f32_e32 v61, v55, v79
	v_mul_f32_e32 v54, 0x3d372713, v56
	v_mul_f32_e32 v54, v56, v54
	v_fma_f32 v54, v56, v54, v56
	v_mul_f32_e32 v54, 0x3f4c422a, v54
	v_add_f32_e32 v54, v54, v54
	v_mul_f32_e32 v54, 0xbfb8aa3b, v54
	v_exp_f32_e32 v62, v54
	v_mul_f32_e32 v54, 0x3d372713, v57
	v_mul_f32_e32 v54, v57, v54
	v_fma_f32 v54, v57, v54, v57
	v_mul_f32_e32 v54, 0x3f4c422a, v54
	v_add_f32_e32 v54, v54, v54
	v_mul_f32_e32 v54, 0xbfb8aa3b, v54
	v_exp_f32_e32 v63, v54
	v_add_f32_e32 v54, v52, v76
	v_add_f32_e32 v55, v53, v77
	v_add_f32_e32 v52, 1.0, v62
	v_mul_f32_e32 v62, 0x3d372713, v58
	v_mul_f32_e32 v62, v58, v62
	v_fma_f32 v62, v58, v62, v58
	v_mul_f32_e32 v62, 0x3f4c422a, v62
	v_add_f32_e32 v53, 1.0, v63
	v_add_f32_e32 v62, v62, v62
	v_rcp_f32_e32 v52, v52
	v_rcp_f32_e32 v53, v53
	v_mul_f32_e32 v62, 0xbfb8aa3b, v62
	v_exp_f32_e32 v62, v62
	v_mul_f32_e32 v52, v56, v52
	v_mul_f32_e32 v53, v57, v53
	v_mul_f32_e32 v56, 0x3d372713, v59
	v_mul_f32_e32 v57, 0x3d372713, v54
	v_cvt_pk_bf16_f32 v52, v52, v53
	v_add_f32_e32 v53, 1.0, v62
	v_mul_f32_e32 v56, v59, v56
	v_mul_f32_e32 v57, v54, v57
	v_rcp_f32_e32 v53, v53
	v_fma_f32 v56, v59, v56, v59
	v_fma_f32 v57, v54, v57, v54
	v_mul_f32_e32 v56, 0x3f4c422a, v56
	v_mul_f32_e32 v57, 0x3f4c422a, v57
	v_add_f32_e32 v56, v56, v56
	v_add_f32_e32 v57, v57, v57
	v_mul_f32_e32 v56, 0xbfb8aa3b, v56
	v_mul_f32_e32 v57, 0xbfb8aa3b, v57
	v_exp_f32_e32 v56, v56
	v_exp_f32_e32 v57, v57
	v_mul_f32_e32 v53, v58, v53
	v_mul_f32_e32 v58, 0x3d372713, v55
	v_mul_f32_e32 v58, v55, v58
	v_fma_f32 v58, v55, v58, v55
	v_mul_f32_e32 v58, 0x3f4c422a, v58
	v_add_f32_e32 v56, 1.0, v56
	v_add_f32_e32 v57, 1.0, v57
	v_add_f32_e32 v58, v58, v58
	v_rcp_f32_e32 v56, v56
	v_rcp_f32_e32 v57, v57
	v_mul_f32_e32 v58, 0xbfb8aa3b, v58
	v_exp_f32_e32 v58, v58
	v_mul_f32_e32 v56, v59, v56
	v_mul_f32_e32 v54, v54, v57
	v_mul_f32_e32 v57, 0x3d372713, v60
	v_cvt_pk_bf16_f32 v53, v53, v56
	v_add_f32_e32 v56, 1.0, v58
	v_mul_f32_e32 v57, v60, v57
	v_mul_f32_e32 v58, 0x3d372713, v61
	v_fma_f32 v57, v60, v57, v60
	v_mul_f32_e32 v58, v61, v58
	v_mul_f32_e32 v57, 0x3f4c422a, v57
	v_fma_f32 v58, v61, v58, v61
	v_add_f32_e32 v57, v57, v57
	v_mul_f32_e32 v58, 0x3f4c422a, v58
	v_mul_f32_e32 v57, 0xbfb8aa3b, v57
	v_add_f32_e32 v58, v58, v58
	v_exp_f32_e32 v57, v57
	v_mul_f32_e32 v58, 0xbfb8aa3b, v58
	v_exp_f32_e32 v58, v58
	v_rcp_f32_e32 v56, v56
	v_add_f32_e32 v57, 1.0, v57
	v_rcp_f32_e32 v57, v57
	v_add_f32_e32 v58, 1.0, v58
	v_rcp_f32_e32 v58, v58
	v_mul_f32_e32 v55, v55, v56
	v_cvt_pk_bf16_f32 v54, v54, v55
	v_mul_f32_e32 v55, v60, v57
	v_mul_f32_e32 v56, v61, v58
	v_cvt_pk_bf16_f32 v55, v55, v56
	global_store_dwordx4 v[68:69], v[52:55], off offset:256
	v_add_f32_e32 v40, v40, v80
	v_add_f32_e32 v41, v41, v81
	v_add_f32_e32 v42, v42, v82
	v_add_f32_e32 v43, v43, v83
	v_add_f32_e32 v54, v46, v94
	v_add_f32_e32 v55, v47, v95
	v_mul_f32_e32 v46, 0x3d372713, v48
	v_mul_f32_e32 v46, v48, v46
	v_fma_f32 v46, v48, v46, v48
	v_mul_f32_e32 v46, 0x3f4c422a, v46
	v_add_f32_e32 v46, v46, v46
	v_mul_f32_e32 v46, 0xbfb8aa3b, v46
	v_exp_f32_e32 v56, v46
	v_mul_f32_e32 v46, 0x3d372713, v49
	v_mul_f32_e32 v46, v49, v46
	v_fma_f32 v46, v49, v46, v49
	v_mul_f32_e32 v46, 0x3f4c422a, v46
	v_add_f32_e32 v46, v46, v46
	v_mul_f32_e32 v46, 0xbfb8aa3b, v46
	v_exp_f32_e32 v57, v46
	v_add_f32_e32 v46, v44, v92
	v_add_f32_e32 v47, v45, v93
	v_add_f32_e32 v44, 1.0, v56
	v_mul_f32_e32 v56, 0x3d372713, v50
	v_mul_f32_e32 v56, v50, v56
	v_fma_f32 v56, v50, v56, v50
	v_mul_f32_e32 v56, 0x3f4c422a, v56
	v_add_f32_e32 v45, 1.0, v57
	v_add_f32_e32 v56, v56, v56
	v_rcp_f32_e32 v44, v44
	v_rcp_f32_e32 v45, v45
	v_mul_f32_e32 v56, 0xbfb8aa3b, v56
	v_exp_f32_e32 v56, v56
	v_mul_f32_e32 v44, v48, v44
	v_mul_f32_e32 v45, v49, v45
	v_mul_f32_e32 v48, 0x3d372713, v51
	v_cvt_pk_bf16_f32 v44, v44, v45
	v_add_f32_e32 v45, 1.0, v56
	v_mul_f32_e32 v48, v51, v48
	v_mul_f32_e32 v49, 0x3d372713, v46
	v_rcp_f32_e32 v45, v45
	v_fma_f32 v48, v51, v48, v51
	v_mul_f32_e32 v49, v46, v49
	v_mul_f32_e32 v48, 0x3f4c422a, v48
	v_fma_f32 v49, v46, v49, v46
	v_add_f32_e32 v48, v48, v48
	v_mul_f32_e32 v49, 0x3f4c422a, v49
	v_mul_f32_e32 v48, 0xbfb8aa3b, v48
	v_add_f32_e32 v49, v49, v49
	v_exp_f32_e32 v48, v48
	v_mul_f32_e32 v49, 0xbfb8aa3b, v49
	v_mul_f32_e32 v45, v50, v45
	v_mul_f32_e32 v50, 0x3d372713, v47
	v_exp_f32_e32 v49, v49
	v_mul_f32_e32 v50, v47, v50
	v_fma_f32 v50, v47, v50, v47
	v_mul_f32_e32 v50, 0x3f4c422a, v50
	v_add_f32_e32 v48, 1.0, v48
	v_add_f32_e32 v50, v50, v50
	v_rcp_f32_e32 v48, v48
	v_add_f32_e32 v49, 1.0, v49
	v_mul_f32_e32 v50, 0xbfb8aa3b, v50
	v_rcp_f32_e32 v49, v49
	v_exp_f32_e32 v50, v50
	v_mul_f32_e32 v48, v51, v48
	v_cvt_pk_bf16_f32 v45, v45, v48
	v_mul_f32_e32 v46, v46, v49
	v_add_f32_e32 v48, 1.0, v50
	v_mul_f32_e32 v49, 0x3d372713, v54
	v_mul_f32_e32 v50, 0x3d372713, v55
	v_mul_f32_e32 v49, v54, v49
	v_mul_f32_e32 v50, v55, v50
	v_fma_f32 v49, v54, v49, v54
	v_fma_f32 v50, v55, v50, v55
	v_mul_f32_e32 v49, 0x3f4c422a, v49
	v_mul_f32_e32 v50, 0x3f4c422a, v50
	v_add_f32_e32 v49, v49, v49
	v_add_f32_e32 v50, v50, v50
	v_mul_f32_e32 v49, 0xbfb8aa3b, v49
	v_mul_f32_e32 v50, 0xbfb8aa3b, v50
	v_exp_f32_e32 v49, v49
	v_exp_f32_e32 v50, v50
	v_rcp_f32_e32 v48, v48
	v_lshl_add_u64 v[52:53], v[148:149], 0, s[14:15]
	v_add_f32_e32 v49, 1.0, v49
	v_add_f32_e32 v50, 1.0, v50
	v_rcp_f32_e32 v49, v49
	v_rcp_f32_e32 v50, v50
	v_mul_f32_e32 v47, v47, v48
	v_cvt_pk_bf16_f32 v46, v46, v47
	v_mul_f32_e32 v47, v54, v49
	v_mul_f32_e32 v48, v55, v50
	v_cvt_pk_bf16_f32 v47, v47, v48
	v_add_co_u32_e32 v48, vcc, s44, v148
	v_add_f32_e32 v32, v32, v96
	v_add_f32_e32 v33, v33, v97
	s_nop 0
	v_addc_co_u32_e32 v49, vcc, 0, v149, vcc
	global_store_dwordx4 v[48:49], v[44:47], off
	v_add_f32_e32 v34, v34, v98
	v_add_f32_e32 v35, v35, v99
	v_add_f32_e32 v24, v24, v80
	v_add_f32_e32 v25, v25, v81
	v_add_f32_e32 v44, v38, v78
	v_add_f32_e32 v45, v39, v79
	v_mul_f32_e32 v38, 0x3d372713, v40
	v_mul_f32_e32 v38, v40, v38
	v_fma_f32 v38, v40, v38, v40
	v_mul_f32_e32 v38, 0x3f4c422a, v38
	v_add_f32_e32 v38, v38, v38
	v_mul_f32_e32 v38, 0xbfb8aa3b, v38
	v_exp_f32_e32 v46, v38
	v_mul_f32_e32 v38, 0x3d372713, v41
	v_mul_f32_e32 v38, v41, v38
	v_fma_f32 v38, v41, v38, v41
	v_mul_f32_e32 v38, 0x3f4c422a, v38
	v_add_f32_e32 v38, v38, v38
	v_mul_f32_e32 v38, 0xbfb8aa3b, v38
	v_exp_f32_e32 v47, v38
	v_add_f32_e32 v38, v36, v76
	v_add_f32_e32 v39, v37, v77
	v_add_f32_e32 v36, 1.0, v46
	v_mul_f32_e32 v46, 0x3d372713, v42
	v_mul_f32_e32 v46, v42, v46
	v_fma_f32 v46, v42, v46, v42
	v_mul_f32_e32 v46, 0x3f4c422a, v46
	v_add_f32_e32 v37, 1.0, v47
	v_add_f32_e32 v46, v46, v46
	v_rcp_f32_e32 v36, v36
	v_rcp_f32_e32 v37, v37
	v_mul_f32_e32 v46, 0xbfb8aa3b, v46
	v_exp_f32_e32 v46, v46
	v_mul_f32_e32 v36, v40, v36
	v_mul_f32_e32 v37, v41, v37
	v_mul_f32_e32 v40, 0x3d372713, v43
	v_mul_f32_e32 v41, 0x3d372713, v38
	v_cvt_pk_bf16_f32 v36, v36, v37
	v_add_f32_e32 v37, 1.0, v46
	v_mul_f32_e32 v40, v43, v40
	v_mul_f32_e32 v41, v38, v41
	v_rcp_f32_e32 v37, v37
	v_fma_f32 v40, v43, v40, v43
	v_fma_f32 v41, v38, v41, v38
	v_mul_f32_e32 v40, 0x3f4c422a, v40
	v_mul_f32_e32 v41, 0x3f4c422a, v41
	v_add_f32_e32 v40, v40, v40
	v_add_f32_e32 v41, v41, v41
	v_mul_f32_e32 v40, 0xbfb8aa3b, v40
	v_mul_f32_e32 v41, 0xbfb8aa3b, v41
	v_exp_f32_e32 v40, v40
	v_exp_f32_e32 v41, v41
	v_mul_f32_e32 v37, v42, v37
	v_mul_f32_e32 v42, 0x3d372713, v39
	v_mul_f32_e32 v42, v39, v42
	v_fma_f32 v42, v39, v42, v39
	v_mul_f32_e32 v42, 0x3f4c422a, v42
	v_add_f32_e32 v40, 1.0, v40
	v_add_f32_e32 v41, 1.0, v41
	v_add_f32_e32 v42, v42, v42
	v_rcp_f32_e32 v40, v40
	v_rcp_f32_e32 v41, v41
	v_mul_f32_e32 v42, 0xbfb8aa3b, v42
	v_exp_f32_e32 v42, v42
	v_mul_f32_e32 v40, v43, v40
	v_mul_f32_e32 v38, v38, v41
	v_mul_f32_e32 v41, 0x3d372713, v44
	v_cvt_pk_bf16_f32 v37, v37, v40
	v_add_f32_e32 v40, 1.0, v42
	v_mul_f32_e32 v41, v44, v41
	v_mul_f32_e32 v42, 0x3d372713, v45
	v_fma_f32 v41, v44, v41, v44
	v_mul_f32_e32 v42, v45, v42
	v_mul_f32_e32 v41, 0x3f4c422a, v41
	v_fma_f32 v42, v45, v42, v45
	v_add_f32_e32 v41, v41, v41
	v_mul_f32_e32 v42, 0x3f4c422a, v42
	v_mul_f32_e32 v41, 0xbfb8aa3b, v41
	v_add_f32_e32 v42, v42, v42
	v_exp_f32_e32 v41, v41
	v_mul_f32_e32 v42, 0xbfb8aa3b, v42
	v_exp_f32_e32 v42, v42
	v_rcp_f32_e32 v40, v40
	v_add_f32_e32 v41, 1.0, v41
	v_rcp_f32_e32 v41, v41
	v_add_f32_e32 v42, 1.0, v42
	v_rcp_f32_e32 v42, v42
	v_mul_f32_e32 v39, v39, v40
	v_cvt_pk_bf16_f32 v38, v38, v39
	v_mul_f32_e32 v39, v44, v41
	v_mul_f32_e32 v40, v45, v42
	v_cvt_pk_bf16_f32 v39, v39, v40
	global_store_dwordx4 v[52:53], v[36:39], off offset:256
	v_add_f32_e32 v26, v26, v82
	v_add_f32_e32 v27, v27, v83
	v_add_f32_e32 v16, v16, v96
	v_add_f32_e32 v17, v17, v97
	v_add_f32_e32 v38, v30, v94
	v_add_f32_e32 v39, v31, v95
	v_mul_f32_e32 v30, 0x3d372713, v32
	v_mul_f32_e32 v30, v32, v30
	v_fma_f32 v30, v32, v30, v32
	v_mul_f32_e32 v30, 0x3f4c422a, v30
	v_add_f32_e32 v30, v30, v30
	v_mul_f32_e32 v30, 0xbfb8aa3b, v30
	v_exp_f32_e32 v40, v30
	v_mul_f32_e32 v30, 0x3d372713, v33
	v_mul_f32_e32 v30, v33, v30
	v_fma_f32 v30, v33, v30, v33
	v_mul_f32_e32 v30, 0x3f4c422a, v30
	v_add_f32_e32 v30, v30, v30
	v_mul_f32_e32 v30, 0xbfb8aa3b, v30
	v_exp_f32_e32 v41, v30
	v_add_f32_e32 v30, v28, v92
	v_add_f32_e32 v31, v29, v93
	v_add_f32_e32 v28, 1.0, v40
	v_mul_f32_e32 v40, 0x3d372713, v34
	v_mul_f32_e32 v40, v34, v40
	v_fma_f32 v40, v34, v40, v34
	v_mul_f32_e32 v40, 0x3f4c422a, v40
	v_add_f32_e32 v29, 1.0, v41
	v_add_f32_e32 v40, v40, v40
	v_rcp_f32_e32 v28, v28
	v_rcp_f32_e32 v29, v29
	v_mul_f32_e32 v40, 0xbfb8aa3b, v40
	v_exp_f32_e32 v40, v40
	v_mul_f32_e32 v28, v32, v28
	v_mul_f32_e32 v29, v33, v29
	v_mul_f32_e32 v32, 0x3d372713, v35
	v_cvt_pk_bf16_f32 v28, v28, v29
	v_add_f32_e32 v29, 1.0, v40
	v_mul_f32_e32 v32, v35, v32
	v_mul_f32_e32 v33, 0x3d372713, v30
	v_rcp_f32_e32 v29, v29
	v_fma_f32 v32, v35, v32, v35
	v_mul_f32_e32 v33, v30, v33
	v_mul_f32_e32 v32, 0x3f4c422a, v32
	v_fma_f32 v33, v30, v33, v30
	v_add_f32_e32 v32, v32, v32
	v_mul_f32_e32 v33, 0x3f4c422a, v33
	v_mul_f32_e32 v32, 0xbfb8aa3b, v32
	v_add_f32_e32 v33, v33, v33
	v_exp_f32_e32 v32, v32
	v_mul_f32_e32 v33, 0xbfb8aa3b, v33
	v_mul_f32_e32 v29, v34, v29
	v_mul_f32_e32 v34, 0x3d372713, v31
	v_exp_f32_e32 v33, v33
	v_mul_f32_e32 v34, v31, v34
	v_fma_f32 v34, v31, v34, v31
	v_mul_f32_e32 v34, 0x3f4c422a, v34
	v_add_f32_e32 v32, 1.0, v32
	v_add_f32_e32 v34, v34, v34
	v_rcp_f32_e32 v32, v32
	v_add_f32_e32 v33, 1.0, v33
	v_mul_f32_e32 v34, 0xbfb8aa3b, v34
	v_rcp_f32_e32 v33, v33
	v_exp_f32_e32 v34, v34
	v_mul_f32_e32 v32, v35, v32
	v_cvt_pk_bf16_f32 v29, v29, v32
	v_mul_f32_e32 v30, v30, v33
	v_add_f32_e32 v32, 1.0, v34
	v_mul_f32_e32 v33, 0x3d372713, v38
	v_mul_f32_e32 v34, 0x3d372713, v39
	v_mul_f32_e32 v33, v38, v33
	v_mul_f32_e32 v34, v39, v34
	v_fma_f32 v33, v38, v33, v38
	v_fma_f32 v34, v39, v34, v39
	v_mul_f32_e32 v33, 0x3f4c422a, v33
	v_mul_f32_e32 v34, 0x3f4c422a, v34
	v_add_f32_e32 v33, v33, v33
	v_add_f32_e32 v34, v34, v34
	v_mul_f32_e32 v33, 0xbfb8aa3b, v33
	v_mul_f32_e32 v34, 0xbfb8aa3b, v34
	v_exp_f32_e32 v33, v33
	v_exp_f32_e32 v34, v34
	v_rcp_f32_e32 v32, v32
	v_lshl_add_u64 v[36:37], v[148:149], 0, s[16:17]
	v_add_f32_e32 v33, 1.0, v33
	v_add_f32_e32 v34, 1.0, v34
	v_rcp_f32_e32 v33, v33
	v_rcp_f32_e32 v34, v34
	v_mul_f32_e32 v31, v31, v32
	v_cvt_pk_bf16_f32 v30, v30, v31
	v_mul_f32_e32 v31, v38, v33
	v_mul_f32_e32 v32, v39, v34
	v_cvt_pk_bf16_f32 v31, v31, v32
	v_add_co_u32_e32 v32, vcc, s45, v148
	v_add_f32_e32 v18, v18, v98
	v_add_f32_e32 v19, v19, v99
	s_nop 0
	v_addc_co_u32_e32 v33, vcc, 0, v149, vcc
	global_store_dwordx4 v[32:33], v[28:31], off
	v_add_f32_e32 v8, v8, v80
	v_add_f32_e32 v9, v9, v81
	v_add_f32_e32 v10, v10, v82
	v_add_f32_e32 v11, v11, v83
	v_add_f32_e32 v28, v22, v78
	v_add_f32_e32 v29, v23, v79
	v_mul_f32_e32 v22, 0x3d372713, v24
	v_mul_f32_e32 v22, v24, v22
	v_fma_f32 v22, v24, v22, v24
	v_mul_f32_e32 v22, 0x3f4c422a, v22
	v_add_f32_e32 v22, v22, v22
	v_mul_f32_e32 v22, 0xbfb8aa3b, v22
	v_exp_f32_e32 v30, v22
	v_mul_f32_e32 v22, 0x3d372713, v25
	v_mul_f32_e32 v22, v25, v22
	v_fma_f32 v22, v25, v22, v25
	v_mul_f32_e32 v22, 0x3f4c422a, v22
	v_add_f32_e32 v22, v22, v22
	v_mul_f32_e32 v22, 0xbfb8aa3b, v22
	v_exp_f32_e32 v31, v22
	v_add_f32_e32 v22, v20, v76
	v_add_f32_e32 v23, v21, v77
	v_add_f32_e32 v20, 1.0, v30
	v_mul_f32_e32 v30, 0x3d372713, v26
	v_mul_f32_e32 v30, v26, v30
	v_fma_f32 v30, v26, v30, v26
	v_mul_f32_e32 v30, 0x3f4c422a, v30
	v_add_f32_e32 v21, 1.0, v31
	v_add_f32_e32 v30, v30, v30
	v_rcp_f32_e32 v20, v20
	v_rcp_f32_e32 v21, v21
	v_mul_f32_e32 v30, 0xbfb8aa3b, v30
	v_exp_f32_e32 v30, v30
	v_mul_f32_e32 v20, v24, v20
	v_mul_f32_e32 v21, v25, v21
	v_mul_f32_e32 v24, 0x3d372713, v27
	v_mul_f32_e32 v25, 0x3d372713, v22
	v_cvt_pk_bf16_f32 v20, v20, v21
	v_add_f32_e32 v21, 1.0, v30
	v_mul_f32_e32 v24, v27, v24
	v_mul_f32_e32 v25, v22, v25
	v_rcp_f32_e32 v21, v21
	v_fma_f32 v24, v27, v24, v27
	v_fma_f32 v25, v22, v25, v22
	v_mul_f32_e32 v24, 0x3f4c422a, v24
	v_mul_f32_e32 v25, 0x3f4c422a, v25
	v_add_f32_e32 v24, v24, v24
	v_add_f32_e32 v25, v25, v25
	v_mul_f32_e32 v24, 0xbfb8aa3b, v24
	v_mul_f32_e32 v25, 0xbfb8aa3b, v25
	v_exp_f32_e32 v24, v24
	v_exp_f32_e32 v25, v25
	v_mul_f32_e32 v21, v26, v21
	v_mul_f32_e32 v26, 0x3d372713, v23
	v_mul_f32_e32 v26, v23, v26
	v_fma_f32 v26, v23, v26, v23
	v_mul_f32_e32 v26, 0x3f4c422a, v26
	v_add_f32_e32 v24, 1.0, v24
	v_add_f32_e32 v25, 1.0, v25
	v_add_f32_e32 v26, v26, v26
	v_rcp_f32_e32 v24, v24
	v_rcp_f32_e32 v25, v25
	v_mul_f32_e32 v26, 0xbfb8aa3b, v26
	v_exp_f32_e32 v26, v26
	v_mul_f32_e32 v24, v27, v24
	v_mul_f32_e32 v22, v22, v25
	v_mul_f32_e32 v25, 0x3d372713, v28
	v_cvt_pk_bf16_f32 v21, v21, v24
	v_add_f32_e32 v24, 1.0, v26
	v_mul_f32_e32 v25, v28, v25
	v_mul_f32_e32 v26, 0x3d372713, v29
	v_fma_f32 v25, v28, v25, v28
	v_mul_f32_e32 v26, v29, v26
	v_mul_f32_e32 v25, 0x3f4c422a, v25
	v_fma_f32 v26, v29, v26, v29
	v_add_f32_e32 v25, v25, v25
	v_mul_f32_e32 v26, 0x3f4c422a, v26
	v_mul_f32_e32 v25, 0xbfb8aa3b, v25
	v_add_f32_e32 v26, v26, v26
	v_exp_f32_e32 v25, v25
	v_mul_f32_e32 v26, 0xbfb8aa3b, v26
	v_exp_f32_e32 v26, v26
	v_rcp_f32_e32 v24, v24
	v_add_f32_e32 v25, 1.0, v25
	v_rcp_f32_e32 v25, v25
	v_add_f32_e32 v26, 1.0, v26
	v_rcp_f32_e32 v26, v26
	v_mul_f32_e32 v23, v23, v24
	v_cvt_pk_bf16_f32 v22, v22, v23
	v_mul_f32_e32 v23, v28, v25
	v_mul_f32_e32 v24, v29, v26
	v_cvt_pk_bf16_f32 v23, v23, v24
	global_store_dwordx4 v[36:37], v[20:23], off offset:256
	s_nop 1
	v_add_f32_e32 v22, v14, v94
	v_add_f32_e32 v23, v15, v95
	v_mul_f32_e32 v14, 0x3d372713, v16
	v_mul_f32_e32 v14, v16, v14
	v_fma_f32 v14, v16, v14, v16
	v_mul_f32_e32 v14, 0x3f4c422a, v14
	v_add_f32_e32 v14, v14, v14
	v_mul_f32_e32 v14, 0xbfb8aa3b, v14
	v_exp_f32_e32 v24, v14
	v_mul_f32_e32 v14, 0x3d372713, v17
	v_mul_f32_e32 v14, v17, v14
	v_fma_f32 v14, v17, v14, v17
	v_mul_f32_e32 v14, 0x3f4c422a, v14
	v_add_f32_e32 v14, v14, v14
	v_mul_f32_e32 v14, 0xbfb8aa3b, v14
	v_exp_f32_e32 v25, v14
	v_add_f32_e32 v14, v12, v92
	v_add_f32_e32 v15, v13, v93
	v_add_f32_e32 v12, 1.0, v24
	v_mul_f32_e32 v24, 0x3d372713, v18
	v_mul_f32_e32 v24, v18, v24
	v_fma_f32 v24, v18, v24, v18
	v_mul_f32_e32 v24, 0x3f4c422a, v24
	v_add_f32_e32 v13, 1.0, v25
	v_add_f32_e32 v24, v24, v24
	v_rcp_f32_e32 v12, v12
	v_rcp_f32_e32 v13, v13
	v_mul_f32_e32 v24, 0xbfb8aa3b, v24
	v_exp_f32_e32 v24, v24
	v_mul_f32_e32 v12, v16, v12
	v_mul_f32_e32 v13, v17, v13
	v_mul_f32_e32 v16, 0x3d372713, v19
	v_cvt_pk_bf16_f32 v12, v12, v13
	v_add_f32_e32 v13, 1.0, v24
	v_mul_f32_e32 v16, v19, v16
	v_mul_f32_e32 v17, 0x3d372713, v14
	v_rcp_f32_e32 v13, v13
	v_fma_f32 v16, v19, v16, v19
	v_mul_f32_e32 v17, v14, v17
	v_mul_f32_e32 v16, 0x3f4c422a, v16
	v_fma_f32 v17, v14, v17, v14
	v_add_f32_e32 v16, v16, v16
	v_mul_f32_e32 v17, 0x3f4c422a, v17
	v_mul_f32_e32 v16, 0xbfb8aa3b, v16
	v_add_f32_e32 v17, v17, v17
	v_exp_f32_e32 v16, v16
	v_mul_f32_e32 v17, 0xbfb8aa3b, v17
	v_mul_f32_e32 v13, v18, v13
	v_mul_f32_e32 v18, 0x3d372713, v15
	v_exp_f32_e32 v17, v17
	v_mul_f32_e32 v18, v15, v18
	v_fma_f32 v18, v15, v18, v15
	v_mul_f32_e32 v18, 0x3f4c422a, v18
	v_add_f32_e32 v16, 1.0, v16
	v_add_f32_e32 v18, v18, v18
	v_rcp_f32_e32 v16, v16
	v_add_f32_e32 v17, 1.0, v17
	v_mul_f32_e32 v18, 0xbfb8aa3b, v18
	v_rcp_f32_e32 v17, v17
	v_exp_f32_e32 v18, v18
	v_mul_f32_e32 v16, v19, v16
	v_cvt_pk_bf16_f32 v13, v13, v16
	v_mul_f32_e32 v14, v14, v17
	v_add_f32_e32 v16, 1.0, v18
	v_mul_f32_e32 v17, 0x3d372713, v22
	v_mul_f32_e32 v18, 0x3d372713, v23
	v_mul_f32_e32 v17, v22, v17
	v_mul_f32_e32 v18, v23, v18
	v_fma_f32 v17, v22, v17, v22
	v_fma_f32 v18, v23, v18, v23
	v_mul_f32_e32 v17, 0x3f4c422a, v17
	v_mul_f32_e32 v18, 0x3f4c422a, v18
	v_add_f32_e32 v17, v17, v17
	v_add_f32_e32 v18, v18, v18
	v_mul_f32_e32 v17, 0xbfb8aa3b, v17
	v_mul_f32_e32 v18, 0xbfb8aa3b, v18
	v_exp_f32_e32 v17, v17
	v_exp_f32_e32 v18, v18
	v_rcp_f32_e32 v16, v16
	v_lshl_add_u64 v[20:21], v[148:149], 0, s[18:19]
	v_add_f32_e32 v17, 1.0, v17
	v_add_f32_e32 v18, 1.0, v18
	v_rcp_f32_e32 v17, v17
	v_rcp_f32_e32 v18, v18
	v_mul_f32_e32 v15, v15, v16
	v_cvt_pk_bf16_f32 v14, v14, v15
	v_mul_f32_e32 v15, v22, v17
	v_mul_f32_e32 v16, v23, v18
	v_cvt_pk_bf16_f32 v15, v15, v16
	v_add_co_u32_e32 v16, vcc, s47, v148
	s_nop 1
	v_addc_co_u32_e32 v17, vcc, 0, v149, vcc
	global_store_dwordx4 v[16:17], v[12:15], off
	s_andn2_b64 vcc, exec, s[4:5]
	s_mov_b64 s[4:5], -1
	v_add_f32_e32 v12, v6, v78
	v_add_f32_e32 v13, v7, v79
	v_mul_f32_e32 v6, 0x3d372713, v8
	v_mul_f32_e32 v6, v8, v6
	v_fma_f32 v6, v8, v6, v8
	v_mul_f32_e32 v6, 0x3f4c422a, v6
	v_add_f32_e32 v6, v6, v6
	v_mul_f32_e32 v6, 0xbfb8aa3b, v6
	v_exp_f32_e32 v14, v6
	v_mul_f32_e32 v6, 0x3d372713, v9
	v_mul_f32_e32 v6, v9, v6
	v_fma_f32 v6, v9, v6, v9
	v_mul_f32_e32 v6, 0x3f4c422a, v6
	v_add_f32_e32 v6, v6, v6
	v_mul_f32_e32 v6, 0xbfb8aa3b, v6
	v_exp_f32_e32 v15, v6
	v_add_f32_e32 v6, v4, v76
	v_add_f32_e32 v7, v5, v77
	v_add_f32_e32 v4, 1.0, v14
	v_mul_f32_e32 v14, 0x3d372713, v10
	v_mul_f32_e32 v14, v10, v14
	v_fma_f32 v14, v10, v14, v10
	v_mul_f32_e32 v14, 0x3f4c422a, v14
	v_add_f32_e32 v5, 1.0, v15
	v_add_f32_e32 v14, v14, v14
	v_rcp_f32_e32 v4, v4
	v_rcp_f32_e32 v5, v5
	v_mul_f32_e32 v14, 0xbfb8aa3b, v14
	v_exp_f32_e32 v14, v14
	v_mul_f32_e32 v4, v8, v4
	v_mul_f32_e32 v5, v9, v5
	v_mul_f32_e32 v8, 0x3d372713, v11
	v_mul_f32_e32 v9, 0x3d372713, v6
	v_cvt_pk_bf16_f32 v4, v4, v5
	v_add_f32_e32 v5, 1.0, v14
	v_mul_f32_e32 v8, v11, v8
	v_mul_f32_e32 v9, v6, v9
	v_rcp_f32_e32 v5, v5
	v_fma_f32 v8, v11, v8, v11
	v_fma_f32 v9, v6, v9, v6
	v_mul_f32_e32 v8, 0x3f4c422a, v8
	v_mul_f32_e32 v9, 0x3f4c422a, v9
	v_add_f32_e32 v8, v8, v8
	v_add_f32_e32 v9, v9, v9
	v_mul_f32_e32 v8, 0xbfb8aa3b, v8
	v_mul_f32_e32 v9, 0xbfb8aa3b, v9
	v_exp_f32_e32 v8, v8
	v_exp_f32_e32 v9, v9
	v_mul_f32_e32 v5, v10, v5
	v_mul_f32_e32 v10, 0x3d372713, v7
	v_mul_f32_e32 v10, v7, v10
	v_fma_f32 v10, v7, v10, v7
	v_mul_f32_e32 v10, 0x3f4c422a, v10
	v_add_f32_e32 v8, 1.0, v8
	v_add_f32_e32 v9, 1.0, v9
	v_add_f32_e32 v10, v10, v10
	v_rcp_f32_e32 v8, v8
	v_rcp_f32_e32 v9, v9
	v_mul_f32_e32 v10, 0xbfb8aa3b, v10
	v_exp_f32_e32 v10, v10
	v_mul_f32_e32 v8, v11, v8
	v_mul_f32_e32 v6, v6, v9
	v_mul_f32_e32 v9, 0x3d372713, v12
	v_cvt_pk_bf16_f32 v5, v5, v8
	v_add_f32_e32 v8, 1.0, v10
	v_mul_f32_e32 v9, v12, v9
	v_mul_f32_e32 v10, 0x3d372713, v13
	v_fma_f32 v9, v12, v9, v12
	v_mul_f32_e32 v10, v13, v10
	v_mul_f32_e32 v9, 0x3f4c422a, v9
	v_fma_f32 v10, v13, v10, v13
	v_add_f32_e32 v9, v9, v9
	v_mul_f32_e32 v10, 0x3f4c422a, v10
	v_mul_f32_e32 v9, 0xbfb8aa3b, v9
	v_add_f32_e32 v10, v10, v10
	v_exp_f32_e32 v9, v9
	v_mul_f32_e32 v10, 0xbfb8aa3b, v10
	v_exp_f32_e32 v10, v10
	v_rcp_f32_e32 v8, v8
	v_add_f32_e32 v9, 1.0, v9
	v_rcp_f32_e32 v9, v9
	v_add_f32_e32 v10, 1.0, v10
	v_rcp_f32_e32 v10, v10
	v_mul_f32_e32 v7, v7, v8
	v_cvt_pk_bf16_f32 v6, v6, v7
	v_mul_f32_e32 v7, v12, v9
	v_mul_f32_e32 v8, v13, v10
	v_cvt_pk_bf16_f32 v7, v7, v8
	global_store_dwordx4 v[20:21], v[4:7], off offset:256
	s_cbranch_vccnz .LBB0_1410
	s_andn2_b64 vcc, exec, s[0:1]
	s_cbranch_vccnz .LBB0_1409
	s_barrier
	s_branch .LBB0_1409

.LBB0_1452:
	s_lshl_b32 s8, s0, 6
	s_add_i32 s8, s8, 0xffff0000
	v_add_u32_e32 v32, s8, v192
	v_mad_i64_i32 v[0:1], s[38:39], v32, s37, v[118:119]
	global_load_dwordx4 v[8:11], v[0:1], off
	global_load_dwordx4 v[12:15], v[0:1], off offset:128
	v_lshlrev_b32_e32 v0, 8, v32
	v_and_b32_e32 v116, 0xfff00, v0
	v_lshl_add_u64 v[0:1], v[120:121], 0, v[116:117]
	v_lshl_add_u64 v[2:3], v[122:123], 0, v[116:117]
	global_load_dwordx4 v[16:19], v[0:1], off
	global_load_dwordx4 v[20:23], v[2:3], off
	global_load_dwordx4 v[24:27], v[0:1], off offset:16
	global_load_dwordx4 v[28:31], v[2:3], off offset:16
	v_add_u32_e32 v48, s8, v193
	v_ashrrev_i32_e32 v33, 31, v32
	v_lshlrev_b32_e32 v34, 8, v48
	v_lshlrev_b64 v[32:33], 10, v[32:33]
	v_and_b32_e32 v116, 0xfff00, v34
	v_mad_i64_i32 v[0:1], s[38:39], v48, s37, v[118:119]
	v_lshl_add_u64 v[50:51], v[126:127], 0, v[32:33]
	v_lshl_add_u64 v[32:33], v[124:125], 0, v[32:33]
	v_lshl_add_u64 v[36:37], v[120:121], 0, v[116:117]
	v_lshl_add_u64 v[44:45], v[122:123], 0, v[116:117]
	global_load_dwordx4 v[4:7], v[0:1], off
	s_nop 0
	global_load_dwordx4 v[0:3], v[0:1], off offset:128
	v_lshl_add_u64 v[52:53], v[32:33], 0, s[22:23]
	global_load_dwordx4 v[32:35], v[36:37], off offset:16
	s_nop 0
	global_load_dwordx4 v[36:39], v[36:37], off
	s_nop 0
	global_load_dwordx4 v[40:43], v[44:45], off offset:16
	s_nop 0
	global_load_dwordx4 v[44:47], v[44:45], off
	v_cndmask_b32_e64 v51, v53, v51, s[6:7]
	v_cndmask_b32_e64 v50, v52, v50, s[6:7]
	v_mov_b32_e32 v133, v117
	v_ashrrev_i32_e32 v49, 31, v48
	v_lshlrev_b64 v[48:49], 10, v[48:49]
	s_waitcnt vmcnt(11)
	v_lshlrev_b32_e32 v57, 16, v11
	v_lshlrev_b32_e32 v56, 16, v10
	s_waitcnt vmcnt(10)
	v_lshlrev_b32_e32 v59, 16, v15
	v_lshlrev_b32_e32 v58, 16, v14
	v_and_b32_e32 v11, 0xffff0000, v11
	v_and_b32_e32 v10, 0xffff0000, v10
	v_and_b32_e32 v15, 0xffff0000, v15
	v_and_b32_e32 v14, 0xffff0000, v14
	s_waitcnt vmcnt(8)
	v_mov_b32_e32 v63, v22
	v_mov_b32_e32 v22, v21
	s_waitcnt vmcnt(6)
	v_mov_b32_e32 v21, v30
	v_mov_b32_e32 v30, v29
	v_lshlrev_b32_e32 v53, 16, v9
	v_lshlrev_b32_e32 v52, 16, v8
	v_lshlrev_b32_e32 v55, 16, v13
	v_lshlrev_b32_e32 v54, 16, v12
	v_and_b32_e32 v9, 0xffff0000, v9
	v_and_b32_e32 v8, 0xffff0000, v8
	v_and_b32_e32 v13, 0xffff0000, v13
	v_and_b32_e32 v12, 0xffff0000, v12
	v_mov_b32_e32 v61, v18
	v_mov_b32_e32 v62, v20
	v_mov_b32_e32 v18, v17
	v_mov_b32_e32 v17, v26
	v_mov_b32_e32 v20, v28
	v_mov_b32_e32 v26, v25
	v_mul_f32_e32 v66, v30, v10
	v_mul_f32_e32 v67, v31, v11
	v_mul_f32_e32 v30, v30, v14
	v_mul_f32_e32 v31, v31, v15
	v_mov_b32_e32 v60, v16
	v_mov_b32_e32 v16, v24
	v_mul_f32_e32 v28, v22, v8
	v_mul_f32_e32 v29, v23, v9
	v_mul_f32_e32 v22, v22, v12
	v_mul_f32_e32 v23, v23, v13
	v_mul_f32_e32 v64, v20, v56
	v_mul_f32_e32 v65, v21, v57
	v_mul_f32_e32 v20, v20, v58
	v_mul_f32_e32 v21, v21, v59
	v_fma_f32 v10, v26, v10, -v30
	v_fma_f32 v11, v27, v11, -v31
	v_mul_f32_e32 v24, v62, v52
	v_mul_f32_e32 v25, v63, v53
	v_mul_f32_e32 v62, v62, v54
	v_mul_f32_e32 v63, v63, v55
	v_fma_f32 v12, v18, v12, v28
	v_fma_f32 v13, v19, v13, v29
	v_fma_f32 v8, v18, v8, -v22
	v_fma_f32 v9, v19, v9, -v23
	v_fma_f32 v18, v16, v58, v64
	v_fma_f32 v19, v17, v59, v65
	v_fma_f32 v16, v16, v56, -v20
	v_fma_f32 v17, v17, v57, -v21
	v_bfe_u32 v20, v11, 16, 1
	v_fma_f32 v28, v60, v52, -v62
	v_fma_f32 v29, v61, v53, -v63
	v_bfe_u32 v30, v16, 16, 1
	v_add3_u32 v11, v11, v20, s42
	v_bfe_u32 v20, v17, 16, 1
	v_fma_f32 v14, v26, v14, v66
	v_fma_f32 v15, v27, v15, v67
	v_bfe_u32 v21, v10, 16, 1
	v_bfe_u32 v26, v28, 16, 1
	v_bfe_u32 v27, v29, 16, 1
	v_add3_u32 v17, v17, v20, s42
	v_add3_u32 v16, v16, v30, s42
	v_bfe_u32 v22, v9, 16, 1
	v_bfe_u32 v23, v8, 16, 1
	v_add3_u32 v10, v10, v21, s42
	v_add3_u32 v20, v29, v27, s42
	v_add3_u32 v21, v28, v26, s42
	v_lshrrev_b32_e32 v16, 16, v16
	v_lshrrev_b32_e32 v17, 16, v17
	v_fma_f32 v24, v60, v54, v24
	v_fma_f32 v25, v61, v55, v25
	v_add3_u32 v8, v8, v23, s42
	v_add3_u32 v9, v9, v22, s42
	v_lshrrev_b32_e32 v21, 16, v21
	v_lshrrev_b32_e32 v20, 16, v20
	v_and_or_b32 v11, v11, s35, v17
	v_and_or_b32 v10, v10, s35, v16
	v_bfe_u32 v16, v15, 16, 1
	v_bfe_u32 v17, v14, 16, 1
	v_and_or_b32 v9, v9, s35, v20
	v_and_or_b32 v8, v8, s35, v21
	v_bfe_u32 v20, v13, 16, 1
	v_bfe_u32 v21, v12, 16, 1
	v_add3_u32 v14, v14, v17, s42
	v_add3_u32 v15, v15, v16, s42
	v_bfe_u32 v16, v24, 16, 1
	v_bfe_u32 v17, v25, 16, 1
	v_add3_u32 v12, v12, v21, s42
	v_add3_u32 v13, v13, v20, s42
	v_bfe_u32 v20, v18, 16, 1
	v_bfe_u32 v21, v19, 16, 1
	v_add3_u32 v17, v25, v17, s42
	v_add3_u32 v16, v24, v16, s42
	v_add3_u32 v19, v19, v21, s42
	v_add3_u32 v18, v18, v20, s42
	v_lshrrev_b32_e32 v16, 16, v16
	v_lshrrev_b32_e32 v17, 16, v17
	v_lshrrev_b32_e32 v18, 16, v18
	v_lshrrev_b32_e32 v19, 16, v19
	v_and_or_b32 v13, v13, s35, v17
	v_and_or_b32 v12, v12, s35, v16
	v_lshl_add_u64 v[16:17], v[50:51], 0, v[132:133]
	v_add_u32_e32 v50, s8, v194
	v_and_or_b32 v15, v15, s35, v19
	v_and_or_b32 v14, v14, s35, v18
	global_store_dwordx4 v[16:17], v[8:11], off
	global_store_dwordx4 v[16:17], v[12:15], off offset:128
	v_lshlrev_b32_e32 v16, 8, v50
	v_and_b32_e32 v116, 0xfff00, v16
	v_lshl_add_u64 v[52:53], v[126:127], 0, v[48:49]
	v_lshl_add_u64 v[48:49], v[124:125], 0, v[48:49]
	v_mad_i64_i32 v[12:13], s[38:39], v50, s37, v[118:119]
	v_lshl_add_u64 v[20:21], v[120:121], 0, v[116:117]
	v_lshl_add_u64 v[28:29], v[122:123], 0, v[116:117]
	v_lshl_add_u64 v[48:49], v[48:49], 0, s[22:23]
	global_load_dwordx4 v[8:11], v[12:13], off
	s_nop 0
	global_load_dwordx4 v[12:15], v[12:13], off offset:128
	s_nop 0
	global_load_dwordx4 v[16:19], v[20:21], off offset:16
	s_nop 0
	global_load_dwordx4 v[20:23], v[20:21], off
	s_nop 0
	global_load_dwordx4 v[24:27], v[28:29], off offset:16
	s_nop 0
	global_load_dwordx4 v[28:31], v[28:29], off
	v_cndmask_b32_e64 v49, v49, v53, s[6:7]
	v_cndmask_b32_e64 v48, v48, v52, s[6:7]
	s_waitcnt vmcnt(13)
	v_lshlrev_b32_e32 v53, 16, v5
	v_lshlrev_b32_e32 v52, 16, v4
	v_and_b32_e32 v5, 0xffff0000, v5
	v_and_b32_e32 v4, 0xffff0000, v4
	s_waitcnt vmcnt(8)
	v_mov_b32_e32 v59, v46
	v_mov_b32_e32 v46, v45
	v_lshlrev_b32_e32 v55, 16, v1
	v_lshlrev_b32_e32 v54, 16, v0
	v_and_b32_e32 v1, 0xffff0000, v1
	v_and_b32_e32 v0, 0xffff0000, v0
	v_mov_b32_e32 v56, v36
	v_mov_b32_e32 v57, v38
	v_mov_b32_e32 v58, v44
	v_mov_b32_e32 v38, v37
	v_mul_f32_e32 v36, v46, v4
	v_mul_f32_e32 v37, v47, v5
	v_mul_f32_e32 v44, v58, v54
	v_mul_f32_e32 v45, v59, v55
	v_fma_f32 v36, v38, v0, v36
	v_fma_f32 v37, v39, v1, v37
	v_mul_f32_e32 v0, v46, v0
	v_mul_f32_e32 v1, v47, v1
	v_mul_f32_e32 v60, v58, v52
	v_mul_f32_e32 v61, v59, v53
	v_fma_f32 v44, v56, v52, -v44
	v_fma_f32 v45, v57, v53, -v45
	v_fma_f32 v0, v38, v4, -v0
	v_fma_f32 v1, v39, v5, -v1
	v_lshlrev_b32_e32 v5, 16, v7
	v_lshlrev_b32_e32 v4, 16, v6
	v_and_b32_e32 v7, 0xffff0000, v7
	v_and_b32_e32 v6, 0xffff0000, v6
	v_mov_b32_e32 v53, v42
	v_mov_b32_e32 v42, v41
	v_lshlrev_b32_e32 v39, 16, v3
	v_lshlrev_b32_e32 v38, 16, v2
	v_and_b32_e32 v3, 0xffff0000, v3
	v_and_b32_e32 v2, 0xffff0000, v2
	v_mov_b32_e32 v46, v32
	v_mov_b32_e32 v47, v34
	v_mov_b32_e32 v52, v40
	v_mov_b32_e32 v34, v33
	v_mul_f32_e32 v32, v42, v6
	v_mul_f32_e32 v33, v43, v7
	v_fma_f32 v60, v56, v54, v60
	v_fma_f32 v61, v57, v55, v61
	v_mul_f32_e32 v54, v52, v4
	v_mul_f32_e32 v55, v53, v5
	v_fma_f32 v32, v34, v2, v32
	v_fma_f32 v33, v35, v3, v33
	v_mul_f32_e32 v2, v42, v2
	v_mul_f32_e32 v3, v43, v3
	v_fma_f32 v54, v46, v38, v54
	v_fma_f32 v55, v47, v39, v55
	v_mul_f32_e32 v38, v52, v38
	v_mul_f32_e32 v39, v53, v39
	v_fma_f32 v2, v34, v6, -v2
	v_fma_f32 v3, v35, v7, -v3
	v_fma_f32 v4, v46, v4, -v38
	v_fma_f32 v5, v47, v5, -v39
	v_bfe_u32 v6, v3, 16, 1
	v_bfe_u32 v7, v2, 16, 1
	v_bfe_u32 v34, v1, 16, 1
	v_bfe_u32 v35, v0, 16, 1
	v_add3_u32 v0, v0, v35, s42
	v_add3_u32 v1, v1, v34, s42
	v_add3_u32 v2, v2, v7, s42
	v_add3_u32 v3, v3, v6, s42
	v_bfe_u32 v6, v44, 16, 1
	v_bfe_u32 v7, v45, 16, 1
	v_bfe_u32 v34, v4, 16, 1
	v_bfe_u32 v35, v5, 16, 1
	v_add3_u32 v5, v5, v35, s42
	v_add3_u32 v4, v4, v34, s42
	v_add3_u32 v7, v45, v7, s42
	v_add3_u32 v6, v44, v6, s42
	v_lshrrev_b32_e32 v6, 16, v6
	v_lshrrev_b32_e32 v7, 16, v7
	v_lshrrev_b32_e32 v4, 16, v4
	v_lshrrev_b32_e32 v5, 16, v5
	v_and_or_b32 v3, v3, s35, v5
	v_and_or_b32 v2, v2, s35, v4
	v_and_or_b32 v1, v1, s35, v7
	v_and_or_b32 v0, v0, s35, v6
	v_bfe_u32 v4, v33, 16, 1
	v_bfe_u32 v5, v32, 16, 1
	v_bfe_u32 v6, v37, 16, 1
	v_bfe_u32 v7, v36, 16, 1
	v_add3_u32 v34, v36, v7, s42
	v_add3_u32 v35, v37, v6, s42
	v_add3_u32 v5, v32, v5, s42
	v_add3_u32 v4, v33, v4, s42
	v_bfe_u32 v6, v60, 16, 1
	v_bfe_u32 v7, v61, 16, 1
	v_bfe_u32 v32, v54, 16, 1
	v_bfe_u32 v33, v55, 16, 1
	v_add3_u32 v33, v55, v33, s42
	v_add3_u32 v32, v54, v32, s42
	v_add3_u32 v7, v61, v7, s42
	v_add3_u32 v6, v60, v6, s42
	v_lshrrev_b32_e32 v36, 16, v6
	v_lshrrev_b32_e32 v37, 16, v7
	v_lshrrev_b32_e32 v6, 16, v32
	v_lshrrev_b32_e32 v7, 16, v33
	v_lshl_add_u64 v[32:33], v[48:49], 0, v[132:133]
	v_add_u32_e32 v48, s8, v195
	v_and_or_b32 v7, v4, s35, v7
	v_and_or_b32 v6, v5, s35, v6
	v_and_or_b32 v5, v35, s35, v37
	v_and_or_b32 v4, v34, s35, v36
	global_store_dwordx4 v[32:33], v[0:3], off
	global_store_dwordx4 v[32:33], v[4:7], off offset:128
	v_lshlrev_b32_e32 v32, 8, v48
	v_and_b32_e32 v116, 0xfff00, v32
	v_mad_i64_i32 v[4:5], s[38:39], v48, s37, v[118:119]
	v_lshl_add_u64 v[36:37], v[120:121], 0, v[116:117]
	v_lshl_add_u64 v[44:45], v[122:123], 0, v[116:117]
	global_load_dwordx4 v[0:3], v[4:5], off
	s_nop 0
	global_load_dwordx4 v[4:7], v[4:5], off offset:128
	s_nop 0
	global_load_dwordx4 v[32:35], v[36:37], off offset:16
	s_nop 0
	global_load_dwordx4 v[36:39], v[36:37], off
	s_nop 0
	global_load_dwordx4 v[40:43], v[44:45], off offset:16
	s_nop 0
	global_load_dwordx4 v[44:47], v[44:45], off
	v_ashrrev_i32_e32 v51, 31, v50
	v_lshlrev_b64 v[50:51], 10, v[50:51]
	v_lshl_add_u64 v[52:53], v[126:127], 0, v[50:51]
	v_lshl_add_u64 v[50:51], v[124:125], 0, v[50:51]
	v_lshl_add_u64 v[50:51], v[50:51], 0, s[22:23]
	v_cndmask_b32_e64 v51, v51, v53, s[6:7]
	v_cndmask_b32_e64 v50, v50, v52, s[6:7]
	s_waitcnt vmcnt(13)
	v_lshlrev_b32_e32 v53, 16, v9
	v_lshlrev_b32_e32 v52, 16, v8
	v_and_b32_e32 v9, 0xffff0000, v9
	v_and_b32_e32 v8, 0xffff0000, v8
	s_waitcnt vmcnt(8)
	v_mov_b32_e32 v59, v30
	v_mov_b32_e32 v30, v29
	v_lshlrev_b32_e32 v55, 16, v13
	v_lshlrev_b32_e32 v54, 16, v12
	v_and_b32_e32 v13, 0xffff0000, v13
	v_and_b32_e32 v12, 0xffff0000, v12
	v_mov_b32_e32 v56, v20
	v_mov_b32_e32 v57, v22
	v_mov_b32_e32 v58, v28
	v_mov_b32_e32 v22, v21
	v_mul_f32_e32 v20, v30, v8
	v_mul_f32_e32 v21, v31, v9
	v_mul_f32_e32 v28, v58, v54
	v_mul_f32_e32 v29, v59, v55
	v_fma_f32 v20, v22, v12, v20
	v_fma_f32 v21, v23, v13, v21
	v_mul_f32_e32 v12, v30, v12
	v_mul_f32_e32 v13, v31, v13
	v_mul_f32_e32 v60, v58, v52
	v_mul_f32_e32 v61, v59, v53
	v_fma_f32 v28, v56, v52, -v28
	v_fma_f32 v29, v57, v53, -v29
	v_fma_f32 v8, v22, v8, -v12
	v_fma_f32 v9, v23, v9, -v13
	v_lshlrev_b32_e32 v13, 16, v11
	v_lshlrev_b32_e32 v12, 16, v10
	v_and_b32_e32 v11, 0xffff0000, v11
	v_and_b32_e32 v10, 0xffff0000, v10
	v_mov_b32_e32 v53, v26
	v_mov_b32_e32 v26, v25
	v_lshlrev_b32_e32 v23, 16, v15
	v_lshlrev_b32_e32 v22, 16, v14
	v_and_b32_e32 v15, 0xffff0000, v15
	v_and_b32_e32 v14, 0xffff0000, v14
	v_mov_b32_e32 v30, v16
	v_mov_b32_e32 v31, v18
	v_mov_b32_e32 v52, v24
	v_mov_b32_e32 v18, v17
	v_mul_f32_e32 v16, v26, v10
	v_mul_f32_e32 v17, v27, v11
	v_fma_f32 v60, v56, v54, v60
	v_fma_f32 v61, v57, v55, v61
	v_mul_f32_e32 v54, v52, v12
	v_mul_f32_e32 v55, v53, v13
	v_fma_f32 v16, v18, v14, v16
	v_fma_f32 v17, v19, v15, v17
	v_mul_f32_e32 v14, v26, v14
	v_mul_f32_e32 v15, v27, v15
	v_fma_f32 v54, v30, v22, v54
	v_fma_f32 v55, v31, v23, v55
	v_mul_f32_e32 v22, v52, v22
	v_mul_f32_e32 v23, v53, v23
	v_fma_f32 v10, v18, v10, -v14
	v_fma_f32 v11, v19, v11, -v15
	v_fma_f32 v12, v30, v12, -v22
	v_fma_f32 v13, v31, v13, -v23
	v_bfe_u32 v14, v11, 16, 1
	v_bfe_u32 v15, v10, 16, 1
	v_bfe_u32 v18, v9, 16, 1
	v_bfe_u32 v19, v8, 16, 1
	v_add3_u32 v8, v8, v19, s42
	v_add3_u32 v9, v9, v18, s42
	v_add3_u32 v10, v10, v15, s42
	v_add3_u32 v11, v11, v14, s42
	v_bfe_u32 v14, v28, 16, 1
	v_bfe_u32 v15, v29, 16, 1
	v_bfe_u32 v18, v12, 16, 1
	v_bfe_u32 v19, v13, 16, 1
	v_add3_u32 v13, v13, v19, s42
	v_add3_u32 v12, v12, v18, s42
	v_add3_u32 v15, v29, v15, s42
	v_add3_u32 v14, v28, v14, s42
	v_lshrrev_b32_e32 v14, 16, v14
	v_lshrrev_b32_e32 v15, 16, v15
	v_lshrrev_b32_e32 v12, 16, v12
	v_lshrrev_b32_e32 v13, 16, v13
	v_and_or_b32 v11, v11, s35, v13
	v_and_or_b32 v10, v10, s35, v12
	v_and_or_b32 v9, v9, s35, v15
	v_and_or_b32 v8, v8, s35, v14
	v_bfe_u32 v12, v17, 16, 1
	v_bfe_u32 v13, v16, 16, 1
	v_bfe_u32 v14, v21, 16, 1
	v_bfe_u32 v15, v20, 16, 1
	v_add3_u32 v18, v20, v15, s42
	v_add3_u32 v19, v21, v14, s42
	v_add3_u32 v13, v16, v13, s42
	v_add3_u32 v12, v17, v12, s42
	v_bfe_u32 v14, v60, 16, 1
	v_bfe_u32 v15, v61, 16, 1
	v_bfe_u32 v16, v54, 16, 1
	v_bfe_u32 v17, v55, 16, 1
	v_add3_u32 v17, v55, v17, s42
	v_add3_u32 v16, v54, v16, s42
	v_add3_u32 v15, v61, v15, s42
	v_add3_u32 v14, v60, v14, s42
	v_ashrrev_i32_e32 v49, 31, v48
	v_lshrrev_b32_e32 v20, 16, v14
	v_lshrrev_b32_e32 v21, 16, v15
	v_lshrrev_b32_e32 v14, 16, v16
	v_lshrrev_b32_e32 v15, 16, v17
	v_lshl_add_u64 v[16:17], v[50:51], 0, v[132:133]
	v_add_u32_e32 v50, s8, v196
	v_and_or_b32 v15, v12, s35, v15
	v_and_or_b32 v14, v13, s35, v14
	v_and_or_b32 v13, v19, s35, v21
	v_and_or_b32 v12, v18, s35, v20
	global_store_dwordx4 v[16:17], v[8:11], off
	global_store_dwordx4 v[16:17], v[12:15], off offset:128
	v_lshlrev_b32_e32 v16, 8, v50
	v_lshlrev_b64 v[48:49], 10, v[48:49]
	v_and_b32_e32 v116, 0xfff00, v16
	v_lshl_add_u64 v[52:53], v[126:127], 0, v[48:49]
	v_lshl_add_u64 v[48:49], v[124:125], 0, v[48:49]
	v_mad_i64_i32 v[12:13], s[38:39], v50, s37, v[118:119]
	v_lshl_add_u64 v[20:21], v[120:121], 0, v[116:117]
	v_lshl_add_u64 v[28:29], v[122:123], 0, v[116:117]
	v_lshl_add_u64 v[48:49], v[48:49], 0, s[22:23]
	global_load_dwordx4 v[8:11], v[12:13], off
	s_nop 0
	global_load_dwordx4 v[12:15], v[12:13], off offset:128
	s_nop 0
	global_load_dwordx4 v[16:19], v[20:21], off offset:16
	s_nop 0
	global_load_dwordx4 v[20:23], v[20:21], off
	s_nop 0
	global_load_dwordx4 v[24:27], v[28:29], off offset:16
	s_nop 0
	global_load_dwordx4 v[28:31], v[28:29], off
	v_cndmask_b32_e64 v49, v49, v53, s[6:7]
	v_cndmask_b32_e64 v48, v48, v52, s[6:7]
	s_waitcnt vmcnt(13)
	v_lshlrev_b32_e32 v53, 16, v1
	v_lshlrev_b32_e32 v52, 16, v0
	v_and_b32_e32 v1, 0xffff0000, v1
	v_and_b32_e32 v0, 0xffff0000, v0
	s_waitcnt vmcnt(8)
	v_mov_b32_e32 v59, v46
	v_mov_b32_e32 v46, v45
	v_lshlrev_b32_e32 v55, 16, v5
	v_lshlrev_b32_e32 v54, 16, v4
	v_and_b32_e32 v5, 0xffff0000, v5
	v_and_b32_e32 v4, 0xffff0000, v4
	v_mov_b32_e32 v56, v36
	v_mov_b32_e32 v57, v38
	v_mov_b32_e32 v58, v44
	v_mov_b32_e32 v38, v37
	v_mul_f32_e32 v36, v46, v0
	v_mul_f32_e32 v37, v47, v1
	v_mul_f32_e32 v44, v58, v54
	v_mul_f32_e32 v45, v59, v55
	v_fma_f32 v36, v38, v4, v36
	v_fma_f32 v37, v39, v5, v37
	v_mul_f32_e32 v4, v46, v4
	v_mul_f32_e32 v5, v47, v5
	v_mul_f32_e32 v60, v58, v52
	v_mul_f32_e32 v61, v59, v53
	v_fma_f32 v44, v56, v52, -v44
	v_fma_f32 v45, v57, v53, -v45
	v_fma_f32 v0, v38, v0, -v4
	v_fma_f32 v1, v39, v1, -v5
	v_lshlrev_b32_e32 v5, 16, v3
	v_lshlrev_b32_e32 v4, 16, v2
	v_and_b32_e32 v3, 0xffff0000, v3
	v_and_b32_e32 v2, 0xffff0000, v2
	v_mov_b32_e32 v53, v42
	v_mov_b32_e32 v42, v41
	v_lshlrev_b32_e32 v39, 16, v7
	v_lshlrev_b32_e32 v38, 16, v6
	v_and_b32_e32 v7, 0xffff0000, v7
	v_and_b32_e32 v6, 0xffff0000, v6
	v_mov_b32_e32 v46, v32
	v_mov_b32_e32 v47, v34
	v_mov_b32_e32 v52, v40
	v_mov_b32_e32 v34, v33
	v_mul_f32_e32 v32, v42, v2
	v_mul_f32_e32 v33, v43, v3
	v_fma_f32 v60, v56, v54, v60
	v_fma_f32 v61, v57, v55, v61
	v_mul_f32_e32 v54, v52, v4
	v_mul_f32_e32 v55, v53, v5
	v_fma_f32 v32, v34, v6, v32
	v_fma_f32 v33, v35, v7, v33
	v_mul_f32_e32 v6, v42, v6
	v_mul_f32_e32 v7, v43, v7
	v_fma_f32 v54, v46, v38, v54
	v_fma_f32 v55, v47, v39, v55
	v_mul_f32_e32 v38, v52, v38
	v_mul_f32_e32 v39, v53, v39
	v_fma_f32 v2, v34, v2, -v6
	v_fma_f32 v3, v35, v3, -v7
	v_fma_f32 v4, v46, v4, -v38
	v_fma_f32 v5, v47, v5, -v39
	v_bfe_u32 v6, v3, 16, 1
	v_bfe_u32 v7, v2, 16, 1
	v_bfe_u32 v34, v1, 16, 1
	v_bfe_u32 v35, v0, 16, 1
	v_add3_u32 v0, v0, v35, s42
	v_add3_u32 v1, v1, v34, s42
	v_add3_u32 v2, v2, v7, s42
	v_add3_u32 v3, v3, v6, s42
	v_bfe_u32 v6, v44, 16, 1
	v_bfe_u32 v7, v45, 16, 1
	v_bfe_u32 v34, v4, 16, 1
	v_bfe_u32 v35, v5, 16, 1
	v_add3_u32 v5, v5, v35, s42
	v_add3_u32 v4, v4, v34, s42
	v_add3_u32 v7, v45, v7, s42
	v_add3_u32 v6, v44, v6, s42
	v_lshrrev_b32_e32 v6, 16, v6
	v_lshrrev_b32_e32 v7, 16, v7
	v_lshrrev_b32_e32 v4, 16, v4
	v_lshrrev_b32_e32 v5, 16, v5
	v_and_or_b32 v3, v3, s35, v5
	v_and_or_b32 v2, v2, s35, v4
	v_and_or_b32 v1, v1, s35, v7
	v_and_or_b32 v0, v0, s35, v6
	v_bfe_u32 v4, v33, 16, 1
	v_bfe_u32 v5, v32, 16, 1
	v_bfe_u32 v6, v37, 16, 1
	v_bfe_u32 v7, v36, 16, 1
	v_add3_u32 v34, v36, v7, s42
	v_add3_u32 v35, v37, v6, s42
	v_add3_u32 v5, v32, v5, s42
	v_add3_u32 v4, v33, v4, s42
	v_bfe_u32 v6, v60, 16, 1
	v_bfe_u32 v7, v61, 16, 1
	v_bfe_u32 v32, v54, 16, 1
	v_bfe_u32 v33, v55, 16, 1
	v_add3_u32 v33, v55, v33, s42
	v_add3_u32 v32, v54, v32, s42
	v_add3_u32 v7, v61, v7, s42
	v_add3_u32 v6, v60, v6, s42
	v_lshrrev_b32_e32 v36, 16, v6
	v_lshrrev_b32_e32 v37, 16, v7
	v_lshrrev_b32_e32 v6, 16, v32
	v_lshrrev_b32_e32 v7, 16, v33
	v_lshl_add_u64 v[32:33], v[48:49], 0, v[132:133]
	v_add_u32_e32 v48, s8, v197
	v_and_or_b32 v7, v4, s35, v7
	v_and_or_b32 v6, v5, s35, v6
	v_and_or_b32 v5, v35, s35, v37
	v_and_or_b32 v4, v34, s35, v36
	global_store_dwordx4 v[32:33], v[0:3], off
	global_store_dwordx4 v[32:33], v[4:7], off offset:128
	v_lshlrev_b32_e32 v32, 8, v48
	v_and_b32_e32 v116, 0xfff00, v32
	v_mad_i64_i32 v[4:5], s[38:39], v48, s37, v[118:119]
	v_lshl_add_u64 v[36:37], v[120:121], 0, v[116:117]
	v_lshl_add_u64 v[44:45], v[122:123], 0, v[116:117]
	global_load_dwordx4 v[0:3], v[4:5], off
	s_nop 0
	global_load_dwordx4 v[4:7], v[4:5], off offset:128
	s_nop 0
	global_load_dwordx4 v[32:35], v[36:37], off offset:16
	s_nop 0
	global_load_dwordx4 v[36:39], v[36:37], off
	s_nop 0
	global_load_dwordx4 v[40:43], v[44:45], off offset:16
	s_nop 0
	global_load_dwordx4 v[44:47], v[44:45], off
	v_ashrrev_i32_e32 v51, 31, v50
	v_lshlrev_b64 v[50:51], 10, v[50:51]
	v_lshl_add_u64 v[52:53], v[126:127], 0, v[50:51]
	v_lshl_add_u64 v[50:51], v[124:125], 0, v[50:51]
	v_lshl_add_u64 v[50:51], v[50:51], 0, s[22:23]
	v_cndmask_b32_e64 v51, v51, v53, s[6:7]
	v_cndmask_b32_e64 v50, v50, v52, s[6:7]
	s_waitcnt vmcnt(13)
	v_lshlrev_b32_e32 v53, 16, v9
	v_lshlrev_b32_e32 v52, 16, v8
	v_and_b32_e32 v9, 0xffff0000, v9
	v_and_b32_e32 v8, 0xffff0000, v8
	s_waitcnt vmcnt(8)
	v_mov_b32_e32 v59, v30
	v_mov_b32_e32 v30, v29
	v_lshlrev_b32_e32 v55, 16, v13
	v_lshlrev_b32_e32 v54, 16, v12
	v_and_b32_e32 v13, 0xffff0000, v13
	v_and_b32_e32 v12, 0xffff0000, v12
	v_mov_b32_e32 v56, v20
	v_mov_b32_e32 v57, v22
	v_mov_b32_e32 v58, v28
	v_mov_b32_e32 v22, v21
	v_mul_f32_e32 v20, v30, v8
	v_mul_f32_e32 v21, v31, v9
	v_mul_f32_e32 v28, v58, v54
	v_mul_f32_e32 v29, v59, v55
	v_fma_f32 v20, v22, v12, v20
	v_fma_f32 v21, v23, v13, v21
	v_mul_f32_e32 v12, v30, v12
	v_mul_f32_e32 v13, v31, v13
	v_mul_f32_e32 v60, v58, v52
	v_mul_f32_e32 v61, v59, v53
	v_fma_f32 v28, v56, v52, -v28
	v_fma_f32 v29, v57, v53, -v29
	v_fma_f32 v8, v22, v8, -v12
	v_fma_f32 v9, v23, v9, -v13
	v_lshlrev_b32_e32 v13, 16, v11
	v_lshlrev_b32_e32 v12, 16, v10
	v_and_b32_e32 v11, 0xffff0000, v11
	v_and_b32_e32 v10, 0xffff0000, v10
	v_mov_b32_e32 v53, v26
	v_mov_b32_e32 v26, v25
	v_lshlrev_b32_e32 v23, 16, v15
	v_lshlrev_b32_e32 v22, 16, v14
	v_and_b32_e32 v15, 0xffff0000, v15
	v_and_b32_e32 v14, 0xffff0000, v14
	v_mov_b32_e32 v30, v16
	v_mov_b32_e32 v31, v18
	v_mov_b32_e32 v52, v24
	v_mov_b32_e32 v18, v17
	v_mul_f32_e32 v16, v26, v10
	v_mul_f32_e32 v17, v27, v11
	v_fma_f32 v60, v56, v54, v60
	v_fma_f32 v61, v57, v55, v61
	v_mul_f32_e32 v54, v52, v12
	v_mul_f32_e32 v55, v53, v13
	v_fma_f32 v16, v18, v14, v16
	v_fma_f32 v17, v19, v15, v17
	v_mul_f32_e32 v14, v26, v14
	v_mul_f32_e32 v15, v27, v15
	v_fma_f32 v54, v30, v22, v54
	v_fma_f32 v55, v31, v23, v55
	v_mul_f32_e32 v22, v52, v22
	v_mul_f32_e32 v23, v53, v23
	v_fma_f32 v10, v18, v10, -v14
	v_fma_f32 v11, v19, v11, -v15
	v_fma_f32 v12, v30, v12, -v22
	v_fma_f32 v13, v31, v13, -v23
	v_bfe_u32 v14, v11, 16, 1
	v_bfe_u32 v15, v10, 16, 1
	v_bfe_u32 v18, v9, 16, 1
	v_bfe_u32 v19, v8, 16, 1
	v_add3_u32 v8, v8, v19, s42
	v_add3_u32 v9, v9, v18, s42
	v_add3_u32 v10, v10, v15, s42
	v_add3_u32 v11, v11, v14, s42
	v_bfe_u32 v14, v28, 16, 1
	v_bfe_u32 v15, v29, 16, 1
	v_bfe_u32 v18, v12, 16, 1
	v_bfe_u32 v19, v13, 16, 1
	v_add3_u32 v13, v13, v19, s42
	v_add3_u32 v12, v12, v18, s42
	v_add3_u32 v15, v29, v15, s42
	v_add3_u32 v14, v28, v14, s42
	v_lshrrev_b32_e32 v14, 16, v14
	v_lshrrev_b32_e32 v15, 16, v15
	v_lshrrev_b32_e32 v12, 16, v12
	v_lshrrev_b32_e32 v13, 16, v13
	v_and_or_b32 v11, v11, s35, v13
	v_and_or_b32 v10, v10, s35, v12
	v_and_or_b32 v9, v9, s35, v15
	v_and_or_b32 v8, v8, s35, v14
	v_bfe_u32 v12, v17, 16, 1
	v_bfe_u32 v13, v16, 16, 1
	v_bfe_u32 v14, v21, 16, 1
	v_bfe_u32 v15, v20, 16, 1
	v_add3_u32 v18, v20, v15, s42
	v_add3_u32 v19, v21, v14, s42
	v_add3_u32 v13, v16, v13, s42
	v_add3_u32 v12, v17, v12, s42
	v_bfe_u32 v14, v60, 16, 1
	v_bfe_u32 v15, v61, 16, 1
	v_bfe_u32 v16, v54, 16, 1
	v_bfe_u32 v17, v55, 16, 1
	v_add3_u32 v17, v55, v17, s42
	v_add3_u32 v16, v54, v16, s42
	v_add3_u32 v15, v61, v15, s42
	v_add3_u32 v14, v60, v14, s42
	v_ashrrev_i32_e32 v49, 31, v48
	v_lshrrev_b32_e32 v20, 16, v14
	v_lshrrev_b32_e32 v21, 16, v15
	v_lshrrev_b32_e32 v14, 16, v16
	v_lshrrev_b32_e32 v15, 16, v17
	v_lshl_add_u64 v[16:17], v[50:51], 0, v[132:133]
	v_add_u32_e32 v50, s8, v198
	v_and_or_b32 v15, v12, s35, v15
	v_and_or_b32 v14, v13, s35, v14
	v_and_or_b32 v13, v19, s35, v21
	v_and_or_b32 v12, v18, s35, v20
	global_store_dwordx4 v[16:17], v[8:11], off
	global_store_dwordx4 v[16:17], v[12:15], off offset:128
	v_lshlrev_b32_e32 v16, 8, v50
	v_lshlrev_b64 v[48:49], 10, v[48:49]
	v_and_b32_e32 v116, 0xfff00, v16
	v_lshl_add_u64 v[52:53], v[126:127], 0, v[48:49]
	v_lshl_add_u64 v[48:49], v[124:125], 0, v[48:49]
	v_mad_i64_i32 v[12:13], s[38:39], v50, s37, v[118:119]
	v_lshl_add_u64 v[20:21], v[120:121], 0, v[116:117]
	v_lshl_add_u64 v[28:29], v[122:123], 0, v[116:117]
	v_lshl_add_u64 v[48:49], v[48:49], 0, s[22:23]
	global_load_dwordx4 v[8:11], v[12:13], off
	s_nop 0
	global_load_dwordx4 v[12:15], v[12:13], off offset:128
	s_nop 0
	global_load_dwordx4 v[16:19], v[20:21], off offset:16
	s_nop 0
	global_load_dwordx4 v[20:23], v[20:21], off
	s_nop 0
	global_load_dwordx4 v[24:27], v[28:29], off offset:16
	s_nop 0
	global_load_dwordx4 v[28:31], v[28:29], off
	v_cndmask_b32_e64 v49, v49, v53, s[6:7]
	v_cndmask_b32_e64 v48, v48, v52, s[6:7]
	s_waitcnt vmcnt(13)
	v_lshlrev_b32_e32 v53, 16, v1
	v_lshlrev_b32_e32 v52, 16, v0
	v_and_b32_e32 v1, 0xffff0000, v1
	v_and_b32_e32 v0, 0xffff0000, v0
	s_waitcnt vmcnt(8)
	v_mov_b32_e32 v59, v46
	v_mov_b32_e32 v46, v45
	v_lshlrev_b32_e32 v55, 16, v5
	v_lshlrev_b32_e32 v54, 16, v4
	v_and_b32_e32 v5, 0xffff0000, v5
	v_and_b32_e32 v4, 0xffff0000, v4
	v_mov_b32_e32 v56, v36
	v_mov_b32_e32 v57, v38
	v_mov_b32_e32 v58, v44
	v_mov_b32_e32 v38, v37
	v_mul_f32_e32 v36, v46, v0
	v_mul_f32_e32 v37, v47, v1
	v_mul_f32_e32 v44, v58, v54
	v_mul_f32_e32 v45, v59, v55
	v_fma_f32 v36, v38, v4, v36
	v_fma_f32 v37, v39, v5, v37
	v_mul_f32_e32 v4, v46, v4
	v_mul_f32_e32 v5, v47, v5
	v_mul_f32_e32 v60, v58, v52
	v_mul_f32_e32 v61, v59, v53
	v_fma_f32 v44, v56, v52, -v44
	v_fma_f32 v45, v57, v53, -v45
	v_fma_f32 v0, v38, v0, -v4
	v_fma_f32 v1, v39, v1, -v5
	v_lshlrev_b32_e32 v5, 16, v3
	v_lshlrev_b32_e32 v4, 16, v2
	v_and_b32_e32 v3, 0xffff0000, v3
	v_and_b32_e32 v2, 0xffff0000, v2
	v_mov_b32_e32 v53, v42
	v_mov_b32_e32 v42, v41
	v_lshlrev_b32_e32 v39, 16, v7
	v_lshlrev_b32_e32 v38, 16, v6
	v_and_b32_e32 v7, 0xffff0000, v7
	v_and_b32_e32 v6, 0xffff0000, v6
	v_mov_b32_e32 v46, v32
	v_mov_b32_e32 v47, v34
	v_mov_b32_e32 v52, v40
	v_mov_b32_e32 v34, v33
	v_mul_f32_e32 v32, v42, v2
	v_mul_f32_e32 v33, v43, v3
	v_fma_f32 v60, v56, v54, v60
	v_fma_f32 v61, v57, v55, v61
	v_mul_f32_e32 v54, v52, v4
	v_mul_f32_e32 v55, v53, v5
	v_fma_f32 v32, v34, v6, v32
	v_fma_f32 v33, v35, v7, v33
	v_mul_f32_e32 v6, v42, v6
	v_mul_f32_e32 v7, v43, v7
	v_fma_f32 v54, v46, v38, v54
	v_fma_f32 v55, v47, v39, v55
	v_mul_f32_e32 v38, v52, v38
	v_mul_f32_e32 v39, v53, v39
	v_fma_f32 v2, v34, v2, -v6
	v_fma_f32 v3, v35, v3, -v7
	v_fma_f32 v4, v46, v4, -v38
	v_fma_f32 v5, v47, v5, -v39
	v_bfe_u32 v6, v3, 16, 1
	v_bfe_u32 v7, v2, 16, 1
	v_bfe_u32 v34, v1, 16, 1
	v_bfe_u32 v35, v0, 16, 1
	v_add3_u32 v0, v0, v35, s42
	v_add3_u32 v1, v1, v34, s42
	v_add3_u32 v2, v2, v7, s42
	v_add3_u32 v3, v3, v6, s42
	v_bfe_u32 v6, v44, 16, 1
	v_bfe_u32 v7, v45, 16, 1
	v_bfe_u32 v34, v4, 16, 1
	v_bfe_u32 v35, v5, 16, 1
	v_add3_u32 v5, v5, v35, s42
	v_add3_u32 v4, v4, v34, s42
	v_add3_u32 v7, v45, v7, s42
	v_add3_u32 v6, v44, v6, s42
	v_lshrrev_b32_e32 v6, 16, v6
	v_lshrrev_b32_e32 v7, 16, v7
	v_lshrrev_b32_e32 v4, 16, v4
	v_lshrrev_b32_e32 v5, 16, v5
	v_and_or_b32 v3, v3, s35, v5
	v_and_or_b32 v2, v2, s35, v4
	v_and_or_b32 v1, v1, s35, v7
	v_and_or_b32 v0, v0, s35, v6
	v_bfe_u32 v4, v33, 16, 1
	v_bfe_u32 v5, v32, 16, 1
	v_bfe_u32 v6, v37, 16, 1
	v_bfe_u32 v7, v36, 16, 1
	v_add3_u32 v34, v36, v7, s42
	v_add3_u32 v35, v37, v6, s42
	v_add3_u32 v5, v32, v5, s42
	v_add3_u32 v4, v33, v4, s42
	v_bfe_u32 v6, v60, 16, 1
	v_bfe_u32 v7, v61, 16, 1
	v_bfe_u32 v32, v54, 16, 1
	v_bfe_u32 v33, v55, 16, 1
	v_add3_u32 v33, v55, v33, s42
	v_add3_u32 v32, v54, v32, s42
	v_add3_u32 v7, v61, v7, s42
	v_add3_u32 v6, v60, v6, s42
	v_lshrrev_b32_e32 v36, 16, v6
	v_lshrrev_b32_e32 v37, 16, v7
	v_lshrrev_b32_e32 v6, 16, v32
	v_lshrrev_b32_e32 v7, 16, v33
	v_lshl_add_u64 v[32:33], v[48:49], 0, v[132:133]
	v_add_u32_e32 v48, s8, v199
	v_and_or_b32 v7, v4, s35, v7
	v_and_or_b32 v6, v5, s35, v6
	v_and_or_b32 v5, v35, s35, v37
	v_and_or_b32 v4, v34, s35, v36
	global_store_dwordx4 v[32:33], v[0:3], off
	global_store_dwordx4 v[32:33], v[4:7], off offset:128
	v_lshlrev_b32_e32 v32, 8, v48
	v_and_b32_e32 v116, 0xfff00, v32
	v_mad_i64_i32 v[4:5], s[8:9], v48, s37, v[118:119]
	v_lshl_add_u64 v[36:37], v[120:121], 0, v[116:117]
	v_lshl_add_u64 v[44:45], v[122:123], 0, v[116:117]
	global_load_dwordx4 v[0:3], v[4:5], off
	s_nop 0
	global_load_dwordx4 v[4:7], v[4:5], off offset:128
	s_nop 0
	global_load_dwordx4 v[32:35], v[36:37], off offset:16
	s_nop 0
	global_load_dwordx4 v[36:39], v[36:37], off
	s_nop 0
	global_load_dwordx4 v[40:43], v[44:45], off offset:16
	s_nop 0
	global_load_dwordx4 v[44:47], v[44:45], off
	v_ashrrev_i32_e32 v51, 31, v50
	v_lshlrev_b64 v[50:51], 10, v[50:51]
	v_lshl_add_u64 v[52:53], v[126:127], 0, v[50:51]
	v_lshl_add_u64 v[50:51], v[124:125], 0, v[50:51]
	v_lshl_add_u64 v[50:51], v[50:51], 0, s[22:23]
	v_cndmask_b32_e64 v51, v51, v53, s[6:7]
	v_cndmask_b32_e64 v50, v50, v52, s[6:7]
	s_waitcnt vmcnt(13)
	v_lshlrev_b32_e32 v53, 16, v9
	v_lshlrev_b32_e32 v52, 16, v8
	v_and_b32_e32 v9, 0xffff0000, v9
	v_and_b32_e32 v8, 0xffff0000, v8
	s_waitcnt vmcnt(8)
	v_mov_b32_e32 v59, v30
	v_mov_b32_e32 v30, v29
	v_lshlrev_b32_e32 v55, 16, v13
	v_lshlrev_b32_e32 v54, 16, v12
	v_and_b32_e32 v13, 0xffff0000, v13
	v_and_b32_e32 v12, 0xffff0000, v12
	v_mov_b32_e32 v56, v20
	v_mov_b32_e32 v57, v22
	v_mov_b32_e32 v58, v28
	v_mov_b32_e32 v22, v21
	v_mul_f32_e32 v20, v30, v8
	v_mul_f32_e32 v21, v31, v9
	v_mul_f32_e32 v28, v58, v54
	v_mul_f32_e32 v29, v59, v55
	v_fma_f32 v20, v22, v12, v20
	v_fma_f32 v21, v23, v13, v21
	v_mul_f32_e32 v12, v30, v12
	v_mul_f32_e32 v13, v31, v13
	v_mul_f32_e32 v60, v58, v52
	v_mul_f32_e32 v61, v59, v53
	v_fma_f32 v28, v56, v52, -v28
	v_fma_f32 v29, v57, v53, -v29
	v_fma_f32 v8, v22, v8, -v12
	v_fma_f32 v9, v23, v9, -v13
	v_lshlrev_b32_e32 v13, 16, v11
	v_lshlrev_b32_e32 v12, 16, v10
	v_and_b32_e32 v11, 0xffff0000, v11
	v_and_b32_e32 v10, 0xffff0000, v10
	v_mov_b32_e32 v53, v26
	v_mov_b32_e32 v26, v25
	v_lshlrev_b32_e32 v23, 16, v15
	v_lshlrev_b32_e32 v22, 16, v14
	v_and_b32_e32 v15, 0xffff0000, v15
	v_and_b32_e32 v14, 0xffff0000, v14
	v_mov_b32_e32 v30, v16
	v_mov_b32_e32 v31, v18
	v_mov_b32_e32 v52, v24
	v_mov_b32_e32 v18, v17
	v_mul_f32_e32 v16, v26, v10
	v_mul_f32_e32 v17, v27, v11
	v_fma_f32 v60, v56, v54, v60
	v_fma_f32 v61, v57, v55, v61
	v_mul_f32_e32 v54, v52, v12
	v_mul_f32_e32 v55, v53, v13
	v_fma_f32 v16, v18, v14, v16
	v_fma_f32 v17, v19, v15, v17
	v_mul_f32_e32 v14, v26, v14
	v_mul_f32_e32 v15, v27, v15
	v_fma_f32 v54, v30, v22, v54
	v_fma_f32 v55, v31, v23, v55
	v_mul_f32_e32 v22, v52, v22
	v_mul_f32_e32 v23, v53, v23
	v_fma_f32 v10, v18, v10, -v14
	v_fma_f32 v11, v19, v11, -v15
	v_fma_f32 v12, v30, v12, -v22
	v_fma_f32 v13, v31, v13, -v23
	v_bfe_u32 v14, v11, 16, 1
	v_bfe_u32 v15, v10, 16, 1
	v_bfe_u32 v18, v9, 16, 1
	v_bfe_u32 v19, v8, 16, 1
	v_add3_u32 v8, v8, v19, s42
	v_add3_u32 v9, v9, v18, s42
	v_add3_u32 v10, v10, v15, s42
	v_add3_u32 v11, v11, v14, s42
	v_bfe_u32 v14, v28, 16, 1
	v_bfe_u32 v15, v29, 16, 1
	v_bfe_u32 v18, v12, 16, 1
	v_bfe_u32 v19, v13, 16, 1
	v_add3_u32 v13, v13, v19, s42
	v_add3_u32 v12, v12, v18, s42
	v_add3_u32 v15, v29, v15, s42
	v_add3_u32 v14, v28, v14, s42
	v_lshrrev_b32_e32 v14, 16, v14
	v_lshrrev_b32_e32 v15, 16, v15
	v_lshrrev_b32_e32 v12, 16, v12
	v_lshrrev_b32_e32 v13, 16, v13
	v_and_or_b32 v11, v11, s35, v13
	v_and_or_b32 v10, v10, s35, v12
	v_and_or_b32 v9, v9, s35, v15
	v_and_or_b32 v8, v8, s35, v14
	v_bfe_u32 v12, v17, 16, 1
	v_bfe_u32 v13, v16, 16, 1
	v_bfe_u32 v14, v21, 16, 1
	v_bfe_u32 v15, v20, 16, 1
	v_add3_u32 v18, v20, v15, s42
	v_add3_u32 v19, v21, v14, s42
	v_add3_u32 v13, v16, v13, s42
	v_add3_u32 v12, v17, v12, s42
	v_bfe_u32 v14, v60, 16, 1
	v_bfe_u32 v15, v61, 16, 1
	v_bfe_u32 v16, v54, 16, 1
	v_bfe_u32 v17, v55, 16, 1
	v_add3_u32 v17, v55, v17, s42
	v_add3_u32 v16, v54, v16, s42
	v_add3_u32 v15, v61, v15, s42
	v_add3_u32 v14, v60, v14, s42
	v_ashrrev_i32_e32 v49, 31, v48
	v_lshrrev_b32_e32 v20, 16, v14
	v_lshrrev_b32_e32 v21, 16, v15
	v_lshrrev_b32_e32 v14, 16, v16
	v_lshrrev_b32_e32 v15, 16, v17
	v_lshl_add_u64 v[16:17], v[50:51], 0, v[132:133]
	v_and_or_b32 v15, v12, s35, v15
	v_and_or_b32 v14, v13, s35, v14
	v_and_or_b32 v13, v19, s35, v21
	v_and_or_b32 v12, v18, s35, v20
	global_store_dwordx4 v[16:17], v[8:11], off
	global_store_dwordx4 v[16:17], v[12:15], off offset:128
	s_waitcnt vmcnt(2)
	v_mov_b32_e32 v17, v46
	v_lshlrev_b64 v[8:9], 10, v[48:49]
	v_lshl_add_u64 v[10:11], v[126:127], 0, v[8:9]
	v_lshl_add_u64 v[8:9], v[124:125], 0, v[8:9]
	v_lshl_add_u64 v[8:9], v[8:9], 0, s[22:23]
	v_cndmask_b32_e64 v9, v9, v11, s[6:7]
	v_cndmask_b32_e64 v8, v8, v10, s[6:7]
	v_lshlrev_b32_e32 v11, 16, v1
	v_lshlrev_b32_e32 v10, 16, v0
	v_and_b32_e32 v1, 0xffff0000, v1
	v_and_b32_e32 v0, 0xffff0000, v0
	v_mov_b32_e32 v46, v45
	v_lshlrev_b32_e32 v13, 16, v5
	v_lshlrev_b32_e32 v12, 16, v4
	v_and_b32_e32 v5, 0xffff0000, v5
	v_and_b32_e32 v4, 0xffff0000, v4
	v_mov_b32_e32 v15, v38
	v_mov_b32_e32 v16, v44
	v_mov_b32_e32 v38, v37
	v_mul_f32_e32 v20, v46, v0
	v_mul_f32_e32 v21, v47, v1
	v_mov_b32_e32 v14, v36
	v_mul_f32_e32 v18, v16, v10
	v_mul_f32_e32 v19, v17, v11
	v_fma_f32 v20, v38, v4, v20
	v_fma_f32 v21, v39, v5, v21
	v_mul_f32_e32 v4, v46, v4
	v_mul_f32_e32 v5, v47, v5
	v_fma_f32 v18, v14, v12, v18
	v_fma_f32 v19, v15, v13, v19
	v_mul_f32_e32 v12, v16, v12
	v_mul_f32_e32 v13, v17, v13
	v_fma_f32 v0, v38, v0, -v4
	v_fma_f32 v1, v39, v1, -v5
	v_lshlrev_b32_e32 v5, 16, v3
	v_lshlrev_b32_e32 v4, 16, v2
	v_and_b32_e32 v3, 0xffff0000, v3
	v_and_b32_e32 v2, 0xffff0000, v2
	v_mov_b32_e32 v17, v42
	v_mov_b32_e32 v42, v41
	v_fma_f32 v10, v14, v10, -v12
	v_fma_f32 v11, v15, v11, -v13
	v_lshlrev_b32_e32 v13, 16, v7
	v_lshlrev_b32_e32 v12, 16, v6
	v_and_b32_e32 v7, 0xffff0000, v7
	v_and_b32_e32 v6, 0xffff0000, v6
	v_mov_b32_e32 v15, v34
	v_mov_b32_e32 v34, v33
	v_mul_f32_e32 v24, v42, v2
	v_mul_f32_e32 v25, v43, v3
	v_mov_b32_e32 v16, v40
	v_fma_f32 v24, v34, v6, v24
	v_fma_f32 v25, v35, v7, v25
	v_mul_f32_e32 v6, v42, v6
	v_mul_f32_e32 v7, v43, v7
	v_mov_b32_e32 v14, v32
	v_fma_f32 v2, v34, v2, -v6
	v_fma_f32 v3, v35, v3, -v7
	v_mul_f32_e32 v22, v16, v4
	v_mul_f32_e32 v23, v17, v5
	v_bfe_u32 v6, v3, 16, 1
	v_bfe_u32 v7, v2, 16, 1
	v_fma_f32 v22, v14, v12, v22
	v_fma_f32 v23, v15, v13, v23
	v_mul_f32_e32 v12, v16, v12
	v_mul_f32_e32 v13, v17, v13
	v_add3_u32 v2, v2, v7, s42
	v_add3_u32 v3, v3, v6, s42
	v_bfe_u32 v6, v10, 16, 1
	v_bfe_u32 v7, v11, 16, 1
	v_fma_f32 v4, v14, v4, -v12
	v_fma_f32 v5, v15, v5, -v13
	v_bfe_u32 v12, v1, 16, 1
	v_bfe_u32 v13, v0, 16, 1
	v_add3_u32 v7, v11, v7, s42
	v_add3_u32 v6, v10, v6, s42
	v_add3_u32 v0, v0, v13, s42
	v_add3_u32 v1, v1, v12, s42
	v_bfe_u32 v12, v4, 16, 1
	v_bfe_u32 v13, v5, 16, 1
	v_lshrrev_b32_e32 v6, 16, v6
	v_lshrrev_b32_e32 v7, 16, v7
	v_add3_u32 v5, v5, v13, s42
	v_add3_u32 v4, v4, v12, s42
	v_and_or_b32 v1, v1, s35, v7
	v_and_or_b32 v0, v0, s35, v6
	v_bfe_u32 v6, v21, 16, 1
	v_bfe_u32 v7, v20, 16, 1
	v_lshrrev_b32_e32 v4, 16, v4
	v_lshrrev_b32_e32 v5, 16, v5
	v_add3_u32 v10, v20, v7, s42
	v_add3_u32 v11, v21, v6, s42
	v_bfe_u32 v6, v18, 16, 1
	v_bfe_u32 v7, v19, 16, 1
	v_bfe_u32 v12, v22, 16, 1
	v_bfe_u32 v13, v23, 16, 1
	v_and_or_b32 v3, v3, s35, v5
	v_and_or_b32 v2, v2, s35, v4
	v_bfe_u32 v4, v25, 16, 1
	v_bfe_u32 v5, v24, 16, 1
	v_add3_u32 v13, v23, v13, s42
	v_add3_u32 v12, v22, v12, s42
	v_add3_u32 v7, v19, v7, s42
	v_add3_u32 v6, v18, v6, s42
	v_add3_u32 v5, v24, v5, s42
	v_add3_u32 v4, v25, v4, s42
	v_lshrrev_b32_e32 v14, 16, v6
	v_lshrrev_b32_e32 v15, 16, v7
	v_lshrrev_b32_e32 v6, 16, v12
	v_lshrrev_b32_e32 v7, 16, v13
	v_lshl_add_u64 v[8:9], v[8:9], 0, v[132:133]
	v_and_or_b32 v7, v4, s35, v7
	v_and_or_b32 v6, v5, s35, v6
	v_and_or_b32 v5, v11, s35, v15
	v_and_or_b32 v4, v10, s35, v14
	global_store_dwordx4 v[8:9], v[0:3], off
	global_store_dwordx4 v[8:9], v[4:7], off offset:128
	s_cbranch_execnz .LBB0_1478

.LBB0_1475:
	s_or_b64 exec, exec, s[8:9]
	s_waitcnt vmcnt(0)
	v_lshlrev_b32_e32 v217, 16, v85
	v_lshlrev_b32_e32 v216, 16, v84
	v_and_b32_e32 v219, 0xffff0000, v85
	v_and_b32_e32 v218, 0xffff0000, v84
	v_lshlrev_b32_e32 v221, 16, v87
	v_lshlrev_b32_e32 v220, 16, v86
	v_and_b32_e32 v223, 0xffff0000, v87
	v_and_b32_e32 v222, 0xffff0000, v86
	v_lshlrev_b32_e32 v229, 16, v83
	v_lshlrev_b32_e32 v228, 16, v82
	v_and_b32_e32 v231, 0xffff0000, v83
	v_and_b32_e32 v230, 0xffff0000, v82
	v_lshlrev_b32_e32 v84, 16, v76
	v_and_b32_e32 v86, 0xffff0000, v76
	v_lshlrev_b32_e32 v85, 16, v77
	v_and_b32_e32 v87, 0xffff0000, v77
	v_mov_b32_e32 v76, v48
	v_mov_b32_e32 v77, v50
	v_mov_b32_e32 v82, v40
	v_mov_b32_e32 v83, v42
	v_mov_b32_e32 v42, v41
	v_mov_b32_e32 v40, v4
	v_mov_b32_e32 v41, v6
	v_mov_b32_e32 v6, v5
	v_mov_b32_e32 v4, v52
	v_mov_b32_e32 v5, v54
	v_lshlrev_b32_e32 v225, 16, v81
	v_lshlrev_b32_e32 v224, 16, v80
	v_and_b32_e32 v227, 0xffff0000, v81
	v_and_b32_e32 v226, 0xffff0000, v80
	v_lshlrev_b32_e32 v232, 16, v78
	v_and_b32_e32 v234, 0xffff0000, v78
	v_lshlrev_b32_e32 v233, 16, v79
	v_and_b32_e32 v235, 0xffff0000, v79
	v_mov_b32_e32 v78, v20
	v_mov_b32_e32 v79, v22
	v_mov_b32_e32 v80, v32
	v_mov_b32_e32 v81, v34
	v_mov_b32_e32 v34, v33
	v_mov_b32_e32 v32, v0
	v_mov_b32_e32 v33, v2
	v_mov_b32_e32 v2, v1
	v_fma_f32 v0, v76, v84, v4
	v_fma_f32 v1, v77, v85, v5
	v_lshlrev_b32_e32 v191, 16, v89
	v_fma_f32 v0, v78, v224, v0
	v_fma_f32 v1, v79, v225, v1
	v_lshlrev_b32_e32 v190, 16, v88
	v_mov_b32_e32 v50, v49
	v_fma_f32 v0, v80, v216, v0
	v_fma_f32 v1, v81, v217, v1
	v_mov_b32_e32 v54, v53
	v_mov_b32_e32 v22, v21
	v_mov_b32_e32 v48, v16
	v_mov_b32_e32 v49, v18
	v_mov_b32_e32 v18, v17
	v_fma_f32 v16, v82, v190, v0
	v_fma_f32 v17, v83, v191, v1
	v_fma_f32 v0, v50, v86, v54
	v_fma_f32 v1, v51, v87, v55
	v_and_b32_e32 v89, 0xffff0000, v89
	v_fma_f32 v0, v22, v226, v0
	v_fma_f32 v1, v23, v227, v1
	v_and_b32_e32 v88, 0xffff0000, v88
	v_fma_f32 v0, v34, v218, v0
	v_fma_f32 v1, v35, v219, v1
	v_mov_b32_e32 v20, v24
	v_mov_b32_e32 v21, v26
	v_mov_b32_e32 v26, v25
	v_fma_f32 v24, v42, v88, v0
	v_fma_f32 v25, v43, v89, v1
	v_mov_b32_e32 v1, v30
	v_mov_b32_e32 v30, v29
	v_mov_b32_e32 v0, v28
	v_fma_f32 v28, v26, v234, v30
	v_fma_f32 v29, v27, v235, v31
	v_lshlrev_b32_e32 v189, 16, v91
	v_fma_f32 v28, v2, v230, v28
	v_fma_f32 v29, v3, v231, v29
	v_lshlrev_b32_e32 v188, 16, v90
	v_and_b32_e32 v91, 0xffff0000, v91
	v_and_b32_e32 v90, 0xffff0000, v90
	v_fma_f32 v52, v20, v232, v0
	v_fma_f32 v53, v21, v233, v1
	v_fma_f32 v28, v6, v222, v28
	v_fma_f32 v29, v7, v223, v29
	v_fma_f32 v52, v32, v228, v52
	v_fma_f32 v53, v33, v229, v53
	v_fma_f32 v28, v18, v90, v28
	v_fma_f32 v29, v19, v91, v29
	v_fma_f32 v52, v40, v220, v52
	v_fma_f32 v53, v41, v221, v53
	v_bfe_u32 v84, v29, 16, 1
	v_bfe_u32 v85, v28, 16, 1
	v_fma_f32 v52, v48, v188, v52
	v_fma_f32 v53, v49, v189, v53
	v_bfe_u32 v86, v25, 16, 1
	v_bfe_u32 v87, v24, 16, 1
	v_add3_u32 v28, v28, v85, s42
	v_add3_u32 v29, v29, v84, s42
	v_bfe_u32 v84, v16, 16, 1
	v_bfe_u32 v85, v17, 16, 1
	v_add3_u32 v24, v24, v87, s42
	v_add3_u32 v25, v25, v86, s42
	v_bfe_u32 v86, v52, 16, 1
	v_bfe_u32 v87, v53, 16, 1
	v_add3_u32 v17, v17, v85, s42
	v_add3_u32 v16, v16, v84, s42
	v_add3_u32 v53, v53, v87, s42
	v_add3_u32 v52, v52, v86, s42
	v_lshrrev_b32_e32 v16, 16, v16
	v_lshrrev_b32_e32 v17, 16, v17
	v_lshrrev_b32_e32 v52, 16, v52
	v_lshrrev_b32_e32 v53, 16, v53
	v_and_or_b32 v85, v25, s35, v17
	v_and_or_b32 v84, v24, s35, v16
	v_fma_f32 v24, v50, v226, v54
	v_fma_f32 v25, v51, v227, v55
	v_and_or_b32 v87, v29, s35, v53
	v_and_or_b32 v86, v28, s35, v52
	v_fma_f32 v24, v22, v218, v24
	v_fma_f32 v25, v23, v219, v25
	v_fma_f32 v28, v20, v228, v0
	v_fma_f32 v29, v21, v229, v1
	v_fma_f32 v52, v26, v230, v30
	v_fma_f32 v53, v27, v231, v31
	v_lshlrev_b32_e32 v187, 16, v93
	v_lshlrev_b32_e32 v186, 16, v92
	v_and_b32_e32 v93, 0xffff0000, v93
	v_and_b32_e32 v92, 0xffff0000, v92
	v_fma_f32 v16, v76, v224, v4
	v_fma_f32 v17, v77, v225, v5
	v_fma_f32 v24, v34, v88, v24
	v_fma_f32 v25, v35, v89, v25
	v_fma_f32 v28, v32, v220, v28
	v_fma_f32 v29, v33, v221, v29
	v_fma_f32 v52, v2, v222, v52
	v_fma_f32 v53, v3, v223, v53
	v_lshlrev_b32_e32 v185, 16, v95
	v_lshlrev_b32_e32 v184, 16, v94
	v_and_b32_e32 v95, 0xffff0000, v95
	v_and_b32_e32 v94, 0xffff0000, v94
	v_fma_f32 v16, v78, v216, v16
	v_fma_f32 v17, v79, v217, v17
	v_fma_f32 v24, v42, v92, v24
	v_fma_f32 v25, v43, v93, v25
	v_fma_f32 v28, v40, v188, v28
	v_fma_f32 v29, v41, v189, v29
	v_fma_f32 v52, v6, v90, v52
	v_fma_f32 v53, v7, v91, v53
	ds_write_b128 v209, v[84:87]
	v_fma_f32 v16, v80, v190, v16
	v_fma_f32 v17, v81, v191, v17
	v_fma_f32 v28, v48, v184, v28
	v_fma_f32 v29, v49, v185, v29
	v_fma_f32 v52, v18, v94, v52
	v_fma_f32 v53, v19, v95, v53
	v_bfe_u32 v86, v25, 16, 1
	v_bfe_u32 v87, v24, 16, 1
	v_fma_f32 v16, v82, v186, v16
	v_fma_f32 v17, v83, v187, v17
	v_bfe_u32 v84, v53, 16, 1
	v_bfe_u32 v85, v52, 16, 1
	v_add3_u32 v24, v24, v87, s42
	v_add3_u32 v25, v25, v86, s42
	v_bfe_u32 v86, v28, 16, 1
	v_bfe_u32 v87, v29, 16, 1
	v_add3_u32 v52, v52, v85, s42
	v_add3_u32 v53, v53, v84, s42
	v_bfe_u32 v84, v16, 16, 1
	v_bfe_u32 v85, v17, 16, 1
	v_add3_u32 v29, v29, v87, s42
	v_add3_u32 v28, v28, v86, s42
	v_add3_u32 v17, v17, v85, s42
	v_add3_u32 v16, v16, v84, s42
	v_lshrrev_b32_e32 v28, 16, v28
	v_lshrrev_b32_e32 v29, 16, v29
	v_lshrrev_b32_e32 v16, 16, v16
	v_lshrrev_b32_e32 v17, 16, v17
	v_and_or_b32 v87, v53, s35, v29
	v_and_or_b32 v86, v52, s35, v28
	v_fma_f32 v52, v26, v222, v30
	v_fma_f32 v53, v27, v223, v31
	v_and_or_b32 v85, v25, s35, v17
	v_and_or_b32 v84, v24, s35, v16
	v_fma_f32 v16, v76, v216, v4
	v_fma_f32 v17, v77, v217, v5
	v_fma_f32 v24, v50, v218, v54
	v_fma_f32 v25, v51, v219, v55
	v_fma_f32 v52, v2, v90, v52
	v_fma_f32 v53, v3, v91, v53
	v_lshlrev_b32_e32 v181, 16, v99
	v_lshlrev_b32_e32 v180, 16, v98
	v_and_b32_e32 v99, 0xffff0000, v99
	v_and_b32_e32 v98, 0xffff0000, v98
	v_fma_f32 v16, v78, v190, v16
	v_fma_f32 v17, v79, v191, v17
	v_fma_f32 v24, v22, v88, v24
	v_fma_f32 v25, v23, v89, v25
	v_fma_f32 v28, v20, v220, v0
	v_fma_f32 v29, v21, v221, v1
	v_fma_f32 v52, v6, v94, v52
	v_fma_f32 v53, v7, v95, v53
	v_lshlrev_b32_e32 v183, 16, v97
	v_lshlrev_b32_e32 v182, 16, v96
	v_and_b32_e32 v97, 0xffff0000, v97
	v_and_b32_e32 v96, 0xffff0000, v96
	v_fma_f32 v16, v80, v186, v16
	v_fma_f32 v17, v81, v187, v17
	v_fma_f32 v24, v34, v92, v24
	v_fma_f32 v25, v35, v93, v25
	v_fma_f32 v28, v32, v188, v28
	v_fma_f32 v29, v33, v189, v29
	v_fma_f32 v52, v18, v98, v52
	v_fma_f32 v53, v19, v99, v53
	ds_write_b128 v209, v[84:87] offset:272
	v_fma_f32 v16, v82, v182, v16
	v_fma_f32 v17, v83, v183, v17
	v_fma_f32 v24, v42, v96, v24
	v_fma_f32 v25, v43, v97, v25
	v_fma_f32 v28, v40, v184, v28
	v_fma_f32 v29, v41, v185, v29
	v_bfe_u32 v84, v53, 16, 1
	v_bfe_u32 v85, v52, 16, 1
	v_fma_f32 v28, v48, v180, v28
	v_fma_f32 v29, v49, v181, v29
	v_bfe_u32 v86, v25, 16, 1
	v_bfe_u32 v87, v24, 16, 1
	v_add3_u32 v52, v52, v85, s42
	v_add3_u32 v53, v53, v84, s42
	v_bfe_u32 v84, v16, 16, 1
	v_bfe_u32 v85, v17, 16, 1
	v_add3_u32 v24, v24, v87, s42
	v_add3_u32 v25, v25, v86, s42
	v_bfe_u32 v86, v28, 16, 1
	v_bfe_u32 v87, v29, 16, 1
	v_add3_u32 v17, v17, v85, s42
	v_add3_u32 v16, v16, v84, s42
	v_add3_u32 v29, v29, v87, s42
	v_add3_u32 v28, v28, v86, s42
	v_lshrrev_b32_e32 v16, 16, v16
	v_lshrrev_b32_e32 v17, 16, v17
	v_lshrrev_b32_e32 v28, 16, v28
	v_lshrrev_b32_e32 v29, 16, v29
	v_and_or_b32 v85, v25, s35, v17
	v_and_or_b32 v84, v24, s35, v16
	v_fma_f32 v24, v50, v88, v54
	v_fma_f32 v25, v51, v89, v55
	v_and_or_b32 v87, v53, s35, v29
	v_and_or_b32 v86, v52, s35, v28
	v_fma_f32 v24, v22, v92, v24
	v_fma_f32 v25, v23, v93, v25
	v_fma_f32 v28, v20, v188, v0
	v_fma_f32 v29, v21, v189, v1
	v_fma_f32 v52, v26, v90, v30
	v_fma_f32 v53, v27, v91, v31
	v_lshlrev_b32_e32 v179, 16, v101
	v_lshlrev_b32_e32 v178, 16, v100
	v_and_b32_e32 v101, 0xffff0000, v101
	v_and_b32_e32 v100, 0xffff0000, v100
	v_fma_f32 v16, v76, v190, v4
	v_fma_f32 v17, v77, v191, v5
	v_fma_f32 v24, v34, v96, v24
	v_fma_f32 v25, v35, v97, v25
	v_fma_f32 v28, v32, v184, v28
	v_fma_f32 v29, v33, v185, v29
	v_fma_f32 v52, v2, v94, v52
	v_fma_f32 v53, v3, v95, v53
	v_lshlrev_b32_e32 v169, 16, v113
	v_lshlrev_b32_e32 v168, 16, v112
	v_and_b32_e32 v167, 0xffff0000, v113
	v_and_b32_e32 v166, 0xffff0000, v112
	v_lshlrev_b32_e32 v165, 16, v115
	v_lshlrev_b32_e32 v164, 16, v114
	v_and_b32_e32 v113, 0xffff0000, v115
	v_and_b32_e32 v112, 0xffff0000, v114
	v_lshlrev_b32_e32 v173, 16, v109
	v_lshlrev_b32_e32 v172, 16, v108
	v_and_b32_e32 v171, 0xffff0000, v109
	v_and_b32_e32 v170, 0xffff0000, v108
	v_lshlrev_b32_e32 v115, 16, v111
	v_lshlrev_b32_e32 v114, 16, v110
	v_and_b32_e32 v109, 0xffff0000, v111
	v_and_b32_e32 v108, 0xffff0000, v110
	v_lshlrev_b32_e32 v177, 16, v105
	v_lshlrev_b32_e32 v176, 16, v104
	v_and_b32_e32 v175, 0xffff0000, v105
	v_and_b32_e32 v174, 0xffff0000, v104
	v_lshlrev_b32_e32 v111, 16, v107
	v_lshlrev_b32_e32 v110, 16, v106
	v_and_b32_e32 v105, 0xffff0000, v107
	v_and_b32_e32 v104, 0xffff0000, v106
	v_lshlrev_b32_e32 v107, 16, v103
	v_lshlrev_b32_e32 v106, 16, v102
	v_and_b32_e32 v103, 0xffff0000, v103
	v_and_b32_e32 v102, 0xffff0000, v102
	v_fma_f32 v16, v78, v186, v16
	v_fma_f32 v17, v79, v187, v17
	v_fma_f32 v24, v42, v100, v24
	v_fma_f32 v25, v43, v101, v25
	v_fma_f32 v28, v40, v180, v28
	v_fma_f32 v29, v41, v181, v29
	v_fma_f32 v52, v6, v98, v52
	v_fma_f32 v53, v7, v99, v53
	ds_write_b128 v209, v[84:87] offset:544
	v_fma_f32 v16, v80, v182, v16
	v_fma_f32 v17, v81, v183, v17
	v_fma_f32 v28, v48, v106, v28
	v_fma_f32 v29, v49, v107, v29
	v_fma_f32 v52, v18, v102, v52
	v_fma_f32 v53, v19, v103, v53
	v_bfe_u32 v86, v25, 16, 1
	v_bfe_u32 v87, v24, 16, 1
	v_fma_f32 v16, v82, v178, v16
	v_fma_f32 v17, v83, v179, v17
	v_bfe_u32 v84, v53, 16, 1
	v_bfe_u32 v85, v52, 16, 1
	v_add3_u32 v24, v24, v87, s42
	v_add3_u32 v25, v25, v86, s42
	v_bfe_u32 v86, v28, 16, 1
	v_bfe_u32 v87, v29, 16, 1
	v_add3_u32 v52, v52, v85, s42
	v_add3_u32 v53, v53, v84, s42
	v_bfe_u32 v84, v16, 16, 1
	v_bfe_u32 v85, v17, 16, 1
	v_add3_u32 v29, v29, v87, s42
	v_add3_u32 v28, v28, v86, s42
	v_add3_u32 v17, v17, v85, s42
	v_add3_u32 v16, v16, v84, s42
	v_lshrrev_b32_e32 v28, 16, v28
	v_lshrrev_b32_e32 v29, 16, v29
	v_lshrrev_b32_e32 v16, 16, v16
	v_lshrrev_b32_e32 v17, 16, v17
	v_and_or_b32 v87, v53, s35, v29
	v_and_or_b32 v86, v52, s35, v28
	v_fma_f32 v52, v26, v94, v30
	v_fma_f32 v53, v27, v95, v31
	v_and_or_b32 v85, v25, s35, v17
	v_and_or_b32 v84, v24, s35, v16
	v_fma_f32 v16, v76, v186, v4
	v_fma_f32 v17, v77, v187, v5
	v_fma_f32 v24, v50, v92, v54
	v_fma_f32 v25, v51, v93, v55
	v_fma_f32 v52, v2, v98, v52
	v_fma_f32 v53, v3, v99, v53
	v_fma_f32 v16, v78, v182, v16
	v_fma_f32 v17, v79, v183, v17
	v_fma_f32 v24, v22, v96, v24
	v_fma_f32 v25, v23, v97, v25
	v_fma_f32 v28, v20, v184, v0
	v_fma_f32 v29, v21, v185, v1
	v_fma_f32 v52, v6, v102, v52
	v_fma_f32 v53, v7, v103, v53
	v_fma_f32 v16, v80, v178, v16
	v_fma_f32 v17, v81, v179, v17
	v_fma_f32 v24, v34, v100, v24
	v_fma_f32 v25, v35, v101, v25
	v_fma_f32 v28, v32, v180, v28
	v_fma_f32 v29, v33, v181, v29
	v_fma_f32 v52, v18, v104, v52
	v_fma_f32 v53, v19, v105, v53
	ds_write_b128 v209, v[84:87] offset:816
	v_fma_f32 v16, v82, v176, v16
	v_fma_f32 v17, v83, v177, v17
	v_fma_f32 v24, v42, v174, v24
	v_fma_f32 v25, v43, v175, v25
	v_fma_f32 v28, v40, v106, v28
	v_fma_f32 v29, v41, v107, v29
	v_bfe_u32 v84, v53, 16, 1
	v_bfe_u32 v85, v52, 16, 1
	v_fma_f32 v28, v48, v110, v28
	v_fma_f32 v29, v49, v111, v29
	v_bfe_u32 v86, v25, 16, 1
	v_bfe_u32 v87, v24, 16, 1
	v_add3_u32 v52, v52, v85, s42
	v_add3_u32 v53, v53, v84, s42
	v_bfe_u32 v84, v16, 16, 1
	v_bfe_u32 v85, v17, 16, 1
	v_add3_u32 v24, v24, v87, s42
	v_add3_u32 v25, v25, v86, s42
	v_bfe_u32 v86, v28, 16, 1
	v_bfe_u32 v87, v29, 16, 1
	v_add3_u32 v17, v17, v85, s42
	v_add3_u32 v16, v16, v84, s42
	v_add3_u32 v29, v29, v87, s42
	v_add3_u32 v28, v28, v86, s42
	v_lshrrev_b32_e32 v16, 16, v16
	v_lshrrev_b32_e32 v17, 16, v17
	v_lshrrev_b32_e32 v28, 16, v28
	v_lshrrev_b32_e32 v29, 16, v29
	v_and_or_b32 v85, v25, s35, v17
	v_and_or_b32 v84, v24, s35, v16
	v_fma_f32 v24, v50, v96, v54
	v_fma_f32 v25, v51, v97, v55
	v_and_or_b32 v87, v53, s35, v29
	v_and_or_b32 v86, v52, s35, v28
	v_fma_f32 v24, v22, v100, v24
	v_fma_f32 v25, v23, v101, v25
	v_fma_f32 v28, v20, v180, v0
	v_fma_f32 v29, v21, v181, v1
	v_fma_f32 v52, v26, v98, v30
	v_fma_f32 v53, v27, v99, v31
	v_fma_f32 v16, v76, v182, v4
	v_fma_f32 v17, v77, v183, v5
	v_fma_f32 v24, v34, v174, v24
	v_fma_f32 v25, v35, v175, v25
	v_fma_f32 v28, v32, v106, v28
	v_fma_f32 v29, v33, v107, v29
	v_fma_f32 v52, v2, v102, v52
	v_fma_f32 v53, v3, v103, v53
	v_fma_f32 v16, v78, v178, v16
	v_fma_f32 v17, v79, v179, v17
	v_fma_f32 v24, v42, v170, v24
	v_fma_f32 v25, v43, v171, v25
	v_fma_f32 v28, v40, v110, v28
	v_fma_f32 v29, v41, v111, v29
	v_fma_f32 v52, v6, v104, v52
	v_fma_f32 v53, v7, v105, v53
	ds_write_b128 v209, v[84:87] offset:1088
	v_fma_f32 v16, v80, v176, v16
	v_fma_f32 v17, v81, v177, v17
	v_fma_f32 v28, v48, v114, v28
	v_fma_f32 v29, v49, v115, v29
	v_fma_f32 v52, v18, v108, v52
	v_fma_f32 v53, v19, v109, v53
	v_bfe_u32 v86, v25, 16, 1
	v_bfe_u32 v87, v24, 16, 1
	v_fma_f32 v16, v82, v172, v16
	v_fma_f32 v17, v83, v173, v17
	v_bfe_u32 v84, v53, 16, 1
	v_bfe_u32 v85, v52, 16, 1
	v_add3_u32 v24, v24, v87, s42
	v_add3_u32 v25, v25, v86, s42
	v_bfe_u32 v86, v28, 16, 1
	v_bfe_u32 v87, v29, 16, 1
	v_add3_u32 v52, v52, v85, s42
	v_add3_u32 v53, v53, v84, s42
	v_bfe_u32 v84, v16, 16, 1
	v_bfe_u32 v85, v17, 16, 1
	v_add3_u32 v29, v29, v87, s42
	v_add3_u32 v28, v28, v86, s42
	v_add3_u32 v17, v17, v85, s42
	v_add3_u32 v16, v16, v84, s42
	v_lshrrev_b32_e32 v28, 16, v28
	v_lshrrev_b32_e32 v29, 16, v29
	v_lshrrev_b32_e32 v16, 16, v16
	v_lshrrev_b32_e32 v17, 16, v17
	v_and_or_b32 v87, v53, s35, v29
	v_and_or_b32 v86, v52, s35, v28
	v_fma_f32 v52, v26, v102, v30
	v_fma_f32 v53, v27, v103, v31
	v_and_or_b32 v85, v25, s35, v17
	v_and_or_b32 v84, v24, s35, v16
	v_fma_f32 v16, v76, v178, v4
	v_fma_f32 v17, v77, v179, v5
	v_fma_f32 v52, v2, v104, v52
	v_fma_f32 v53, v3, v105, v53
	v_fma_f32 v16, v78, v176, v16
	v_fma_f32 v17, v79, v177, v17
	v_fma_f32 v24, v50, v100, v54
	v_fma_f32 v25, v51, v101, v55
	v_fma_f32 v52, v6, v108, v52
	v_fma_f32 v53, v7, v109, v53
	v_fma_f32 v16, v80, v172, v16
	v_fma_f32 v17, v81, v173, v17
	v_fma_f32 v24, v22, v174, v24
	v_fma_f32 v25, v23, v175, v25
	v_fma_f32 v52, v18, v112, v52
	v_fma_f32 v53, v19, v113, v53
	ds_write_b128 v209, v[84:87] offset:1360
	v_fma_f32 v16, v82, v168, v16
	v_fma_f32 v17, v83, v169, v17
	v_fma_f32 v24, v34, v170, v24
	v_fma_f32 v25, v35, v171, v25
	v_bfe_u32 v84, v53, 16, 1
	v_bfe_u32 v85, v52, 16, 1
	v_fma_f32 v24, v42, v166, v24
	v_fma_f32 v25, v43, v167, v25
	v_add3_u32 v52, v52, v85, s42
	v_add3_u32 v53, v53, v84, s42
	v_bfe_u32 v84, v16, 16, 1
	v_bfe_u32 v85, v17, 16, 1
	v_bfe_u32 v86, v25, 16, 1
	v_bfe_u32 v87, v24, 16, 1
	v_add3_u32 v17, v17, v85, s42
	v_add3_u32 v16, v16, v84, s42
	v_fma_f32 v4, v76, v176, v4
	v_fma_f32 v5, v77, v177, v5
	v_add3_u32 v24, v24, v87, s42
	v_add3_u32 v25, v25, v86, s42
	v_lshrrev_b32_e32 v16, 16, v16
	v_lshrrev_b32_e32 v17, 16, v17
	v_fma_f32 v4, v78, v172, v4
	v_fma_f32 v5, v79, v173, v5
	v_and_or_b32 v85, v25, s35, v17
	v_and_or_b32 v84, v24, s35, v16
	v_lshlrev_b32_e32 v17, 16, v73
	v_lshlrev_b32_e32 v16, 16, v72
	v_fma_f32 v4, v80, v168, v4
	v_fma_f32 v5, v81, v169, v5
	v_fma_f32 v28, v20, v106, v0
	v_fma_f32 v29, v21, v107, v1
	v_fma_f32 v4, v82, v16, v4
	v_fma_f32 v5, v83, v17, v5
	v_fma_f32 v16, v50, v174, v54
	v_fma_f32 v17, v51, v175, v55
	v_fma_f32 v0, v20, v110, v0
	v_fma_f32 v1, v21, v111, v1
	v_fma_f32 v16, v22, v170, v16
	v_fma_f32 v17, v23, v171, v17
	v_fma_f32 v20, v26, v104, v30
	v_fma_f32 v21, v27, v105, v31
	v_and_b32_e32 v25, 0xffff0000, v73
	v_and_b32_e32 v24, 0xffff0000, v72
	v_fma_f32 v16, v34, v166, v16
	v_fma_f32 v17, v35, v167, v17
	v_fma_f32 v2, v2, v108, v20
	v_fma_f32 v3, v3, v109, v21
	v_fma_f32 v28, v32, v110, v28
	v_fma_f32 v29, v33, v111, v29
	v_fma_f32 v16, v42, v24, v16
	v_fma_f32 v17, v43, v25, v17
	v_and_b32_e32 v25, 0xffff0000, v75
	v_and_b32_e32 v24, 0xffff0000, v74
	v_fma_f32 v0, v32, v114, v0
	v_fma_f32 v1, v33, v115, v1
	v_fma_f32 v2, v6, v112, v2
	v_fma_f32 v3, v7, v113, v3
	v_fma_f32 v28, v40, v114, v28
	v_fma_f32 v29, v41, v115, v29
	v_lshlrev_b32_e32 v23, 16, v75
	v_lshlrev_b32_e32 v22, 16, v74
	v_fma_f32 v0, v40, v164, v0
	v_fma_f32 v1, v41, v165, v1
	v_fma_f32 v2, v18, v24, v2
	v_fma_f32 v3, v19, v25, v3
	v_fma_f32 v28, v48, v164, v28
	v_fma_f32 v29, v49, v165, v29
	v_fma_f32 v0, v48, v22, v0
	v_fma_f32 v1, v49, v23, v1
	v_bfe_u32 v6, v3, 16, 1
	v_bfe_u32 v7, v2, 16, 1
	v_bfe_u32 v18, v17, 16, 1
	v_bfe_u32 v19, v16, 16, 1
	v_bfe_u32 v86, v28, 16, 1
	v_bfe_u32 v87, v29, 16, 1
	v_add3_u32 v16, v16, v19, s42
	v_add3_u32 v17, v17, v18, s42
	v_add3_u32 v2, v2, v7, s42
	v_add3_u32 v3, v3, v6, s42
	v_bfe_u32 v6, v4, 16, 1
	v_bfe_u32 v7, v5, 16, 1
	v_bfe_u32 v18, v0, 16, 1
	v_bfe_u32 v19, v1, 16, 1
	v_add3_u32 v29, v29, v87, s42
	v_add3_u32 v28, v28, v86, s42
	v_add3_u32 v1, v1, v19, s42
	v_add3_u32 v0, v0, v18, s42
	v_add3_u32 v5, v5, v7, s42
	v_add3_u32 v4, v4, v6, s42
	v_lshrrev_b32_e32 v28, 16, v28
	v_lshrrev_b32_e32 v29, 16, v29
	v_lshrrev_b32_e32 v4, 16, v4
	v_lshrrev_b32_e32 v5, 16, v5
	v_lshrrev_b32_e32 v0, 16, v0
	v_lshrrev_b32_e32 v1, 16, v1
	s_lshl_b32 s0, s58, 16
	v_and_or_b32 v87, v53, s35, v29
	v_and_or_b32 v86, v52, s35, v28
	v_and_or_b32 v3, v3, s35, v1
	v_and_or_b32 v2, v2, s35, v0
	v_and_or_b32 v1, v17, s35, v5
	v_and_or_b32 v0, v16, s35, v4
	v_lshl_add_u64 v[22:23], v[128:129], 0, s[0:1]
	ds_write_b128 v209, v[84:87] offset:1632
	ds_write_b128 v209, v[0:3] offset:1904
	ds_write_b128 v210, v[8:11]
	ds_write_b128 v210, v[12:15] offset:272
	ds_write_b128 v210, v[36:39] offset:544
	ds_write_b128 v210, v[44:47] offset:816
	ds_write_b128 v210, v[56:59] offset:1088
	ds_write_b128 v210, v[60:63] offset:1360
	ds_write_b128 v210, v[64:67] offset:1632
	ds_write_b128 v210, v[68:71] offset:1904
	v_lshl_add_u64 v[0:1], v[22:23], 0, v[134:135]
	s_waitcnt lgkmcnt(0)
	s_barrier
	global_load_dword v4, v[0:1], off
	global_load_dword v5, v[0:1], off offset:512
	v_lshl_add_u64 v[18:19], v[130:131], 0, s[0:1]
	v_lshl_add_u64 v[2:3], v[18:19], 0, v[134:135]
	global_load_dword v6, v[2:3], off
	global_load_dword v7, v[2:3], off offset:512
	global_load_dword v8, v[0:1], off offset:1024
	global_load_dword v9, v[0:1], off offset:1536
	global_load_dword v10, v[2:3], off offset:1024
	global_load_dword v11, v[2:3], off offset:1536
	global_load_dword v12, v[0:1], off offset:2048
	global_load_dword v13, v[0:1], off offset:2560
	global_load_dword v14, v[2:3], off offset:2048
	global_load_dword v15, v[2:3], off offset:2560
	global_load_dword v16, v[0:1], off offset:3072
	global_load_dword v17, v[0:1], off offset:3584
	global_load_dword v20, v[2:3], off offset:3072
	global_load_dword v21, v[2:3], off offset:3584
	v_lshl_add_u64 v[0:1], v[22:23], 0, v[136:137]
	global_load_dword v24, v[0:1], off
	global_load_dword v25, v[0:1], off offset:512
	v_lshl_add_u64 v[0:1], v[18:19], 0, v[136:137]
	global_load_dword v26, v[0:1], off
	global_load_dword v27, v[0:1], off offset:512
	v_add_u32_e32 v116, s57, v205
	s_mov_b64 s[8:9], 0
	s_waitcnt vmcnt(19)
	v_bfe_u32 v2, v4, 16, 1
	v_add3_u32 v0, v4, v2, s42
	v_lshl_add_u64 v[2:3], v[22:23], 0, v[138:139]
	global_load_dword v28, v[2:3], off
	global_load_dword v29, v[2:3], off offset:512
	v_lshl_add_u64 v[2:3], v[18:19], 0, v[138:139]
	global_load_dword v30, v[2:3], off
	global_load_dword v31, v[2:3], off offset:512
	s_waitcnt vmcnt(22)
	v_bfe_u32 v1, v5, 16, 1
	v_lshrrev_b32_e32 v0, 16, v0
	v_add3_u32 v1, v5, v1, s42
	v_and_or_b32 v0, v1, s35, v0
	s_waitcnt vmcnt(21)
	v_bfe_u32 v1, v6, 16, 1
	v_add3_u32 v1, v6, v1, s42
	s_waitcnt vmcnt(20)
	v_bfe_u32 v4, v7, 16, 1
	v_lshrrev_b32_e32 v1, 16, v1
	v_add3_u32 v4, v7, v4, s42
	v_and_or_b32 v4, v4, s35, v1
	s_waitcnt vmcnt(19)
	v_bfe_u32 v1, v8, 16, 1
	v_add3_u32 v1, v8, v1, s42
	v_lshl_add_u64 v[2:3], v[22:23], 0, v[140:141]
	s_waitcnt vmcnt(18)
	v_bfe_u32 v5, v9, 16, 1
	global_load_dword v32, v[2:3], off
	global_load_dword v33, v[2:3], off offset:512
	v_lshrrev_b32_e32 v1, 16, v1
	v_add3_u32 v2, v9, v5, s42
	v_and_or_b32 v1, v2, s35, v1
	v_lshl_add_u64 v[2:3], v[18:19], 0, v[140:141]
	global_load_dword v34, v[2:3], off
	global_load_dword v35, v[2:3], off offset:512
	s_waitcnt vmcnt(21)
	v_bfe_u32 v5, v10, 16, 1
	s_waitcnt vmcnt(19)
	v_bfe_u32 v2, v12, 16, 1
	v_add3_u32 v5, v10, v5, s42
	v_bfe_u32 v6, v11, 16, 1
	v_add3_u32 v2, v12, v2, s42
	s_waitcnt vmcnt(18)
	v_bfe_u32 v3, v13, 16, 1
	v_lshrrev_b32_e32 v5, 16, v5
	v_add3_u32 v6, v11, v6, s42
	v_lshrrev_b32_e32 v2, 16, v2
	v_add3_u32 v3, v13, v3, s42
	v_and_or_b32 v5, v6, s35, v5
	v_lshl_add_u64 v[6:7], v[22:23], 0, v[142:143]
	v_and_or_b32 v2, v3, s35, v2
	s_waitcnt vmcnt(17)
	v_bfe_u32 v3, v14, 16, 1
	global_load_dword v36, v[6:7], off
	global_load_dword v37, v[6:7], off offset:512
	v_add3_u32 v3, v14, v3, s42
	s_waitcnt vmcnt(18)
	v_bfe_u32 v6, v15, 16, 1
	v_lshrrev_b32_e32 v3, 16, v3
	v_add3_u32 v6, v15, v6, s42
	v_and_or_b32 v6, v6, s35, v3
	v_lshl_add_u64 v[8:9], v[18:19], 0, v[142:143]
	s_waitcnt vmcnt(17)
	v_bfe_u32 v3, v16, 16, 1
	global_load_dword v38, v[8:9], off
	global_load_dword v39, v[8:9], off offset:512
	v_add3_u32 v3, v16, v3, s42
	s_waitcnt vmcnt(18)
	v_bfe_u32 v7, v17, 16, 1
	v_lshrrev_b32_e32 v3, 16, v3
	v_add3_u32 v7, v17, v7, s42
	v_lshl_add_u64 v[14:15], v[18:19], 0, v[146:147]
	v_lshl_add_u64 v[16:17], v[18:19], 0, v[148:149]
	v_and_or_b32 v3, v7, s35, v3
	s_waitcnt vmcnt(17)
	v_bfe_u32 v7, v20, 16, 1
	global_load_dword v40, v[16:17], off offset:512
	v_add3_u32 v7, v20, v7, s42
	s_waitcnt vmcnt(17)
	v_bfe_u32 v10, v21, 16, 1
	v_lshrrev_b32_e32 v7, 16, v7
	v_add3_u32 v10, v21, v10, s42
	v_and_or_b32 v7, v10, s35, v7
	s_waitcnt vmcnt(16)
	v_bfe_u32 v10, v24, 16, 1
	v_add3_u32 v10, v24, v10, s42
	s_waitcnt vmcnt(13)
	v_bfe_u32 v12, v27, 16, 1
	v_add3_u32 v12, v27, v12, s42
	s_waitcnt vmcnt(11)
	v_bfe_u32 v13, v29, 16, 1
	v_add3_u32 v13, v29, v13, s42
	global_load_dword v29, v[14:15], off
	v_lshl_add_u64 v[8:9], v[22:23], 0, v[144:145]
	global_load_dword v20, v[8:9], off
	global_load_dword v24, v[8:9], off offset:512
	v_bfe_u32 v9, v25, 16, 1
	v_lshrrev_b32_e32 v8, 16, v10
	v_add3_u32 v9, v25, v9, s42
	v_and_or_b32 v8, v9, s35, v8
	v_bfe_u32 v9, v26, 16, 1
	v_add3_u32 v9, v26, v9, s42
	v_lshl_add_u64 v[10:11], v[18:19], 0, v[144:145]
	v_lshrrev_b32_e32 v9, 16, v9
	global_load_dword v25, v[10:11], off
	global_load_dword v26, v[10:11], off offset:512
	v_and_or_b32 v12, v12, s35, v9
	v_bfe_u32 v9, v28, 16, 1
	v_add3_u32 v9, v28, v9, s42
	v_lshrrev_b32_e32 v9, 16, v9
	v_and_or_b32 v9, v13, s35, v9
	s_waitcnt vmcnt(15)
	v_bfe_u32 v13, v30, 16, 1
	v_add3_u32 v13, v30, v13, s42
	global_load_dword v30, v[14:15], off offset:512
	v_lshl_add_u64 v[10:11], v[22:23], 0, v[146:147]
	global_load_dword v27, v[10:11], off
	global_load_dword v28, v[10:11], off offset:512
	s_waitcnt vmcnt(17)
	v_bfe_u32 v11, v31, 16, 1
	v_lshrrev_b32_e32 v10, 16, v13
	v_add3_u32 v11, v31, v11, s42
	v_and_or_b32 v13, v11, s35, v10
	s_waitcnt vmcnt(16)
	v_bfe_u32 v10, v32, 16, 1
	v_add3_u32 v10, v32, v10, s42
	s_waitcnt vmcnt(15)
	v_bfe_u32 v11, v33, 16, 1
	v_lshrrev_b32_e32 v10, 16, v10
	v_add3_u32 v11, v33, v11, s42
	v_and_or_b32 v10, v11, s35, v10
	s_waitcnt vmcnt(14)
	v_bfe_u32 v11, v34, 16, 1
	v_lshl_add_u64 v[14:15], v[22:23], 0, v[148:149]
	global_load_dword v31, v[14:15], off
	global_load_dword v32, v[14:15], off offset:512
	v_add3_u32 v11, v34, v11, s42
	s_waitcnt vmcnt(15)
	v_bfe_u32 v14, v35, 16, 1
	v_lshrrev_b32_e32 v11, 16, v11
	v_add3_u32 v14, v35, v14, s42
	v_and_or_b32 v14, v14, s35, v11
	s_waitcnt vmcnt(14)
	v_bfe_u32 v11, v36, 16, 1
	v_add3_u32 v11, v36, v11, s42
	s_waitcnt vmcnt(13)
	v_bfe_u32 v15, v37, 16, 1
	v_lshrrev_b32_e32 v11, 16, v11
	v_add3_u32 v15, v37, v15, s42
	v_and_or_b32 v11, v15, s35, v11
	s_waitcnt vmcnt(12)
	v_bfe_u32 v15, v38, 16, 1
	v_add3_u32 v15, v38, v15, s42
	s_waitcnt vmcnt(11)
	v_bfe_u32 v21, v39, 16, 1
	v_lshrrev_b32_e32 v15, 16, v15
	v_add3_u32 v21, v39, v21, s42
	v_and_or_b32 v15, v21, s35, v15
	global_load_dword v33, v[16:17], off
	s_waitcnt vmcnt(9)
	v_bfe_u32 v21, v20, 16, 1
	v_add3_u32 v20, v20, v21, s42
	v_lshrrev_b32_e32 v34, 16, v20
	v_lshl_add_u64 v[20:21], v[18:19], 0, v[154:155]
	global_load_dword v47, v[20:21], off
	global_load_dword v48, v[20:21], off offset:512
	v_lshl_add_u64 v[16:17], v[22:23], 0, v[150:151]
	global_load_dword v41, v[16:17], off
	global_load_dword v36, v[16:17], off offset:512
	v_lshl_add_u64 v[20:21], v[22:23], 0, v[156:157]
	global_load_dword v49, v[20:21], off
	v_lshl_add_u64 v[16:17], v[18:19], 0, v[150:151]
	global_load_dword v42, v[16:17], off
	global_load_dword v37, v[16:17], off offset:512
	v_lshl_add_u64 v[16:17], v[22:23], 0, v[152:153]
	global_load_dword v43, v[16:17], off
	global_load_dword v38, v[16:17], off offset:512
	global_load_dword v50, v[20:21], off offset:512
	v_lshl_add_u64 v[16:17], v[18:19], 0, v[152:153]
	global_load_dword v44, v[16:17], off
	global_load_dword v39, v[16:17], off offset:512
	v_lshl_add_u64 v[16:17], v[22:23], 0, v[154:155]
	global_load_dword v45, v[16:17], off
	global_load_dword v46, v[16:17], off offset:512
	v_lshl_add_u64 v[22:23], v[22:23], 0, v[158:159]
	global_load_dword v53, v[22:23], off
	s_waitcnt vmcnt(23)
	v_bfe_u32 v16, v24, 16, 1
	s_waitcnt vmcnt(22)
	v_bfe_u32 v17, v25, 16, 1
	v_add3_u32 v16, v24, v16, s42
	v_add3_u32 v17, v25, v17, s42
	v_lshl_add_u64 v[24:25], v[18:19], 0, v[156:157]
	global_load_dword v51, v[24:25], off
	global_load_dword v52, v[24:25], off offset:512
	s_waitcnt vmcnt(23)
	v_bfe_u32 v20, v26, 16, 1
	v_lshrrev_b32_e32 v17, 16, v17
	v_add3_u32 v20, v26, v20, s42
	v_and_or_b32 v20, v20, s35, v17
	s_waitcnt vmcnt(21)
	v_bfe_u32 v17, v27, 16, 1
	v_add3_u32 v17, v27, v17, s42
	global_load_dword v27, v[22:23], off offset:512
	v_lshl_add_u64 v[18:19], v[18:19], 0, v[158:159]
	global_load_dword v54, v[18:19], off
	global_load_dword v55, v[18:19], off offset:512
	v_and_or_b32 v16, v16, s35, v34
	v_lshlrev_b64 v[34:35], 2, v[116:117]
	v_lshl_add_u64 v[18:19], s[20:21], 0, v[34:35]
	global_load_dword v56, v[18:19], off
	s_waitcnt vmcnt(24)
	v_bfe_u32 v21, v28, 16, 1
	v_lshrrev_b32_e32 v17, 16, v17
	v_add3_u32 v21, v28, v21, s42
	v_and_or_b32 v17, v21, s35, v17
	v_bfe_u32 v21, v29, 16, 1
	v_add3_u32 v18, v29, v21, s42
	v_bfe_u32 v19, v30, 16, 1
	v_lshrrev_b32_e32 v18, 16, v18
	v_add3_u32 v19, v30, v19, s42
	v_and_or_b32 v21, v19, s35, v18
	s_waitcnt vmcnt(23)
	v_bfe_u32 v18, v31, 16, 1
	v_add3_u32 v18, v31, v18, s42
	s_waitcnt vmcnt(22)
	v_bfe_u32 v19, v32, 16, 1
	v_lshrrev_b32_e32 v18, 16, v18
	v_add3_u32 v19, v32, v19, s42
	v_and_or_b32 v18, v19, s35, v18
	s_waitcnt vmcnt(21)
	v_bfe_u32 v19, v33, 16, 1
	v_add3_u32 v19, v33, v19, s42
	v_bfe_u32 v22, v40, 16, 1
	v_lshrrev_b32_e32 v19, 16, v19
	v_add3_u32 v22, v40, v22, s42
	v_and_or_b32 v22, v22, s35, v19
	s_waitcnt vmcnt(19)
	v_bfe_u32 v29, v48, 16, 1
	v_add3_u32 v29, v48, v29, s42
	s_waitcnt vmcnt(18)
	v_bfe_u32 v19, v41, 16, 1
	v_add3_u32 v19, v41, v19, s42
	s_waitcnt vmcnt(17)
	v_bfe_u32 v23, v36, 16, 1
	v_lshrrev_b32_e32 v19, 16, v19
	v_add3_u32 v23, v36, v23, s42
	v_and_or_b32 v19, v23, s35, v19
	s_waitcnt vmcnt(15)
	v_bfe_u32 v23, v42, 16, 1
	v_add3_u32 v23, v42, v23, s42
	s_waitcnt vmcnt(14)
	v_bfe_u32 v24, v37, 16, 1
	v_lshrrev_b32_e32 v23, 16, v23
	v_add3_u32 v24, v37, v24, s42
	v_and_or_b32 v23, v24, s35, v23
	s_waitcnt vmcnt(13)
	v_bfe_u32 v24, v43, 16, 1
	v_add3_u32 v24, v43, v24, s42
	s_waitcnt vmcnt(12)
	v_bfe_u32 v25, v38, 16, 1
	v_lshrrev_b32_e32 v24, 16, v24
	v_add3_u32 v25, v38, v25, s42
	v_and_or_b32 v24, v25, s35, v24
	s_waitcnt vmcnt(10)
	v_bfe_u32 v25, v44, 16, 1
	v_add3_u32 v25, v44, v25, s42
	s_waitcnt vmcnt(9)
	v_bfe_u32 v26, v39, 16, 1
	v_lshrrev_b32_e32 v25, 16, v25
	v_add3_u32 v26, v39, v26, s42
	v_and_or_b32 v28, v26, s35, v25
	s_waitcnt vmcnt(8)
	v_bfe_u32 v25, v45, 16, 1
	v_add3_u32 v25, v45, v25, s42
	s_waitcnt vmcnt(7)
	v_bfe_u32 v26, v46, 16, 1
	v_lshrrev_b32_e32 v25, 16, v25
	v_add3_u32 v26, v46, v26, s42
	v_and_or_b32 v25, v26, s35, v25
	v_bfe_u32 v26, v47, 16, 1
	v_add3_u32 v26, v47, v26, s42
	v_lshrrev_b32_e32 v26, 16, v26
	v_and_or_b32 v29, v29, s35, v26
	v_bfe_u32 v26, v49, 16, 1
	v_add3_u32 v26, v49, v26, s42
	v_bfe_u32 v30, v50, 16, 1
	v_lshrrev_b32_e32 v26, 16, v26
	v_add3_u32 v30, v50, v30, s42
	v_and_or_b32 v26, v30, s35, v26
	s_waitcnt vmcnt(5)
	v_bfe_u32 v30, v51, 16, 1
	v_add3_u32 v30, v51, v30, s42
	s_waitcnt vmcnt(4)
	v_bfe_u32 v31, v52, 16, 1
	v_lshrrev_b32_e32 v30, 16, v30
	v_add3_u32 v31, v52, v31, s42
	v_and_or_b32 v30, v31, s35, v30
	v_bfe_u32 v31, v53, 16, 1
	v_add3_u32 v31, v53, v31, s42
	s_waitcnt vmcnt(3)
	v_bfe_u32 v32, v27, 16, 1
	v_lshrrev_b32_e32 v31, 16, v31
	v_add3_u32 v27, v27, v32, s42
	v_and_or_b32 v27, v27, s35, v31
	s_waitcnt vmcnt(2)
	v_bfe_u32 v31, v54, 16, 1
	v_add3_u32 v31, v54, v31, s42
	s_waitcnt vmcnt(1)
	v_bfe_u32 v32, v55, 16, 1
	v_lshrrev_b32_e32 v31, 16, v31
	v_add3_u32 v32, v55, v32, s42
	v_and_or_b32 v31, v32, s35, v31
	v_lshl_add_u64 v[32:33], s[18:19], 0, v[34:35]
	global_load_dword v32, v[32:33], off
	s_waitcnt vmcnt(1)
	v_mul_f32_e32 v33, 0xbfb8aa3b, v56
	v_exp_f32_e32 v33, v33
	v_lshl_add_u64 v[34:35], s[10:11], 0, v[34:35]
	global_load_dword v36, v[34:35], off
	v_mov_b32_e32 v42, 1.0
	v_add_f32_e32 v37, 1.0, v33
	v_add_f32_e32 v34, -1.0, v37
	v_sub_f32_e32 v35, v34, v37
	v_add_f32_e32 v35, 1.0, v35
	v_sub_f32_e32 v34, v33, v34
	v_add_f32_e32 v38, v34, v35
	v_frexp_mant_f32_e32 v39, v37
	v_cvt_f64_f32_e32 v[34:35], v37
	v_frexp_exp_i32_f64_e32 v34, v[34:35]
	v_cmp_gt_f32_e32 vcc, s43, v39
	v_mov_b32_e32 v52, v207
	s_nop 0
	v_subbrev_co_u32_e32 v43, vcc, 0, v34, vcc
	v_sub_u32_e32 v34, 0, v43
	v_ldexp_f32 v35, v37, v34
	v_add_f32_e32 v37, -1.0, v35
	v_add_f32_e32 v39, 1.0, v35
	v_ldexp_f32 v34, v38, v34
	v_add_f32_e32 v38, 1.0, v37
	v_add_f32_e32 v40, -1.0, v39
	v_sub_f32_e32 v38, v35, v38
	v_sub_f32_e32 v35, v35, v40
	v_add_f32_e32 v38, v34, v38
	v_add_f32_e32 v34, v34, v35
	v_add_f32_e32 v46, v39, v34
	v_rcp_f32_e32 v48, v46
	v_sub_f32_e32 v35, v46, v39
	v_sub_f32_e32 v47, v34, v35
	v_add_f32_e32 v35, v37, v38
	v_sub_f32_e32 v34, v35, v37
	v_mul_f32_e32 v49, v35, v48
	v_sub_f32_e32 v37, v38, v34
	v_mul_f32_e32 v38, v46, v49
	v_fma_f32 v40, v49, v46, -v38
	v_fmac_f32_e32 v40, v49, v47
	v_add_f32_e32 v34, v38, v40
	v_sub_f32_e32 v39, v35, v34
	v_add_f32_e64 v44, v34, -v38
	v_add_f32_e64 v45, v35, -v39
	v_mov_b32_e32 v41, v34
	v_add_f32_e64 v34, v44, -v40
	v_add_f32_e64 v35, v45, -v41
	v_cmp_neq_f32_e32 vcc, s45, v33
	v_add_f32_e32 v35, v37, v35
	v_add_f32_e32 v34, v34, v35
	v_add_f32_e32 v35, v39, v34
	v_mul_f32_e32 v37, v48, v35
	v_mul_f32_e32 v38, v46, v37
	v_fma_f32 v40, v37, v46, -v38
	v_fmac_f32_e32 v40, v37, v47
	v_sub_f32_e32 v39, v39, v35
	v_add_f32_e32 v46, v34, v39
	v_add_f32_e32 v34, v38, v40
	v_sub_f32_e32 v39, v35, v34
	v_add_f32_e64 v44, v34, -v38
	v_add_f32_e64 v45, v35, -v39
	v_mov_b32_e32 v41, v34
	v_add_f32_e64 v34, v44, -v40
	v_add_f32_e64 v35, v45, -v41
	s_nop 0
	v_add_f32_e32 v35, v46, v35
	v_add_f32_e32 v34, v34, v35
	v_add_f32_e32 v35, v49, v37
	v_add_f32_e32 v34, v39, v34
	v_sub_f32_e32 v38, v35, v49
	v_mul_f32_e32 v34, v48, v34
	v_sub_f32_e32 v37, v37, v38
	v_add_f32_e32 v37, v37, v34
	v_add_f32_e32 v38, v35, v37
	v_mul_f32_e32 v40, v38, v38
	v_fmamk_f32 v34, v40, 0x3e9b6dac, v211
	v_fmaak_f32 v161, v40, v34, 0x3f2aaada
	v_cvt_f32_i32_e32 v34, v43
	v_sub_f32_e32 v35, v38, v35
	v_sub_f32_e32 v35, v37, v35
	v_ldexp_f32 v37, v35, 1
	v_mul_f32_e32 v35, v38, v40
	v_mul_f32_e32 v40, v34, v160
	v_mul_f32_e32 v41, v35, v161
	v_ldexp_f32 v39, v38, 1
	v_fma_f32 v38, v34, s44, -v40
	v_fmac_f32_e32 v38, 0xb102e308, v34
	v_add_f32_e32 v34, v40, v38
	v_add_f32_e32 v35, v41, v39
	v_mov_b32_e32 v44, v40
	v_sub_f32_e32 v39, v35, v39
	v_sub_f32_e32 v39, v41, v39
	v_add_f32_e32 v45, v37, v39
	v_add_f32_e64 v40, v34, -v40
	v_add_f32_e64 v41, v35, -v41
	v_add_f32_e32 v46, v34, v44
	v_add_f32_e32 v47, v35, v45
	v_mov_b32_e32 v39, v34
	v_mov_b32_e32 v41, v47
	v_add_f32_e64 v48, v38, -v40
	v_add_f32_e64 v49, v39, -v41
	v_add_f32_e32 v38, v38, v40
	v_add_f32_e32 v39, v39, v41
	v_mov_b32_e32 v44, v45
	v_add_f32_e64 v40, v39, -v34
	v_add_f32_e64 v41, v38, -v35
	v_add_f32_e64 v50, v46, -v40
	v_add_f32_e64 v51, v47, -v40
	v_mov_b32_e32 v46, v47
	v_mov_b32_e32 v47, v39
	v_pk_mov_b32 v[40:41], v[34:35], v[40:41] op_sel:[1,0]
	v_mov_b32_e32 v45, v34
	v_add_f32_e64 v40, v46, -v40
	v_add_f32_e64 v41, v47, -v41
	v_mov_b32_e32 v50, v48
	v_add_f32_e64 v34, v44, -v40
	v_add_f32_e64 v35, v45, -v41
	v_mov_b32_e32 v49, v39
	v_add_f32_e32 v40, v50, v34
	v_add_f32_e32 v41, v51, v35
	v_mov_b32_e32 v50, v203
	v_add_f32_e32 v44, v40, v41
	v_add_f32_e32 v45, v41, v40
	v_mov_b32_e32 v51, v208
	v_pk_add_f32 v[38:39], v[38:39], v[44:45] op_sel:[1,0] op_sel_hi:[0,1]
	v_mov_b32_e32 v41, v38
	v_add_f32_e64 v46, v40, -v48
	v_add_f32_e64 v47, v41, -v49
	v_mov_b32_e32 v35, v44
	v_sub_f32_e32 v37, v40, v46
	v_add_f32_e64 v34, v34, -v46
	v_add_f32_e64 v35, v35, -v47
	v_sub_f32_e32 v37, v48, v37
	v_add_f32_e32 v34, v34, v37
	v_add_f32_e32 v34, v34, v35
	v_add_f32_e32 v34, v38, v34
	v_cndmask_b32_e32 v34, v212, v34, vcc
	v_cmp_ngt_f32_e32 vcc, -1.0, v33
	v_add_u32_e32 v44, s56, v206
	v_ashrrev_i32_e32 v45, 31, v44
	v_cndmask_b32_e32 v34, v213, v34, vcc
	v_cmp_neq_f32_e32 vcc, -1.0, v33
	v_lshlrev_b64 v[44:45], 12, v[44:45]
	v_lshlrev_b32_e32 v46, 1, v116
	v_cndmask_b32_e32 v34, v214, v34, vcc
	v_cmp_lt_f32_e64 vcc, |v33|, s46
	v_mov_b32_e32 v47, v117
	v_lshl_add_u64 v[44:45], v[44:45], 0, v[46:47]
	v_cndmask_b32_e32 v33, v34, v33, vcc
	v_mul_f32_e32 v33, 0xc1000000, v33
	v_mul_f32_e32 v40, 0x3fb8aa3b, v33
	s_waitcnt vmcnt(1)
	v_mov_b32_e32 v33, v32
	v_mov_b32_e32 v34, v32
	v_mov_b32_e32 v35, v32
	s_waitcnt vmcnt(0)
	v_mov_b32_e32 v37, v36
	v_mov_b32_e32 v38, v36
	v_mov_b32_e32 v39, v36
	v_mov_b32_e32 v41, v40
	v_lshl_add_u64 v[44:45], s[94:95], 0, v[44:45]
.LBB0_1476:
	v_add_u32_e32 v53, 0, v50
	v_add_u32_e32 v43, 0, v52
	v_add_u32_e32 v70, 0, v51
	ds_read_b128 v[54:57], v53
	ds_read_b128 v[58:61], v53 offset:64
	ds_read_b128 v[62:65], v53 offset:128
	ds_read_b128 v[66:69], v53 offset:192
	ds_read_u16 v88, v43
	v_add_u32_e32 v89, 0x12100, v70
	v_add_u32_e32 v90, 0x12210, v70
	v_add_u32_e32 v94, 0x12320, v70
	v_add_u32_e32 v95, 0x12430, v70
	v_add_u32_e32 v96, 0x12540, v70
	v_add_u32_e32 v97, 0x12650, v70
	v_add_u32_e32 v98, 0x12760, v70
	v_add_u32_e32 v99, 0x12870, v70
	s_waitcnt lgkmcnt(4)
	v_mfma_f32_16x16x32_bf16 v[70:73], v[54:57], v[0:3], v[32:35]
	ds_read_u16 v91, v43 offset:272
	ds_read_u16 v92, v89
	ds_read_u16 v93, v90
	v_mov_b64_e32 v[46:47], s[36:37]
	s_waitcnt lgkmcnt(3)
	v_lshlrev_b32_e32 v88, 16, v88
	v_mfma_f32_16x16x32_bf16 v[54:57], v[54:57], v[4:7], v[36:39]
	s_waitcnt lgkmcnt(2)
	v_lshlrev_b32_e32 v89, 16, v91
	s_waitcnt lgkmcnt(1)
	v_lshlrev_b32_e32 v90, 16, v92
	s_waitcnt lgkmcnt(0)
	v_lshlrev_b32_e32 v91, 16, v93
	v_mfma_f32_16x16x32_bf16 v[70:73], v[58:61], v[8:11], v[70:73]
	v_mul_f32_e64 v92, v90, v90
	v_mul_f32_e64 v93, v91, v91
	v_lshl_add_u64 v[48:49], v[44:45], 0, s[8:9]
	v_add_co_u32_e32 v74, vcc, s47, v48
	v_mfma_f32_16x16x32_bf16 v[54:57], v[58:61], v[12:15], v[54:57]
	s_nop 0
	v_addc_co_u32_e32 v75, vcc, 0, v49, vcc
	v_add_co_u32_e32 v76, vcc, s48, v48
	v_mfma_f32_16x16x32_bf16 v[58:61], v[62:65], v[16:19], v[70:73]
	s_nop 0
	v_addc_co_u32_e32 v77, vcc, 0, v49, vcc
	v_add_co_u32_e32 v78, vcc, s49, v48
	v_mfma_f32_16x16x32_bf16 v[58:61], v[66:69], v[24:27], v[58:61]
	v_fma_f32 v70, -v92, s34, v46
	v_fma_f32 v71, -v93, s34, v46
	v_addc_co_u32_e32 v79, vcc, 0, v49, vcc
	v_mfma_f32_16x16x32_bf16 v[54:57], v[62:65], v[20:23], v[54:57]
	v_mul_f32_e64 v70, v70, v90
	v_mul_f32_e64 v71, v71, v91
	s_nop 1
	v_mul_f32_e32 v58, s30, v58
	v_mul_f32_e32 v59, s30, v59
	v_mul_f32_e32 v60, s30, v60
	v_mul_f32_e32 v61, s30, v61
	v_exp_f32_e32 v58, v58
	v_exp_f32_e32 v59, v59
	v_exp_f32_e32 v60, v60
	v_exp_f32_e32 v61, v61
	v_mfma_f32_16x16x32_bf16 v[54:57], v[66:69], v[28:31], v[54:57]
	v_add_f32_e64 v58, v58, 1.0
	v_add_f32_e64 v59, v59, 1.0
	v_exp_f32_e32 v70, v70
	v_add_f32_e32 v60, 1.0, v60
	v_add_f32_e32 v61, 1.0, v61
	v_rcp_f32_e32 v58, v58
	v_rcp_f32_e32 v59, v59
	v_rcp_f32_e32 v60, v60
	v_rcp_f32_e32 v61, v61
	v_mul_f32_e32 v54, s30, v54
	v_mul_f32_e32 v55, s30, v55
	v_mul_f32_e32 v58, v40, v58
	v_mul_f32_e32 v59, v41, v59
	v_exp_f32_e32 v54, v54
	v_exp_f32_e32 v55, v55
	v_mul_f32_e32 v60, v40, v60
	v_mul_f32_e32 v61, v41, v61
	v_exp_f32_e32 v58, v58
	v_exp_f32_e32 v59, v59
	v_exp_f32_e32 v60, v60
	v_exp_f32_e32 v61, v61
	v_exp_f32_e32 v71, v71
	v_add_f32_e32 v54, 1.0, v54
	v_add_f32_e32 v55, 1.0, v55
	v_fma_f32 v64, -v58, v58, 1.0
	v_fma_f32 v65, -v59, v59, 1.0
	v_rcp_f32_e32 v54, v54
	v_rcp_f32_e32 v55, v55
	v_fma_f32 v66, -v60, v60, 1.0
	v_fma_f32 v67, -v61, v61, 1.0
	v_max_f32_e32 v68, 0, v64
	v_max_f32_e32 v65, 0, v65
	v_add_f32_e32 v62, 1.0, v70
	v_add_f32_e32 v63, 1.0, v71
	v_max_f32_e32 v69, 0, v66
	v_max_f32_e32 v71, 0, v67
	v_sqrt_f32_e32 v66, v68
	v_sqrt_f32_e32 v67, v65
	v_rcp_f32_e32 v62, v62
	v_rcp_f32_e32 v63, v63
	v_mul_f32_e32 v56, s30, v56
	v_mul_f32_e32 v57, s30, v57
	v_mul_f32_e32 v54, v54, v88
	v_mul_f32_e32 v55, v55, v89
	v_exp_f32_e32 v56, v56
	v_exp_f32_e32 v57, v57
	v_mul_f32_e32 v42, v42, v58
	v_mul_f32_e32 v54, v54, v66
	v_mul_f32_e32 v55, v55, v67
	v_mul_f32_e32 v62, v62, v90
	v_mul_f32_e32 v63, v63, v91
	v_mul_f32_e32 v64, v59, v42
	v_fma_f32 v54, v163, v58, v54
	v_mul_f32_e32 v70, v42, v62
	v_mul_f32_e32 v42, v64, v63
	v_mul_f32_e32 v58, v62, v54
	v_fmac_f32_e32 v55, v59, v54
	v_cvt_pk_bf16_f32 v54, v58, v70
	v_mul_f32_e32 v58, v63, v55
	global_store_short v[74:75], v54, off offset:-4096
	global_store_short_d16_hi v[76:77], v54, off offset:-4096
	v_cvt_pk_bf16_f32 v42, v58, v42
	ds_read_u16 v54, v43 offset:544
	ds_read_u16 v59, v43 offset:816
	ds_read_u16 v62, v94
	ds_read_u16 v63, v95
	v_add_f32_e32 v56, 1.0, v56
	v_add_f32_e32 v57, 1.0, v57
	v_sqrt_f32_e32 v68, v69
	v_rcp_f32_e32 v56, v56
	v_rcp_f32_e32 v57, v57
	v_sqrt_f32_e32 v69, v71
	s_waitcnt lgkmcnt(3)
	v_lshlrev_b32_e32 v58, 16, v54
	s_waitcnt lgkmcnt(2)
	v_lshlrev_b32_e32 v59, 16, v59
	s_waitcnt lgkmcnt(1)
	v_lshlrev_b32_e32 v62, 16, v62
	s_waitcnt lgkmcnt(0)
	v_lshlrev_b32_e32 v63, 16, v63
	v_mul_f32_e32 v56, v56, v58
	v_mul_f32_e32 v57, v57, v59
	v_mul_f32_e32 v58, v62, v62
	v_mul_f32_e32 v59, v63, v63
	v_mul_f32_e32 v66, v56, v68
	v_mul_f32_e32 v67, v57, v69
	v_fma_f32 v58, -v58, s34, v46
	v_fma_f32 v59, -v59, s34, v46
	v_fma_f32 v65, v60, v55, v66
	v_mul_f32_e32 v58, v58, v62
	v_mul_f32_e32 v59, v59, v63
	v_mov_b32_e32 v66, v61
	v_exp_f32_e32 v54, v58
	v_exp_f32_e32 v55, v59
	v_mul_f32_e32 v58, v60, v64
	v_mul_f32_e32 v59, v61, v65
	global_store_short v[74:75], v42, off
	global_store_short_d16_hi v[76:77], v42, off
	v_mul_f32_e32 v74, v66, v58
	v_mul_f32_e32 v75, v67, v59
	v_add_f32_e32 v54, 1.0, v54
	v_add_f32_e32 v55, 1.0, v55
	v_fma_f32 v76, v56, v68, v58
	v_fma_f32 v77, v57, v69, v59
	v_rcp_f32_e32 v54, v54
	v_rcp_f32_e32 v55, v55
	v_add_co_u32_e32 v80, vcc, s50, v48
	s_add_u32 s8, s8, 0x8000
	v_mul_f32_e32 v54, v54, v62
	v_mul_f32_e32 v55, v55, v63
	v_addc_co_u32_e32 v81, vcc, 0, v49, vcc
	v_mul_f32_e32 v42, v65, v54
	v_mul_f32_e32 v54, v58, v54
	v_mul_f32_e32 v56, v77, v55
	v_mul_f32_e32 v55, v74, v55
	v_cvt_pk_bf16_f32 v42, v42, v54
	global_store_short v[78:79], v42, off offset:-4096
	global_store_short_d16_hi v[80:81], v42, off offset:-4096
	v_cvt_pk_bf16_f32 v42, v56, v55
	ds_read_b128 v[54:57], v53 offset:1088
	ds_read_b128 v[58:61], v53 offset:1152
	ds_read_b128 v[62:65], v53 offset:1216
	s_waitcnt lgkmcnt(2)
	v_mfma_f32_16x16x32_bf16 v[66:69], v[54:57], v[0:3], v[32:35]
	ds_read_b128 v[70:73], v53 offset:1280
	ds_read_u16 v53, v43 offset:1088
	ds_read_u16 v75, v43 offset:1360
	ds_read_u16 v76, v96
	ds_read_u16 v88, v97
	global_store_short_d16_hi v[80:81], v42, off
	v_mfma_f32_16x16x32_bf16 v[54:57], v[54:57], v[4:7], v[36:39]
	global_store_short v[78:79], v42, off
	s_waitcnt lgkmcnt(1)
	v_lshlrev_b32_e32 v80, 16, v76
	s_waitcnt lgkmcnt(0)
	v_lshlrev_b32_e32 v81, 16, v88
	v_mfma_f32_16x16x32_bf16 v[66:69], v[58:61], v[8:11], v[66:69]
	v_mul_f32_e64 v88, v80, v80
	v_mul_f32_e64 v89, v81, v81
	v_lshlrev_b32_e32 v78, 16, v53
	v_lshlrev_b32_e32 v79, 16, v75
	v_mfma_f32_16x16x32_bf16 v[54:57], v[58:61], v[12:15], v[54:57]
	v_add_co_u32_e32 v82, vcc, s51, v48
	s_addc_u32 s9, s9, 0
	v_mfma_f32_16x16x32_bf16 v[58:61], v[62:65], v[16:19], v[66:69]
	v_addc_co_u32_e32 v83, vcc, 0, v49, vcc
	v_add_co_u32_e32 v84, vcc, s52, v48
	v_mfma_f32_16x16x32_bf16 v[58:61], v[70:73], v[24:27], v[58:61]
	v_fma_f32 v66, -v88, s34, v46
	v_fma_f32 v67, -v89, s34, v46
	v_addc_co_u32_e32 v85, vcc, 0, v49, vcc
	v_mfma_f32_16x16x32_bf16 v[54:57], v[62:65], v[20:23], v[54:57]
	v_mul_f32_e64 v66, v66, v80
	v_mul_f32_e64 v67, v67, v81
	s_nop 1
	v_mul_f32_e32 v58, s30, v58
	v_mul_f32_e32 v59, s30, v59
	v_mul_f32_e32 v60, s30, v60
	v_mul_f32_e32 v61, s30, v61
	v_exp_f32_e32 v58, v58
	v_exp_f32_e32 v59, v59
	v_exp_f32_e32 v60, v60
	v_exp_f32_e32 v61, v61
	v_mfma_f32_16x16x32_bf16 v[54:57], v[70:73], v[28:31], v[54:57]
	v_add_f32_e64 v58, v58, 1.0
	v_add_f32_e64 v59, v59, 1.0
	v_exp_f32_e32 v66, v66
	v_add_f32_e32 v60, 1.0, v60
	v_add_f32_e32 v61, 1.0, v61
	v_rcp_f32_e32 v58, v58
	v_rcp_f32_e32 v59, v59
	v_rcp_f32_e32 v60, v60
	v_rcp_f32_e32 v61, v61
	v_mul_f32_e32 v54, s30, v54
	v_mul_f32_e32 v55, s30, v55
	v_mul_f32_e32 v58, v40, v58
	v_mul_f32_e32 v59, v41, v59
	v_exp_f32_e32 v54, v54
	v_exp_f32_e32 v55, v55
	v_mul_f32_e32 v60, v40, v60
	v_mul_f32_e32 v61, v41, v61
	v_exp_f32_e32 v58, v58
	v_exp_f32_e32 v59, v59
	v_exp_f32_e32 v67, v67
	v_exp_f32_e32 v60, v60
	v_exp_f32_e32 v61, v61
	v_add_f32_e32 v54, 1.0, v54
	v_add_f32_e32 v55, 1.0, v55
	v_fma_f32 v64, -v58, v58, 1.0
	v_fma_f32 v65, -v59, v59, 1.0
	v_add_f32_e32 v62, 1.0, v66
	v_add_f32_e32 v63, 1.0, v67
	v_rcp_f32_e32 v54, v54
	v_rcp_f32_e32 v55, v55
	v_fma_f32 v66, -v60, v60, 1.0
	v_fma_f32 v67, -v61, v61, 1.0
	v_max_f32_e32 v53, 0, v64
	v_max_f32_e32 v65, 0, v65
	v_max_f32_e32 v68, 0, v66
	v_max_f32_e32 v69, 0, v67
	v_sqrt_f32_e32 v66, v53
	v_sqrt_f32_e32 v67, v65
	v_rcp_f32_e32 v62, v62
	v_rcp_f32_e32 v63, v63
	v_mul_f32_e32 v54, v54, v78
	v_mul_f32_e32 v55, v55, v79
	v_mul_f32_e32 v56, s30, v56
	v_mul_f32_e32 v57, s30, v57
	v_mul_f32_e32 v54, v54, v66
	v_mul_f32_e32 v55, v55, v67
	v_mul_f32_e32 v62, v62, v80
	v_mul_f32_e32 v63, v63, v81
	v_exp_f32_e32 v56, v56
	v_exp_f32_e32 v57, v57
	v_mul_f32_e32 v42, v74, v58
	v_fma_f32 v53, v77, v58, v54
	v_mul_f32_e32 v64, v59, v42
	v_mul_f32_e32 v54, v62, v53
	v_fmac_f32_e32 v55, v59, v53
	v_mul_f32_e32 v70, v42, v62
	v_mul_f32_e32 v42, v64, v63
	v_cvt_pk_bf16_f32 v53, v54, v70
	v_mul_f32_e32 v54, v63, v55
	global_store_short v[82:83], v53, off offset:-4096
	global_store_short_d16_hi v[84:85], v53, off offset:-4096
	v_cvt_pk_bf16_f32 v42, v54, v42
	ds_read_u16 v53, v43 offset:1632
	ds_read_u16 v43, v43 offset:1904
	ds_read_u16 v54, v98
	ds_read_u16 v59, v99
	v_add_f32_e32 v56, 1.0, v56
	v_add_f32_e32 v57, 1.0, v57
	global_store_short v[82:83], v42, off
	global_store_short_d16_hi v[84:85], v42, off
	v_rcp_f32_e32 v56, v56
	v_rcp_f32_e32 v57, v57
	s_waitcnt lgkmcnt(3)
	v_lshlrev_b32_e32 v42, 16, v53
	s_waitcnt lgkmcnt(2)
	v_lshlrev_b32_e32 v43, 16, v43
	s_waitcnt lgkmcnt(1)
	v_lshlrev_b32_e32 v58, 16, v54
	s_waitcnt lgkmcnt(0)
	v_lshlrev_b32_e32 v59, 16, v59
	v_mul_f32_e32 v42, v56, v42
	v_mul_f32_e32 v43, v57, v43
	v_mul_f32_e32 v56, v58, v58
	v_mul_f32_e32 v57, v59, v59
	v_sqrt_f32_e32 v68, v68
	v_fma_f32 v47, -v57, s34, v46
	v_fma_f32 v46, -v56, s34, v46
	v_sqrt_f32_e32 v69, v69
	v_mul_f32_e32 v46, v46, v58
	v_mul_f32_e32 v47, v47, v59
	v_add_co_u32_e32 v86, vcc, s53, v48
	v_exp_f32_e32 v46, v46
	v_exp_f32_e32 v47, v47
	v_mul_f32_e32 v42, v42, v68
	v_mul_f32_e32 v43, v43, v69
	v_addc_co_u32_e32 v87, vcc, 0, v49, vcc
	v_add_f32_e32 v46, 1.0, v46
	v_add_f32_e32 v47, 1.0, v47
	v_fma_f32 v65, v60, v55, v42
	v_rcp_f32_e32 v46, v46
	v_rcp_f32_e32 v47, v47
	v_mov_b32_e32 v42, v61
	v_mul_f32_e32 v54, v60, v64
	v_mul_f32_e32 v55, v61, v65
	v_fma_f32 v162, v60, v64, v42
	v_fma_f32 v163, v61, v65, v43
	v_mul_f32_e32 v42, v42, v54
	v_mul_f32_e32 v43, v43, v55
	v_mul_f32_e32 v46, v46, v58
	v_mul_f32_e32 v47, v47, v59
	v_add_co_u32_e32 v48, vcc, s54, v48
	v_mul_f32_e32 v43, v65, v46
	v_mul_f32_e32 v46, v54, v46
	v_cvt_pk_bf16_f32 v43, v43, v46
	v_add_u32_e32 v52, 0x880, v52
	v_add_u32_e32 v51, 0x880, v51
	v_add_u32_e32 v50, 0x880, v50
	v_addc_co_u32_e32 v49, vcc, 0, v49, vcc
	s_cmp_lg_u32 s8, 0x40000
	v_mul_f32_e32 v53, v163, v47
	v_mul_f32_e32 v47, v42, v47
	global_store_short v[86:87], v43, off offset:-4096
	global_store_short_d16_hi v[48:49], v43, off offset:-4096
	v_cvt_pk_bf16_f32 v43, v53, v47
	global_store_short v[86:87], v43, off
	global_store_short_d16_hi v[48:49], v43, off
	s_cbranch_scc1 .LBB0_1476
	s_lshl_b32 s0, s41, 6
	s_lshl_b32 s8, s40, 2
	s_or_b32 s0, s8, s0
	v_add_u32_e32 v0, s0, v204
	v_ashrrev_i32_e32 v1, 31, v0
	v_lshlrev_b64 v[0:1], 14, v[0:1]
	v_lshl_add_u64 v[0:1], s[16:17], 0, v[0:1]
	v_mov_b32_e32 v43, v163
	v_lshl_add_u64 v[0:1], v[116:117], 3, v[0:1]
	global_store_dwordx2 v[0:1], v[42:43], off

.LBB0_1575:
	v_lshrrev_b32_e32 v2, 1, v0
	v_ashrrev_i32_e32 v41, 7, v0
	v_and_b32_e32 v8, 24, v2
	v_bfe_u32 v40, v0, 6, 1
	v_lshl_or_b32 v8, v41, 5, v8
	v_lshl_or_b32 v2, v40, 6, v1
	v_ashrrev_i32_e32 v9, 31, v8
	v_or_b32_e32 v10, 1, v8
	v_or_b32_e32 v12, 2, v8
	v_or_b32_e32 v14, 3, v8
	v_or_b32_e32 v18, 4, v8
	v_or_b32_e32 v20, 5, v8
	v_or_b32_e32 v22, 6, v8
	v_or_b32_e32 v24, 7, v8
	s_waitcnt lgkmcnt(0)
	v_lshl_add_u64 v[16:17], s[6:7], 0, v[2:3]
	v_lshl_add_u64 v[26:27], v[8:9], 2, s[4:5]
	v_lshlrev_b64 v[8:9], 7, v[8:9]
	v_ashrrev_i32_e32 v11, 31, v10
	v_ashrrev_i32_e32 v13, 31, v12
	v_ashrrev_i32_e32 v15, 31, v14
	v_ashrrev_i32_e32 v19, 31, v18
	v_ashrrev_i32_e32 v21, 31, v20
	v_ashrrev_i32_e32 v23, 31, v22
	v_ashrrev_i32_e32 v25, 31, v24
	v_lshl_add_u64 v[28:29], v[16:17], 0, v[8:9]
	v_lshlrev_b64 v[30:31], 7, v[10:11]
	v_lshlrev_b64 v[32:33], 7, v[12:13]
	v_lshlrev_b64 v[34:35], 7, v[14:15]
	global_load_dwordx4 v[8:11], v[26:27], off offset:16
	global_load_dwordx4 v[12:15], v[26:27], off
	v_lshlrev_b64 v[18:19], 7, v[18:19]
	v_lshlrev_b64 v[20:21], 7, v[20:21]
	v_lshlrev_b64 v[22:23], 7, v[22:23]
	v_lshlrev_b64 v[24:25], 7, v[24:25]
	v_lshl_add_u64 v[26:27], v[16:17], 0, v[30:31]
	v_lshl_add_u64 v[30:31], v[16:17], 0, v[32:33]
	v_lshl_add_u64 v[32:33], v[16:17], 0, v[34:35]
	v_lshl_add_u64 v[18:19], v[16:17], 0, v[18:19]
	v_lshl_add_u64 v[20:21], v[16:17], 0, v[20:21]
	v_lshl_add_u64 v[22:23], v[16:17], 0, v[22:23]
	v_lshl_add_u64 v[16:17], v[16:17], 0, v[24:25]
	global_load_dword v24, v[28:29], off
	global_load_dword v34, v[26:27], off
	global_load_dword v25, v[30:31], off
	global_load_dword v35, v[32:33], off
	global_load_dword v36, v[18:19], off
	global_load_dword v38, v[20:21], off
	global_load_dword v37, v[22:23], off
	global_load_dword v39, v[16:17], off
	v_lshlrev_b32_e32 v2, 2, v41
	v_lshl_or_b32 v16, v40, 1, v2
	v_ashrrev_i32_e32 v17, 31, v16
	v_or_b32_e32 v18, 1, v16
	v_lshlrev_b64 v[16:17], 10, v[16:17]
	v_lshl_add_u64 v[16:17], v[4:5], 0, v[16:17]
	v_add_u32_e32 v0, s8, v0
	v_ashrrev_i32_e32 v19, 31, v18
	v_cmp_lt_i32_e32 vcc, s11, v0
	v_lshlrev_b64 v[18:19], 10, v[18:19]
	s_or_b64 s[2:3], vcc, s[2:3]
	v_lshl_add_u64 v[18:19], v[4:5], 0, v[18:19]
	s_waitcnt vmcnt(9)
	v_mov_b32_e32 v22, v8
	s_waitcnt vmcnt(8)
	v_mov_b32_e32 v20, v12
	v_mov_b32_e32 v21, v14
	v_mov_b32_e32 v14, v13
	v_mov_b32_e32 v23, v10
	v_mov_b32_e32 v10, v9
	s_waitcnt vmcnt(5)
	v_mul_f32_e32 v8, v20, v24
	v_mul_f32_e32 v9, v21, v25
	s_waitcnt vmcnt(4)
	v_mul_f32_e32 v12, v14, v34
	v_mul_f32_e32 v13, v15, v35
	v_and_b32_sdwa v2, v9, v7 dst_sel:DWORD dst_unused:UNUSED_PAD src0_sel:WORD_1 src1_sel:DWORD
	v_and_b32_sdwa v30, v8, v7 dst_sel:DWORD dst_unused:UNUSED_PAD src0_sel:WORD_1 src1_sel:DWORD
	s_waitcnt vmcnt(1)
	v_mul_f32_e32 v26, v22, v36
	v_mul_f32_e32 v27, v23, v37
	s_waitcnt vmcnt(0)
	v_mul_f32_e32 v28, v10, v38
	v_mul_f32_e32 v29, v11, v39
	v_and_b32_sdwa v31, v13, v7 dst_sel:DWORD dst_unused:UNUSED_PAD src0_sel:WORD_1 src1_sel:DWORD
	v_and_b32_sdwa v32, v12, v7 dst_sel:DWORD dst_unused:UNUSED_PAD src0_sel:WORD_1 src1_sel:DWORD
	v_and_b32_sdwa v33, v27, v7 dst_sel:DWORD dst_unused:UNUSED_PAD src0_sel:WORD_1 src1_sel:DWORD
	v_and_b32_sdwa v40, v26, v7 dst_sel:DWORD dst_unused:UNUSED_PAD src0_sel:WORD_1 src1_sel:DWORD
	v_and_b32_sdwa v41, v29, v7 dst_sel:DWORD dst_unused:UNUSED_PAD src0_sel:WORD_1 src1_sel:DWORD
	v_and_b32_sdwa v42, v28, v7 dst_sel:DWORD dst_unused:UNUSED_PAD src0_sel:WORD_1 src1_sel:DWORD
	v_add3_u32 v2, v9, v2, s9
	v_add3_u32 v43, v8, v30, s9
	v_add3_u32 v8, v13, v31, s9
	v_add3_u32 v12, v12, v32, s9
	v_add3_u32 v32, v27, v33, s9
	v_add3_u32 v33, v26, v40, s9
	v_add3_u32 v13, v29, v41, s9
	v_add3_u32 v28, v28, v42, s9
	v_and_b32_e32 v9, 0xffff0000, v8
	v_and_b32_e32 v8, 0xffff0000, v12
	v_and_b32_e32 v27, 0xffff0000, v2
	v_and_b32_e32 v26, 0xffff0000, v43
	v_and_b32_e32 v29, 0xffff0000, v13
	v_and_b32_e32 v28, 0xffff0000, v28
	v_and_b32_e32 v31, 0xffff0000, v32
	v_and_b32_e32 v30, 0xffff0000, v33
	v_or_b32_sdwa v12, v8, v43 dst_sel:DWORD dst_unused:UNUSED_PAD src0_sel:DWORD src1_sel:WORD_1
	v_fma_f32 v20, v20, v24, -v26
	v_fma_f32 v21, v21, v25, -v27
	v_fma_f32 v24, v14, v34, -v8
	v_fma_f32 v25, v15, v35, -v9
	v_or_b32_sdwa v13, v9, v2 dst_sel:DWORD dst_unused:UNUSED_PAD src0_sel:DWORD src1_sel:WORD_1
	v_fma_f32 v8, v22, v36, -v30
	v_fma_f32 v9, v23, v37, -v31
	v_fma_f32 v10, v10, v38, -v28
	v_fma_f32 v11, v11, v39, -v29
	v_or_b32_sdwa v14, v28, v33 dst_sel:DWORD dst_unused:UNUSED_PAD src0_sel:DWORD src1_sel:WORD_1
	v_or_b32_sdwa v15, v29, v32 dst_sel:DWORD dst_unused:UNUSED_PAD src0_sel:DWORD src1_sel:WORD_1
	v_bfe_u32 v2, v11, 16, 1
	v_bfe_u32 v27, v20, 16, 1
	v_bfe_u32 v28, v21, 16, 1
	v_bfe_u32 v29, v8, 16, 1
	v_bfe_u32 v30, v9, 16, 1
	v_bfe_u32 v22, v10, 16, 1
	v_bfe_u32 v23, v25, 16, 1
	v_bfe_u32 v26, v24, 16, 1
	global_store_dwordx4 v[16:17], v[12:15], off
	v_add3_u32 v2, v11, v2, s9
	v_add3_u32 v9, v9, v30, s9
	v_add3_u32 v8, v8, v29, s9
	v_add3_u32 v11, v21, v28, s9
	v_add3_u32 v14, v20, v27, s9
	v_add3_u32 v12, v24, v26, s9
	v_add3_u32 v13, v25, v23, s9
	v_add3_u32 v10, v10, v22, s9
	v_lshrrev_b32_e32 v14, 16, v14
	v_lshrrev_b32_e32 v15, 16, v11
	v_lshrrev_b32_e32 v8, 16, v8
	v_lshrrev_b32_e32 v9, 16, v9
	v_and_or_b32 v11, v2, s10, v9
	v_and_or_b32 v10, v10, s10, v8
	v_and_or_b32 v9, v13, s10, v15
	v_and_or_b32 v8, v12, s10, v14
	global_store_dwordx4 v[18:19], v[8:11], off
	s_andn2_b64 exec, exec, s[2:3]
	s_cbranch_execnz .LBB0_1575

.LBB0_1581:
	v_mov_b32_e32 v58, v46
	v_mov_b32_e32 v59, v44
	v_mov_b32_e32 v44, v47
	v_mov_b32_e32 v46, v42
	v_mov_b32_e32 v47, v40
	v_mov_b32_e32 v40, v43
	v_fma_f32 v44, v58, v52, v44
	v_fma_f32 v45, v59, v53, v45
	v_fma_f32 v40, v46, v54, v40
	v_fma_f32 v41, v47, v55, v41
	v_cndmask_b32_e64 v43, v53, v45, s[14:15]
	v_cndmask_b32_e64 v41, v55, v41, s[14:15]
	v_cndmask_b32_e64 v40, v54, v40, s[14:15]
	v_cndmask_b32_e64 v42, v52, v44, s[14:15]
	v_mov_b32_e32 v44, v38
	v_mov_b32_e32 v45, v36
	v_mov_b32_e32 v36, v39
	v_mov_b32_e32 v38, v34
	v_mov_b32_e32 v39, v32
	v_mov_b32_e32 v32, v35
	v_fma_f32 v36, v44, v42, v36
	v_fma_f32 v37, v45, v43, v37
	v_fma_f32 v32, v38, v40, v32
	v_fma_f32 v33, v39, v41, v33
	v_cndmask_b32_e64 v35, v43, v37, s[12:13]
	v_cndmask_b32_e64 v34, v42, v36, s[12:13]
	v_cndmask_b32_e64 v33, v41, v33, s[12:13]
	v_cndmask_b32_e64 v32, v40, v32, s[12:13]
	v_mov_b32_e32 v36, v30
	v_mov_b32_e32 v37, v28
	v_mov_b32_e32 v28, v31
	v_mov_b32_e32 v30, v22
	v_mov_b32_e32 v31, v20
	v_mov_b32_e32 v20, v23
	v_fma_f32 v28, v36, v34, v28
	v_fma_f32 v29, v37, v35, v29
	v_fma_f32 v20, v30, v32, v20
	v_fma_f32 v21, v31, v33, v21
	v_cndmask_b32_e64 v23, v35, v29, s[10:11]
	v_cndmask_b32_e64 v22, v34, v28, s[10:11]
	v_cndmask_b32_e64 v21, v33, v21, s[10:11]
	v_cndmask_b32_e64 v20, v32, v20, s[10:11]
	s_waitcnt vmcnt(5)
	v_mov_b32_e32 v28, v26
	v_mov_b32_e32 v29, v24
	v_mov_b32_e32 v24, v27
	s_waitcnt vmcnt(4)
	v_mov_b32_e32 v26, v18
	v_mov_b32_e32 v27, v16
	v_mov_b32_e32 v16, v19
	v_fma_f32 v24, v28, v22, v24
	v_fma_f32 v25, v29, v23, v25
	v_fma_f32 v16, v26, v20, v16
	v_fma_f32 v17, v27, v21, v17
	v_cndmask_b32_e64 v19, v23, v25, s[8:9]
	v_cndmask_b32_e64 v18, v22, v24, s[8:9]
	v_cndmask_b32_e64 v17, v21, v17, s[8:9]
	v_cndmask_b32_e64 v16, v20, v16, s[8:9]
	s_waitcnt vmcnt(3)
	v_mov_b32_e32 v20, v14
	v_mov_b32_e32 v21, v12
	v_mov_b32_e32 v12, v15
	s_waitcnt vmcnt(2)
	v_mov_b32_e32 v14, v10
	v_mov_b32_e32 v15, v8
	v_mov_b32_e32 v8, v11
	v_fma_f32 v12, v20, v18, v12
	v_fma_f32 v13, v21, v19, v13
	v_fma_f32 v8, v14, v16, v8
	v_fma_f32 v9, v15, v17, v9
	v_cndmask_b32_e64 v11, v19, v13, s[6:7]
	v_cndmask_b32_e64 v10, v18, v12, s[6:7]
	v_cndmask_b32_e64 v9, v17, v9, s[6:7]
	v_cndmask_b32_e64 v8, v16, v8, s[6:7]
	s_waitcnt vmcnt(1)
	v_mov_b32_e32 v12, v6
	v_mov_b32_e32 v13, v4
	v_mov_b32_e32 v4, v7
	s_waitcnt vmcnt(0)
	v_mov_b32_e32 v6, v2
	v_mov_b32_e32 v7, v0
	v_mov_b32_e32 v0, v3
	v_fma_f32 v4, v12, v10, v4
	v_fma_f32 v5, v13, v11, v5
	v_fma_f32 v0, v6, v8, v0
	v_fma_f32 v1, v7, v9, v1
	v_cndmask_b32_e64 v52, v10, v4, s[4:5]
	v_cndmask_b32_e64 v53, v11, v5, s[4:5]
	v_cndmask_b32_e64 v54, v8, v0, s[4:5]
	v_cndmask_b32_e64 v55, v9, v1, s[4:5]
	s_add_i32 s65, s65, 8
	s_mov_b64 s[4:5], 0x20000
	s_cmp_ge_u32 s65, s64
	v_lshl_add_u64 v[56:57], v[56:57], 0, s[4:5]
	s_cbranch_scc1 .LBB0_1578
.LBB0_1582:
	s_add_i32 s78, s65, 1
	s_add_i32 s6, s65, 2
	s_cmp_lt_u32 s6, s64
	s_cselect_b64 s[14:15], -1, 0
	s_and_b64 s[4:5], s[14:15], exec
	s_cselect_b32 s4, s6, s19
	s_add_i32 s4, s4, s18
	s_ashr_i32 s5, s4, 31
	s_lshl_b64 s[66:67], s[4:5], 14
	s_add_i32 s6, s65, 3
	s_cmp_lt_u32 s6, s64
	s_cselect_b64 s[12:13], -1, 0
	s_and_b64 s[4:5], s[12:13], exec
	s_cselect_b32 s4, s6, s19
	s_add_i32 s4, s4, s18
	s_ashr_i32 s5, s4, 31
	s_lshl_b64 s[68:69], s[4:5], 14
	s_add_i32 s6, s65, 4
	s_cmp_lt_u32 s6, s64
	s_cselect_b64 s[10:11], -1, 0
	s_and_b64 s[4:5], s[10:11], exec
	s_cselect_b32 s4, s6, s19
	s_add_i32 s4, s4, s18
	s_ashr_i32 s5, s4, 31
	s_lshl_b64 s[70:71], s[4:5], 14
	s_add_i32 s6, s65, 5
	s_cmp_lt_u32 s6, s64
	s_cselect_b64 s[8:9], -1, 0
	s_and_b64 s[4:5], s[8:9], exec
	s_cselect_b32 s4, s6, s19
	s_add_i32 s4, s4, s18
	s_ashr_i32 s5, s4, 31
	s_lshl_b64 s[72:73], s[4:5], 14
	s_add_i32 s74, s65, 6
	s_cmp_lt_u32 s74, s64
	s_cselect_b64 s[6:7], -1, 0
	s_and_b64 s[4:5], s[6:7], exec
	s_cselect_b32 s4, s74, s19
	s_add_i32 s4, s4, s18
	s_ashr_i32 s5, s4, 31
	s_lshl_b64 s[74:75], s[4:5], 14
	s_add_i32 s79, s65, 7
	s_cmp_lt_u32 s79, s64
	s_cselect_b64 s[4:5], -1, 0
	s_and_b64 s[76:77], s[4:5], exec
	v_lshl_add_u64 v[0:1], v[50:51], 0, s[66:67]
	s_cselect_b32 s76, s79, s19
	global_load_dwordx4 v[44:47], v[0:1], off offset:16
	global_load_dwordx4 v[40:43], v[0:1], off
	v_lshl_add_u64 v[0:1], v[50:51], 0, s[68:69]
	s_add_i32 s76, s76, s18
	global_load_dwordx4 v[36:39], v[0:1], off offset:16
	global_load_dwordx4 v[32:35], v[0:1], off
	v_lshl_add_u64 v[0:1], v[50:51], 0, s[70:71]
	s_ashr_i32 s77, s76, 31
	global_load_dwordx4 v[28:31], v[0:1], off offset:16
	global_load_dwordx4 v[20:23], v[0:1], off
	v_lshl_add_u64 v[0:1], v[50:51], 0, s[72:73]
	s_lshl_b64 s[76:77], s[76:77], 14
	global_load_dwordx4 v[58:61], v[56:57], off offset:16
	global_load_dwordx4 v[62:65], v[56:57], off
	global_load_dwordx4 v[24:27], v[0:1], off offset:16
	global_load_dwordx4 v[16:19], v[0:1], off
	v_lshl_add_u64 v[0:1], v[50:51], 0, s[74:75]
	global_load_dwordx4 v[12:15], v[0:1], off offset:16
	global_load_dwordx4 v[8:11], v[0:1], off
	v_lshl_add_u64 v[0:1], v[50:51], 0, s[76:77]
	global_load_dwordx4 v[4:7], v[0:1], off offset:16
	s_nop 0
	global_load_dwordx4 v[0:3], v[0:1], off
	s_cmp_ge_u32 s78, s64
	s_waitcnt vmcnt(6)
	v_mov_b32_e32 v66, v64
	v_mov_b32_e32 v67, v62
	v_mov_b32_e32 v62, v65
	v_fma_f32 v54, v54, v66, v62
	v_fma_f32 v55, v55, v67, v63
	v_mov_b32_e32 v62, v60
	v_mov_b32_e32 v63, v58
	v_mov_b32_e32 v58, v61
	v_fma_f32 v52, v52, v62, v58
	v_fma_f32 v53, v53, v63, v59
	s_cbranch_scc1 .LBB0_1581
	v_add_co_u32_e32 v58, vcc, 0x4000, v56
	s_mov_b64 s[66:67], 0x4000
	s_nop 0
	v_addc_co_u32_e32 v59, vcc, 0, v57, vcc
	v_lshl_add_u64 v[62:63], v[56:57], 0, s[66:67]
	global_load_dwordx4 v[58:61], v[58:59], off
	s_nop 0
	global_load_dwordx4 v[62:65], v[62:63], off offset:16
	s_waitcnt vmcnt(1)
	v_mov_b32_e32 v66, v60
	v_mov_b32_e32 v67, v58
	v_mov_b32_e32 v58, v61
	s_waitcnt vmcnt(0)
	v_mov_b32_e32 v60, v64
	v_mov_b32_e32 v61, v62
	v_mov_b32_e32 v62, v65
	v_fma_f32 v54, v54, v66, v58
	v_fma_f32 v55, v55, v67, v59
	v_fma_f32 v52, v52, v60, v62
	v_fma_f32 v53, v53, v61, v63
	s_branch .LBB0_1581

.LBB0_2179:
	s_lshl_b32 s6, s56, 8
	v_mbcnt_lo_u32_b32 v128, -1, 0
	v_mbcnt_hi_u32_b32 v128, -1, v128
	s_add_i32 s6, s6, s45
	v_and_or_b32 v130, v128, 15, s6
	s_lshl_b32 s6, s55, 8
	v_ashrrev_i32_e32 v128, 1, v128
	s_or_b32 s6, s6, s46
	v_and_b32_e32 v128, -8, v128
	v_add_u32_e32 v128, s6, v128
	v_mov_b64_e32 v[132:133], s[12:13]
	v_ashrrev_i32_e32 v129, 31, v128
	v_mad_i64_i32 v[136:137], s[6:7], v130, s51, v[132:133]
	v_lshlrev_b64 v[128:129], 1, v[128:129]
	v_lshl_add_u64 v[140:141], v[136:137], 0, v[128:129]
	global_load_dwordx4 v[136:139], v[140:141], off
	s_nop 0
	global_load_dwordx4 v[140:143], v[140:141], off offset:256
	v_or_b32_e32 v156, 16, v130
	v_mul_f32_e32 v154, s16, v112
	v_mul_f32_e32 v155, s16, v113
	v_mad_i64_i32 v[112:113], s[6:7], v156, s51, v[132:133]
	v_lshl_add_u64 v[112:113], v[112:113], 0, v[128:129]
	v_mul_f32_e32 v144, s16, v122
	v_mul_f32_e32 v145, s16, v123
	v_mul_f32_e32 v146, s16, v120
	v_mul_f32_e32 v147, s16, v121
	v_mul_f32_e32 v148, s16, v118
	v_mul_f32_e32 v149, s16, v119
	v_mul_f32_e32 v150, s16, v116
	v_mul_f32_e32 v151, s16, v117
	global_load_dwordx4 v[120:123], v[112:113], off
	global_load_dwordx4 v[116:119], v[112:113], off offset:256
	v_ashrrev_i32_e32 v131, 31, v130
	v_mul_f32_e32 v152, s16, v114
	v_mul_f32_e32 v153, s16, v115
	v_lshlrev_b64 v[114:115], 12, v[130:131]
	v_lshl_add_u64 v[114:115], s[2:3], 0, v[114:115]
	v_lshl_add_u64 v[158:159], v[114:115], 0, v[128:129]
	v_mul_f32_e32 v126, s16, v126
	v_mul_f32_e32 v127, s16, v127
	v_mul_f32_e32 v124, s16, v124
	v_mul_f32_e32 v125, s16, v125
	v_mul_f32_e32 v108, s16, v108
	v_mul_f32_e32 v109, s16, v109
	v_mul_f32_e32 v110, s16, v110
	v_mul_f32_e32 v111, s16, v111
	v_ashrrev_i32_e32 v157, 31, v156
	v_mul_f32_e32 v106, s16, v106
	v_mul_f32_e32 v107, s16, v107
	v_mul_f32_e32 v104, s16, v104
	v_mul_f32_e32 v105, s16, v105
	v_mul_f32_e32 v102, s16, v102
	v_mul_f32_e32 v103, s16, v103
	v_mul_f32_e32 v100, s16, v100
	v_mul_f32_e32 v101, s16, v101
	v_mul_f32_e32 v96, s16, v96
	v_mul_f32_e32 v97, s16, v97
	v_mul_f32_e32 v98, s16, v98
	v_mul_f32_e32 v99, s16, v99
	v_mul_f32_e32 v94, s16, v94
	v_mul_f32_e32 v95, s16, v95
	v_mul_f32_e32 v92, s16, v92
	v_mul_f32_e32 v93, s16, v93
	v_mul_f32_e32 v90, s16, v90
	v_mul_f32_e32 v91, s16, v91
	v_mul_f32_e32 v88, s16, v88
	v_mul_f32_e32 v89, s16, v89
	v_mul_f32_e32 v86, s16, v86
	v_mul_f32_e32 v87, s16, v87
	v_mul_f32_e32 v84, s16, v84
	v_mul_f32_e32 v85, s16, v85
	v_mul_f32_e32 v80, s16, v80
	v_mul_f32_e32 v81, s16, v81
	v_mul_f32_e32 v82, s16, v82
	v_mul_f32_e32 v83, s16, v83
	v_mul_f32_e32 v78, s16, v78
	v_mul_f32_e32 v79, s16, v79
	v_mul_f32_e32 v76, s16, v76
	v_mul_f32_e32 v77, s16, v77
	v_mul_f32_e32 v74, s16, v74
	v_mul_f32_e32 v75, s16, v75
	v_mul_f32_e32 v72, s16, v72
	v_mul_f32_e32 v73, s16, v73
	v_mul_f32_e32 v70, s16, v70
	v_mul_f32_e32 v71, s16, v71
	v_mul_f32_e32 v68, s16, v68
	v_mul_f32_e32 v69, s16, v69
	v_mul_f32_e32 v64, s16, v64
	v_mul_f32_e32 v65, s16, v65
	v_mul_f32_e32 v66, s16, v66
	v_mul_f32_e32 v67, s16, v67
	v_mul_f32_e32 v62, s16, v62
	v_mul_f32_e32 v63, s16, v63
	v_mul_f32_e32 v60, s16, v60
	v_mul_f32_e32 v61, s16, v61
	v_mul_f32_e32 v58, s16, v58
	v_mul_f32_e32 v59, s16, v59
	v_mul_f32_e32 v56, s16, v56
	v_mul_f32_e32 v57, s16, v57
	v_mul_f32_e32 v54, s16, v54
	v_mul_f32_e32 v55, s16, v55
	v_mul_f32_e32 v52, s16, v52
	v_mul_f32_e32 v53, s16, v53
	v_mul_f32_e32 v48, s16, v48
	v_mul_f32_e32 v49, s16, v49
	v_mul_f32_e32 v50, s16, v50
	v_mul_f32_e32 v51, s16, v51
	v_mul_f32_e32 v46, s16, v46
	v_mul_f32_e32 v47, s16, v47
	v_mul_f32_e32 v44, s16, v44
	v_mul_f32_e32 v45, s16, v45
	v_mul_f32_e32 v42, s16, v42
	v_mul_f32_e32 v43, s16, v43
	v_mul_f32_e32 v40, s16, v40
	v_mul_f32_e32 v41, s16, v41
	v_mul_f32_e32 v38, s16, v38
	v_mul_f32_e32 v39, s16, v39
	v_mul_f32_e32 v36, s16, v36
	v_mul_f32_e32 v37, s16, v37
	v_mul_f32_e32 v32, s16, v32
	v_mul_f32_e32 v33, s16, v33
	v_mul_f32_e32 v34, s16, v34
	v_mul_f32_e32 v35, s16, v35
	v_mul_f32_e32 v30, s16, v30
	v_mul_f32_e32 v31, s16, v31
	v_mul_f32_e32 v28, s16, v28
	v_mul_f32_e32 v29, s16, v29
	v_mul_f32_e32 v26, s16, v26
	v_mul_f32_e32 v27, s16, v27
	v_mul_f32_e32 v24, s16, v24
	v_mul_f32_e32 v25, s16, v25
	v_mul_f32_e32 v22, s16, v22
	v_mul_f32_e32 v23, s16, v23
	v_mul_f32_e32 v20, s16, v20
	v_mul_f32_e32 v21, s16, v21
	v_mul_f32_e32 v18, s16, v18
	v_mul_f32_e32 v19, s16, v19
	v_mul_f32_e32 v16, s16, v16
	v_mul_f32_e32 v17, s16, v17
	v_mul_f32_e32 v14, s16, v14
	v_mul_f32_e32 v15, s16, v15
	v_mul_f32_e32 v12, s16, v12
	v_mul_f32_e32 v13, s16, v13
	v_mul_f32_e32 v10, s16, v10
	v_mul_f32_e32 v11, s16, v11
	v_mul_f32_e32 v8, s16, v8
	v_mul_f32_e32 v9, s16, v9
	v_mul_f32_e32 v6, s16, v6
	v_mul_f32_e32 v7, s16, v7
	v_mul_f32_e32 v4, s16, v4
	v_mul_f32_e32 v5, s16, v5
	v_mul_f32_e32 v2, s16, v2
	v_mul_f32_e32 v3, s16, v3
	v_mul_f32_e32 v0, s16, v0
	v_mul_f32_e32 v1, s16, v1
	s_andn2_b64 vcc, exec, s[18:19]
	s_waitcnt vmcnt(3)
	v_lshlrev_b32_e32 v112, 16, v136
	v_and_b32_e32 v113, 0xffff0000, v136
	v_lshlrev_b32_e32 v114, 16, v137
	v_and_b32_e32 v115, 0xffff0000, v137
	v_lshlrev_b32_e32 v131, 16, v138
	v_and_b32_e32 v136, 0xffff0000, v138
	v_mul_f32_e32 v112, 0xbfb8aa3b, v112
	v_mul_f32_e32 v113, 0xbfb8aa3b, v113
	v_mul_f32_e32 v114, 0xbfb8aa3b, v114
	v_lshlrev_b32_e32 v137, 16, v139
	v_and_b32_e32 v138, 0xffff0000, v139
	v_mul_f32_e32 v115, 0xbfb8aa3b, v115
	v_mul_f32_e32 v131, 0xbfb8aa3b, v131
	v_mul_f32_e32 v136, 0xbfb8aa3b, v136
	v_exp_f32_e32 v112, v112
	v_exp_f32_e32 v113, v113
	v_exp_f32_e32 v114, v114
	v_mul_f32_e32 v137, 0xbfb8aa3b, v137
	v_mul_f32_e32 v138, 0xbfb8aa3b, v138
	v_exp_f32_e32 v115, v115
	v_exp_f32_e32 v131, v131
	v_exp_f32_e32 v136, v136
	v_exp_f32_e32 v137, v137
	v_exp_f32_e32 v138, v138
	v_add_f32_e32 v112, 1.0, v112
	v_add_f32_e32 v113, 1.0, v113
	v_add_f32_e32 v114, 1.0, v114
	v_add_f32_e32 v115, 1.0, v115
	v_add_f32_e32 v131, 1.0, v131
	v_add_f32_e32 v136, 1.0, v136
	v_rcp_f32_e32 v112, v112
	v_rcp_f32_e32 v113, v113
	v_rcp_f32_e32 v114, v114
	v_add_f32_e32 v137, 1.0, v137
	v_add_f32_e32 v138, 1.0, v138
	v_rcp_f32_e32 v115, v115
	v_rcp_f32_e32 v131, v131
	v_rcp_f32_e32 v136, v136
	v_rcp_f32_e32 v137, v137
	v_rcp_f32_e32 v138, v138
	v_mul_f32_e32 v112, v124, v112
	v_mul_f32_e32 v113, v125, v113
	v_mul_f32_e32 v114, v126, v114
	s_waitcnt vmcnt(2)
	v_lshlrev_b32_e32 v139, 16, v140
	v_and_b32_e32 v140, 0xffff0000, v140
	v_lshlrev_b32_e32 v160, 16, v141
	v_mul_f32_e32 v115, v127, v115
	v_mul_f32_e32 v124, v146, v131
	v_mul_f32_e32 v125, v147, v136
	v_cvt_pk_bf16_f32 v112, v112, v113
	v_cvt_pk_bf16_f32 v113, v114, v115
	v_cvt_pk_bf16_f32 v114, v124, v125
	v_mul_f32_e32 v140, 0xbfb8aa3b, v140
	v_mul_f32_e32 v160, 0xbfb8aa3b, v160
	v_mul_f32_e32 v126, v144, v137
	v_mul_f32_e32 v127, v145, v138
	v_cvt_pk_bf16_f32 v115, v126, v127
	global_store_dwordx4 v[158:159], v[112:115], off
	v_mul_f32_e32 v139, 0xbfb8aa3b, v139
	v_exp_f32_e32 v140, v140
	v_and_b32_e32 v114, 0xffff0000, v141
	v_exp_f32_e32 v160, v160
	v_mul_f32_e32 v114, 0xbfb8aa3b, v114
	v_lshlrev_b32_e32 v124, 16, v142
	v_and_b32_e32 v125, 0xffff0000, v142
	v_lshlrev_b32_e32 v126, 16, v143
	v_and_b32_e32 v127, 0xffff0000, v143
	v_exp_f32_e32 v139, v139
	v_exp_f32_e32 v114, v114
	v_mul_f32_e32 v124, 0xbfb8aa3b, v124
	v_mul_f32_e32 v125, 0xbfb8aa3b, v125
	v_mul_f32_e32 v126, 0xbfb8aa3b, v126
	v_mul_f32_e32 v127, 0xbfb8aa3b, v127
	v_exp_f32_e32 v124, v124
	v_exp_f32_e32 v125, v125
	v_exp_f32_e32 v126, v126
	v_exp_f32_e32 v127, v127
	v_add_f32_e32 v140, 1.0, v140
	v_add_f32_e32 v113, 1.0, v160
	v_add_f32_e32 v139, 1.0, v139
	v_rcp_f32_e32 v112, v140
	v_rcp_f32_e32 v113, v113
	v_add_f32_e32 v114, 1.0, v114
	v_rcp_f32_e32 v139, v139
	v_rcp_f32_e32 v114, v114
	v_add_f32_e32 v124, 1.0, v124
	v_add_f32_e32 v125, 1.0, v125
	v_add_f32_e32 v126, 1.0, v126
	v_add_f32_e32 v127, 1.0, v127
	v_rcp_f32_e32 v124, v124
	v_rcp_f32_e32 v125, v125
	v_rcp_f32_e32 v126, v126
	v_rcp_f32_e32 v127, v127
	v_mul_f32_e32 v112, v151, v112
	v_mul_f32_e32 v113, v148, v113
	v_mul_f32_e32 v115, v150, v139
	v_mul_f32_e32 v114, v149, v114
	v_cvt_pk_bf16_f32 v112, v115, v112
	v_cvt_pk_bf16_f32 v113, v113, v114
	v_or_b32_e32 v136, 32, v130
	v_mul_f32_e32 v124, v154, v124
	v_mul_f32_e32 v125, v155, v125
	v_mul_f32_e32 v126, v152, v126
	v_mul_f32_e32 v127, v153, v127
	v_cvt_pk_bf16_f32 v114, v124, v125
	v_cvt_pk_bf16_f32 v115, v126, v127
	global_store_dwordx4 v[158:159], v[112:115], off offset:256
	s_waitcnt vmcnt(3)
	v_lshlrev_b32_e32 v131, 16, v120
	v_and_b32_e32 v120, 0xffff0000, v120
	v_mad_i64_i32 v[112:113], s[6:7], v136, s51, v[132:133]
	v_lshl_add_u64 v[112:113], v[112:113], 0, v[128:129]
	v_mul_f32_e32 v120, 0xbfb8aa3b, v120
	global_load_dwordx4 v[124:127], v[112:113], off
	s_nop 0
	global_load_dwordx4 v[112:115], v[112:113], off offset:256
	v_exp_f32_e32 v120, v120
	v_lshlrev_b32_e32 v140, 16, v121
	v_and_b32_e32 v121, 0xffff0000, v121
	v_mul_f32_e32 v121, 0xbfb8aa3b, v121
	v_add_f32_e32 v120, 1.0, v120
	v_rcp_f32_e32 v120, v120
	v_exp_f32_e32 v121, v121
	v_mul_f32_e32 v131, 0xbfb8aa3b, v131
	v_mul_f32_e32 v140, 0xbfb8aa3b, v140
	v_mul_f32_e32 v109, v109, v120
	v_add_f32_e32 v120, 1.0, v121
	v_lshlrev_b32_e32 v121, 16, v122
	v_and_b32_e32 v122, 0xffff0000, v122
	v_mul_f32_e32 v121, 0xbfb8aa3b, v121
	v_mul_f32_e32 v122, 0xbfb8aa3b, v122
	v_rcp_f32_e32 v120, v120
	v_exp_f32_e32 v121, v121
	v_exp_f32_e32 v122, v122
	v_exp_f32_e32 v131, v131
	v_mul_f32_e32 v111, v111, v120
	v_add_f32_e32 v120, 1.0, v121
	v_add_f32_e32 v121, 1.0, v122
	v_lshlrev_b32_e32 v122, 16, v123
	v_and_b32_e32 v123, 0xffff0000, v123
	v_mul_f32_e32 v122, 0xbfb8aa3b, v122
	v_mul_f32_e32 v123, 0xbfb8aa3b, v123
	v_exp_f32_e32 v140, v140
	v_exp_f32_e32 v122, v122
	v_exp_f32_e32 v123, v123
	v_add_f32_e32 v131, 1.0, v131
	v_add_f32_e32 v140, 1.0, v140
	v_add_f32_e32 v122, 1.0, v122
	v_add_f32_e32 v123, 1.0, v123
	v_rcp_f32_e32 v131, v131
	v_rcp_f32_e32 v140, v140
	v_rcp_f32_e32 v120, v120
	v_rcp_f32_e32 v121, v121
	v_rcp_f32_e32 v122, v122
	v_rcp_f32_e32 v123, v123
	v_lshlrev_b64 v[138:139], 12, v[156:157]
	v_lshl_add_u64 v[138:139], s[2:3], 0, v[138:139]
	v_lshl_add_u64 v[138:139], v[138:139], 0, v[128:129]
	v_mul_f32_e32 v108, v108, v131
	v_mul_f32_e32 v110, v110, v140
	v_mul_f32_e32 v120, v104, v120
	v_mul_f32_e32 v121, v105, v121
	v_mul_f32_e32 v122, v106, v122
	v_mul_f32_e32 v107, v107, v123
	v_cvt_pk_bf16_f32 v104, v108, v109
	v_cvt_pk_bf16_f32 v105, v110, v111
	v_cvt_pk_bf16_f32 v106, v120, v121
	v_cvt_pk_bf16_f32 v107, v122, v107
	global_store_dwordx4 v[138:139], v[104:107], off
	v_ashrrev_i32_e32 v137, 31, v136
	s_waitcnt vmcnt(2)
	v_and_b32_e32 v109, 0xffff0000, v124
	v_and_b32_e32 v105, 0xffff0000, v116
	v_lshlrev_b32_e32 v106, 16, v117
	v_lshlrev_b32_e32 v104, 16, v116
	v_mul_f32_e32 v105, 0xbfb8aa3b, v105
	v_mul_f32_e32 v106, 0xbfb8aa3b, v106
	v_mul_f32_e32 v104, 0xbfb8aa3b, v104
	v_exp_f32_e32 v105, v105
	v_exp_f32_e32 v106, v106
	v_exp_f32_e32 v104, v104
	v_and_b32_e32 v107, 0xffff0000, v117
	v_add_f32_e32 v105, 1.0, v105
	v_add_f32_e32 v106, 1.0, v106
	v_add_f32_e32 v104, 1.0, v104
	v_rcp_f32_e32 v105, v105
	v_rcp_f32_e32 v106, v106
	v_mul_f32_e32 v107, 0xbfb8aa3b, v107
	v_rcp_f32_e32 v104, v104
	v_exp_f32_e32 v107, v107
	v_mul_f32_e32 v101, v101, v105
	v_mul_f32_e32 v102, v102, v106
	v_lshlrev_b32_e32 v105, 16, v118
	v_and_b32_e32 v106, 0xffff0000, v118
	v_mul_f32_e32 v100, v100, v104
	v_add_f32_e32 v104, 1.0, v107
	v_mul_f32_e32 v105, 0xbfb8aa3b, v105
	v_mul_f32_e32 v106, 0xbfb8aa3b, v106
	v_rcp_f32_e32 v104, v104
	v_exp_f32_e32 v105, v105
	v_exp_f32_e32 v106, v106
	v_and_b32_e32 v107, 0xffff0000, v119
	v_mul_f32_e32 v103, v103, v104
	v_add_f32_e32 v104, 1.0, v105
	v_add_f32_e32 v105, 1.0, v106
	v_lshlrev_b32_e32 v106, 16, v119
	v_mul_f32_e32 v106, 0xbfb8aa3b, v106
	v_mul_f32_e32 v107, 0xbfb8aa3b, v107
	v_exp_f32_e32 v106, v106
	v_exp_f32_e32 v107, v107
	v_rcp_f32_e32 v104, v104
	v_rcp_f32_e32 v105, v105
	v_add_f32_e32 v106, 1.0, v106
	v_add_f32_e32 v107, 1.0, v107
	v_rcp_f32_e32 v106, v106
	v_rcp_f32_e32 v107, v107
	v_mul_f32_e32 v104, v96, v104
	v_mul_f32_e32 v105, v97, v105
	v_mul_f32_e32 v106, v98, v106
	v_mul_f32_e32 v99, v99, v107
	v_cvt_pk_bf16_f32 v96, v100, v101
	v_cvt_pk_bf16_f32 v97, v102, v103
	v_cvt_pk_bf16_f32 v98, v104, v105
	v_or_b32_e32 v104, 48, v130
	v_cvt_pk_bf16_f32 v99, v106, v99
	global_store_dwordx4 v[138:139], v[96:99], off offset:256
	v_lshlrev_b32_e32 v110, 16, v125
	v_lshlrev_b32_e32 v108, 16, v124
	v_mad_i64_i32 v[96:97], s[6:7], v104, s51, v[132:133]
	v_lshl_add_u64 v[96:97], v[96:97], 0, v[128:129]
	global_load_dwordx4 v[100:103], v[96:97], off
	s_nop 0
	global_load_dwordx4 v[96:99], v[96:97], off offset:256
	v_mul_f32_e32 v109, 0xbfb8aa3b, v109
	v_mul_f32_e32 v110, 0xbfb8aa3b, v110
	v_mul_f32_e32 v108, 0xbfb8aa3b, v108
	v_exp_f32_e32 v109, v109
	v_exp_f32_e32 v110, v110
	v_exp_f32_e32 v108, v108
	v_and_b32_e32 v111, 0xffff0000, v125
	v_add_f32_e32 v109, 1.0, v109
	v_add_f32_e32 v110, 1.0, v110
	v_add_f32_e32 v108, 1.0, v108
	v_rcp_f32_e32 v109, v109
	v_rcp_f32_e32 v110, v110
	v_mul_f32_e32 v111, 0xbfb8aa3b, v111
	v_rcp_f32_e32 v108, v108
	v_exp_f32_e32 v111, v111
	v_mul_f32_e32 v93, v93, v109
	v_mul_f32_e32 v94, v94, v110
	v_lshlrev_b32_e32 v109, 16, v126
	v_and_b32_e32 v110, 0xffff0000, v126
	v_mul_f32_e32 v92, v92, v108
	v_add_f32_e32 v108, 1.0, v111
	v_mul_f32_e32 v109, 0xbfb8aa3b, v109
	v_mul_f32_e32 v110, 0xbfb8aa3b, v110
	v_rcp_f32_e32 v108, v108
	v_exp_f32_e32 v109, v109
	v_exp_f32_e32 v110, v110
	v_and_b32_e32 v111, 0xffff0000, v127
	v_mul_f32_e32 v95, v95, v108
	v_add_f32_e32 v108, 1.0, v109
	v_add_f32_e32 v109, 1.0, v110
	v_lshlrev_b32_e32 v110, 16, v127
	v_mul_f32_e32 v110, 0xbfb8aa3b, v110
	v_mul_f32_e32 v111, 0xbfb8aa3b, v111
	v_exp_f32_e32 v110, v110
	v_exp_f32_e32 v111, v111
	v_rcp_f32_e32 v108, v108
	v_rcp_f32_e32 v109, v109
	v_add_f32_e32 v110, 1.0, v110
	v_add_f32_e32 v111, 1.0, v111
	v_rcp_f32_e32 v110, v110
	v_rcp_f32_e32 v111, v111
	v_lshlrev_b64 v[106:107], 12, v[136:137]
	v_lshl_add_u64 v[106:107], s[2:3], 0, v[106:107]
	v_lshl_add_u64 v[106:107], v[106:107], 0, v[128:129]
	v_mul_f32_e32 v108, v88, v108
	v_mul_f32_e32 v109, v89, v109
	v_mul_f32_e32 v110, v90, v110
	v_mul_f32_e32 v91, v91, v111
	v_cvt_pk_bf16_f32 v88, v92, v93
	v_cvt_pk_bf16_f32 v89, v94, v95
	v_cvt_pk_bf16_f32 v90, v108, v109
	v_cvt_pk_bf16_f32 v91, v110, v91
	global_store_dwordx4 v[106:107], v[88:91], off
	v_ashrrev_i32_e32 v105, 31, v104
	s_waitcnt vmcnt(2)
	v_and_b32_e32 v93, 0xffff0000, v100
	v_and_b32_e32 v89, 0xffff0000, v112
	v_lshlrev_b32_e32 v90, 16, v113
	v_lshlrev_b32_e32 v88, 16, v112
	v_mul_f32_e32 v89, 0xbfb8aa3b, v89
	v_mul_f32_e32 v90, 0xbfb8aa3b, v90
	v_mul_f32_e32 v88, 0xbfb8aa3b, v88
	v_exp_f32_e32 v89, v89
	v_exp_f32_e32 v90, v90
	v_exp_f32_e32 v88, v88
	v_and_b32_e32 v91, 0xffff0000, v113
	v_add_f32_e32 v89, 1.0, v89
	v_add_f32_e32 v90, 1.0, v90
	v_add_f32_e32 v88, 1.0, v88
	v_rcp_f32_e32 v89, v89
	v_rcp_f32_e32 v90, v90
	v_mul_f32_e32 v91, 0xbfb8aa3b, v91
	v_rcp_f32_e32 v88, v88
	v_exp_f32_e32 v91, v91
	v_mul_f32_e32 v85, v85, v89
	v_mul_f32_e32 v86, v86, v90
	v_lshlrev_b32_e32 v89, 16, v114
	v_and_b32_e32 v90, 0xffff0000, v114
	v_mul_f32_e32 v84, v84, v88
	v_add_f32_e32 v88, 1.0, v91
	v_mul_f32_e32 v89, 0xbfb8aa3b, v89
	v_mul_f32_e32 v90, 0xbfb8aa3b, v90
	v_rcp_f32_e32 v88, v88
	v_exp_f32_e32 v89, v89
	v_exp_f32_e32 v90, v90
	v_and_b32_e32 v91, 0xffff0000, v115
	v_mul_f32_e32 v87, v87, v88
	v_add_f32_e32 v88, 1.0, v89
	v_add_f32_e32 v89, 1.0, v90
	v_lshlrev_b32_e32 v90, 16, v115
	v_mul_f32_e32 v90, 0xbfb8aa3b, v90
	v_mul_f32_e32 v91, 0xbfb8aa3b, v91
	v_exp_f32_e32 v90, v90
	v_exp_f32_e32 v91, v91
	v_rcp_f32_e32 v88, v88
	v_rcp_f32_e32 v89, v89
	v_add_f32_e32 v90, 1.0, v90
	v_add_f32_e32 v91, 1.0, v91
	v_rcp_f32_e32 v90, v90
	v_rcp_f32_e32 v91, v91
	v_mul_f32_e32 v88, v80, v88
	v_mul_f32_e32 v89, v81, v89
	v_mul_f32_e32 v90, v82, v90
	v_mul_f32_e32 v83, v83, v91
	v_cvt_pk_bf16_f32 v80, v84, v85
	v_cvt_pk_bf16_f32 v81, v86, v87
	v_cvt_pk_bf16_f32 v82, v88, v89
	v_add_u32_e32 v88, 0x80, v130
	v_cvt_pk_bf16_f32 v83, v90, v83
	global_store_dwordx4 v[106:107], v[80:83], off offset:256
	v_lshlrev_b32_e32 v94, 16, v101
	v_lshlrev_b32_e32 v92, 16, v100
	v_mad_i64_i32 v[80:81], s[6:7], v88, s51, v[132:133]
	v_lshl_add_u64 v[80:81], v[80:81], 0, v[128:129]
	v_mul_f32_e32 v93, 0xbfb8aa3b, v93
	v_mul_f32_e32 v94, 0xbfb8aa3b, v94
	global_load_dwordx4 v[84:87], v[80:81], off
	s_nop 0
	global_load_dwordx4 v[80:83], v[80:81], off offset:256
	v_mul_f32_e32 v92, 0xbfb8aa3b, v92
	v_exp_f32_e32 v93, v93
	v_exp_f32_e32 v94, v94
	v_exp_f32_e32 v92, v92
	v_and_b32_e32 v95, 0xffff0000, v101
	v_add_f32_e32 v93, 1.0, v93
	v_add_f32_e32 v94, 1.0, v94
	v_add_f32_e32 v92, 1.0, v92
	v_rcp_f32_e32 v93, v93
	v_rcp_f32_e32 v94, v94
	v_mul_f32_e32 v95, 0xbfb8aa3b, v95
	v_rcp_f32_e32 v92, v92
	v_exp_f32_e32 v95, v95
	v_mul_f32_e32 v77, v77, v93
	v_mul_f32_e32 v78, v78, v94
	v_lshlrev_b32_e32 v93, 16, v102
	v_and_b32_e32 v94, 0xffff0000, v102
	v_mul_f32_e32 v76, v76, v92
	v_add_f32_e32 v92, 1.0, v95
	v_mul_f32_e32 v93, 0xbfb8aa3b, v93
	v_mul_f32_e32 v94, 0xbfb8aa3b, v94
	v_rcp_f32_e32 v92, v92
	v_exp_f32_e32 v93, v93
	v_exp_f32_e32 v94, v94
	v_and_b32_e32 v95, 0xffff0000, v103
	v_mul_f32_e32 v79, v79, v92
	v_add_f32_e32 v92, 1.0, v93
	v_add_f32_e32 v93, 1.0, v94
	v_lshlrev_b32_e32 v94, 16, v103
	v_mul_f32_e32 v94, 0xbfb8aa3b, v94
	v_mul_f32_e32 v95, 0xbfb8aa3b, v95
	v_exp_f32_e32 v94, v94
	v_exp_f32_e32 v95, v95
	v_rcp_f32_e32 v92, v92
	v_rcp_f32_e32 v93, v93
	v_add_f32_e32 v94, 1.0, v94
	v_add_f32_e32 v95, 1.0, v95
	v_rcp_f32_e32 v94, v94
	v_rcp_f32_e32 v95, v95
	v_lshlrev_b64 v[90:91], 12, v[104:105]
	v_lshl_add_u64 v[90:91], s[2:3], 0, v[90:91]
	v_lshl_add_u64 v[90:91], v[90:91], 0, v[128:129]
	v_mul_f32_e32 v92, v72, v92
	v_mul_f32_e32 v93, v73, v93
	v_mul_f32_e32 v94, v74, v94
	v_mul_f32_e32 v75, v75, v95
	v_cvt_pk_bf16_f32 v72, v76, v77
	v_cvt_pk_bf16_f32 v73, v78, v79
	v_cvt_pk_bf16_f32 v74, v92, v93
	v_cvt_pk_bf16_f32 v75, v94, v75
	global_store_dwordx4 v[90:91], v[72:75], off
	v_ashrrev_i32_e32 v89, 31, v88
	s_waitcnt vmcnt(2)
	v_and_b32_e32 v77, 0xffff0000, v84
	v_and_b32_e32 v73, 0xffff0000, v96
	v_lshlrev_b32_e32 v74, 16, v97
	v_lshlrev_b32_e32 v72, 16, v96
	v_mul_f32_e32 v73, 0xbfb8aa3b, v73
	v_mul_f32_e32 v74, 0xbfb8aa3b, v74
	v_mul_f32_e32 v72, 0xbfb8aa3b, v72
	v_exp_f32_e32 v73, v73
	v_exp_f32_e32 v74, v74
	v_exp_f32_e32 v72, v72
	v_and_b32_e32 v75, 0xffff0000, v97
	v_add_f32_e32 v73, 1.0, v73
	v_add_f32_e32 v74, 1.0, v74
	v_add_f32_e32 v72, 1.0, v72
	v_rcp_f32_e32 v73, v73
	v_rcp_f32_e32 v74, v74
	v_mul_f32_e32 v75, 0xbfb8aa3b, v75
	v_rcp_f32_e32 v72, v72
	v_exp_f32_e32 v75, v75
	v_mul_f32_e32 v69, v69, v73
	v_mul_f32_e32 v70, v70, v74
	v_lshlrev_b32_e32 v73, 16, v98
	v_and_b32_e32 v74, 0xffff0000, v98
	v_mul_f32_e32 v68, v68, v72
	v_add_f32_e32 v72, 1.0, v75
	v_mul_f32_e32 v73, 0xbfb8aa3b, v73
	v_mul_f32_e32 v74, 0xbfb8aa3b, v74
	v_rcp_f32_e32 v72, v72
	v_exp_f32_e32 v73, v73
	v_exp_f32_e32 v74, v74
	v_and_b32_e32 v75, 0xffff0000, v99
	v_mul_f32_e32 v71, v71, v72
	v_add_f32_e32 v72, 1.0, v73
	v_add_f32_e32 v73, 1.0, v74
	v_lshlrev_b32_e32 v74, 16, v99
	v_mul_f32_e32 v74, 0xbfb8aa3b, v74
	v_mul_f32_e32 v75, 0xbfb8aa3b, v75
	v_exp_f32_e32 v74, v74
	v_exp_f32_e32 v75, v75
	v_rcp_f32_e32 v72, v72
	v_rcp_f32_e32 v73, v73
	v_add_f32_e32 v74, 1.0, v74
	v_add_f32_e32 v75, 1.0, v75
	v_rcp_f32_e32 v74, v74
	v_rcp_f32_e32 v75, v75
	v_mul_f32_e32 v72, v64, v72
	v_mul_f32_e32 v73, v65, v73
	v_mul_f32_e32 v74, v66, v74
	v_mul_f32_e32 v67, v67, v75
	v_cvt_pk_bf16_f32 v64, v68, v69
	v_cvt_pk_bf16_f32 v65, v70, v71
	v_cvt_pk_bf16_f32 v66, v72, v73
	v_add_u32_e32 v72, 0x90, v130
	v_cvt_pk_bf16_f32 v67, v74, v67
	global_store_dwordx4 v[90:91], v[64:67], off offset:256
	v_lshlrev_b32_e32 v78, 16, v85
	v_lshlrev_b32_e32 v76, 16, v84
	v_mad_i64_i32 v[64:65], s[6:7], v72, s51, v[132:133]
	v_lshl_add_u64 v[64:65], v[64:65], 0, v[128:129]
	global_load_dwordx4 v[68:71], v[64:65], off
	s_nop 0
	global_load_dwordx4 v[64:67], v[64:65], off offset:256
	v_mul_f32_e32 v77, 0xbfb8aa3b, v77
	v_mul_f32_e32 v78, 0xbfb8aa3b, v78
	v_mul_f32_e32 v76, 0xbfb8aa3b, v76
	v_exp_f32_e32 v77, v77
	v_exp_f32_e32 v78, v78
	v_exp_f32_e32 v76, v76
	v_and_b32_e32 v79, 0xffff0000, v85
	v_add_f32_e32 v77, 1.0, v77
	v_add_f32_e32 v78, 1.0, v78
	v_add_f32_e32 v76, 1.0, v76
	v_rcp_f32_e32 v77, v77
	v_rcp_f32_e32 v78, v78
	v_mul_f32_e32 v79, 0xbfb8aa3b, v79
	v_rcp_f32_e32 v76, v76
	v_exp_f32_e32 v79, v79
	v_mul_f32_e32 v61, v61, v77
	v_mul_f32_e32 v62, v62, v78
	v_lshlrev_b32_e32 v77, 16, v86
	v_and_b32_e32 v78, 0xffff0000, v86
	v_mul_f32_e32 v60, v60, v76
	v_add_f32_e32 v76, 1.0, v79
	v_mul_f32_e32 v77, 0xbfb8aa3b, v77
	v_mul_f32_e32 v78, 0xbfb8aa3b, v78
	v_rcp_f32_e32 v76, v76
	v_exp_f32_e32 v77, v77
	v_exp_f32_e32 v78, v78
	v_and_b32_e32 v79, 0xffff0000, v87
	v_mul_f32_e32 v63, v63, v76
	v_add_f32_e32 v76, 1.0, v77
	v_add_f32_e32 v77, 1.0, v78
	v_lshlrev_b32_e32 v78, 16, v87
	v_mul_f32_e32 v78, 0xbfb8aa3b, v78
	v_mul_f32_e32 v79, 0xbfb8aa3b, v79
	v_exp_f32_e32 v78, v78
	v_exp_f32_e32 v79, v79
	v_rcp_f32_e32 v76, v76
	v_rcp_f32_e32 v77, v77
	v_add_f32_e32 v78, 1.0, v78
	v_add_f32_e32 v79, 1.0, v79
	v_rcp_f32_e32 v78, v78
	v_rcp_f32_e32 v79, v79
	v_lshlrev_b64 v[74:75], 12, v[88:89]
	v_lshl_add_u64 v[74:75], s[2:3], 0, v[74:75]
	v_lshl_add_u64 v[74:75], v[74:75], 0, v[128:129]
	v_mul_f32_e32 v76, v56, v76
	v_mul_f32_e32 v77, v57, v77
	v_mul_f32_e32 v78, v58, v78
	v_mul_f32_e32 v59, v59, v79
	v_cvt_pk_bf16_f32 v56, v60, v61
	v_cvt_pk_bf16_f32 v57, v62, v63
	v_cvt_pk_bf16_f32 v58, v76, v77
	v_cvt_pk_bf16_f32 v59, v78, v59
	global_store_dwordx4 v[74:75], v[56:59], off
	v_ashrrev_i32_e32 v73, 31, v72
	s_waitcnt vmcnt(2)
	v_and_b32_e32 v61, 0xffff0000, v68
	v_and_b32_e32 v57, 0xffff0000, v80
	v_lshlrev_b32_e32 v58, 16, v81
	v_lshlrev_b32_e32 v56, 16, v80
	v_mul_f32_e32 v57, 0xbfb8aa3b, v57
	v_mul_f32_e32 v58, 0xbfb8aa3b, v58
	v_mul_f32_e32 v56, 0xbfb8aa3b, v56
	v_exp_f32_e32 v57, v57
	v_exp_f32_e32 v58, v58
	v_exp_f32_e32 v56, v56
	v_and_b32_e32 v59, 0xffff0000, v81
	v_add_f32_e32 v57, 1.0, v57
	v_add_f32_e32 v58, 1.0, v58
	v_add_f32_e32 v56, 1.0, v56
	v_rcp_f32_e32 v57, v57
	v_rcp_f32_e32 v58, v58
	v_mul_f32_e32 v59, 0xbfb8aa3b, v59
	v_rcp_f32_e32 v56, v56
	v_exp_f32_e32 v59, v59
	v_mul_f32_e32 v53, v53, v57
	v_mul_f32_e32 v54, v54, v58
	v_lshlrev_b32_e32 v57, 16, v82
	v_and_b32_e32 v58, 0xffff0000, v82
	v_mul_f32_e32 v52, v52, v56
	v_add_f32_e32 v56, 1.0, v59
	v_mul_f32_e32 v57, 0xbfb8aa3b, v57
	v_mul_f32_e32 v58, 0xbfb8aa3b, v58
	v_rcp_f32_e32 v56, v56
	v_exp_f32_e32 v57, v57
	v_exp_f32_e32 v58, v58
	v_and_b32_e32 v59, 0xffff0000, v83
	v_mul_f32_e32 v55, v55, v56
	v_add_f32_e32 v56, 1.0, v57
	v_add_f32_e32 v57, 1.0, v58
	v_lshlrev_b32_e32 v58, 16, v83
	v_mul_f32_e32 v58, 0xbfb8aa3b, v58
	v_mul_f32_e32 v59, 0xbfb8aa3b, v59
	v_exp_f32_e32 v58, v58
	v_exp_f32_e32 v59, v59
	v_rcp_f32_e32 v56, v56
	v_rcp_f32_e32 v57, v57
	v_add_f32_e32 v58, 1.0, v58
	v_add_f32_e32 v59, 1.0, v59
	v_rcp_f32_e32 v58, v58
	v_rcp_f32_e32 v59, v59
	v_mul_f32_e32 v56, v48, v56
	v_mul_f32_e32 v57, v49, v57
	v_mul_f32_e32 v58, v50, v58
	v_mul_f32_e32 v51, v51, v59
	v_cvt_pk_bf16_f32 v48, v52, v53
	v_cvt_pk_bf16_f32 v49, v54, v55
	v_cvt_pk_bf16_f32 v50, v56, v57
	v_add_u32_e32 v56, 0xa0, v130
	v_cvt_pk_bf16_f32 v51, v58, v51
	global_store_dwordx4 v[74:75], v[48:51], off offset:256
	v_lshlrev_b32_e32 v62, 16, v69
	v_lshlrev_b32_e32 v60, 16, v68
	v_mad_i64_i32 v[48:49], s[6:7], v56, s51, v[132:133]
	v_lshl_add_u64 v[48:49], v[48:49], 0, v[128:129]
	v_mul_f32_e32 v61, 0xbfb8aa3b, v61
	v_mul_f32_e32 v62, 0xbfb8aa3b, v62
	global_load_dwordx4 v[52:55], v[48:49], off
	s_nop 0
	global_load_dwordx4 v[48:51], v[48:49], off offset:256
	v_mul_f32_e32 v60, 0xbfb8aa3b, v60
	v_exp_f32_e32 v61, v61
	v_exp_f32_e32 v62, v62
	v_exp_f32_e32 v60, v60
	v_and_b32_e32 v63, 0xffff0000, v69
	v_add_f32_e32 v61, 1.0, v61
	v_add_f32_e32 v62, 1.0, v62
	v_add_f32_e32 v60, 1.0, v60
	v_rcp_f32_e32 v61, v61
	v_rcp_f32_e32 v62, v62
	v_mul_f32_e32 v63, 0xbfb8aa3b, v63
	v_rcp_f32_e32 v60, v60
	v_exp_f32_e32 v63, v63
	v_mul_f32_e32 v45, v45, v61
	v_mul_f32_e32 v46, v46, v62
	v_lshlrev_b32_e32 v61, 16, v70
	v_and_b32_e32 v62, 0xffff0000, v70
	v_mul_f32_e32 v44, v44, v60
	v_add_f32_e32 v60, 1.0, v63
	v_mul_f32_e32 v61, 0xbfb8aa3b, v61
	v_mul_f32_e32 v62, 0xbfb8aa3b, v62
	v_rcp_f32_e32 v60, v60
	v_exp_f32_e32 v61, v61
	v_exp_f32_e32 v62, v62
	v_and_b32_e32 v63, 0xffff0000, v71
	v_mul_f32_e32 v47, v47, v60
	v_add_f32_e32 v60, 1.0, v61
	v_add_f32_e32 v61, 1.0, v62
	v_lshlrev_b32_e32 v62, 16, v71
	v_mul_f32_e32 v62, 0xbfb8aa3b, v62
	v_mul_f32_e32 v63, 0xbfb8aa3b, v63
	v_exp_f32_e32 v62, v62
	v_exp_f32_e32 v63, v63
	v_rcp_f32_e32 v60, v60
	v_rcp_f32_e32 v61, v61
	v_add_f32_e32 v62, 1.0, v62
	v_add_f32_e32 v63, 1.0, v63
	v_rcp_f32_e32 v62, v62
	v_rcp_f32_e32 v63, v63
	v_lshlrev_b64 v[58:59], 12, v[72:73]
	v_lshl_add_u64 v[58:59], s[2:3], 0, v[58:59]
	v_lshl_add_u64 v[58:59], v[58:59], 0, v[128:129]
	v_mul_f32_e32 v60, v40, v60
	v_mul_f32_e32 v61, v41, v61
	v_mul_f32_e32 v62, v42, v62
	v_mul_f32_e32 v43, v43, v63
	v_cvt_pk_bf16_f32 v40, v44, v45
	v_cvt_pk_bf16_f32 v41, v46, v47
	v_cvt_pk_bf16_f32 v42, v60, v61
	v_cvt_pk_bf16_f32 v43, v62, v43
	global_store_dwordx4 v[58:59], v[40:43], off
	v_ashrrev_i32_e32 v57, 31, v56
	s_waitcnt vmcnt(2)
	v_and_b32_e32 v45, 0xffff0000, v52
	v_and_b32_e32 v41, 0xffff0000, v64
	v_lshlrev_b32_e32 v42, 16, v65
	v_lshlrev_b32_e32 v40, 16, v64
	v_mul_f32_e32 v41, 0xbfb8aa3b, v41
	v_mul_f32_e32 v42, 0xbfb8aa3b, v42
	v_mul_f32_e32 v40, 0xbfb8aa3b, v40
	v_exp_f32_e32 v41, v41
	v_exp_f32_e32 v42, v42
	v_exp_f32_e32 v40, v40
	v_and_b32_e32 v43, 0xffff0000, v65
	v_add_f32_e32 v41, 1.0, v41
	v_add_f32_e32 v42, 1.0, v42
	v_add_f32_e32 v40, 1.0, v40
	v_rcp_f32_e32 v41, v41
	v_rcp_f32_e32 v42, v42
	v_mul_f32_e32 v43, 0xbfb8aa3b, v43
	v_rcp_f32_e32 v40, v40
	v_exp_f32_e32 v43, v43
	v_mul_f32_e32 v37, v37, v41
	v_mul_f32_e32 v38, v38, v42
	v_lshlrev_b32_e32 v41, 16, v66
	v_and_b32_e32 v42, 0xffff0000, v66
	v_mul_f32_e32 v36, v36, v40
	v_add_f32_e32 v40, 1.0, v43
	v_mul_f32_e32 v41, 0xbfb8aa3b, v41
	v_mul_f32_e32 v42, 0xbfb8aa3b, v42
	v_rcp_f32_e32 v40, v40
	v_exp_f32_e32 v41, v41
	v_exp_f32_e32 v42, v42
	v_and_b32_e32 v43, 0xffff0000, v67
	v_mul_f32_e32 v39, v39, v40
	v_add_f32_e32 v40, 1.0, v41
	v_add_f32_e32 v41, 1.0, v42
	v_lshlrev_b32_e32 v42, 16, v67
	v_mul_f32_e32 v42, 0xbfb8aa3b, v42
	v_mul_f32_e32 v43, 0xbfb8aa3b, v43
	v_exp_f32_e32 v42, v42
	v_exp_f32_e32 v43, v43
	v_rcp_f32_e32 v40, v40
	v_rcp_f32_e32 v41, v41
	v_add_f32_e32 v42, 1.0, v42
	v_add_f32_e32 v43, 1.0, v43
	v_rcp_f32_e32 v42, v42
	v_rcp_f32_e32 v43, v43
	v_mul_f32_e32 v40, v32, v40
	v_mul_f32_e32 v41, v33, v41
	v_mul_f32_e32 v42, v34, v42
	v_mul_f32_e32 v35, v35, v43
	v_cvt_pk_bf16_f32 v32, v36, v37
	v_cvt_pk_bf16_f32 v33, v38, v39
	v_cvt_pk_bf16_f32 v34, v40, v41
	v_add_u32_e32 v40, 0xb0, v130
	v_cvt_pk_bf16_f32 v35, v42, v35
	global_store_dwordx4 v[58:59], v[32:35], off offset:256
	v_lshlrev_b32_e32 v46, 16, v53
	v_lshlrev_b32_e32 v44, 16, v52
	v_mad_i64_i32 v[32:33], s[6:7], v40, s51, v[132:133]
	v_lshl_add_u64 v[32:33], v[32:33], 0, v[128:129]
	global_load_dwordx4 v[36:39], v[32:33], off
	s_nop 0
	global_load_dwordx4 v[32:35], v[32:33], off offset:256
	v_mul_f32_e32 v45, 0xbfb8aa3b, v45
	v_mul_f32_e32 v46, 0xbfb8aa3b, v46
	v_mul_f32_e32 v44, 0xbfb8aa3b, v44
	v_exp_f32_e32 v45, v45
	v_exp_f32_e32 v46, v46
	v_exp_f32_e32 v44, v44
	v_and_b32_e32 v47, 0xffff0000, v53
	v_add_f32_e32 v45, 1.0, v45
	v_add_f32_e32 v46, 1.0, v46
	v_add_f32_e32 v44, 1.0, v44
	v_rcp_f32_e32 v45, v45
	v_rcp_f32_e32 v46, v46
	v_mul_f32_e32 v47, 0xbfb8aa3b, v47
	v_rcp_f32_e32 v44, v44
	v_exp_f32_e32 v47, v47
	v_mul_f32_e32 v29, v29, v45
	v_mul_f32_e32 v30, v30, v46
	v_lshlrev_b32_e32 v45, 16, v54
	v_and_b32_e32 v46, 0xffff0000, v54
	v_mul_f32_e32 v28, v28, v44
	v_add_f32_e32 v44, 1.0, v47
	v_mul_f32_e32 v45, 0xbfb8aa3b, v45
	v_mul_f32_e32 v46, 0xbfb8aa3b, v46
	v_rcp_f32_e32 v44, v44
	v_exp_f32_e32 v45, v45
	v_exp_f32_e32 v46, v46
	v_and_b32_e32 v47, 0xffff0000, v55
	v_mul_f32_e32 v31, v31, v44
	v_add_f32_e32 v44, 1.0, v45
	v_add_f32_e32 v45, 1.0, v46
	v_lshlrev_b32_e32 v46, 16, v55
	v_mul_f32_e32 v46, 0xbfb8aa3b, v46
	v_mul_f32_e32 v47, 0xbfb8aa3b, v47
	v_exp_f32_e32 v46, v46
	v_exp_f32_e32 v47, v47
	v_rcp_f32_e32 v44, v44
	v_rcp_f32_e32 v45, v45
	v_add_f32_e32 v46, 1.0, v46
	v_add_f32_e32 v47, 1.0, v47
	v_rcp_f32_e32 v46, v46
	v_rcp_f32_e32 v47, v47
	v_lshlrev_b64 v[42:43], 12, v[56:57]
	v_lshl_add_u64 v[42:43], s[2:3], 0, v[42:43]
	v_lshl_add_u64 v[42:43], v[42:43], 0, v[128:129]
	v_mul_f32_e32 v44, v24, v44
	v_mul_f32_e32 v45, v25, v45
	v_mul_f32_e32 v46, v26, v46
	v_mul_f32_e32 v27, v27, v47
	v_cvt_pk_bf16_f32 v24, v28, v29
	v_cvt_pk_bf16_f32 v25, v30, v31
	v_cvt_pk_bf16_f32 v26, v44, v45
	v_cvt_pk_bf16_f32 v27, v46, v27
	global_store_dwordx4 v[42:43], v[24:27], off
	v_ashrrev_i32_e32 v41, 31, v40
	s_mov_b64 s[6:7], -1
	s_waitcnt vmcnt(5)
	v_and_b32_e32 v25, 0xffff0000, v48
	v_lshlrev_b32_e32 v26, 16, v49
	v_lshlrev_b32_e32 v24, 16, v48
	v_mul_f32_e32 v25, 0xbfb8aa3b, v25
	v_mul_f32_e32 v26, 0xbfb8aa3b, v26
	v_mul_f32_e32 v24, 0xbfb8aa3b, v24
	v_exp_f32_e32 v25, v25
	v_exp_f32_e32 v26, v26
	v_exp_f32_e32 v24, v24
	v_and_b32_e32 v27, 0xffff0000, v49
	v_add_f32_e32 v25, 1.0, v25
	v_add_f32_e32 v26, 1.0, v26
	v_add_f32_e32 v24, 1.0, v24
	v_rcp_f32_e32 v25, v25
	v_rcp_f32_e32 v26, v26
	v_mul_f32_e32 v27, 0xbfb8aa3b, v27
	v_rcp_f32_e32 v24, v24
	v_exp_f32_e32 v27, v27
	v_mul_f32_e32 v21, v21, v25
	v_mul_f32_e32 v22, v22, v26
	v_lshlrev_b32_e32 v25, 16, v50
	v_and_b32_e32 v26, 0xffff0000, v50
	v_mul_f32_e32 v20, v20, v24
	v_add_f32_e32 v24, 1.0, v27
	v_mul_f32_e32 v25, 0xbfb8aa3b, v25
	v_mul_f32_e32 v26, 0xbfb8aa3b, v26
	v_rcp_f32_e32 v24, v24
	v_exp_f32_e32 v25, v25
	v_exp_f32_e32 v26, v26
	v_and_b32_e32 v27, 0xffff0000, v51
	v_mul_f32_e32 v23, v23, v24
	v_add_f32_e32 v24, 1.0, v25
	v_add_f32_e32 v25, 1.0, v26
	v_lshlrev_b32_e32 v26, 16, v51
	v_mul_f32_e32 v27, 0xbfb8aa3b, v27
	v_mul_f32_e32 v26, 0xbfb8aa3b, v26
	v_exp_f32_e32 v27, v27
	v_exp_f32_e32 v26, v26
	v_rcp_f32_e32 v24, v24
	v_rcp_f32_e32 v25, v25
	v_add_f32_e32 v27, 1.0, v27
	v_add_f32_e32 v26, 1.0, v26
	v_rcp_f32_e32 v27, v27
	v_rcp_f32_e32 v26, v26
	v_mul_f32_e32 v24, v16, v24
	v_mul_f32_e32 v25, v17, v25
	v_mul_f32_e32 v19, v19, v27
	v_mul_f32_e32 v26, v18, v26
	v_cvt_pk_bf16_f32 v16, v20, v21
	v_cvt_pk_bf16_f32 v17, v22, v23
	v_cvt_pk_bf16_f32 v18, v24, v25
	v_cvt_pk_bf16_f32 v19, v26, v19
	global_store_dwordx4 v[42:43], v[16:19], off offset:256
	s_waitcnt vmcnt(3)
	v_lshlrev_b32_e32 v20, 16, v37
	v_mul_f32_e32 v20, 0xbfb8aa3b, v20
	v_and_b32_e32 v19, 0xffff0000, v36
	v_lshlrev_b32_e32 v18, 16, v36
	v_mul_f32_e32 v19, 0xbfb8aa3b, v19
	v_mul_f32_e32 v18, 0xbfb8aa3b, v18
	v_exp_f32_e32 v19, v19
	v_exp_f32_e32 v20, v20
	v_exp_f32_e32 v18, v18
	v_and_b32_e32 v21, 0xffff0000, v37
	v_add_f32_e32 v19, 1.0, v19
	v_add_f32_e32 v20, 1.0, v20
	v_add_f32_e32 v18, 1.0, v18
	v_rcp_f32_e32 v19, v19
	v_rcp_f32_e32 v20, v20
	v_mul_f32_e32 v21, 0xbfb8aa3b, v21
	v_rcp_f32_e32 v18, v18
	v_exp_f32_e32 v21, v21
	v_mul_f32_e32 v13, v13, v19
	v_mul_f32_e32 v14, v14, v20
	v_lshlrev_b32_e32 v19, 16, v38
	v_and_b32_e32 v20, 0xffff0000, v38
	v_mul_f32_e32 v12, v12, v18
	v_add_f32_e32 v18, 1.0, v21
	v_mul_f32_e32 v19, 0xbfb8aa3b, v19
	v_mul_f32_e32 v20, 0xbfb8aa3b, v20
	v_rcp_f32_e32 v18, v18
	v_exp_f32_e32 v19, v19
	v_exp_f32_e32 v20, v20
	v_and_b32_e32 v21, 0xffff0000, v39
	v_mul_f32_e32 v15, v15, v18
	v_add_f32_e32 v18, 1.0, v19
	v_add_f32_e32 v19, 1.0, v20
	v_lshlrev_b32_e32 v20, 16, v39
	v_mul_f32_e32 v20, 0xbfb8aa3b, v20
	v_mul_f32_e32 v21, 0xbfb8aa3b, v21
	v_exp_f32_e32 v20, v20
	v_exp_f32_e32 v21, v21
	v_rcp_f32_e32 v18, v18
	v_rcp_f32_e32 v19, v19
	v_add_f32_e32 v20, 1.0, v20
	v_add_f32_e32 v21, 1.0, v21
	v_rcp_f32_e32 v20, v20
	v_rcp_f32_e32 v21, v21
	v_lshlrev_b64 v[16:17], 12, v[40:41]
	v_lshl_add_u64 v[16:17], s[2:3], 0, v[16:17]
	v_lshl_add_u64 v[16:17], v[16:17], 0, v[128:129]
	v_mul_f32_e32 v18, v8, v18
	v_mul_f32_e32 v19, v9, v19
	v_mul_f32_e32 v20, v10, v20
	v_mul_f32_e32 v11, v11, v21
	v_cvt_pk_bf16_f32 v8, v12, v13
	v_cvt_pk_bf16_f32 v9, v14, v15
	v_cvt_pk_bf16_f32 v10, v18, v19
	v_cvt_pk_bf16_f32 v11, v20, v11
	global_store_dwordx4 v[16:17], v[8:11], off
	s_waitcnt vmcnt(3)
	s_nop 0
	v_and_b32_e32 v9, 0xffff0000, v32
	v_lshlrev_b32_e32 v10, 16, v33
	v_lshlrev_b32_e32 v8, 16, v32
	v_mul_f32_e32 v9, 0xbfb8aa3b, v9
	v_mul_f32_e32 v10, 0xbfb8aa3b, v10
	v_mul_f32_e32 v8, 0xbfb8aa3b, v8
	v_exp_f32_e32 v9, v9
	v_exp_f32_e32 v10, v10
	v_exp_f32_e32 v8, v8
	v_and_b32_e32 v11, 0xffff0000, v33
	v_add_f32_e32 v9, 1.0, v9
	v_add_f32_e32 v10, 1.0, v10
	v_add_f32_e32 v8, 1.0, v8
	v_rcp_f32_e32 v9, v9
	v_rcp_f32_e32 v10, v10
	v_mul_f32_e32 v11, 0xbfb8aa3b, v11
	v_rcp_f32_e32 v8, v8
	v_exp_f32_e32 v11, v11
	v_mul_f32_e32 v5, v5, v9
	v_mul_f32_e32 v6, v6, v10
	v_lshlrev_b32_e32 v9, 16, v34
	v_and_b32_e32 v10, 0xffff0000, v34
	v_mul_f32_e32 v4, v4, v8
	v_add_f32_e32 v8, 1.0, v11
	v_mul_f32_e32 v9, 0xbfb8aa3b, v9
	v_mul_f32_e32 v10, 0xbfb8aa3b, v10
	v_rcp_f32_e32 v8, v8
	v_exp_f32_e32 v9, v9
	v_exp_f32_e32 v10, v10
	v_and_b32_e32 v11, 0xffff0000, v35
	v_mul_f32_e32 v7, v7, v8
	v_add_f32_e32 v8, 1.0, v9
	v_add_f32_e32 v9, 1.0, v10
	v_lshlrev_b32_e32 v10, 16, v35
	v_mul_f32_e32 v11, 0xbfb8aa3b, v11
	v_mul_f32_e32 v10, 0xbfb8aa3b, v10
	v_exp_f32_e32 v11, v11
	v_exp_f32_e32 v10, v10
	v_rcp_f32_e32 v8, v8
	v_rcp_f32_e32 v9, v9
	v_add_f32_e32 v11, 1.0, v11
	v_add_f32_e32 v10, 1.0, v10
	v_rcp_f32_e32 v11, v11
	v_rcp_f32_e32 v10, v10
	v_mul_f32_e32 v8, v0, v8
	v_mul_f32_e32 v9, v1, v9
	v_mul_f32_e32 v3, v3, v11
	v_mul_f32_e32 v10, v2, v10
	v_cvt_pk_bf16_f32 v0, v4, v5
	v_cvt_pk_bf16_f32 v1, v6, v7
	v_cvt_pk_bf16_f32 v2, v8, v9
	v_cvt_pk_bf16_f32 v3, v10, v3
	global_store_dwordx4 v[16:17], v[0:3], off offset:256
	s_cbranch_vccnz .LBB0_2171
	s_andn2_b64 vcc, exec, s[0:1]
	s_cbranch_vccnz .LBB0_2170
	s_barrier
	s_branch .LBB0_2170

.LBB0_2203:
	s_lshl_b32 s6, s58, 8
	v_mbcnt_lo_u32_b32 v128, -1, 0
	v_mbcnt_hi_u32_b32 v128, -1, v128
	s_add_i32 s6, s6, s47
	v_and_or_b32 v146, v128, 15, s6
	s_lshl_b32 s6, s57, 8
	v_ashrrev_i32_e32 v128, 1, v128
	s_or_b32 s6, s6, s48
	v_and_b32_e32 v128, -8, v128
	v_add_u32_e32 v144, s6, v128
	v_mov_b64_e32 v[150:151], s[14:15]
	v_ashrrev_i32_e32 v145, 31, v144
	v_mad_i64_i32 v[128:129], s[6:7], v146, s53, v[150:151]
	v_lshlrev_b64 v[148:149], 1, v[144:145]
	v_lshl_add_u64 v[128:129], v[128:129], 0, v[148:149]
	global_load_dwordx4 v[138:141], v[128:129], off
	global_load_dwordx4 v[164:167], v[128:129], off offset:256
	v_ashrrev_i32_e32 v147, 31, v146
	v_lshlrev_b64 v[130:131], 12, v[146:147]
	v_lshl_add_u64 v[130:131], s[12:13], 0, v[130:131]
	v_lshl_add_u64 v[130:131], v[130:131], 0, v[148:149]
	global_load_dwordx4 v[160:163], v[130:131], off
	v_mul_f32_e32 v174, s18, v120
	v_mul_f32_e32 v175, s18, v121
	v_or_b32_e32 v120, 16, v146
	v_mul_f32_e32 v172, s18, v122
	v_mul_f32_e32 v173, s18, v123
	v_mad_i64_i32 v[122:123], s[6:7], v120, s53, v[150:151]
	v_mul_f32_e32 v142, s18, v126
	v_mul_f32_e32 v143, s18, v127
	v_mul_f32_e32 v154, s18, v124
	v_mul_f32_e32 v155, s18, v125
	v_lshl_add_u64 v[122:123], v[122:123], 0, v[148:149]
	global_load_dwordx4 v[168:171], v[130:131], off offset:256
	global_load_dwordx4 v[132:135], v[122:123], off
	global_load_dwordx4 v[124:127], v[122:123], off offset:256
	v_ashrrev_i32_e32 v121, 31, v120
	v_lshlrev_b64 v[152:153], 11, v[120:121]
	v_lshlrev_b64 v[120:121], 12, v[120:121]
	v_lshl_add_u64 v[120:121], s[12:13], 0, v[120:121]
	v_lshl_add_u64 v[120:121], v[120:121], 0, v[148:149]
	global_load_dwordx4 v[128:131], v[120:121], off
	s_nop 0
	global_load_dwordx4 v[120:123], v[120:121], off offset:256
	v_lshlrev_b64 v[136:137], 11, v[146:147]
	v_mul_f32_e32 v116, s18, v116
	v_mul_f32_e32 v117, s18, v117
	v_mul_f32_e32 v118, s18, v118
	v_mul_f32_e32 v119, s18, v119
	v_mul_f32_e32 v112, s18, v112
	v_mul_f32_e32 v113, s18, v113
	v_mul_f32_e32 v114, s18, v114
	v_mul_f32_e32 v115, s18, v115
	v_mul_f32_e32 v108, s18, v108
	v_mul_f32_e32 v109, s18, v109
	v_mul_f32_e32 v110, s18, v110
	v_mul_f32_e32 v111, s18, v111
	v_mul_f32_e32 v104, s18, v104
	v_mul_f32_e32 v105, s18, v105
	v_mul_f32_e32 v106, s18, v106
	v_mul_f32_e32 v107, s18, v107
	v_mul_f32_e32 v100, s18, v100
	v_mul_f32_e32 v101, s18, v101
	v_mul_f32_e32 v102, s18, v102
	v_mul_f32_e32 v103, s18, v103
	v_mul_f32_e32 v96, s18, v96
	v_mul_f32_e32 v97, s18, v97
	v_mul_f32_e32 v92, s18, v92
	v_mul_f32_e32 v93, s18, v93
	v_mul_f32_e32 v98, s18, v98
	v_mul_f32_e32 v99, s18, v99
	v_mul_f32_e32 v94, s18, v94
	v_mul_f32_e32 v95, s18, v95
	v_mul_f32_e32 v88, s18, v88
	v_mul_f32_e32 v89, s18, v89
	v_mul_f32_e32 v90, s18, v90
	v_mul_f32_e32 v91, s18, v91
	v_mul_f32_e32 v84, s18, v84
	v_mul_f32_e32 v85, s18, v85
	v_mul_f32_e32 v86, s18, v86
	v_mul_f32_e32 v87, s18, v87
	v_mul_f32_e32 v80, s18, v80
	v_mul_f32_e32 v81, s18, v81
	v_mul_f32_e32 v82, s18, v82
	v_mul_f32_e32 v83, s18, v83
	v_mul_f32_e32 v76, s18, v76
	v_mul_f32_e32 v77, s18, v77
	v_mul_f32_e32 v78, s18, v78
	v_mul_f32_e32 v79, s18, v79
	v_mul_f32_e32 v72, s18, v72
	v_mul_f32_e32 v73, s18, v73
	v_mul_f32_e32 v74, s18, v74
	v_mul_f32_e32 v75, s18, v75
	v_mul_f32_e32 v68, s18, v68
	v_mul_f32_e32 v69, s18, v69
	v_mul_f32_e32 v70, s18, v70
	v_mul_f32_e32 v71, s18, v71
	v_mul_f32_e32 v64, s18, v64
	v_mul_f32_e32 v65, s18, v65
	v_mul_f32_e32 v66, s18, v66
	v_mul_f32_e32 v67, s18, v67
	v_mul_f32_e32 v60, s18, v60
	v_mul_f32_e32 v61, s18, v61
	v_mul_f32_e32 v62, s18, v62
	v_mul_f32_e32 v63, s18, v63
	v_mul_f32_e32 v56, s18, v56
	v_mul_f32_e32 v57, s18, v57
	v_mul_f32_e32 v58, s18, v58
	v_mul_f32_e32 v59, s18, v59
	v_mul_f32_e32 v52, s18, v52
	v_mul_f32_e32 v53, s18, v53
	v_mul_f32_e32 v54, s18, v54
	v_mul_f32_e32 v55, s18, v55
	v_mul_f32_e32 v48, s18, v48
	v_mul_f32_e32 v49, s18, v49
	v_mul_f32_e32 v50, s18, v50
	v_mul_f32_e32 v51, s18, v51
	v_mul_f32_e32 v44, s18, v44
	v_mul_f32_e32 v45, s18, v45
	v_mul_f32_e32 v46, s18, v46
	v_mul_f32_e32 v47, s18, v47
	v_mul_f32_e32 v40, s18, v40
	v_mul_f32_e32 v41, s18, v41
	v_mul_f32_e32 v42, s18, v42
	v_mul_f32_e32 v43, s18, v43
	v_mul_f32_e32 v36, s18, v36
	v_mul_f32_e32 v37, s18, v37
	v_mul_f32_e32 v38, s18, v38
	v_mul_f32_e32 v39, s18, v39
	v_mul_f32_e32 v32, s18, v32
	v_mul_f32_e32 v33, s18, v33
	v_mul_f32_e32 v28, s18, v28
	v_mul_f32_e32 v29, s18, v29
	v_mul_f32_e32 v34, s18, v34
	v_mul_f32_e32 v35, s18, v35
	v_mul_f32_e32 v30, s18, v30
	v_mul_f32_e32 v31, s18, v31
	v_mul_f32_e32 v24, s18, v24
	v_mul_f32_e32 v25, s18, v25
	v_mul_f32_e32 v26, s18, v26
	v_mul_f32_e32 v27, s18, v27
	v_mul_f32_e32 v20, s18, v20
	v_mul_f32_e32 v21, s18, v21
	v_mul_f32_e32 v22, s18, v22
	v_mul_f32_e32 v23, s18, v23
	v_mul_f32_e32 v16, s18, v16
	v_mul_f32_e32 v17, s18, v17
	v_mul_f32_e32 v18, s18, v18
	v_mul_f32_e32 v19, s18, v19
	v_mul_f32_e32 v12, s18, v12
	v_mul_f32_e32 v13, s18, v13
	v_mul_f32_e32 v14, s18, v14
	v_mul_f32_e32 v15, s18, v15
	v_mul_f32_e32 v8, s18, v8
	v_mul_f32_e32 v9, s18, v9
	v_mul_f32_e32 v10, s18, v10
	v_mul_f32_e32 v11, s18, v11
	v_mul_f32_e32 v4, s18, v4
	v_mul_f32_e32 v5, s18, v5
	s_waitcnt vmcnt(7)
	v_lshlrev_b32_e32 v147, 16, v138
	v_and_b32_e32 v138, 0xffff0000, v138
	v_lshlrev_b32_e32 v176, 16, v139
	v_and_b32_e32 v139, 0xffff0000, v139
	v_lshlrev_b32_e32 v178, 16, v140
	v_and_b32_e32 v140, 0xffff0000, v140
	v_mul_f32_e32 v147, 0xbfb8aa3b, v147
	v_mul_f32_e32 v138, 0xbfb8aa3b, v138
	v_mul_f32_e32 v139, 0xbfb8aa3b, v139
	v_mul_f32_e32 v178, 0xbfb8aa3b, v178
	v_mul_f32_e32 v140, 0xbfb8aa3b, v140
	v_exp_f32_e32 v147, v147
	v_exp_f32_e32 v138, v138
	v_exp_f32_e32 v139, v139
	v_exp_f32_e32 v178, v178
	v_exp_f32_e32 v140, v140
	v_lshlrev_b32_e32 v180, 16, v141
	v_and_b32_e32 v141, 0xffff0000, v141
	v_mul_f32_e32 v180, 0xbfb8aa3b, v180
	v_mul_f32_e32 v141, 0xbfb8aa3b, v141
	v_add_f32_e32 v147, 1.0, v147
	v_add_f32_e32 v138, 1.0, v138
	v_exp_f32_e32 v180, v180
	v_exp_f32_e32 v141, v141
	v_add_f32_e32 v139, 1.0, v139
	v_add_f32_e32 v178, 1.0, v178
	v_add_f32_e32 v140, 1.0, v140
	v_rcp_f32_e32 v147, v147
	v_rcp_f32_e32 v138, v138
	v_rcp_f32_e32 v139, v139
	v_rcp_f32_e32 v178, v178
	v_rcp_f32_e32 v140, v140
	s_waitcnt vmcnt(5)
	v_lshlrev_b32_e32 v159, 16, v160
	v_and_b32_e32 v160, 0xffff0000, v160
	v_lshlrev_b32_e32 v177, 16, v161
	v_and_b32_e32 v161, 0xffff0000, v161
	v_lshlrev_b32_e32 v179, 16, v162
	v_and_b32_e32 v162, 0xffff0000, v162
	v_add_f32_e32 v180, 1.0, v180
	v_fmac_f32_e32 v159, v154, v147
	v_fmac_f32_e32 v160, v155, v138
	v_add_f32_e32 v138, 1.0, v141
	v_rcp_f32_e32 v180, v180
	v_fmac_f32_e32 v161, v143, v139
	v_fmac_f32_e32 v179, v174, v178
	v_fmac_f32_e32 v162, v175, v140
	v_mul_f32_e32 v139, 0x41800000, v159
	v_mul_f32_e32 v140, 0x41800000, v160
	v_rcp_f32_e32 v141, v138
	v_mov_b32_e32 v138, 0
	v_mul_f32_e32 v147, 0x41800000, v179
	v_mul_f32_e32 v154, 0x41800000, v162
	v_cvt_pk_fp8_f32 v138, v139, v140
	v_mov_b32_e32 v139, 0
	v_cvt_pk_fp8_f32 v139, v147, v154
	v_lshlrev_b32_e32 v181, 16, v163
	v_and_b32_e32 v159, 0xffff0000, v163
	v_mul_f32_e32 v176, 0xbfb8aa3b, v176
	v_fmac_f32_e32 v181, v172, v180
	v_fmac_f32_e32 v159, v173, v141
	v_exp_f32_e32 v176, v176
	v_mul_f32_e32 v155, 0x41800000, v181
	v_mul_f32_e32 v140, 0x41800000, v159
	v_cvt_pk_fp8_f32 v139, v155, v140 op_sel:[0,0,1]
	v_lshlrev_b32_e32 v140, 16, v164
	v_mul_f32_e32 v140, 0xbfb8aa3b, v140
	v_exp_f32_e32 v140, v140
	v_add_f32_e32 v176, 1.0, v176
	v_rcp_f32_e32 v176, v176
	v_and_b32_e32 v141, 0xffff0000, v164
	v_add_f32_e32 v140, 1.0, v140
	v_mul_f32_e32 v141, 0xbfb8aa3b, v141
	v_rcp_f32_e32 v140, v140
	v_exp_f32_e32 v141, v141
	v_fmac_f32_e32 v177, v142, v176
	v_mul_f32_e32 v142, 0x41800000, v177
	v_mul_f32_e32 v143, 0x41800000, v161
	v_cvt_pk_fp8_f32 v138, v142, v143 op_sel:[0,0,1]
	s_waitcnt vmcnt(4)
	v_lshlrev_b32_e32 v142, 16, v168
	v_fmac_f32_e32 v142, v116, v140
	v_add_f32_e32 v140, 1.0, v141
	v_lshlrev_b32_e32 v141, 16, v165
	v_mul_f32_e32 v141, 0xbfb8aa3b, v141
	v_rcp_f32_e32 v140, v140
	v_exp_f32_e32 v141, v141
	v_mul_f32_e32 v116, 0x41800000, v142
	v_and_b32_e32 v142, 0xffff0000, v168
	v_fmac_f32_e32 v142, v117, v140
	v_add_f32_e32 v140, 1.0, v141
	v_and_b32_e32 v141, 0xffff0000, v165
	v_mul_f32_e32 v141, 0xbfb8aa3b, v141
	v_rcp_f32_e32 v140, v140
	v_exp_f32_e32 v141, v141
	v_mul_f32_e32 v117, 0x41800000, v142
	v_lshlrev_b32_e32 v142, 16, v169
	v_fmac_f32_e32 v142, v118, v140
	v_add_f32_e32 v140, 1.0, v141
	v_lshlrev_b32_e32 v141, 16, v166
	v_mul_f32_e32 v141, 0xbfb8aa3b, v141
	v_rcp_f32_e32 v140, v140
	v_exp_f32_e32 v141, v141
	v_mul_f32_e32 v118, 0x41800000, v142
	v_and_b32_e32 v142, 0xffff0000, v169
	v_fmac_f32_e32 v142, v119, v140
	v_add_f32_e32 v140, 1.0, v141
	v_and_b32_e32 v141, 0xffff0000, v166
	v_mul_f32_e32 v141, 0xbfb8aa3b, v141
	v_rcp_f32_e32 v140, v140
	v_exp_f32_e32 v141, v141
	v_mul_f32_e32 v119, 0x41800000, v142
	v_lshlrev_b32_e32 v142, 16, v170
	v_fmac_f32_e32 v142, v112, v140
	v_add_f32_e32 v112, 1.0, v141
	v_lshlrev_b32_e32 v141, 16, v167
	v_rcp_f32_e32 v112, v112
	v_mul_f32_e32 v141, 0xbfb8aa3b, v141
	v_exp_f32_e32 v141, v141
	v_mul_f32_e32 v140, 0x41800000, v142
	v_and_b32_e32 v142, 0xffff0000, v170
	v_fmac_f32_e32 v142, v113, v112
	v_and_b32_e32 v113, 0xffff0000, v167
	v_add_f32_e32 v112, 1.0, v141
	v_mul_f32_e32 v113, 0xbfb8aa3b, v113
	v_rcp_f32_e32 v112, v112
	v_exp_f32_e32 v113, v113
	v_lshlrev_b32_e32 v141, 16, v171
	v_mul_f32_e32 v142, 0x41800000, v142
	v_fmac_f32_e32 v141, v114, v112
	v_add_f32_e32 v112, 1.0, v113
	v_mul_f32_e32 v114, 0x41800000, v141
	v_rcp_f32_e32 v141, v112
	v_mov_b32_e32 v112, 0
	v_mov_b32_e32 v113, 0
	v_cvt_pk_fp8_f32 v112, v116, v117
	v_cvt_pk_fp8_f32 v113, v140, v142
	v_and_b32_e32 v143, 0xffff0000, v171
	s_waitcnt vmcnt(3)
	v_lshlrev_b32_e32 v147, 16, v132
	v_fmac_f32_e32 v143, v115, v141
	v_mul_f32_e32 v147, 0xbfb8aa3b, v147
	v_mul_f32_e32 v115, 0x41800000, v143
	v_exp_f32_e32 v147, v147
	v_cvt_pk_fp8_f32 v112, v118, v119 op_sel:[0,0,1]
	v_cvt_pk_fp8_f32 v113, v114, v115 op_sel:[0,0,1]
	v_lshl_add_u64 v[114:115], s[2:3], 0, v[136:137]
	v_lshl_add_u64 v[114:115], v[114:115], 0, v[144:145]
	v_and_b32_e32 v132, 0xffff0000, v132
	global_store_dwordx2 v[114:115], v[138:139], off
	global_store_dwordx2 v[114:115], v[112:113], off offset:128
	v_or_b32_e32 v112, 32, v146
	v_add_f32_e32 v147, 1.0, v147
	v_mul_f32_e32 v132, 0xbfb8aa3b, v132
	v_mad_i64_i32 v[114:115], s[6:7], v112, s53, v[150:151]
	v_rcp_f32_e32 v147, v147
	v_exp_f32_e32 v132, v132
	v_lshl_add_u64 v[114:115], v[114:115], 0, v[148:149]
	global_load_dwordx4 v[140:143], v[114:115], off
	global_load_dwordx4 v[116:119], v[114:115], off offset:256
	s_waitcnt vmcnt(5)
	v_lshlrev_b32_e32 v159, 16, v128
	v_fmac_f32_e32 v159, v108, v147
	v_add_f32_e32 v132, 1.0, v132
	v_lshlrev_b32_e32 v147, 16, v133
	v_rcp_f32_e32 v132, v132
	v_mul_f32_e32 v147, 0xbfb8aa3b, v147
	v_exp_f32_e32 v147, v147
	v_ashrrev_i32_e32 v113, 31, v112
	v_and_b32_e32 v128, 0xffff0000, v128
	v_lshlrev_b64 v[154:155], 11, v[112:113]
	v_lshlrev_b64 v[112:113], 12, v[112:113]
	v_fmac_f32_e32 v128, v109, v132
	v_and_b32_e32 v132, 0xffff0000, v133
	v_lshl_add_u64 v[112:113], s[12:13], 0, v[112:113]
	v_mul_f32_e32 v109, 0x41800000, v128
	v_add_f32_e32 v128, 1.0, v147
	v_mul_f32_e32 v132, 0xbfb8aa3b, v132
	v_lshl_add_u64 v[112:113], v[112:113], 0, v[148:149]
	v_rcp_f32_e32 v128, v128
	v_exp_f32_e32 v132, v132
	global_load_dwordx4 v[136:139], v[112:113], off
	s_nop 0
	global_load_dwordx4 v[112:115], v[112:113], off offset:256
	v_lshlrev_b32_e32 v133, 16, v129
	v_fmac_f32_e32 v133, v110, v128
	v_add_f32_e32 v128, 1.0, v132
	v_rcp_f32_e32 v128, v128
	v_lshlrev_b32_e32 v132, 16, v134
	v_mul_f32_e32 v132, 0xbfb8aa3b, v132
	v_exp_f32_e32 v132, v132
	v_and_b32_e32 v129, 0xffff0000, v129
	v_fmac_f32_e32 v129, v111, v128
	v_mul_f32_e32 v111, 0x41800000, v129
	v_and_b32_e32 v129, 0xffff0000, v134
	v_add_f32_e32 v128, 1.0, v132
	v_mul_f32_e32 v129, 0xbfb8aa3b, v129
	v_rcp_f32_e32 v128, v128
	v_exp_f32_e32 v129, v129
	v_lshlrev_b32_e32 v132, 16, v130
	v_and_b32_e32 v130, 0xffff0000, v130
	v_fmac_f32_e32 v132, v104, v128
	v_add_f32_e32 v104, 1.0, v129
	v_lshlrev_b32_e32 v129, 16, v135
	v_rcp_f32_e32 v104, v104
	v_mul_f32_e32 v129, 0xbfb8aa3b, v129
	v_exp_f32_e32 v129, v129
	v_mul_f32_e32 v128, 0x41800000, v132
	v_fmac_f32_e32 v130, v105, v104
	v_and_b32_e32 v105, 0xffff0000, v135
	v_add_f32_e32 v104, 1.0, v129
	v_mul_f32_e32 v105, 0xbfb8aa3b, v105
	v_rcp_f32_e32 v104, v104
	v_exp_f32_e32 v105, v105
	v_lshlrev_b32_e32 v129, 16, v131
	v_mul_f32_e32 v130, 0x41800000, v130
	v_fmac_f32_e32 v129, v106, v104
	v_add_f32_e32 v104, 1.0, v105
	v_mul_f32_e32 v106, 0x41800000, v129
	v_rcp_f32_e32 v129, v104
	v_mov_b32_e32 v105, 0
	v_cvt_pk_fp8_f32 v105, v128, v130
	v_and_b32_e32 v131, 0xffff0000, v131
	v_fmac_f32_e32 v131, v107, v129
	v_mul_f32_e32 v107, 0x41800000, v131
	v_cvt_pk_fp8_f32 v105, v106, v107 op_sel:[0,0,1]
	v_lshlrev_b32_e32 v106, 16, v124
	v_mul_f32_e32 v106, 0xbfb8aa3b, v106
	v_exp_f32_e32 v106, v106
	v_and_b32_e32 v107, 0xffff0000, v124
	v_mul_f32_e32 v107, 0xbfb8aa3b, v107
	v_exp_f32_e32 v107, v107
	v_add_f32_e32 v106, 1.0, v106
	v_rcp_f32_e32 v106, v106
	v_mul_f32_e32 v108, 0x41800000, v159
	v_mov_b32_e32 v104, 0
	v_cvt_pk_fp8_f32 v104, v108, v109
	s_waitcnt vmcnt(6)
	v_lshlrev_b32_e32 v108, 16, v120
	v_fmac_f32_e32 v108, v100, v106
	v_add_f32_e32 v106, 1.0, v107
	v_lshlrev_b32_e32 v107, 16, v125
	v_mul_f32_e32 v107, 0xbfb8aa3b, v107
	v_rcp_f32_e32 v106, v106
	v_exp_f32_e32 v107, v107
	v_mul_f32_e32 v100, 0x41800000, v108
	v_and_b32_e32 v108, 0xffff0000, v120
	v_fmac_f32_e32 v108, v101, v106
	v_add_f32_e32 v106, 1.0, v107
	v_and_b32_e32 v107, 0xffff0000, v125
	v_mul_f32_e32 v107, 0xbfb8aa3b, v107
	v_rcp_f32_e32 v106, v106
	v_exp_f32_e32 v107, v107
	v_mul_f32_e32 v101, 0x41800000, v108
	v_lshlrev_b32_e32 v108, 16, v121
	v_fmac_f32_e32 v108, v102, v106
	v_add_f32_e32 v106, 1.0, v107
	v_lshlrev_b32_e32 v107, 16, v126
	v_mul_f32_e32 v107, 0xbfb8aa3b, v107
	v_rcp_f32_e32 v106, v106
	v_exp_f32_e32 v107, v107
	v_mul_f32_e32 v102, 0x41800000, v108
	v_and_b32_e32 v108, 0xffff0000, v121
	v_fmac_f32_e32 v108, v103, v106
	v_add_f32_e32 v106, 1.0, v107
	v_and_b32_e32 v107, 0xffff0000, v126
	v_mul_f32_e32 v107, 0xbfb8aa3b, v107
	v_rcp_f32_e32 v106, v106
	v_exp_f32_e32 v107, v107
	v_mul_f32_e32 v103, 0x41800000, v108
	v_lshlrev_b32_e32 v108, 16, v122
	v_fmac_f32_e32 v108, v96, v106
	v_add_f32_e32 v96, 1.0, v107
	v_lshlrev_b32_e32 v107, 16, v127
	v_mul_f32_e32 v106, 0x41800000, v108
	v_mul_f32_e32 v107, 0xbfb8aa3b, v107
	v_and_b32_e32 v108, 0xffff0000, v122
	s_waitcnt vmcnt(3)
	v_lshlrev_b32_e32 v122, 16, v140
	v_rcp_f32_e32 v96, v96
	v_exp_f32_e32 v107, v107
	v_mul_f32_e32 v122, 0xbfb8aa3b, v122
	v_exp_f32_e32 v122, v122
	v_fmac_f32_e32 v108, v97, v96
	v_add_f32_e32 v96, 1.0, v107
	v_lshlrev_b32_e32 v107, 16, v123
	v_and_b32_e32 v109, 0xffff0000, v123
	v_and_b32_e32 v123, 0xffff0000, v140
	v_and_b32_e32 v97, 0xffff0000, v127
	v_add_f32_e32 v122, 1.0, v122
	v_mul_f32_e32 v123, 0xbfb8aa3b, v123
	v_mul_f32_e32 v97, 0xbfb8aa3b, v97
	v_rcp_f32_e32 v122, v122
	v_exp_f32_e32 v123, v123
	v_rcp_f32_e32 v96, v96
	v_exp_f32_e32 v97, v97
	s_waitcnt vmcnt(1)
	v_lshlrev_b32_e32 v124, 16, v136
	v_fmac_f32_e32 v124, v92, v122
	v_add_f32_e32 v122, 1.0, v123
	v_lshlrev_b32_e32 v123, 16, v141
	v_fmac_f32_e32 v107, v98, v96
	v_add_f32_e32 v96, 1.0, v97
	v_mul_f32_e32 v123, 0xbfb8aa3b, v123
	v_mul_f32_e32 v98, 0x41800000, v107
	v_rcp_f32_e32 v107, v96
	v_rcp_f32_e32 v122, v122
	v_exp_f32_e32 v123, v123
	v_mul_f32_e32 v108, 0x41800000, v108
	v_mov_b32_e32 v96, 0
	v_mov_b32_e32 v97, 0
	v_cvt_pk_fp8_f32 v96, v100, v101
	v_cvt_pk_fp8_f32 v97, v106, v108
	v_mul_f32_e32 v92, 0x41800000, v124
	v_and_b32_e32 v124, 0xffff0000, v136
	v_mul_f32_e32 v110, 0x41800000, v133
	v_fmac_f32_e32 v109, v99, v107
	v_fmac_f32_e32 v124, v93, v122
	v_add_f32_e32 v122, 1.0, v123
	v_and_b32_e32 v123, 0xffff0000, v141
	v_cvt_pk_fp8_f32 v104, v110, v111 op_sel:[0,0,1]
	v_mul_f32_e32 v99, 0x41800000, v109
	v_mul_f32_e32 v123, 0xbfb8aa3b, v123
	v_cvt_pk_fp8_f32 v96, v102, v103 op_sel:[0,0,1]
	v_cvt_pk_fp8_f32 v97, v98, v99 op_sel:[0,0,1]
	v_rcp_f32_e32 v122, v122
	v_exp_f32_e32 v123, v123
	v_lshl_add_u64 v[98:99], s[2:3], 0, v[152:153]
	v_lshl_add_u64 v[98:99], v[98:99], 0, v[144:145]
	global_store_dwordx2 v[98:99], v[104:105], off
	global_store_dwordx2 v[98:99], v[96:97], off offset:128
	v_or_b32_e32 v96, 48, v146
	v_mul_f32_e32 v93, 0x41800000, v124
	v_lshlrev_b32_e32 v124, 16, v137
	v_mad_i64_i32 v[98:99], s[6:7], v96, s53, v[150:151]
	v_fmac_f32_e32 v124, v94, v122
	v_add_f32_e32 v122, 1.0, v123
	v_lshlrev_b32_e32 v123, 16, v142
	v_lshl_add_u64 v[98:99], v[98:99], 0, v[148:149]
	v_mul_f32_e32 v123, 0xbfb8aa3b, v123
	global_load_dwordx4 v[108:111], v[98:99], off
	global_load_dwordx4 v[100:103], v[98:99], off offset:256
	v_rcp_f32_e32 v122, v122
	v_exp_f32_e32 v123, v123
	v_mul_f32_e32 v94, 0x41800000, v124
	v_and_b32_e32 v124, 0xffff0000, v137
	v_fmac_f32_e32 v124, v95, v122
	v_add_f32_e32 v122, 1.0, v123
	v_and_b32_e32 v123, 0xffff0000, v142
	v_mul_f32_e32 v123, 0xbfb8aa3b, v123
	v_ashrrev_i32_e32 v97, 31, v96
	v_rcp_f32_e32 v122, v122
	v_exp_f32_e32 v123, v123
	v_lshlrev_b64 v[120:121], 11, v[96:97]
	v_lshlrev_b64 v[96:97], 12, v[96:97]
	v_lshl_add_u64 v[96:97], s[12:13], 0, v[96:97]
	v_lshl_add_u64 v[96:97], v[96:97], 0, v[148:149]
	v_mul_f32_e32 v95, 0x41800000, v124
	v_lshlrev_b32_e32 v124, 16, v138
	global_load_dwordx4 v[104:107], v[96:97], off
	s_nop 0
	global_load_dwordx4 v[96:99], v[96:97], off offset:256
	v_fmac_f32_e32 v124, v88, v122
	v_add_f32_e32 v88, 1.0, v123
	v_lshlrev_b32_e32 v123, 16, v143
	v_rcp_f32_e32 v88, v88
	v_mul_f32_e32 v123, 0xbfb8aa3b, v123
	v_exp_f32_e32 v123, v123
	v_mul_f32_e32 v122, 0x41800000, v124
	v_and_b32_e32 v124, 0xffff0000, v138
	v_fmac_f32_e32 v124, v89, v88
	v_and_b32_e32 v89, 0xffff0000, v143
	v_add_f32_e32 v88, 1.0, v123
	v_mul_f32_e32 v89, 0xbfb8aa3b, v89
	v_rcp_f32_e32 v88, v88
	v_exp_f32_e32 v89, v89
	v_lshlrev_b32_e32 v123, 16, v139
	v_mul_f32_e32 v124, 0x41800000, v124
	v_fmac_f32_e32 v123, v90, v88
	v_add_f32_e32 v88, 1.0, v89
	v_mul_f32_e32 v90, 0x41800000, v123
	v_rcp_f32_e32 v123, v88
	v_mov_b32_e32 v89, 0
	v_cvt_pk_fp8_f32 v89, v122, v124
	v_and_b32_e32 v125, 0xffff0000, v139
	v_fmac_f32_e32 v125, v91, v123
	v_mul_f32_e32 v91, 0x41800000, v125
	v_cvt_pk_fp8_f32 v89, v90, v91 op_sel:[0,0,1]
	v_lshlrev_b32_e32 v90, 16, v116
	v_mul_f32_e32 v90, 0xbfb8aa3b, v90
	v_exp_f32_e32 v90, v90
	v_and_b32_e32 v91, 0xffff0000, v116
	v_mul_f32_e32 v91, 0xbfb8aa3b, v91
	v_exp_f32_e32 v91, v91
	v_add_f32_e32 v90, 1.0, v90
	v_rcp_f32_e32 v90, v90
	v_mov_b32_e32 v88, 0
	v_cvt_pk_fp8_f32 v88, v92, v93
	s_waitcnt vmcnt(6)
	v_lshlrev_b32_e32 v92, 16, v112
	v_fmac_f32_e32 v92, v84, v90
	v_add_f32_e32 v90, 1.0, v91
	v_lshlrev_b32_e32 v91, 16, v117
	v_mul_f32_e32 v91, 0xbfb8aa3b, v91
	v_rcp_f32_e32 v90, v90
	v_exp_f32_e32 v91, v91
	v_mul_f32_e32 v84, 0x41800000, v92
	v_and_b32_e32 v92, 0xffff0000, v112
	v_fmac_f32_e32 v92, v85, v90
	v_add_f32_e32 v90, 1.0, v91
	v_and_b32_e32 v91, 0xffff0000, v117
	v_mul_f32_e32 v91, 0xbfb8aa3b, v91
	v_rcp_f32_e32 v90, v90
	v_exp_f32_e32 v91, v91
	v_mul_f32_e32 v85, 0x41800000, v92
	v_lshlrev_b32_e32 v92, 16, v113
	v_fmac_f32_e32 v92, v86, v90
	v_add_f32_e32 v90, 1.0, v91
	v_lshlrev_b32_e32 v91, 16, v118
	v_mul_f32_e32 v91, 0xbfb8aa3b, v91
	v_rcp_f32_e32 v90, v90
	v_exp_f32_e32 v91, v91
	v_mul_f32_e32 v86, 0x41800000, v92
	v_and_b32_e32 v92, 0xffff0000, v113
	v_fmac_f32_e32 v92, v87, v90
	v_add_f32_e32 v90, 1.0, v91
	v_and_b32_e32 v91, 0xffff0000, v118
	v_mul_f32_e32 v91, 0xbfb8aa3b, v91
	v_rcp_f32_e32 v90, v90
	v_exp_f32_e32 v91, v91
	v_mul_f32_e32 v87, 0x41800000, v92
	v_lshlrev_b32_e32 v92, 16, v114
	v_fmac_f32_e32 v92, v80, v90
	v_add_f32_e32 v80, 1.0, v91
	v_lshlrev_b32_e32 v91, 16, v119
	v_rcp_f32_e32 v80, v80
	v_mul_f32_e32 v91, 0xbfb8aa3b, v91
	v_exp_f32_e32 v91, v91
	v_mul_f32_e32 v90, 0x41800000, v92
	v_and_b32_e32 v92, 0xffff0000, v114
	v_fmac_f32_e32 v92, v81, v80
	v_and_b32_e32 v81, 0xffff0000, v119
	v_add_f32_e32 v80, 1.0, v91
	v_mul_f32_e32 v81, 0xbfb8aa3b, v81
	v_rcp_f32_e32 v80, v80
	v_exp_f32_e32 v81, v81
	v_lshlrev_b32_e32 v91, 16, v115
	v_mul_f32_e32 v92, 0x41800000, v92
	v_fmac_f32_e32 v91, v82, v80
	v_add_f32_e32 v80, 1.0, v81
	v_mul_f32_e32 v82, 0x41800000, v91
	v_rcp_f32_e32 v91, v80
	v_mov_b32_e32 v80, 0
	v_mov_b32_e32 v81, 0
	v_cvt_pk_fp8_f32 v80, v84, v85
	v_cvt_pk_fp8_f32 v81, v90, v92
	v_and_b32_e32 v93, 0xffff0000, v115
	v_fmac_f32_e32 v93, v83, v91
	s_waitcnt vmcnt(3)
	v_lshlrev_b32_e32 v114, 16, v108
	v_cvt_pk_fp8_f32 v88, v94, v95 op_sel:[0,0,1]
	v_mul_f32_e32 v83, 0x41800000, v93
	v_mul_f32_e32 v114, 0xbfb8aa3b, v114
	v_cvt_pk_fp8_f32 v80, v86, v87 op_sel:[0,0,1]
	v_cvt_pk_fp8_f32 v81, v82, v83 op_sel:[0,0,1]
	v_exp_f32_e32 v114, v114
	v_lshl_add_u64 v[82:83], s[2:3], 0, v[154:155]
	v_lshl_add_u64 v[82:83], v[82:83], 0, v[144:145]
	global_store_dwordx2 v[82:83], v[88:89], off
	global_store_dwordx2 v[82:83], v[80:81], off offset:128
	v_add_u32_e32 v80, 0x80, v146
	v_and_b32_e32 v108, 0xffff0000, v108
	v_mad_i64_i32 v[82:83], s[6:7], v80, s53, v[150:151]
	v_add_f32_e32 v114, 1.0, v114
	v_mul_f32_e32 v108, 0xbfb8aa3b, v108
	v_lshl_add_u64 v[82:83], v[82:83], 0, v[148:149]
	v_rcp_f32_e32 v114, v114
	v_exp_f32_e32 v108, v108
	global_load_dwordx4 v[92:95], v[82:83], off
	global_load_dwordx4 v[84:87], v[82:83], off offset:256
	s_waitcnt vmcnt(5)
	v_lshlrev_b32_e32 v115, 16, v104
	v_fmac_f32_e32 v115, v76, v114
	v_add_f32_e32 v108, 1.0, v108
	v_lshlrev_b32_e32 v114, 16, v109
	v_rcp_f32_e32 v108, v108
	v_mul_f32_e32 v114, 0xbfb8aa3b, v114
	v_exp_f32_e32 v114, v114
	v_ashrrev_i32_e32 v81, 31, v80
	v_lshlrev_b64 v[112:113], 11, v[80:81]
	v_lshlrev_b64 v[80:81], 12, v[80:81]
	v_and_b32_e32 v104, 0xffff0000, v104
	v_lshl_add_u64 v[80:81], s[12:13], 0, v[80:81]
	v_fmac_f32_e32 v104, v77, v108
	v_and_b32_e32 v108, 0xffff0000, v109
	v_lshl_add_u64 v[80:81], v[80:81], 0, v[148:149]
	v_mul_f32_e32 v77, 0x41800000, v104
	v_add_f32_e32 v104, 1.0, v114
	v_mul_f32_e32 v108, 0xbfb8aa3b, v108
	global_load_dwordx4 v[88:91], v[80:81], off
	s_nop 0
	global_load_dwordx4 v[80:83], v[80:81], off offset:256
	v_rcp_f32_e32 v104, v104
	v_exp_f32_e32 v108, v108
	v_lshlrev_b32_e32 v109, 16, v105
	v_and_b32_e32 v105, 0xffff0000, v105
	v_fmac_f32_e32 v109, v78, v104
	v_add_f32_e32 v104, 1.0, v108
	v_rcp_f32_e32 v104, v104
	v_lshlrev_b32_e32 v108, 16, v110
	v_mul_f32_e32 v108, 0xbfb8aa3b, v108
	v_exp_f32_e32 v108, v108
	v_fmac_f32_e32 v105, v79, v104
	v_mul_f32_e32 v79, 0x41800000, v105
	v_and_b32_e32 v105, 0xffff0000, v110
	v_add_f32_e32 v104, 1.0, v108
	v_mul_f32_e32 v105, 0xbfb8aa3b, v105
	v_rcp_f32_e32 v104, v104
	v_exp_f32_e32 v105, v105
	v_lshlrev_b32_e32 v108, 16, v106
	v_and_b32_e32 v106, 0xffff0000, v106
	v_fmac_f32_e32 v108, v72, v104
	v_add_f32_e32 v72, 1.0, v105
	v_lshlrev_b32_e32 v105, 16, v111
	v_rcp_f32_e32 v72, v72
	v_mul_f32_e32 v105, 0xbfb8aa3b, v105
	v_exp_f32_e32 v105, v105
	v_mul_f32_e32 v104, 0x41800000, v108
	v_fmac_f32_e32 v106, v73, v72
	v_and_b32_e32 v73, 0xffff0000, v111
	v_add_f32_e32 v72, 1.0, v105
	v_mul_f32_e32 v73, 0xbfb8aa3b, v73
	v_rcp_f32_e32 v72, v72
	v_exp_f32_e32 v73, v73
	v_lshlrev_b32_e32 v105, 16, v107
	v_mul_f32_e32 v106, 0x41800000, v106
	v_fmac_f32_e32 v105, v74, v72
	v_add_f32_e32 v72, 1.0, v73
	v_mul_f32_e32 v74, 0x41800000, v105
	v_rcp_f32_e32 v105, v72
	v_mov_b32_e32 v73, 0
	v_cvt_pk_fp8_f32 v73, v104, v106
	v_and_b32_e32 v107, 0xffff0000, v107
	v_fmac_f32_e32 v107, v75, v105
	v_mul_f32_e32 v75, 0x41800000, v107
	v_cvt_pk_fp8_f32 v73, v74, v75 op_sel:[0,0,1]
	v_lshlrev_b32_e32 v74, 16, v100
	v_mul_f32_e32 v74, 0xbfb8aa3b, v74
	v_exp_f32_e32 v74, v74
	v_and_b32_e32 v75, 0xffff0000, v100
	v_mul_f32_e32 v75, 0xbfb8aa3b, v75
	v_exp_f32_e32 v75, v75
	v_add_f32_e32 v74, 1.0, v74
	v_rcp_f32_e32 v74, v74
	v_mul_f32_e32 v76, 0x41800000, v115
	v_mov_b32_e32 v72, 0
	v_cvt_pk_fp8_f32 v72, v76, v77
	s_waitcnt vmcnt(6)
	v_lshlrev_b32_e32 v76, 16, v96
	v_fmac_f32_e32 v76, v68, v74
	v_add_f32_e32 v74, 1.0, v75
	v_lshlrev_b32_e32 v75, 16, v101
	v_mul_f32_e32 v75, 0xbfb8aa3b, v75
	v_rcp_f32_e32 v74, v74
	v_exp_f32_e32 v75, v75
	v_mul_f32_e32 v68, 0x41800000, v76
	v_and_b32_e32 v76, 0xffff0000, v96
	v_fmac_f32_e32 v76, v69, v74
	v_add_f32_e32 v74, 1.0, v75
	v_and_b32_e32 v75, 0xffff0000, v101
	v_mul_f32_e32 v75, 0xbfb8aa3b, v75
	v_rcp_f32_e32 v74, v74
	v_exp_f32_e32 v75, v75
	v_mul_f32_e32 v69, 0x41800000, v76
	v_lshlrev_b32_e32 v76, 16, v97
	v_fmac_f32_e32 v76, v70, v74
	v_add_f32_e32 v74, 1.0, v75
	v_lshlrev_b32_e32 v75, 16, v102
	v_mul_f32_e32 v75, 0xbfb8aa3b, v75
	v_rcp_f32_e32 v74, v74
	v_exp_f32_e32 v75, v75
	v_mul_f32_e32 v70, 0x41800000, v76
	v_and_b32_e32 v76, 0xffff0000, v97
	v_fmac_f32_e32 v76, v71, v74
	v_add_f32_e32 v74, 1.0, v75
	v_and_b32_e32 v75, 0xffff0000, v102
	v_rcp_f32_e32 v74, v74
	v_mul_f32_e32 v75, 0xbfb8aa3b, v75
	v_exp_f32_e32 v75, v75
	v_mul_f32_e32 v71, 0x41800000, v76
	v_lshlrev_b32_e32 v76, 16, v98
	v_fmac_f32_e32 v76, v64, v74
	v_mul_f32_e32 v74, 0x41800000, v76
	v_add_f32_e32 v64, 1.0, v75
	v_lshlrev_b32_e32 v75, 16, v103
	v_and_b32_e32 v76, 0xffff0000, v98
	s_waitcnt vmcnt(3)
	v_lshlrev_b32_e32 v98, 16, v92
	v_rcp_f32_e32 v64, v64
	v_mul_f32_e32 v75, 0xbfb8aa3b, v75
	v_mul_f32_e32 v98, 0xbfb8aa3b, v98
	v_exp_f32_e32 v75, v75
	v_exp_f32_e32 v98, v98
	v_fmac_f32_e32 v76, v65, v64
	v_and_b32_e32 v65, 0xffff0000, v103
	v_and_b32_e32 v92, 0xffff0000, v92
	v_add_f32_e32 v64, 1.0, v75
	v_mul_f32_e32 v65, 0xbfb8aa3b, v65
	v_add_f32_e32 v98, 1.0, v98
	v_mul_f32_e32 v92, 0xbfb8aa3b, v92
	v_rcp_f32_e32 v64, v64
	v_exp_f32_e32 v65, v65
	v_rcp_f32_e32 v98, v98
	v_exp_f32_e32 v92, v92
	v_lshlrev_b32_e32 v75, 16, v99
	v_and_b32_e32 v77, 0xffff0000, v99
	s_waitcnt vmcnt(1)
	v_lshlrev_b32_e32 v99, 16, v88
	v_fmac_f32_e32 v75, v66, v64
	v_add_f32_e32 v64, 1.0, v65
	v_fmac_f32_e32 v99, v60, v98
	v_add_f32_e32 v92, 1.0, v92
	v_lshlrev_b32_e32 v98, 16, v93
	v_mul_f32_e32 v66, 0x41800000, v75
	v_rcp_f32_e32 v75, v64
	v_rcp_f32_e32 v92, v92
	v_mul_f32_e32 v98, 0xbfb8aa3b, v98
	v_mul_f32_e32 v76, 0x41800000, v76
	v_mov_b32_e32 v64, 0
	v_mov_b32_e32 v65, 0
	v_exp_f32_e32 v98, v98
	v_cvt_pk_fp8_f32 v64, v68, v69
	v_cvt_pk_fp8_f32 v65, v74, v76
	v_and_b32_e32 v88, 0xffff0000, v88
	v_mul_f32_e32 v78, 0x41800000, v109
	v_fmac_f32_e32 v77, v67, v75
	v_fmac_f32_e32 v88, v61, v92
	v_and_b32_e32 v92, 0xffff0000, v93
	v_cvt_pk_fp8_f32 v72, v78, v79 op_sel:[0,0,1]
	v_mul_f32_e32 v67, 0x41800000, v77
	v_mul_f32_e32 v61, 0x41800000, v88
	v_add_f32_e32 v88, 1.0, v98
	v_mul_f32_e32 v92, 0xbfb8aa3b, v92
	v_cvt_pk_fp8_f32 v64, v70, v71 op_sel:[0,0,1]
	v_cvt_pk_fp8_f32 v65, v66, v67 op_sel:[0,0,1]
	v_rcp_f32_e32 v88, v88
	v_exp_f32_e32 v92, v92
	v_lshl_add_u64 v[66:67], s[2:3], 0, v[120:121]
	v_lshl_add_u64 v[66:67], v[66:67], 0, v[144:145]
	global_store_dwordx2 v[66:67], v[72:73], off
	global_store_dwordx2 v[66:67], v[64:65], off offset:128
	v_add_u32_e32 v64, 0x90, v146
	v_lshlrev_b32_e32 v93, 16, v89
	v_mad_i64_i32 v[66:67], s[6:7], v64, s53, v[150:151]
	v_fmac_f32_e32 v93, v62, v88
	v_add_f32_e32 v88, 1.0, v92
	v_lshl_add_u64 v[66:67], v[66:67], 0, v[148:149]
	v_rcp_f32_e32 v88, v88
	v_lshlrev_b32_e32 v92, 16, v94
	global_load_dwordx4 v[76:79], v[66:67], off
	global_load_dwordx4 v[68:71], v[66:67], off offset:256
	v_mul_f32_e32 v92, 0xbfb8aa3b, v92
	v_exp_f32_e32 v92, v92
	v_and_b32_e32 v89, 0xffff0000, v89
	v_fmac_f32_e32 v89, v63, v88
	v_mul_f32_e32 v63, 0x41800000, v89
	v_and_b32_e32 v89, 0xffff0000, v94
	v_add_f32_e32 v88, 1.0, v92
	v_mul_f32_e32 v89, 0xbfb8aa3b, v89
	v_ashrrev_i32_e32 v65, 31, v64
	v_rcp_f32_e32 v88, v88
	v_exp_f32_e32 v89, v89
	v_lshlrev_b64 v[96:97], 11, v[64:65]
	v_lshlrev_b64 v[64:65], 12, v[64:65]
	v_lshl_add_u64 v[64:65], s[12:13], 0, v[64:65]
	v_lshl_add_u64 v[64:65], v[64:65], 0, v[148:149]
	v_lshlrev_b32_e32 v92, 16, v90
	global_load_dwordx4 v[72:75], v[64:65], off
	s_nop 0
	global_load_dwordx4 v[64:67], v[64:65], off offset:256
	v_fmac_f32_e32 v92, v56, v88
	v_add_f32_e32 v56, 1.0, v89
	v_lshlrev_b32_e32 v89, 16, v95
	v_rcp_f32_e32 v56, v56
	v_mul_f32_e32 v89, 0xbfb8aa3b, v89
	v_exp_f32_e32 v89, v89
	v_and_b32_e32 v90, 0xffff0000, v90
	v_fmac_f32_e32 v90, v57, v56
	v_and_b32_e32 v57, 0xffff0000, v95
	v_add_f32_e32 v56, 1.0, v89
	v_mul_f32_e32 v57, 0xbfb8aa3b, v57
	v_rcp_f32_e32 v56, v56
	v_exp_f32_e32 v57, v57
	v_lshlrev_b32_e32 v89, 16, v91
	v_mul_f32_e32 v88, 0x41800000, v92
	v_fmac_f32_e32 v89, v58, v56
	v_add_f32_e32 v56, 1.0, v57
	v_mul_f32_e32 v58, 0x41800000, v89
	v_rcp_f32_e32 v89, v56
	v_mul_f32_e32 v90, 0x41800000, v90
	v_mov_b32_e32 v57, 0
	v_cvt_pk_fp8_f32 v57, v88, v90
	v_and_b32_e32 v91, 0xffff0000, v91
	v_fmac_f32_e32 v91, v59, v89
	v_mul_f32_e32 v59, 0x41800000, v91
	v_cvt_pk_fp8_f32 v57, v58, v59 op_sel:[0,0,1]
	v_lshlrev_b32_e32 v58, 16, v84
	v_mul_f32_e32 v58, 0xbfb8aa3b, v58
	v_exp_f32_e32 v58, v58
	v_and_b32_e32 v59, 0xffff0000, v84
	v_mul_f32_e32 v59, 0xbfb8aa3b, v59
	v_exp_f32_e32 v59, v59
	v_add_f32_e32 v58, 1.0, v58
	v_rcp_f32_e32 v58, v58
	v_mul_f32_e32 v60, 0x41800000, v99
	v_mov_b32_e32 v56, 0
	v_cvt_pk_fp8_f32 v56, v60, v61
	s_waitcnt vmcnt(6)
	v_lshlrev_b32_e32 v60, 16, v80
	v_fmac_f32_e32 v60, v52, v58
	v_add_f32_e32 v58, 1.0, v59
	v_lshlrev_b32_e32 v59, 16, v85
	v_mul_f32_e32 v59, 0xbfb8aa3b, v59
	v_rcp_f32_e32 v58, v58
	v_exp_f32_e32 v59, v59
	v_mul_f32_e32 v52, 0x41800000, v60
	v_and_b32_e32 v60, 0xffff0000, v80
	v_fmac_f32_e32 v60, v53, v58
	v_add_f32_e32 v58, 1.0, v59
	v_and_b32_e32 v59, 0xffff0000, v85
	v_mul_f32_e32 v59, 0xbfb8aa3b, v59
	v_rcp_f32_e32 v58, v58
	v_exp_f32_e32 v59, v59
	v_mul_f32_e32 v53, 0x41800000, v60
	v_lshlrev_b32_e32 v60, 16, v81
	v_fmac_f32_e32 v60, v54, v58
	v_add_f32_e32 v58, 1.0, v59
	v_lshlrev_b32_e32 v59, 16, v86
	v_mul_f32_e32 v59, 0xbfb8aa3b, v59
	v_rcp_f32_e32 v58, v58
	v_exp_f32_e32 v59, v59
	v_mul_f32_e32 v54, 0x41800000, v60
	v_and_b32_e32 v60, 0xffff0000, v81
	v_fmac_f32_e32 v60, v55, v58
	v_add_f32_e32 v58, 1.0, v59
	v_and_b32_e32 v59, 0xffff0000, v86
	v_mul_f32_e32 v59, 0xbfb8aa3b, v59
	v_rcp_f32_e32 v58, v58
	v_exp_f32_e32 v59, v59
	v_mul_f32_e32 v55, 0x41800000, v60
	v_lshlrev_b32_e32 v60, 16, v82
	v_fmac_f32_e32 v60, v48, v58
	v_add_f32_e32 v48, 1.0, v59
	v_lshlrev_b32_e32 v59, 16, v87
	v_rcp_f32_e32 v48, v48
	v_mul_f32_e32 v59, 0xbfb8aa3b, v59
	v_exp_f32_e32 v59, v59
	v_mul_f32_e32 v58, 0x41800000, v60
	v_and_b32_e32 v60, 0xffff0000, v82
	v_fmac_f32_e32 v60, v49, v48
	v_and_b32_e32 v49, 0xffff0000, v87
	v_add_f32_e32 v48, 1.0, v59
	v_mul_f32_e32 v49, 0xbfb8aa3b, v49
	v_rcp_f32_e32 v48, v48
	v_exp_f32_e32 v49, v49
	v_lshlrev_b32_e32 v59, 16, v83
	v_mul_f32_e32 v60, 0x41800000, v60
	v_fmac_f32_e32 v59, v50, v48
	v_add_f32_e32 v48, 1.0, v49
	v_mul_f32_e32 v50, 0x41800000, v59
	v_rcp_f32_e32 v59, v48
	v_mov_b32_e32 v48, 0
	v_mov_b32_e32 v49, 0
	v_cvt_pk_fp8_f32 v48, v52, v53
	v_cvt_pk_fp8_f32 v49, v58, v60
	v_and_b32_e32 v61, 0xffff0000, v83
	v_mul_f32_e32 v62, 0x41800000, v93
	v_fmac_f32_e32 v61, v51, v59
	s_waitcnt vmcnt(3)
	v_lshlrev_b32_e32 v82, 16, v76
	v_cvt_pk_fp8_f32 v56, v62, v63 op_sel:[0,0,1]
	v_mul_f32_e32 v51, 0x41800000, v61
	v_mul_f32_e32 v82, 0xbfb8aa3b, v82
	v_cvt_pk_fp8_f32 v48, v54, v55 op_sel:[0,0,1]
	v_cvt_pk_fp8_f32 v49, v50, v51 op_sel:[0,0,1]
	v_exp_f32_e32 v82, v82
	v_lshl_add_u64 v[50:51], s[2:3], 0, v[112:113]
	v_lshl_add_u64 v[50:51], v[50:51], 0, v[144:145]
	global_store_dwordx2 v[50:51], v[56:57], off
	global_store_dwordx2 v[50:51], v[48:49], off offset:128
	v_add_u32_e32 v48, 0xa0, v146
	v_and_b32_e32 v76, 0xffff0000, v76
	v_mad_i64_i32 v[50:51], s[6:7], v48, s53, v[150:151]
	v_add_f32_e32 v82, 1.0, v82
	v_mul_f32_e32 v76, 0xbfb8aa3b, v76
	v_lshl_add_u64 v[50:51], v[50:51], 0, v[148:149]
	v_rcp_f32_e32 v82, v82
	v_exp_f32_e32 v76, v76
	global_load_dwordx4 v[60:63], v[50:51], off
	global_load_dwordx4 v[52:55], v[50:51], off offset:256
	s_waitcnt vmcnt(5)
	v_lshlrev_b32_e32 v83, 16, v72
	v_fmac_f32_e32 v83, v44, v82
	v_add_f32_e32 v76, 1.0, v76
	v_lshlrev_b32_e32 v82, 16, v77
	v_rcp_f32_e32 v76, v76
	v_mul_f32_e32 v82, 0xbfb8aa3b, v82
	v_exp_f32_e32 v82, v82
	v_ashrrev_i32_e32 v49, 31, v48
	v_lshlrev_b64 v[80:81], 11, v[48:49]
	v_lshlrev_b64 v[48:49], 12, v[48:49]
	v_and_b32_e32 v72, 0xffff0000, v72
	v_lshl_add_u64 v[48:49], s[12:13], 0, v[48:49]
	v_fmac_f32_e32 v72, v45, v76
	v_and_b32_e32 v76, 0xffff0000, v77
	v_lshl_add_u64 v[48:49], v[48:49], 0, v[148:149]
	v_mul_f32_e32 v45, 0x41800000, v72
	v_add_f32_e32 v72, 1.0, v82
	v_mul_f32_e32 v76, 0xbfb8aa3b, v76
	global_load_dwordx4 v[56:59], v[48:49], off
	s_nop 0
	global_load_dwordx4 v[48:51], v[48:49], off offset:256
	v_rcp_f32_e32 v72, v72
	v_exp_f32_e32 v76, v76
	v_lshlrev_b32_e32 v77, 16, v73
	v_and_b32_e32 v73, 0xffff0000, v73
	v_fmac_f32_e32 v77, v46, v72
	v_add_f32_e32 v72, 1.0, v76
	v_rcp_f32_e32 v72, v72
	v_lshlrev_b32_e32 v76, 16, v78
	v_mul_f32_e32 v76, 0xbfb8aa3b, v76
	v_exp_f32_e32 v76, v76
	v_fmac_f32_e32 v73, v47, v72
	v_mul_f32_e32 v47, 0x41800000, v73
	v_and_b32_e32 v73, 0xffff0000, v78
	v_add_f32_e32 v72, 1.0, v76
	v_mul_f32_e32 v73, 0xbfb8aa3b, v73
	v_rcp_f32_e32 v72, v72
	v_exp_f32_e32 v73, v73
	v_lshlrev_b32_e32 v76, 16, v74
	v_and_b32_e32 v74, 0xffff0000, v74
	v_fmac_f32_e32 v76, v40, v72
	v_add_f32_e32 v40, 1.0, v73
	v_lshlrev_b32_e32 v73, 16, v79
	v_rcp_f32_e32 v40, v40
	v_mul_f32_e32 v73, 0xbfb8aa3b, v73
	v_exp_f32_e32 v73, v73
	v_mul_f32_e32 v72, 0x41800000, v76
	v_fmac_f32_e32 v74, v41, v40
	v_and_b32_e32 v41, 0xffff0000, v79
	v_add_f32_e32 v40, 1.0, v73
	v_mul_f32_e32 v41, 0xbfb8aa3b, v41
	v_rcp_f32_e32 v40, v40
	v_exp_f32_e32 v41, v41
	v_lshlrev_b32_e32 v73, 16, v75
	v_mul_f32_e32 v74, 0x41800000, v74
	v_fmac_f32_e32 v73, v42, v40
	v_add_f32_e32 v40, 1.0, v41
	v_mul_f32_e32 v42, 0x41800000, v73
	v_rcp_f32_e32 v73, v40
	v_mov_b32_e32 v41, 0
	v_cvt_pk_fp8_f32 v41, v72, v74
	v_and_b32_e32 v75, 0xffff0000, v75
	v_fmac_f32_e32 v75, v43, v73
	v_mul_f32_e32 v43, 0x41800000, v75
	v_cvt_pk_fp8_f32 v41, v42, v43 op_sel:[0,0,1]
	v_lshlrev_b32_e32 v42, 16, v68
	v_mul_f32_e32 v42, 0xbfb8aa3b, v42
	v_exp_f32_e32 v42, v42
	v_and_b32_e32 v43, 0xffff0000, v68
	v_mul_f32_e32 v43, 0xbfb8aa3b, v43
	v_exp_f32_e32 v43, v43
	v_add_f32_e32 v42, 1.0, v42
	v_rcp_f32_e32 v42, v42
	v_mul_f32_e32 v44, 0x41800000, v83
	v_mov_b32_e32 v40, 0
	v_cvt_pk_fp8_f32 v40, v44, v45
	s_waitcnt vmcnt(6)
	v_lshlrev_b32_e32 v44, 16, v64
	v_fmac_f32_e32 v44, v36, v42
	v_add_f32_e32 v42, 1.0, v43
	v_lshlrev_b32_e32 v43, 16, v69
	v_mul_f32_e32 v43, 0xbfb8aa3b, v43
	v_rcp_f32_e32 v42, v42
	v_exp_f32_e32 v43, v43
	v_mul_f32_e32 v36, 0x41800000, v44
	v_and_b32_e32 v44, 0xffff0000, v64
	v_fmac_f32_e32 v44, v37, v42
	v_add_f32_e32 v42, 1.0, v43
	v_and_b32_e32 v43, 0xffff0000, v69
	v_mul_f32_e32 v43, 0xbfb8aa3b, v43
	v_rcp_f32_e32 v42, v42
	v_exp_f32_e32 v43, v43
	v_mul_f32_e32 v37, 0x41800000, v44
	v_lshlrev_b32_e32 v44, 16, v65
	v_fmac_f32_e32 v44, v38, v42
	v_add_f32_e32 v42, 1.0, v43
	v_lshlrev_b32_e32 v43, 16, v70
	v_mul_f32_e32 v43, 0xbfb8aa3b, v43
	v_rcp_f32_e32 v42, v42
	v_exp_f32_e32 v43, v43
	v_mul_f32_e32 v38, 0x41800000, v44
	v_and_b32_e32 v44, 0xffff0000, v65
	v_fmac_f32_e32 v44, v39, v42
	v_add_f32_e32 v42, 1.0, v43
	v_rcp_f32_e32 v42, v42
	v_mul_f32_e32 v39, 0x41800000, v44
	v_and_b32_e32 v43, 0xffff0000, v70
	v_lshlrev_b32_e32 v44, 16, v66
	v_mul_f32_e32 v43, 0xbfb8aa3b, v43
	v_fmac_f32_e32 v44, v32, v42
	v_exp_f32_e32 v43, v43
	v_mul_f32_e32 v42, 0x41800000, v44
	v_and_b32_e32 v44, 0xffff0000, v66
	s_waitcnt vmcnt(3)
	v_lshlrev_b32_e32 v66, 16, v60
	v_mul_f32_e32 v66, 0xbfb8aa3b, v66
	v_exp_f32_e32 v66, v66
	v_add_f32_e32 v32, 1.0, v43
	v_lshlrev_b32_e32 v43, 16, v71
	v_mul_f32_e32 v43, 0xbfb8aa3b, v43
	v_and_b32_e32 v60, 0xffff0000, v60
	v_rcp_f32_e32 v32, v32
	v_exp_f32_e32 v43, v43
	v_add_f32_e32 v66, 1.0, v66
	v_mul_f32_e32 v60, 0xbfb8aa3b, v60
	v_rcp_f32_e32 v66, v66
	v_exp_f32_e32 v60, v60
	v_fmac_f32_e32 v44, v33, v32
	v_add_f32_e32 v32, 1.0, v43
	v_and_b32_e32 v33, 0xffff0000, v71
	v_lshlrev_b32_e32 v43, 16, v67
	v_and_b32_e32 v45, 0xffff0000, v67
	s_waitcnt vmcnt(1)
	v_lshlrev_b32_e32 v67, 16, v56
	v_mul_f32_e32 v33, 0xbfb8aa3b, v33
	v_fmac_f32_e32 v67, v28, v66
	v_add_f32_e32 v60, 1.0, v60
	v_lshlrev_b32_e32 v66, 16, v61
	v_rcp_f32_e32 v32, v32
	v_exp_f32_e32 v33, v33
	v_rcp_f32_e32 v60, v60
	v_mul_f32_e32 v66, 0xbfb8aa3b, v66
	v_exp_f32_e32 v66, v66
	v_and_b32_e32 v56, 0xffff0000, v56
	v_fmac_f32_e32 v43, v34, v32
	v_add_f32_e32 v32, 1.0, v33
	v_fmac_f32_e32 v56, v29, v60
	v_and_b32_e32 v60, 0xffff0000, v61
	v_mul_f32_e32 v34, 0x41800000, v43
	v_rcp_f32_e32 v43, v32
	v_mul_f32_e32 v29, 0x41800000, v56
	v_add_f32_e32 v56, 1.0, v66
	v_mul_f32_e32 v60, 0xbfb8aa3b, v60
	v_mul_f32_e32 v44, 0x41800000, v44
	v_mov_b32_e32 v32, 0
	v_mov_b32_e32 v33, 0
	v_rcp_f32_e32 v56, v56
	v_exp_f32_e32 v60, v60
	v_cvt_pk_fp8_f32 v32, v36, v37
	v_cvt_pk_fp8_f32 v33, v42, v44
	v_mul_f32_e32 v46, 0x41800000, v77
	v_fmac_f32_e32 v45, v35, v43
	v_lshlrev_b32_e32 v61, 16, v57
	v_cvt_pk_fp8_f32 v40, v46, v47 op_sel:[0,0,1]
	v_mul_f32_e32 v35, 0x41800000, v45
	v_fmac_f32_e32 v61, v30, v56
	v_add_f32_e32 v56, 1.0, v60
	v_cvt_pk_fp8_f32 v32, v38, v39 op_sel:[0,0,1]
	v_cvt_pk_fp8_f32 v33, v34, v35 op_sel:[0,0,1]
	v_rcp_f32_e32 v56, v56
	v_lshlrev_b32_e32 v60, 16, v62
	v_lshl_add_u64 v[34:35], s[2:3], 0, v[96:97]
	v_mul_f32_e32 v60, 0xbfb8aa3b, v60
	v_lshl_add_u64 v[34:35], v[34:35], 0, v[144:145]
	v_exp_f32_e32 v60, v60
	global_store_dwordx2 v[34:35], v[40:41], off
	global_store_dwordx2 v[34:35], v[32:33], off offset:128
	v_add_u32_e32 v32, 0xb0, v146
	v_and_b32_e32 v57, 0xffff0000, v57
	v_mad_i64_i32 v[34:35], s[6:7], v32, s53, v[150:151]
	v_fmac_f32_e32 v57, v31, v56
	v_lshl_add_u64 v[34:35], v[34:35], 0, v[148:149]
	v_mul_f32_e32 v31, 0x41800000, v57
	v_and_b32_e32 v57, 0xffff0000, v62
	global_load_dwordx4 v[44:47], v[34:35], off
	global_load_dwordx4 v[36:39], v[34:35], off offset:256
	v_add_f32_e32 v56, 1.0, v60
	v_mul_f32_e32 v57, 0xbfb8aa3b, v57
	v_rcp_f32_e32 v56, v56
	v_exp_f32_e32 v57, v57
	v_lshlrev_b32_e32 v60, 16, v58
	v_ashrrev_i32_e32 v33, 31, v32
	v_fmac_f32_e32 v60, v24, v56
	v_add_f32_e32 v24, 1.0, v57
	v_lshlrev_b32_e32 v57, 16, v63
	v_rcp_f32_e32 v24, v24
	v_mul_f32_e32 v57, 0xbfb8aa3b, v57
	v_lshlrev_b64 v[64:65], 11, v[32:33]
	v_lshlrev_b64 v[32:33], 12, v[32:33]
	v_exp_f32_e32 v57, v57
	v_lshl_add_u64 v[32:33], s[12:13], 0, v[32:33]
	v_lshl_add_u64 v[32:33], v[32:33], 0, v[148:149]
	v_and_b32_e32 v58, 0xffff0000, v58
	global_load_dwordx4 v[40:43], v[32:33], off
	s_nop 0
	global_load_dwordx4 v[32:35], v[32:33], off offset:256
	v_fmac_f32_e32 v58, v25, v24
	v_and_b32_e32 v25, 0xffff0000, v63
	v_add_f32_e32 v24, 1.0, v57
	v_mul_f32_e32 v25, 0xbfb8aa3b, v25
	v_rcp_f32_e32 v24, v24
	v_exp_f32_e32 v25, v25
	v_lshlrev_b32_e32 v57, 16, v59
	v_mul_f32_e32 v56, 0x41800000, v60
	v_fmac_f32_e32 v57, v26, v24
	v_add_f32_e32 v24, 1.0, v25
	v_mul_f32_e32 v26, 0x41800000, v57
	v_rcp_f32_e32 v57, v24
	v_mul_f32_e32 v58, 0x41800000, v58
	v_mov_b32_e32 v25, 0
	v_cvt_pk_fp8_f32 v25, v56, v58
	v_and_b32_e32 v59, 0xffff0000, v59
	v_fmac_f32_e32 v59, v27, v57
	v_mul_f32_e32 v27, 0x41800000, v59
	v_cvt_pk_fp8_f32 v25, v26, v27 op_sel:[0,0,1]
	v_lshlrev_b32_e32 v26, 16, v52
	v_mul_f32_e32 v26, 0xbfb8aa3b, v26
	v_exp_f32_e32 v26, v26
	v_and_b32_e32 v27, 0xffff0000, v52
	v_mul_f32_e32 v27, 0xbfb8aa3b, v27
	v_exp_f32_e32 v27, v27
	v_add_f32_e32 v26, 1.0, v26
	v_rcp_f32_e32 v26, v26
	v_mul_f32_e32 v28, 0x41800000, v67
	v_mov_b32_e32 v24, 0
	v_cvt_pk_fp8_f32 v24, v28, v29
	s_waitcnt vmcnt(6)
	v_lshlrev_b32_e32 v28, 16, v48
	v_fmac_f32_e32 v28, v20, v26
	v_add_f32_e32 v26, 1.0, v27
	v_lshlrev_b32_e32 v27, 16, v53
	v_mul_f32_e32 v27, 0xbfb8aa3b, v27
	v_rcp_f32_e32 v26, v26
	v_exp_f32_e32 v27, v27
	v_mul_f32_e32 v20, 0x41800000, v28
	v_and_b32_e32 v28, 0xffff0000, v48
	v_fmac_f32_e32 v28, v21, v26
	v_add_f32_e32 v26, 1.0, v27
	v_and_b32_e32 v27, 0xffff0000, v53
	v_mul_f32_e32 v27, 0xbfb8aa3b, v27
	v_rcp_f32_e32 v26, v26
	v_exp_f32_e32 v27, v27
	v_mul_f32_e32 v21, 0x41800000, v28
	v_lshlrev_b32_e32 v28, 16, v49
	v_fmac_f32_e32 v28, v22, v26
	v_add_f32_e32 v26, 1.0, v27
	v_lshlrev_b32_e32 v27, 16, v54
	v_mul_f32_e32 v27, 0xbfb8aa3b, v27
	v_rcp_f32_e32 v26, v26
	v_exp_f32_e32 v27, v27
	v_mul_f32_e32 v22, 0x41800000, v28
	v_and_b32_e32 v28, 0xffff0000, v49
	v_fmac_f32_e32 v28, v23, v26
	v_add_f32_e32 v26, 1.0, v27
	v_and_b32_e32 v27, 0xffff0000, v54
	v_mul_f32_e32 v27, 0xbfb8aa3b, v27
	v_rcp_f32_e32 v26, v26
	v_exp_f32_e32 v27, v27
	v_mul_f32_e32 v23, 0x41800000, v28
	v_lshlrev_b32_e32 v28, 16, v50
	v_fmac_f32_e32 v28, v16, v26
	v_add_f32_e32 v16, 1.0, v27
	v_lshlrev_b32_e32 v27, 16, v55
	v_rcp_f32_e32 v16, v16
	v_mul_f32_e32 v27, 0xbfb8aa3b, v27
	v_exp_f32_e32 v27, v27
	v_mul_f32_e32 v26, 0x41800000, v28
	v_and_b32_e32 v28, 0xffff0000, v50
	v_fmac_f32_e32 v28, v17, v16
	v_and_b32_e32 v17, 0xffff0000, v55
	v_add_f32_e32 v16, 1.0, v27
	v_mul_f32_e32 v17, 0xbfb8aa3b, v17
	v_rcp_f32_e32 v16, v16
	v_exp_f32_e32 v17, v17
	v_lshlrev_b32_e32 v27, 16, v51
	v_mul_f32_e32 v28, 0x41800000, v28
	v_fmac_f32_e32 v27, v18, v16
	v_add_f32_e32 v16, 1.0, v17
	v_mul_f32_e32 v18, 0x41800000, v27
	v_rcp_f32_e32 v27, v16
	v_mov_b32_e32 v16, 0
	v_mov_b32_e32 v17, 0
	v_cvt_pk_fp8_f32 v16, v20, v21
	v_cvt_pk_fp8_f32 v17, v26, v28
	v_and_b32_e32 v29, 0xffff0000, v51
	v_mul_f32_e32 v30, 0x41800000, v61
	v_fmac_f32_e32 v29, v19, v27
	v_cvt_pk_fp8_f32 v24, v30, v31 op_sel:[0,0,1]
	v_mul_f32_e32 v19, 0x41800000, v29
	v_cvt_pk_fp8_f32 v16, v22, v23 op_sel:[0,0,1]
	v_cvt_pk_fp8_f32 v17, v18, v19 op_sel:[0,0,1]
	v_lshl_add_u64 v[18:19], s[2:3], 0, v[80:81]
	v_lshl_add_u64 v[18:19], v[18:19], 0, v[144:145]
	global_store_dwordx2 v[18:19], v[24:25], off
	global_store_dwordx2 v[18:19], v[16:17], off offset:128
	s_waitcnt vmcnt(5)
	v_lshlrev_b32_e32 v16, 16, v44
	v_mul_f32_e32 v16, 0xbfb8aa3b, v16
	v_exp_f32_e32 v16, v16
	v_and_b32_e32 v17, 0xffff0000, v44
	v_mul_f32_e32 v17, 0xbfb8aa3b, v17
	v_exp_f32_e32 v17, v17
	v_add_f32_e32 v16, 1.0, v16
	v_rcp_f32_e32 v16, v16
	s_waitcnt vmcnt(3)
	v_lshlrev_b32_e32 v18, 16, v40
	v_and_b32_e32 v19, 0xffff0000, v43
	v_mul_f32_e32 v6, s18, v6
	v_mul_f32_e32 v7, s18, v7
	v_fmac_f32_e32 v18, v12, v16
	v_add_f32_e32 v16, 1.0, v17
	v_lshlrev_b32_e32 v17, 16, v45
	v_mul_f32_e32 v17, 0xbfb8aa3b, v17
	v_rcp_f32_e32 v16, v16
	v_exp_f32_e32 v17, v17
	v_mul_f32_e32 v12, 0x41800000, v18
	v_and_b32_e32 v18, 0xffff0000, v40
	v_fmac_f32_e32 v18, v13, v16
	v_add_f32_e32 v16, 1.0, v17
	v_and_b32_e32 v17, 0xffff0000, v45
	v_mul_f32_e32 v17, 0xbfb8aa3b, v17
	v_rcp_f32_e32 v16, v16
	v_exp_f32_e32 v17, v17
	v_mul_f32_e32 v13, 0x41800000, v18
	v_lshlrev_b32_e32 v18, 16, v41
	v_fmac_f32_e32 v18, v14, v16
	v_add_f32_e32 v16, 1.0, v17
	v_lshlrev_b32_e32 v17, 16, v46
	v_mul_f32_e32 v17, 0xbfb8aa3b, v17
	v_rcp_f32_e32 v16, v16
	v_exp_f32_e32 v17, v17
	v_mul_f32_e32 v14, 0x41800000, v18
	v_and_b32_e32 v18, 0xffff0000, v41
	v_fmac_f32_e32 v18, v15, v16
	v_add_f32_e32 v16, 1.0, v17
	v_and_b32_e32 v17, 0xffff0000, v46
	v_mul_f32_e32 v17, 0xbfb8aa3b, v17
	v_rcp_f32_e32 v16, v16
	v_exp_f32_e32 v17, v17
	v_mul_f32_e32 v15, 0x41800000, v18
	v_lshlrev_b32_e32 v18, 16, v42
	v_fmac_f32_e32 v18, v8, v16
	v_add_f32_e32 v8, 1.0, v17
	v_lshlrev_b32_e32 v17, 16, v47
	v_rcp_f32_e32 v8, v8
	v_mul_f32_e32 v17, 0xbfb8aa3b, v17
	v_exp_f32_e32 v17, v17
	v_mul_f32_e32 v16, 0x41800000, v18
	v_and_b32_e32 v18, 0xffff0000, v42
	v_fmac_f32_e32 v18, v9, v8
	v_and_b32_e32 v9, 0xffff0000, v47
	v_add_f32_e32 v8, 1.0, v17
	v_mul_f32_e32 v9, 0xbfb8aa3b, v9
	v_rcp_f32_e32 v8, v8
	v_exp_f32_e32 v9, v9
	v_lshlrev_b32_e32 v17, 16, v43
	v_mul_f32_e32 v18, 0x41800000, v18
	v_fmac_f32_e32 v17, v10, v8
	v_add_f32_e32 v8, 1.0, v9
	v_mul_f32_e32 v10, 0x41800000, v17
	v_rcp_f32_e32 v17, v8
	v_mov_b32_e32 v9, 0
	v_cvt_pk_fp8_f32 v9, v16, v18
	v_mov_b32_e32 v8, 0
	v_fmac_f32_e32 v19, v11, v17
	v_mul_f32_e32 v11, 0x41800000, v19
	v_cvt_pk_fp8_f32 v9, v10, v11 op_sel:[0,0,1]
	v_lshlrev_b32_e32 v10, 16, v36
	v_mul_f32_e32 v10, 0xbfb8aa3b, v10
	v_exp_f32_e32 v10, v10
	v_and_b32_e32 v11, 0xffff0000, v36
	v_mul_f32_e32 v11, 0xbfb8aa3b, v11
	v_exp_f32_e32 v11, v11
	v_add_f32_e32 v10, 1.0, v10
	v_rcp_f32_e32 v10, v10
	v_cvt_pk_fp8_f32 v8, v12, v13
	s_waitcnt vmcnt(2)
	v_lshlrev_b32_e32 v12, 16, v32
	v_mul_f32_e32 v0, s18, v0
	v_mul_f32_e32 v1, s18, v1
	v_fmac_f32_e32 v12, v4, v10
	v_add_f32_e32 v10, 1.0, v11
	v_lshlrev_b32_e32 v11, 16, v37
	v_mul_f32_e32 v11, 0xbfb8aa3b, v11
	v_rcp_f32_e32 v10, v10
	v_exp_f32_e32 v11, v11
	v_mul_f32_e32 v4, 0x41800000, v12
	v_and_b32_e32 v12, 0xffff0000, v32
	v_fmac_f32_e32 v12, v5, v10
	v_add_f32_e32 v10, 1.0, v11
	v_and_b32_e32 v11, 0xffff0000, v37
	v_mul_f32_e32 v11, 0xbfb8aa3b, v11
	v_rcp_f32_e32 v10, v10
	v_exp_f32_e32 v11, v11
	v_mul_f32_e32 v5, 0x41800000, v12
	v_lshlrev_b32_e32 v12, 16, v33
	v_fmac_f32_e32 v12, v6, v10
	v_add_f32_e32 v10, 1.0, v11
	v_lshlrev_b32_e32 v11, 16, v38
	v_mul_f32_e32 v11, 0xbfb8aa3b, v11
	v_rcp_f32_e32 v10, v10
	v_exp_f32_e32 v11, v11
	v_mul_f32_e32 v6, 0x41800000, v12
	v_and_b32_e32 v12, 0xffff0000, v33
	v_fmac_f32_e32 v12, v7, v10
	v_add_f32_e32 v10, 1.0, v11
	v_and_b32_e32 v11, 0xffff0000, v38
	v_mul_f32_e32 v11, 0xbfb8aa3b, v11
	v_rcp_f32_e32 v10, v10
	v_exp_f32_e32 v11, v11
	v_mul_f32_e32 v7, 0x41800000, v12
	v_lshlrev_b32_e32 v12, 16, v34
	v_fmac_f32_e32 v12, v0, v10
	v_add_f32_e32 v0, 1.0, v11
	v_lshlrev_b32_e32 v11, 16, v39
	v_rcp_f32_e32 v0, v0
	v_mul_f32_e32 v11, 0xbfb8aa3b, v11
	v_exp_f32_e32 v11, v11
	v_mul_f32_e32 v10, 0x41800000, v12
	v_and_b32_e32 v12, 0xffff0000, v34
	v_fmac_f32_e32 v12, v1, v0
	v_and_b32_e32 v1, 0xffff0000, v39
	v_add_f32_e32 v0, 1.0, v11
	v_mul_f32_e32 v1, 0xbfb8aa3b, v1
	v_rcp_f32_e32 v0, v0
	v_exp_f32_e32 v1, v1
	v_mul_f32_e32 v2, s18, v2
	v_mul_f32_e32 v3, s18, v3
	v_lshlrev_b32_e32 v11, 16, v35
	v_fmac_f32_e32 v11, v2, v0
	v_add_f32_e32 v0, 1.0, v1
	v_mul_f32_e32 v2, 0x41800000, v11
	v_rcp_f32_e32 v11, v0
	v_mul_f32_e32 v12, 0x41800000, v12
	v_mov_b32_e32 v0, 0
	v_mov_b32_e32 v1, 0
	v_cvt_pk_fp8_f32 v0, v4, v5
	v_cvt_pk_fp8_f32 v1, v10, v12
	v_and_b32_e32 v13, 0xffff0000, v35
	v_fmac_f32_e32 v13, v3, v11
	v_cvt_pk_fp8_f32 v8, v14, v15 op_sel:[0,0,1]
	v_mul_f32_e32 v3, 0x41800000, v13
	v_cvt_pk_fp8_f32 v0, v6, v7 op_sel:[0,0,1]
	v_cvt_pk_fp8_f32 v1, v2, v3 op_sel:[0,0,1]
	v_lshl_add_u64 v[2:3], s[2:3], 0, v[64:65]
	v_lshl_add_u64 v[2:3], v[2:3], 0, v[144:145]
	s_andn2_b64 vcc, exec, s[20:21]
	s_mov_b64 s[6:7], -1
	global_store_dwordx2 v[2:3], v[8:9], off
	global_store_dwordx2 v[2:3], v[0:1], off offset:128
	s_cbranch_vccnz .LBB0_2195
	s_andn2_b64 vcc, exec, s[0:1]
	s_cbranch_vccnz .LBB0_2194
	s_barrier
	s_branch .LBB0_2194

.LBB0_2281:
	s_lshl_b32 s6, s55, 8
	v_mbcnt_lo_u32_b32 v128, -1, 0
	v_mbcnt_hi_u32_b32 v128, -1, v128
	s_add_i32 s6, s6, s45
	v_and_or_b32 v132, v128, 15, s6
	s_lshl_b32 s6, s54, 8
	v_ashrrev_i32_e32 v128, 1, v128
	s_or_b32 s6, s6, s46
	v_and_b32_e32 v128, -8, v128
	v_add_u32_e32 v128, s6, v128
	v_ashrrev_i32_e32 v133, 31, v132
	v_lshlrev_b64 v[130:131], 13, v[132:133]
	v_ashrrev_i32_e32 v129, 31, v128
	v_lshl_add_u64 v[134:135], s[12:13], 0, v[130:131]
	v_lshlrev_b64 v[130:131], 2, v[128:129]
	v_or_b32_e32 v170, 16, v132
	v_lshl_add_u64 v[134:135], v[134:135], 0, v[130:131]
	v_ashrrev_i32_e32 v171, 31, v170
	global_load_dwordx4 v[138:141], v[134:135], off
	global_load_dwordx4 v[142:145], v[134:135], off offset:16
	global_load_dwordx4 v[146:149], v[134:135], off offset:512
	global_load_dwordx4 v[150:153], v[134:135], off offset:528
	v_lshlrev_b64 v[134:135], 13, v[170:171]
	v_lshl_add_u64 v[134:135], s[12:13], 0, v[134:135]
	v_lshl_add_u64 v[134:135], v[134:135], 0, v[130:131]
	global_load_dwordx4 v[154:157], v[134:135], off
	global_load_dwordx4 v[158:161], v[134:135], off offset:16
	global_load_dwordx4 v[162:165], v[134:135], off offset:512
	global_load_dwordx4 v[166:169], v[134:135], off offset:528
	v_or_b32_e32 v134, 32, v132
	v_lshlrev_b64 v[174:175], 12, v[132:133]
	v_ashrrev_i32_e32 v135, 31, v134
	v_or_b32_e32 v172, 48, v132
	v_lshl_add_u64 v[174:175], s[2:3], 0, v[174:175]
	v_lshlrev_b64 v[128:129], 1, v[128:129]
	v_lshlrev_b64 v[176:177], 13, v[134:135]
	v_ashrrev_i32_e32 v173, 31, v172
	v_lshlrev_b64 v[170:171], 12, v[170:171]
	v_lshl_add_u64 v[174:175], v[174:175], 0, v[128:129]
	v_lshl_add_u64 v[176:177], s[12:13], 0, v[176:177]
	v_lshlrev_b64 v[178:179], 13, v[172:173]
	v_lshl_add_u64 v[170:171], s[2:3], 0, v[170:171]
	v_lshl_add_u64 v[176:177], v[176:177], 0, v[130:131]
	v_lshl_add_u64 v[178:179], s[12:13], 0, v[178:179]
	v_lshl_add_u64 v[170:171], v[170:171], 0, v[128:129]
	v_lshl_add_u64 v[178:179], v[178:179], 0, v[130:131]
	v_lshlrev_b64 v[134:135], 12, v[134:135]
	v_lshl_add_u64 v[134:135], s[2:3], 0, v[134:135]
	v_lshl_add_u64 v[134:135], v[134:135], 0, v[128:129]
	s_andn2_b64 vcc, exec, s[18:19]
	s_mov_b64 s[6:7], -1
	s_waitcnt vmcnt(7)
	v_fma_f32 v126, v126, s16, v140
	v_fma_f32 v127, v127, s16, v141
	v_fma_f32 v124, v124, s16, v138
	v_fma_f32 v125, v125, s16, v139
	s_waitcnt vmcnt(6)
	v_fma_f32 v122, v122, s16, v144
	v_fma_f32 v123, v123, s16, v145
	v_fma_f32 v120, v120, s16, v142
	v_fma_f32 v121, v121, s16, v143
	s_waitcnt vmcnt(4)
	v_fma_f32 v138, v106, s16, v152
	v_fma_f32 v139, v107, s16, v153
	v_fma_f32 v140, v104, s16, v150
	v_fma_f32 v141, v105, s16, v151
	v_cvt_pk_bf16_f32 v104, v124, v125
	v_cvt_pk_bf16_f32 v105, v126, v127
	v_cvt_pk_bf16_f32 v106, v120, v121
	v_cvt_pk_bf16_f32 v107, v122, v123
	v_fma_f32 v110, v110, s16, v148
	v_fma_f32 v111, v111, s16, v149
	v_fma_f32 v108, v108, s16, v146
	v_fma_f32 v109, v109, s16, v147
	global_store_dwordx4 v[174:175], v[104:107], off
	s_waitcnt vmcnt(4)
	v_fma_f32 v120, v118, s16, v156
	v_fma_f32 v121, v119, s16, v157
	v_fma_f32 v122, v116, s16, v154
	v_fma_f32 v123, v117, s16, v155
	v_cvt_pk_bf16_f32 v104, v108, v109
	v_cvt_pk_bf16_f32 v105, v110, v111
	v_cvt_pk_bf16_f32 v106, v140, v141
	v_cvt_pk_bf16_f32 v107, v138, v139
	global_store_dwordx4 v[174:175], v[104:107], off offset:256
	s_waitcnt vmcnt(4)
	v_fma_f32 v124, v114, s16, v160
	v_fma_f32 v125, v115, s16, v161
	global_load_dwordx4 v[104:107], v[176:177], off offset:16
	global_load_dwordx4 v[108:111], v[176:177], off
	v_fma_f32 v126, v112, s16, v158
	v_fma_f32 v127, v113, s16, v159
	global_load_dwordx4 v[112:115], v[176:177], off offset:528
	global_load_dwordx4 v[116:119], v[176:177], off offset:512
	s_waitcnt vmcnt(6)
	v_fma_f32 v138, v98, s16, v168
	v_fma_f32 v139, v99, s16, v169
	v_fma_f32 v140, v96, s16, v166
	v_fma_f32 v141, v97, s16, v167
	v_cvt_pk_bf16_f32 v96, v122, v123
	v_cvt_pk_bf16_f32 v97, v120, v121
	v_cvt_pk_bf16_f32 v98, v126, v127
	v_cvt_pk_bf16_f32 v99, v124, v125
	v_fma_f32 v102, v102, s16, v164
	v_fma_f32 v103, v103, s16, v165
	v_fma_f32 v100, v100, s16, v162
	v_fma_f32 v101, v101, s16, v163
	global_store_dwordx4 v[170:171], v[96:99], off
	v_lshlrev_b64 v[144:145], 12, v[172:173]
	v_lshl_add_u64 v[144:145], s[2:3], 0, v[144:145]
	v_cvt_pk_bf16_f32 v96, v100, v101
	v_cvt_pk_bf16_f32 v97, v102, v103
	v_cvt_pk_bf16_f32 v98, v140, v141
	v_cvt_pk_bf16_f32 v99, v138, v139
	global_store_dwordx4 v[170:171], v[96:99], off offset:256
	global_load_dwordx4 v[98:101], v[178:179], off
	s_nop 0
	global_load_dwordx4 v[120:123], v[178:179], off offset:16
	global_load_dwordx4 v[124:127], v[178:179], off offset:512
	global_load_dwordx4 v[138:141], v[178:179], off offset:528
	v_add_u32_e32 v96, 0x80, v132
	v_ashrrev_i32_e32 v97, 31, v96
	v_add_u32_e32 v102, 0x90, v132
	v_lshlrev_b64 v[142:143], 13, v[96:97]
	v_ashrrev_i32_e32 v103, 31, v102
	v_lshl_add_u64 v[142:143], s[12:13], 0, v[142:143]
	v_lshlrev_b64 v[146:147], 13, v[102:103]
	v_lshl_add_u64 v[142:143], v[142:143], 0, v[130:131]
	v_lshl_add_u64 v[146:147], s[12:13], 0, v[146:147]
	v_lshl_add_u64 v[144:145], v[144:145], 0, v[128:129]
	v_lshl_add_u64 v[146:147], v[146:147], 0, v[130:131]
	v_lshlrev_b64 v[96:97], 12, v[96:97]
	v_lshl_add_u64 v[96:97], s[2:3], 0, v[96:97]
	v_lshlrev_b64 v[102:103], 12, v[102:103]
	v_lshl_add_u64 v[96:97], v[96:97], 0, v[128:129]
	v_lshl_add_u64 v[102:103], s[2:3], 0, v[102:103]
	v_lshl_add_u64 v[102:103], v[102:103], 0, v[128:129]
	s_waitcnt vmcnt(9)
	v_fma_f32 v90, v90, s16, v106
	v_fma_f32 v91, v91, s16, v107
	s_waitcnt vmcnt(8)
	v_fma_f32 v94, v94, s16, v110
	v_fma_f32 v95, v95, s16, v111
	v_fma_f32 v92, v92, s16, v108
	v_fma_f32 v93, v93, s16, v109
	v_fma_f32 v88, v88, s16, v104
	v_fma_f32 v89, v89, s16, v105
	s_waitcnt vmcnt(7)
	v_fma_f32 v104, v74, s16, v114
	v_fma_f32 v105, v75, s16, v115
	v_fma_f32 v106, v72, s16, v112
	v_fma_f32 v107, v73, s16, v113
	v_cvt_pk_bf16_f32 v72, v92, v93
	v_cvt_pk_bf16_f32 v73, v94, v95
	v_cvt_pk_bf16_f32 v74, v88, v89
	v_cvt_pk_bf16_f32 v75, v90, v91
	s_waitcnt vmcnt(6)
	v_fma_f32 v78, v78, s16, v118
	v_fma_f32 v79, v79, s16, v119
	v_fma_f32 v76, v76, s16, v116
	v_fma_f32 v77, v77, s16, v117
	global_store_dwordx4 v[134:135], v[72:75], off
	s_waitcnt vmcnt(4)
	v_fma_f32 v88, v86, s16, v100
	v_fma_f32 v89, v87, s16, v101
	v_cvt_pk_bf16_f32 v72, v76, v77
	v_cvt_pk_bf16_f32 v73, v78, v79
	v_cvt_pk_bf16_f32 v74, v106, v107
	v_cvt_pk_bf16_f32 v75, v104, v105
	global_store_dwordx4 v[134:135], v[72:75], off offset:256
	v_fma_f32 v90, v84, s16, v98
	v_fma_f32 v91, v85, s16, v99
	s_waitcnt vmcnt(4)
	v_fma_f32 v92, v82, s16, v122
	v_fma_f32 v93, v83, s16, v123
	global_load_dwordx4 v[72:75], v[142:143], off offset:16
	global_load_dwordx4 v[76:79], v[142:143], off
	v_fma_f32 v94, v80, s16, v120
	v_fma_f32 v95, v81, s16, v121
	global_load_dwordx4 v[80:83], v[142:143], off offset:528
	global_load_dwordx4 v[84:87], v[142:143], off offset:512
	s_waitcnt vmcnt(6)
	v_fma_f32 v98, v66, s16, v140
	v_fma_f32 v99, v67, s16, v141
	v_fma_f32 v100, v64, s16, v138
	v_fma_f32 v101, v65, s16, v139
	v_cvt_pk_bf16_f32 v64, v90, v91
	v_cvt_pk_bf16_f32 v65, v88, v89
	v_cvt_pk_bf16_f32 v66, v94, v95
	v_cvt_pk_bf16_f32 v67, v92, v93
	v_fma_f32 v70, v70, s16, v126
	v_fma_f32 v71, v71, s16, v127
	v_fma_f32 v68, v68, s16, v124
	v_fma_f32 v69, v69, s16, v125
	global_store_dwordx4 v[144:145], v[64:67], off
	s_waitcnt vmcnt(4)
	v_fma_f32 v58, v58, s16, v74
	v_fma_f32 v59, v59, s16, v75
	v_cvt_pk_bf16_f32 v64, v68, v69
	v_cvt_pk_bf16_f32 v65, v70, v71
	v_cvt_pk_bf16_f32 v66, v100, v101
	v_cvt_pk_bf16_f32 v67, v98, v99
	global_store_dwordx4 v[144:145], v[64:67], off offset:256
	global_load_dwordx4 v[66:69], v[146:147], off
	s_nop 0
	global_load_dwordx4 v[88:91], v[146:147], off offset:16
	global_load_dwordx4 v[92:95], v[146:147], off offset:512
	global_load_dwordx4 v[98:101], v[146:147], off offset:528
	v_add_u32_e32 v64, 0xa0, v132
	v_ashrrev_i32_e32 v65, 31, v64
	v_add_u32_e32 v70, 0xb0, v132
	v_lshlrev_b64 v[104:105], 13, v[64:65]
	v_ashrrev_i32_e32 v71, 31, v70
	v_lshl_add_u64 v[104:105], s[12:13], 0, v[104:105]
	s_waitcnt vmcnt(8)
	v_fma_f32 v62, v62, s16, v78
	v_fma_f32 v63, v63, s16, v79
	v_fma_f32 v60, v60, s16, v76
	v_fma_f32 v61, v61, s16, v77
	v_fma_f32 v56, v56, s16, v72
	v_fma_f32 v57, v57, s16, v73
	s_waitcnt vmcnt(7)
	v_fma_f32 v72, v42, s16, v82
	v_fma_f32 v73, v43, s16, v83
	v_fma_f32 v74, v40, s16, v80
	v_fma_f32 v75, v41, s16, v81
	v_cvt_pk_bf16_f32 v40, v60, v61
	v_cvt_pk_bf16_f32 v41, v62, v63
	v_cvt_pk_bf16_f32 v42, v56, v57
	v_cvt_pk_bf16_f32 v43, v58, v59
	v_lshlrev_b64 v[106:107], 13, v[70:71]
	v_lshl_add_u64 v[104:105], v[104:105], 0, v[130:131]
	s_waitcnt vmcnt(6)
	v_fma_f32 v46, v46, s16, v86
	v_fma_f32 v47, v47, s16, v87
	v_fma_f32 v44, v44, s16, v84
	v_fma_f32 v45, v45, s16, v85
	global_store_dwordx4 v[96:97], v[40:43], off
	v_lshl_add_u64 v[106:107], s[12:13], 0, v[106:107]
	v_lshl_add_u64 v[106:107], v[106:107], 0, v[130:131]
	v_cvt_pk_bf16_f32 v40, v44, v45
	v_cvt_pk_bf16_f32 v41, v46, v47
	v_cvt_pk_bf16_f32 v42, v74, v75
	v_cvt_pk_bf16_f32 v43, v72, v73
	global_store_dwordx4 v[96:97], v[40:43], off offset:256
	global_load_dwordx4 v[40:43], v[104:105], off offset:16
	s_nop 0
	global_load_dwordx4 v[44:47], v[104:105], off
	v_lshlrev_b64 v[64:65], 12, v[64:65]
	v_lshl_add_u64 v[64:65], s[2:3], 0, v[64:65]
	v_lshl_add_u64 v[64:65], v[64:65], 0, v[128:129]
	s_waitcnt vmcnt(7)
	v_fma_f32 v56, v54, s16, v68
	v_fma_f32 v57, v55, s16, v69
	v_fma_f32 v58, v52, s16, v66
	v_fma_f32 v59, v53, s16, v67
	s_waitcnt vmcnt(6)
	v_fma_f32 v60, v50, s16, v90
	v_fma_f32 v61, v51, s16, v91
	v_fma_f32 v62, v48, s16, v88
	v_fma_f32 v63, v49, s16, v89
	global_load_dwordx4 v[48:51], v[104:105], off offset:528
	global_load_dwordx4 v[52:55], v[104:105], off offset:512
	s_waitcnt vmcnt(6)
	v_fma_f32 v66, v34, s16, v100
	v_fma_f32 v67, v35, s16, v101
	v_fma_f32 v68, v32, s16, v98
	v_fma_f32 v69, v33, s16, v99
	v_cvt_pk_bf16_f32 v32, v58, v59
	v_cvt_pk_bf16_f32 v33, v56, v57
	v_cvt_pk_bf16_f32 v34, v62, v63
	v_cvt_pk_bf16_f32 v35, v60, v61
	v_fma_f32 v38, v38, s16, v94
	v_fma_f32 v39, v39, s16, v95
	v_fma_f32 v36, v36, s16, v92
	v_fma_f32 v37, v37, s16, v93
	global_store_dwordx4 v[102:103], v[32:35], off
	s_waitcnt vmcnt(4)
	v_fma_f32 v26, v26, s16, v42
	v_fma_f32 v27, v27, s16, v43
	v_cvt_pk_bf16_f32 v32, v36, v37
	v_cvt_pk_bf16_f32 v33, v38, v39
	v_cvt_pk_bf16_f32 v34, v68, v69
	v_cvt_pk_bf16_f32 v35, v66, v67
	global_store_dwordx4 v[102:103], v[32:35], off offset:256
	global_load_dwordx4 v[32:35], v[106:107], off
	s_nop 0
	global_load_dwordx4 v[36:39], v[106:107], off offset:16
	global_load_dwordx4 v[56:59], v[106:107], off offset:512
	global_load_dwordx4 v[60:63], v[106:107], off offset:528
	v_lshlrev_b64 v[66:67], 12, v[70:71]
	s_waitcnt vmcnt(8)
	v_fma_f32 v30, v30, s16, v46
	v_fma_f32 v31, v31, s16, v47
	v_fma_f32 v28, v28, s16, v44
	v_fma_f32 v29, v29, s16, v45
	v_fma_f32 v24, v24, s16, v40
	v_fma_f32 v25, v25, s16, v41
	v_lshl_add_u64 v[66:67], s[2:3], 0, v[66:67]
	v_lshl_add_u64 v[66:67], v[66:67], 0, v[128:129]
	s_waitcnt vmcnt(7)
	v_fma_f32 v40, v10, s16, v50
	v_fma_f32 v41, v11, s16, v51
	v_fma_f32 v42, v8, s16, v48
	v_fma_f32 v43, v9, s16, v49
	v_cvt_pk_bf16_f32 v8, v28, v29
	v_cvt_pk_bf16_f32 v9, v30, v31
	v_cvt_pk_bf16_f32 v10, v24, v25
	v_cvt_pk_bf16_f32 v11, v26, v27
	s_waitcnt vmcnt(6)
	v_fma_f32 v14, v14, s16, v54
	v_fma_f32 v15, v15, s16, v55
	v_fma_f32 v12, v12, s16, v52
	v_fma_f32 v13, v13, s16, v53
	global_store_dwordx4 v[64:65], v[8:11], off
	s_waitcnt vmcnt(2)
	v_fma_f32 v6, v6, s16, v58
	v_fma_f32 v7, v7, s16, v59
	v_cvt_pk_bf16_f32 v8, v12, v13
	v_cvt_pk_bf16_f32 v9, v14, v15
	v_cvt_pk_bf16_f32 v10, v42, v43
	v_cvt_pk_bf16_f32 v11, v40, v41
	global_store_dwordx4 v[64:65], v[8:11], off offset:256
	v_fma_f32 v12, v18, s16, v38
	v_fma_f32 v13, v19, s16, v39
	v_fma_f32 v14, v16, s16, v36
	v_fma_f32 v15, v17, s16, v37
	v_fma_f32 v8, v22, s16, v34
	v_fma_f32 v9, v23, s16, v35
	v_fma_f32 v10, v20, s16, v32
	v_fma_f32 v11, v21, s16, v33
	s_waitcnt vmcnt(2)
	v_fma_f32 v16, v2, s16, v62
	v_fma_f32 v17, v3, s16, v63
	v_fma_f32 v18, v0, s16, v60
	v_fma_f32 v19, v1, s16, v61
	v_cvt_pk_bf16_f32 v0, v10, v11
	v_cvt_pk_bf16_f32 v1, v8, v9
	v_cvt_pk_bf16_f32 v2, v14, v15
	v_cvt_pk_bf16_f32 v3, v12, v13
	v_fma_f32 v4, v4, s16, v56
	v_fma_f32 v5, v5, s16, v57
	global_store_dwordx4 v[66:67], v[0:3], off
	s_nop 1
	v_cvt_pk_bf16_f32 v0, v4, v5
	v_cvt_pk_bf16_f32 v1, v6, v7
	v_cvt_pk_bf16_f32 v2, v18, v19
	v_cvt_pk_bf16_f32 v3, v16, v17
	global_store_dwordx4 v[66:67], v[0:3], off offset:256
	s_cbranch_vccnz .LBB0_2273
	s_andn2_b64 vcc, exec, s[0:1]
	s_cbranch_vccnz .LBB0_2272
	s_barrier
	s_branch .LBB0_2272

.LBB0_2481:
	v_mbcnt_lo_u32_b32 v24, -1, 0
	v_mbcnt_hi_u32_b32 v24, -1, v24
	s_lshl_b32 s6, s37, 7
	v_ashrrev_i32_e32 v0, 1, v24
	v_and_b32_e32 v0, -8, v0
	s_or_b32 s6, s6, s68
	s_ashr_i32 s37, s36, 31
	s_lshl_b32 s14, s75, 8
	v_add_u32_e32 v26, s6, v0
	s_lshl_b64 s[6:7], s[36:37], 13
	s_add_u32 s10, s0, s6
	s_addc_u32 s11, s1, s7
	v_ashrrev_i32_e32 v27, 31, v26
	s_add_u32 s6, s2, s6
	v_lshlrev_b64 v[0:1], 2, v[26:27]
	s_addc_u32 s7, s3, s7
	v_lshl_add_u64 v[2:3], s[10:11], 0, v[0:1]
	v_lshl_add_u64 v[0:1], s[6:7], 0, v[0:1]
	global_load_dwordx4 v[12:15], v[2:3], off
	global_load_dwordx4 v[8:11], v[0:1], off
	global_load_dwordx4 v[4:7], v[2:3], off offset:16
	s_nop 0
	global_load_dwordx4 v[0:3], v[0:1], off offset:16
	v_mov_b64_e32 v[16:17], s[24:25]
	v_mov_b64_e32 v[22:23], s[26:27]
	v_mov_b64_e32 v[18:19], s[28:29]
	v_mov_b64_e32 v[20:21], s[30:31]
	v_mov_b32_e32 v30, 0
	v_mov_b32_e32 v31, 0
	s_add_i32 s14, s14, s67
	v_and_or_b32 v28, v24, 15, s14
	v_ashrrev_i32_e32 v29, 31, v28
	v_readlane_b32 s80, v254, 14
	v_lshlrev_b64 v[24:25], 11, v[28:29]
	v_readlane_b32 s81, v254, 15
	v_or_b32_e32 v32, 16, v28
	v_ashrrev_i32_e32 v33, 31, v32
	v_lshl_add_u64 v[24:25], s[80:81], 0, v[24:25]
	v_lshl_add_u64 v[24:25], v[24:25], 0, v[26:27]
	s_mov_b32 s6, 0x40000
	s_waitcnt vmcnt(3)
	v_fma_f32 v34, v192, v16, v12
	v_fma_f32 v35, v193, v17, v13
	s_waitcnt vmcnt(1)
	v_fma_f32 v42, v188, v16, v4
	v_fma_f32 v43, v189, v17, v5
	v_med3_f32 v34, v34, s72, v198
	v_med3_f32 v35, v35, s72, v198
	v_mul_f32_e32 v54, v34, v22
	v_mul_f32_e32 v55, v35, v23
	v_fma_f32 v36, v184, v16, v8
	v_fma_f32 v37, v185, v17, v9
	v_med3_f32 v42, v42, s72, v198
	v_med3_f32 v43, v43, s72, v198
	v_mul_f32_e32 v58, v42, v22
	v_mul_f32_e32 v59, v43, v23
	v_exp_f32_e32 v54, v54
	v_exp_f32_e32 v55, v55
	s_waitcnt vmcnt(0)
	v_fma_f32 v44, v180, v16, v0
	v_fma_f32 v45, v181, v17, v1
	v_med3_f32 v36, v36, s73, v198
	v_med3_f32 v37, v37, s73, v198
	v_exp_f32_e32 v58, v58
	v_exp_f32_e32 v59, v59
	s_nop 0
	v_add_f32_e32 v54, v54, v18
	v_add_f32_e32 v55, v55, v19
	v_med3_f32 v44, v44, s73, v198
	v_med3_f32 v45, v45, s73, v198
	v_fma_f32 v36, v36, v20, v20
	v_fma_f32 v37, v37, v21, v21
	s_nop 0
	v_add_f32_e32 v58, v58, v18
	v_add_f32_e32 v59, v59, v19
	v_rcp_f32_e32 v54, v54
	v_rcp_f32_e32 v55, v55
	s_nop 0
	v_mul_f32_e32 v34, v34, v54
	v_mul_f32_e32 v35, v35, v55
	v_fma_f32 v38, v194, v16, v14
	v_fma_f32 v39, v195, v17, v15
	v_fma_f32 v46, v190, v16, v6
	v_fma_f32 v47, v191, v17, v7
	v_fma_f32 v44, v44, v20, v20
	v_fma_f32 v45, v45, v21, v21
	v_rcp_f32_e32 v58, v58
	v_rcp_f32_e32 v59, v59
	s_nop 0
	v_mul_f32_e32 v42, v42, v58
	v_mul_f32_e32 v43, v43, v59
	v_mul_f32_e32 v34, v36, v34
	v_mul_f32_e32 v35, v37, v35
	v_med3_f32 v38, v38, s72, v198
	v_mul_f32_e32 v36, v44, v42
	v_mul_f32_e32 v37, v45, v43
	v_cvt_pk_fp8_f32 v30, v34, v35
	v_cvt_pk_fp8_f32 v31, v36, v37
	v_med3_f32 v39, v39, s72, v198
	v_med3_f32 v46, v46, s72, v198
	v_med3_f32 v47, v47, s72, v198
	v_mul_f32_e32 v56, v38, v22
	v_mul_f32_e32 v57, v39, v23
	v_mul_f32_e32 v60, v46, v22
	v_mul_f32_e32 v61, v47, v23
	v_fma_f32 v40, v186, v16, v10
	v_fma_f32 v41, v187, v17, v11
	v_fma_f32 v48, v182, v16, v2
	v_fma_f32 v49, v183, v17, v3
	v_fma_f32 v50, v176, v16, v12
	v_fma_f32 v51, v177, v17, v13
	v_fma_f32 v52, v172, v16, v8
	v_fma_f32 v53, v173, v17, v9
	s_nop 0
	v_exp_f32_e32 v56, v56
	v_exp_f32_e32 v57, v57
	v_exp_f32_e32 v60, v60
	v_exp_f32_e32 v61, v61
	v_med3_f32 v40, v40, s73, v198
	v_med3_f32 v41, v41, s73, v198
	v_med3_f32 v48, v48, s73, v198
	v_med3_f32 v49, v49, s73, v198
	s_nop 0
	v_add_f32_e32 v56, v56, v18
	v_add_f32_e32 v57, v57, v19
	s_nop 0
	v_add_f32_e32 v60, v60, v18
	v_add_f32_e32 v61, v61, v19
	v_fma_f32 v40, v40, v20, v20
	v_fma_f32 v41, v41, v21, v21
	v_fma_f32 v48, v48, v20, v20
	v_fma_f32 v49, v49, v21, v21
	v_med3_f32 v50, v50, s72, v198
	v_rcp_f32_e32 v56, v56
	v_rcp_f32_e32 v57, v57
	v_rcp_f32_e32 v60, v60
	v_rcp_f32_e32 v61, v61
	s_nop 0
	v_mul_f32_e32 v38, v38, v56
	v_mul_f32_e32 v39, v39, v57
	s_nop 0
	v_mul_f32_e32 v46, v46, v60
	v_mul_f32_e32 v47, v47, v61
	v_med3_f32 v51, v51, s72, v198
	v_mul_f32_e32 v34, v40, v38
	v_mul_f32_e32 v35, v41, v39
	v_mul_f32_e32 v36, v48, v46
	v_mul_f32_e32 v37, v49, v47
	v_mul_f32_e32 v62, v50, v22
	v_mul_f32_e32 v63, v51, v23
	v_mov_b32_e32 v38, 0
	v_cvt_pk_fp8_f32 v30, v34, v35 op_sel:[0,0,1]
	v_cvt_pk_fp8_f32 v31, v36, v37 op_sel:[0,0,1]
	v_exp_f32_e32 v62, v62
	v_exp_f32_e32 v63, v63
	s_nop 0
	v_add_f32_e32 v34, v62, v18
	v_add_f32_e32 v35, v63, v19
	global_store_dwordx2 v[24:25], v[30:31], off
	v_rcp_f32_e32 v34, v34
	v_rcp_f32_e32 v35, v35
	v_med3_f32 v30, v52, s73, v198
	v_med3_f32 v31, v53, s73, v198
	v_fma_f32 v30, v30, v20, v20
	v_fma_f32 v31, v31, v21, v21
	s_nop 0
	v_mul_f32_e32 v34, v50, v34
	v_mul_f32_e32 v35, v51, v35
	v_mov_b32_e32 v39, 0
	v_mul_f32_e32 v30, v30, v34
	v_mul_f32_e32 v31, v31, v35
	v_fma_f32 v34, v178, v16, v14
	v_fma_f32 v35, v179, v17, v15
	s_nop 0
	v_med3_f32 v34, v34, s72, v198
	v_med3_f32 v35, v35, s72, v198
	v_mul_f32_e32 v36, v34, v22
	v_mul_f32_e32 v37, v35, v23
	v_cvt_pk_fp8_f32 v38, v30, v31
	v_exp_f32_e32 v36, v36
	v_exp_f32_e32 v37, v37
	v_fma_f32 v30, v174, v16, v10
	v_fma_f32 v31, v175, v17, v11
	s_nop 0
	v_add_f32_e32 v36, v36, v18
	v_add_f32_e32 v37, v37, v19
	s_nop 0
	v_rcp_f32_e32 v36, v36
	v_rcp_f32_e32 v37, v37
	v_med3_f32 v30, v30, s73, v198
	v_med3_f32 v31, v31, s73, v198
	v_fma_f32 v30, v30, v20, v20
	v_fma_f32 v31, v31, v21, v21
	s_nop 0
	v_mul_f32_e32 v34, v34, v36
	v_mul_f32_e32 v35, v35, v37
	v_fma_f32 v36, v168, v16, v4
	v_fma_f32 v37, v169, v17, v5
	s_nop 0
	v_med3_f32 v36, v36, s72, v198
	v_med3_f32 v37, v37, s72, v198
	v_mul_f32_e32 v40, v36, v22
	v_mul_f32_e32 v41, v37, v23
	v_mul_f32_e32 v30, v30, v34
	v_mul_f32_e32 v31, v31, v35
	s_nop 0
	v_exp_f32_e32 v40, v40
	v_exp_f32_e32 v41, v41
	v_cvt_pk_fp8_f32 v38, v30, v31 op_sel:[0,0,1]
	v_fma_f32 v30, v164, v16, v0
	v_fma_f32 v31, v165, v17, v1
	s_nop 0
	v_add_f32_e32 v34, v40, v18
	v_add_f32_e32 v35, v41, v19
	s_nop 0
	v_rcp_f32_e32 v34, v34
	v_rcp_f32_e32 v35, v35
	v_med3_f32 v30, v30, s73, v198
	v_med3_f32 v31, v31, s73, v198
	v_fma_f32 v30, v30, v20, v20
	v_fma_f32 v31, v31, v21, v21
	s_nop 0
	v_mul_f32_e32 v34, v36, v34
	v_mul_f32_e32 v35, v37, v35
	s_nop 0
	v_mul_f32_e32 v30, v30, v34
	v_mul_f32_e32 v31, v31, v35
	v_fma_f32 v34, v170, v16, v6
	v_fma_f32 v35, v171, v17, v7
	s_nop 0
	v_cvt_pk_fp8_f32 v39, v30, v31
	v_med3_f32 v34, v34, s72, v198
	v_med3_f32 v35, v35, s72, v198
	v_mul_f32_e32 v36, v34, v22
	v_mul_f32_e32 v37, v35, v23
	v_fma_f32 v30, v166, v16, v2
	v_fma_f32 v31, v167, v17, v3
	s_nop 0
	v_exp_f32_e32 v36, v36
	v_exp_f32_e32 v37, v37
	v_med3_f32 v30, v30, s73, v198
	v_med3_f32 v31, v31, s73, v198
	s_nop 0
	v_add_f32_e32 v36, v36, v18
	v_add_f32_e32 v37, v37, v19
	v_fma_f32 v30, v30, v20, v20
	v_fma_f32 v31, v31, v21, v21
	s_nop 0
	v_rcp_f32_e32 v36, v36
	v_rcp_f32_e32 v37, v37
	s_nop 0
	v_mul_f32_e32 v34, v34, v36
	v_mul_f32_e32 v35, v35, v37
	v_fma_f32 v36, v156, v16, v8
	v_fma_f32 v37, v157, v17, v9
	s_nop 0
	v_mul_f32_e32 v30, v30, v34
	v_mul_f32_e32 v31, v31, v35
	v_med3_f32 v36, v36, s73, v198
	v_cvt_pk_fp8_f32 v39, v30, v31 op_sel:[0,0,1]
	v_lshlrev_b64 v[30:31], 11, v[32:33]
	v_lshl_add_u64 v[30:31], s[80:81], 0, v[30:31]
	v_lshl_add_u64 v[30:31], v[30:31], 0, v[26:27]
	global_store_dwordx2 v[30:31], v[38:39], off
	v_fma_f32 v30, v160, v16, v12
	v_fma_f32 v31, v161, v17, v13
	v_med3_f32 v37, v37, s73, v198
	v_med3_f32 v30, v30, s72, v198
	v_med3_f32 v31, v31, s72, v198
	v_mul_f32_e32 v32, v30, v22
	v_mul_f32_e32 v33, v31, v23
	v_fma_f32 v36, v36, v20, v20
	v_fma_f32 v37, v37, v21, v21
	v_mov_b32_e32 v38, 0
	v_exp_f32_e32 v32, v32
	v_exp_f32_e32 v33, v33
	s_nop 0
	v_add_f32_e32 v32, v32, v18
	v_add_f32_e32 v33, v33, v19
	v_mov_b32_e32 v39, 0
	v_rcp_f32_e32 v32, v32
	v_rcp_f32_e32 v33, v33
	s_nop 0
	v_mul_f32_e32 v30, v30, v32
	v_mul_f32_e32 v31, v31, v33
	v_fma_f32 v32, v162, v16, v14
	v_fma_f32 v33, v163, v17, v15
	v_or_b32_e32 v34, 32, v28
	v_mul_f32_e32 v30, v36, v30
	v_mul_f32_e32 v31, v37, v31
	v_med3_f32 v32, v32, s72, v198
	v_med3_f32 v33, v33, s72, v198
	v_mul_f32_e32 v36, v32, v22
	v_mul_f32_e32 v37, v33, v23
	v_cvt_pk_fp8_f32 v38, v30, v31
	v_exp_f32_e32 v36, v36
	v_exp_f32_e32 v37, v37
	v_fma_f32 v30, v158, v16, v10
	v_fma_f32 v31, v159, v17, v11
	s_nop 0
	v_add_f32_e32 v36, v36, v18
	v_add_f32_e32 v37, v37, v19
	v_ashrrev_i32_e32 v35, 31, v34
	v_rcp_f32_e32 v36, v36
	v_rcp_f32_e32 v37, v37
	v_med3_f32 v30, v30, s73, v198
	v_med3_f32 v31, v31, s73, v198
	v_fma_f32 v30, v30, v20, v20
	v_fma_f32 v31, v31, v21, v21
	s_nop 0
	v_mul_f32_e32 v32, v32, v36
	v_mul_f32_e32 v33, v33, v37
	v_fma_f32 v36, v152, v16, v4
	v_fma_f32 v37, v153, v17, v5
	v_or_b32_e32 v28, 48, v28
	v_med3_f32 v36, v36, s72, v198
	v_med3_f32 v37, v37, s72, v198
	v_mul_f32_e32 v40, v36, v22
	v_mul_f32_e32 v41, v37, v23
	v_mul_f32_e32 v30, v30, v32
	v_mul_f32_e32 v31, v31, v33
	v_ashrrev_i32_e32 v29, 31, v28
	v_exp_f32_e32 v40, v40
	v_exp_f32_e32 v41, v41
	v_cvt_pk_fp8_f32 v38, v30, v31 op_sel:[0,0,1]
	v_fma_f32 v30, v148, v16, v0
	v_fma_f32 v31, v149, v17, v1
	s_nop 0
	v_add_f32_e32 v32, v40, v18
	v_add_f32_e32 v33, v41, v19
	v_lshlrev_b64 v[28:29], 11, v[28:29]
	v_rcp_f32_e32 v32, v32
	v_rcp_f32_e32 v33, v33
	v_med3_f32 v30, v30, s73, v198
	v_med3_f32 v31, v31, s73, v198
	v_fma_f32 v30, v30, v20, v20
	v_fma_f32 v31, v31, v21, v21
	s_nop 0
	v_mul_f32_e32 v32, v36, v32
	v_mul_f32_e32 v33, v37, v33
	v_lshl_add_u64 v[28:29], s[80:81], 0, v[28:29]
	v_mul_f32_e32 v30, v30, v32
	v_mul_f32_e32 v31, v31, v33
	v_fma_f32 v32, v154, v16, v6
	v_fma_f32 v33, v155, v17, v7
	s_nop 0
	v_cvt_pk_fp8_f32 v39, v30, v31
	v_med3_f32 v32, v32, s72, v198
	v_med3_f32 v33, v33, s72, v198
	v_mul_f32_e32 v36, v32, v22
	v_mul_f32_e32 v37, v33, v23
	v_fma_f32 v30, v150, v16, v2
	v_fma_f32 v31, v151, v17, v3
	s_nop 0
	v_exp_f32_e32 v36, v36
	v_exp_f32_e32 v37, v37
	v_med3_f32 v30, v30, s73, v198
	v_med3_f32 v31, v31, s73, v198
	s_nop 0
	v_add_f32_e32 v36, v36, v18
	v_add_f32_e32 v37, v37, v19
	v_fma_f32 v30, v30, v20, v20
	v_fma_f32 v31, v31, v21, v21
	s_nop 0
	v_rcp_f32_e32 v36, v36
	v_rcp_f32_e32 v37, v37
	s_nop 0
	v_mul_f32_e32 v32, v32, v36
	v_mul_f32_e32 v33, v33, v37
	v_mov_b32_e32 v36, 0
	v_mul_f32_e32 v30, v30, v32
	v_mul_f32_e32 v31, v31, v33
	v_mov_b32_e32 v37, 0
	v_cvt_pk_fp8_f32 v39, v30, v31 op_sel:[0,0,1]
	v_lshlrev_b64 v[30:31], 11, v[34:35]
	v_lshl_add_u64 v[30:31], s[80:81], 0, v[30:31]
	v_lshl_add_u64 v[30:31], v[30:31], 0, v[26:27]
	global_store_dwordx2 v[30:31], v[38:39], off
	v_fma_f32 v30, v144, v16, v12
	v_fma_f32 v31, v145, v17, v13
	v_fma_f32 v34, v140, v16, v8
	v_fma_f32 v35, v141, v17, v9
	v_lshl_add_u64 v[26:27], v[28:29], 0, v[26:27]
	v_med3_f32 v30, v30, s72, v198
	v_med3_f32 v31, v31, s72, v198
	v_mul_f32_e32 v32, v30, v22
	v_mul_f32_e32 v33, v31, v23
	v_med3_f32 v34, v34, s73, v198
	v_exp_f32_e32 v32, v32
	v_exp_f32_e32 v33, v33
	s_nop 0
	v_add_f32_e32 v32, v32, v18
	v_add_f32_e32 v33, v33, v19
	v_med3_f32 v35, v35, s73, v198
	v_rcp_f32_e32 v32, v32
	v_rcp_f32_e32 v33, v33
	v_fma_f32 v34, v34, v20, v20
	v_fma_f32 v35, v35, v21, v21
	s_nop 0
	v_mul_f32_e32 v30, v30, v32
	v_mul_f32_e32 v31, v31, v33
	v_fma_f32 v32, v146, v16, v14
	v_fma_f32 v33, v147, v17, v15
	s_nop 0
	v_mul_f32_e32 v30, v34, v30
	v_mul_f32_e32 v31, v35, v31
	v_med3_f32 v32, v32, s72, v198
	v_med3_f32 v33, v33, s72, v198
	v_mul_f32_e32 v34, v32, v22
	v_mul_f32_e32 v35, v33, v23
	v_cvt_pk_fp8_f32 v36, v30, v31
	v_exp_f32_e32 v34, v34
	v_exp_f32_e32 v35, v35
	v_fma_f32 v30, v142, v16, v10
	v_fma_f32 v31, v143, v17, v11
	s_nop 0
	v_add_f32_e32 v34, v34, v18
	v_add_f32_e32 v35, v35, v19
	s_nop 0
	v_rcp_f32_e32 v34, v34
	v_rcp_f32_e32 v35, v35
	v_med3_f32 v30, v30, s73, v198
	v_med3_f32 v31, v31, s73, v198
	v_fma_f32 v30, v30, v20, v20
	v_fma_f32 v31, v31, v21, v21
	s_nop 0
	v_mul_f32_e32 v32, v32, v34
	v_mul_f32_e32 v33, v33, v35
	v_fma_f32 v34, v136, v16, v4
	v_fma_f32 v35, v137, v17, v5
	s_nop 0
	v_med3_f32 v34, v34, s72, v198
	v_med3_f32 v35, v35, s72, v198
	v_mul_f32_e32 v38, v34, v22
	v_mul_f32_e32 v39, v35, v23
	v_mul_f32_e32 v30, v30, v32
	v_mul_f32_e32 v31, v31, v33
	s_nop 0
	v_exp_f32_e32 v38, v38
	v_exp_f32_e32 v39, v39
	v_cvt_pk_fp8_f32 v36, v30, v31 op_sel:[0,0,1]
	v_fma_f32 v30, v132, v16, v0
	v_fma_f32 v31, v133, v17, v1
	s_nop 0
	v_add_f32_e32 v32, v38, v18
	v_add_f32_e32 v33, v39, v19
	s_nop 0
	v_rcp_f32_e32 v32, v32
	v_rcp_f32_e32 v33, v33
	v_med3_f32 v30, v30, s73, v198
	v_med3_f32 v31, v31, s73, v198
	v_fma_f32 v30, v30, v20, v20
	v_fma_f32 v31, v31, v21, v21
	s_nop 0
	v_mul_f32_e32 v32, v34, v32
	v_mul_f32_e32 v33, v35, v33
	s_nop 0
	v_mul_f32_e32 v30, v30, v32
	v_mul_f32_e32 v31, v31, v33
	v_fma_f32 v32, v138, v16, v6
	v_fma_f32 v33, v139, v17, v7
	s_nop 0
	v_cvt_pk_fp8_f32 v37, v30, v31
	v_med3_f32 v32, v32, s72, v198
	v_med3_f32 v33, v33, s72, v198
	v_mul_f32_e32 v34, v32, v22
	v_mul_f32_e32 v35, v33, v23
	v_fma_f32 v30, v134, v16, v2
	v_fma_f32 v31, v135, v17, v3
	s_nop 0
	v_exp_f32_e32 v34, v34
	v_exp_f32_e32 v35, v35
	v_med3_f32 v30, v30, s73, v198
	v_med3_f32 v31, v31, s73, v198
	s_nop 0
	v_add_f32_e32 v34, v34, v18
	v_add_f32_e32 v35, v35, v19
	v_fma_f32 v30, v30, v20, v20
	v_fma_f32 v31, v31, v21, v21
	s_nop 0
	v_rcp_f32_e32 v34, v34
	v_rcp_f32_e32 v35, v35
	s_nop 0
	v_mul_f32_e32 v32, v32, v34
	v_mul_f32_e32 v33, v33, v35
	s_nop 0
	v_mul_f32_e32 v30, v30, v32
	v_mul_f32_e32 v31, v31, v33
	s_nop 0
	v_cvt_pk_fp8_f32 v37, v30, v31 op_sel:[0,0,1]
	v_fma_f32 v30, v128, v16, v12
	v_fma_f32 v31, v129, v17, v13
	global_store_dwordx2 v[26:27], v[36:37], off
	v_med3_f32 v30, v30, s72, v198
	v_med3_f32 v31, v31, s72, v198
	v_mul_f32_e32 v32, v30, v22
	v_mul_f32_e32 v33, v31, v23
	v_fma_f32 v26, v124, v16, v8
	v_fma_f32 v27, v125, v17, v9
	s_nop 0
	v_exp_f32_e32 v32, v32
	v_exp_f32_e32 v33, v33
	s_nop 0
	v_add_f32_e32 v28, v32, v18
	v_add_f32_e32 v29, v33, v19
	v_med3_f32 v26, v26, s73, v198
	v_rcp_f32_e32 v28, v28
	v_rcp_f32_e32 v29, v29
	v_med3_f32 v27, v27, s73, v198
	v_fma_f32 v26, v26, v20, v20
	v_fma_f32 v27, v27, v21, v21
	s_nop 0
	v_mul_f32_e32 v28, v30, v28
	v_mul_f32_e32 v29, v31, v29
	v_mov_b32_e32 v32, 0
	v_mul_f32_e32 v26, v26, v28
	v_mul_f32_e32 v27, v27, v29
	v_fma_f32 v28, v130, v16, v14
	v_fma_f32 v29, v131, v17, v15
	v_mov_b32_e32 v33, 0
	v_med3_f32 v28, v28, s72, v198
	v_med3_f32 v29, v29, s72, v198
	v_mul_f32_e32 v30, v28, v22
	v_mul_f32_e32 v31, v29, v23
	v_cvt_pk_fp8_f32 v32, v26, v27
	v_exp_f32_e32 v30, v30
	v_exp_f32_e32 v31, v31
	v_fma_f32 v26, v126, v16, v10
	v_fma_f32 v27, v127, v17, v11
	s_nop 0
	v_add_f32_e32 v30, v30, v18
	v_add_f32_e32 v31, v31, v19
	s_nop 0
	v_rcp_f32_e32 v30, v30
	v_rcp_f32_e32 v31, v31
	v_med3_f32 v26, v26, s73, v198
	v_med3_f32 v27, v27, s73, v198
	v_fma_f32 v26, v26, v20, v20
	v_fma_f32 v27, v27, v21, v21
	s_nop 0
	v_mul_f32_e32 v28, v28, v30
	v_mul_f32_e32 v29, v29, v31
	v_fma_f32 v30, v120, v16, v4
	v_fma_f32 v31, v121, v17, v5
	s_nop 0
	v_med3_f32 v30, v30, s72, v198
	v_med3_f32 v31, v31, s72, v198
	v_mul_f32_e32 v34, v30, v22
	v_mul_f32_e32 v35, v31, v23
	v_mul_f32_e32 v26, v26, v28
	v_mul_f32_e32 v27, v27, v29
	s_nop 0
	v_exp_f32_e32 v34, v34
	v_exp_f32_e32 v35, v35
	v_cvt_pk_fp8_f32 v32, v26, v27 op_sel:[0,0,1]
	v_fma_f32 v26, v116, v16, v0
	v_fma_f32 v27, v117, v17, v1
	s_nop 0
	v_add_f32_e32 v28, v34, v18
	v_add_f32_e32 v29, v35, v19
	s_nop 0
	v_rcp_f32_e32 v28, v28
	v_rcp_f32_e32 v29, v29
	v_med3_f32 v26, v26, s73, v198
	v_med3_f32 v27, v27, s73, v198
	v_fma_f32 v26, v26, v20, v20
	v_fma_f32 v27, v27, v21, v21
	s_nop 0
	v_mul_f32_e32 v28, v30, v28
	v_mul_f32_e32 v29, v31, v29
	s_nop 0
	v_mul_f32_e32 v26, v26, v28
	v_mul_f32_e32 v27, v27, v29
	v_fma_f32 v28, v122, v16, v6
	v_fma_f32 v29, v123, v17, v7
	s_nop 0
	v_cvt_pk_fp8_f32 v33, v26, v27
	v_med3_f32 v28, v28, s72, v198
	v_med3_f32 v29, v29, s72, v198
	v_mul_f32_e32 v30, v28, v22
	v_mul_f32_e32 v31, v29, v23
	v_fma_f32 v26, v118, v16, v2
	v_fma_f32 v27, v119, v17, v3
	s_nop 0
	v_exp_f32_e32 v30, v30
	v_exp_f32_e32 v31, v31
	v_med3_f32 v26, v26, s73, v198
	v_med3_f32 v27, v27, s73, v198
	s_nop 0
	v_add_f32_e32 v30, v30, v18
	v_add_f32_e32 v31, v31, v19
	v_fma_f32 v26, v26, v20, v20
	v_fma_f32 v27, v27, v21, v21
	s_nop 0
	v_rcp_f32_e32 v30, v30
	v_rcp_f32_e32 v31, v31
	s_nop 0
	v_mul_f32_e32 v28, v28, v30
	v_mul_f32_e32 v29, v29, v31
	v_add_co_u32_e32 v30, vcc, s6, v24
	v_mul_f32_e32 v26, v26, v28
	v_mul_f32_e32 v27, v27, v29
	s_mov_b32 s6, 0x48000
	v_cvt_pk_fp8_f32 v33, v26, v27 op_sel:[0,0,1]
	v_fma_f32 v26, v112, v16, v12
	v_fma_f32 v27, v113, v17, v13
	v_addc_co_u32_e32 v31, vcc, 0, v25, vcc
	v_med3_f32 v26, v26, s72, v198
	v_med3_f32 v27, v27, s72, v198
	v_mul_f32_e32 v28, v26, v22
	v_mul_f32_e32 v29, v27, v23
	global_store_dwordx2 v[30:31], v[32:33], off
	v_exp_f32_e32 v28, v28
	v_exp_f32_e32 v29, v29
	v_fma_f32 v30, v108, v16, v8
	v_fma_f32 v31, v109, v17, v9
	s_nop 0
	v_add_f32_e32 v28, v28, v18
	v_add_f32_e32 v29, v29, v19
	v_mov_b32_e32 v32, 0
	v_rcp_f32_e32 v28, v28
	v_rcp_f32_e32 v29, v29
	v_med3_f32 v30, v30, s73, v198
	v_med3_f32 v31, v31, s73, v198
	v_fma_f32 v30, v30, v20, v20
	v_fma_f32 v31, v31, v21, v21
	s_nop 0
	v_mul_f32_e32 v26, v26, v28
	v_mul_f32_e32 v27, v27, v29
	v_fma_f32 v28, v114, v16, v14
	v_fma_f32 v29, v115, v17, v15
	v_mov_b32_e32 v33, 0
	v_mul_f32_e32 v26, v30, v26
	v_mul_f32_e32 v27, v31, v27
	v_med3_f32 v28, v28, s72, v198
	v_med3_f32 v29, v29, s72, v198
	v_mul_f32_e32 v30, v28, v22
	v_mul_f32_e32 v31, v29, v23
	v_cvt_pk_fp8_f32 v32, v26, v27
	v_exp_f32_e32 v30, v30
	v_exp_f32_e32 v31, v31
	v_fma_f32 v26, v110, v16, v10
	v_fma_f32 v27, v111, v17, v11
	s_nop 0
	v_add_f32_e32 v30, v30, v18
	v_add_f32_e32 v31, v31, v19
	s_nop 0
	v_rcp_f32_e32 v30, v30
	v_rcp_f32_e32 v31, v31
	v_med3_f32 v26, v26, s73, v198
	v_med3_f32 v27, v27, s73, v198
	v_fma_f32 v26, v26, v20, v20
	v_fma_f32 v27, v27, v21, v21
	s_nop 0
	v_mul_f32_e32 v28, v28, v30
	v_mul_f32_e32 v29, v29, v31
	v_fma_f32 v30, v104, v16, v4
	v_fma_f32 v31, v105, v17, v5
	s_nop 0
	v_med3_f32 v30, v30, s72, v198
	v_med3_f32 v31, v31, s72, v198
	v_mul_f32_e32 v34, v30, v22
	v_mul_f32_e32 v35, v31, v23
	v_mul_f32_e32 v26, v26, v28
	v_mul_f32_e32 v27, v27, v29
	s_nop 0
	v_exp_f32_e32 v34, v34
	v_exp_f32_e32 v35, v35
	v_cvt_pk_fp8_f32 v32, v26, v27 op_sel:[0,0,1]
	v_fma_f32 v26, v100, v16, v0
	v_fma_f32 v27, v101, v17, v1
	s_nop 0
	v_add_f32_e32 v28, v34, v18
	v_add_f32_e32 v29, v35, v19
	s_nop 0
	v_rcp_f32_e32 v28, v28
	v_rcp_f32_e32 v29, v29
	v_med3_f32 v26, v26, s73, v198
	v_med3_f32 v27, v27, s73, v198
	v_fma_f32 v26, v26, v20, v20
	v_fma_f32 v27, v27, v21, v21
	s_nop 0
	v_mul_f32_e32 v28, v30, v28
	v_mul_f32_e32 v29, v31, v29
	s_nop 0
	v_mul_f32_e32 v26, v26, v28
	v_mul_f32_e32 v27, v27, v29
	v_fma_f32 v28, v106, v16, v6
	v_fma_f32 v29, v107, v17, v7
	s_nop 0
	v_cvt_pk_fp8_f32 v33, v26, v27
	v_med3_f32 v28, v28, s72, v198
	v_med3_f32 v29, v29, s72, v198
	v_mul_f32_e32 v30, v28, v22
	v_mul_f32_e32 v31, v29, v23
	v_fma_f32 v26, v102, v16, v2
	v_fma_f32 v27, v103, v17, v3
	s_nop 0
	v_exp_f32_e32 v30, v30
	v_exp_f32_e32 v31, v31
	v_med3_f32 v26, v26, s73, v198
	v_med3_f32 v27, v27, s73, v198
	s_nop 0
	v_add_f32_e32 v30, v30, v18
	v_add_f32_e32 v31, v31, v19
	v_fma_f32 v26, v26, v20, v20
	v_fma_f32 v27, v27, v21, v21
	s_nop 0
	v_rcp_f32_e32 v30, v30
	v_rcp_f32_e32 v31, v31
	s_nop 0
	v_mul_f32_e32 v28, v28, v30
	v_mul_f32_e32 v29, v29, v31
	v_add_co_u32_e32 v30, vcc, s6, v24
	v_mul_f32_e32 v26, v26, v28
	v_mul_f32_e32 v27, v27, v29
	s_mov_b32 s6, 0x50000
	v_cvt_pk_fp8_f32 v33, v26, v27 op_sel:[0,0,1]
	v_fma_f32 v26, v96, v16, v12
	v_fma_f32 v27, v97, v17, v13
	v_addc_co_u32_e32 v31, vcc, 0, v25, vcc
	v_med3_f32 v26, v26, s72, v198
	v_med3_f32 v27, v27, s72, v198
	v_mul_f32_e32 v28, v26, v22
	v_mul_f32_e32 v29, v27, v23
	global_store_dwordx2 v[30:31], v[32:33], off
	v_exp_f32_e32 v28, v28
	v_exp_f32_e32 v29, v29
	v_fma_f32 v30, v92, v16, v8
	v_fma_f32 v31, v93, v17, v9
	s_nop 0
	v_add_f32_e32 v28, v28, v18
	v_add_f32_e32 v29, v29, v19
	v_mov_b32_e32 v32, 0
	v_rcp_f32_e32 v28, v28
	v_rcp_f32_e32 v29, v29
	v_med3_f32 v30, v30, s73, v198
	v_med3_f32 v31, v31, s73, v198
	v_fma_f32 v30, v30, v20, v20
	v_fma_f32 v31, v31, v21, v21
	s_nop 0
	v_mul_f32_e32 v26, v26, v28
	v_mul_f32_e32 v27, v27, v29
	v_fma_f32 v28, v98, v16, v14
	v_fma_f32 v29, v99, v17, v15
	v_mov_b32_e32 v33, 0
	v_mul_f32_e32 v26, v30, v26
	v_mul_f32_e32 v27, v31, v27
	v_med3_f32 v28, v28, s72, v198
	v_med3_f32 v29, v29, s72, v198
	v_mul_f32_e32 v30, v28, v22
	v_mul_f32_e32 v31, v29, v23
	v_cvt_pk_fp8_f32 v32, v26, v27
	v_exp_f32_e32 v30, v30
	v_exp_f32_e32 v31, v31
	v_fma_f32 v26, v94, v16, v10
	v_fma_f32 v27, v95, v17, v11
	s_nop 0
	v_add_f32_e32 v30, v30, v18
	v_add_f32_e32 v31, v31, v19
	v_fma_f32 v12, v80, v16, v12
	v_fma_f32 v13, v81, v17, v13
	v_fma_f32 v8, v76, v16, v8
	v_fma_f32 v9, v77, v17, v9
	v_fma_f32 v10, v78, v16, v10
	v_fma_f32 v11, v79, v17, v11
	s_nop 0
	v_rcp_f32_e32 v30, v30
	v_rcp_f32_e32 v31, v31
	v_med3_f32 v26, v26, s73, v198
	v_med3_f32 v27, v27, s73, v198
	v_fma_f32 v26, v26, v20, v20
	v_fma_f32 v27, v27, v21, v21
	s_nop 0
	v_mul_f32_e32 v28, v28, v30
	v_mul_f32_e32 v29, v29, v31
	v_fma_f32 v30, v88, v16, v4
	v_fma_f32 v31, v89, v17, v5
	v_med3_f32 v12, v12, s72, v198
	v_med3_f32 v30, v30, s72, v198
	v_med3_f32 v31, v31, s72, v198
	v_mul_f32_e32 v34, v30, v22
	v_mul_f32_e32 v35, v31, v23
	v_mul_f32_e32 v26, v26, v28
	v_mul_f32_e32 v27, v27, v29
	v_med3_f32 v13, v13, s72, v198
	v_exp_f32_e32 v34, v34
	v_exp_f32_e32 v35, v35
	v_cvt_pk_fp8_f32 v32, v26, v27 op_sel:[0,0,1]
	v_fma_f32 v26, v84, v16, v0
	v_fma_f32 v27, v85, v17, v1
	s_nop 0
	v_add_f32_e32 v28, v34, v18
	v_add_f32_e32 v29, v35, v19
	v_med3_f32 v8, v8, s73, v198
	v_rcp_f32_e32 v28, v28
	v_rcp_f32_e32 v29, v29
	v_med3_f32 v26, v26, s73, v198
	v_med3_f32 v27, v27, s73, v198
	v_fma_f32 v26, v26, v20, v20
	v_fma_f32 v27, v27, v21, v21
	s_nop 0
	v_mul_f32_e32 v28, v30, v28
	v_mul_f32_e32 v29, v31, v29
	v_med3_f32 v9, v9, s73, v198
	v_mul_f32_e32 v26, v26, v28
	v_mul_f32_e32 v27, v27, v29
	v_fma_f32 v28, v90, v16, v6
	v_fma_f32 v29, v91, v17, v7
	v_fma_f32 v8, v8, v20, v20
	v_fma_f32 v9, v9, v21, v21
	v_med3_f32 v10, v10, s73, v198
	v_med3_f32 v28, v28, s72, v198
	v_med3_f32 v29, v29, s72, v198
	v_mul_f32_e32 v30, v28, v22
	v_mul_f32_e32 v31, v29, v23
	v_cvt_pk_fp8_f32 v33, v26, v27
	v_fma_f32 v26, v86, v16, v2
	v_fma_f32 v27, v87, v17, v3
	v_exp_f32_e32 v30, v30
	v_exp_f32_e32 v31, v31
	v_med3_f32 v26, v26, s73, v198
	v_med3_f32 v27, v27, s73, v198
	s_nop 0
	v_add_f32_e32 v30, v30, v18
	v_add_f32_e32 v31, v31, v19
	v_fma_f32 v26, v26, v20, v20
	v_fma_f32 v27, v27, v21, v21
	v_med3_f32 v11, v11, s73, v198
	v_rcp_f32_e32 v30, v30
	v_rcp_f32_e32 v31, v31
	s_nop 0
	v_mul_f32_e32 v28, v28, v30
	v_mul_f32_e32 v29, v29, v31
	v_fma_f32 v4, v72, v16, v4
	v_fma_f32 v5, v73, v17, v5
	v_fma_f32 v10, v10, v20, v20
	v_fma_f32 v11, v11, v21, v21
	v_fma_f32 v0, v68, v16, v0
	v_fma_f32 v1, v69, v17, v1
	v_fma_f32 v2, v70, v16, v2
	v_fma_f32 v3, v71, v17, v3
	s_nop 0
	v_mul_f32_e32 v26, v26, v28
	v_mul_f32_e32 v27, v27, v29
	v_med3_f32 v4, v4, s72, v198
	v_cvt_pk_fp8_f32 v33, v26, v27 op_sel:[0,0,1]
	v_mul_f32_e32 v26, v12, v22
	v_mul_f32_e32 v27, v13, v23
	v_med3_f32 v5, v5, s72, v198
	v_exp_f32_e32 v26, v26
	v_exp_f32_e32 v27, v27
	s_nop 0
	v_add_f32_e32 v26, v26, v18
	v_add_f32_e32 v27, v27, v19
	v_med3_f32 v0, v0, s73, v198
	v_rcp_f32_e32 v26, v26
	v_rcp_f32_e32 v27, v27
	s_nop 0
	v_mul_f32_e32 v12, v12, v26
	v_mul_f32_e32 v13, v13, v27
	v_mul_f32_e32 v26, v4, v22
	v_mul_f32_e32 v27, v5, v23
	v_med3_f32 v1, v1, s73, v198
	v_mul_f32_e32 v8, v8, v12
	v_mul_f32_e32 v9, v9, v13
	v_fma_f32 v12, v82, v16, v14
	v_fma_f32 v13, v83, v17, v15
	v_exp_f32_e32 v26, v26
	v_med3_f32 v12, v12, s72, v198
	v_med3_f32 v13, v13, s72, v198
	v_mul_f32_e32 v14, v12, v22
	v_mul_f32_e32 v15, v13, v23
	v_exp_f32_e32 v27, v27
	v_exp_f32_e32 v14, v14
	v_exp_f32_e32 v15, v15
	s_nop 0
	v_add_f32_e32 v14, v14, v18
	v_add_f32_e32 v15, v15, v19
	v_fma_f32 v0, v0, v20, v20
	v_fma_f32 v1, v1, v21, v21
	v_add_co_u32_e32 v28, vcc, s6, v24
	v_rcp_f32_e32 v14, v14
	v_rcp_f32_e32 v15, v15
	s_nop 0
	v_mul_f32_e32 v12, v12, v14
	v_mul_f32_e32 v13, v13, v15
	v_med3_f32 v2, v2, s73, v198
	v_mul_f32_e32 v10, v10, v12
	v_mul_f32_e32 v11, v11, v13
	s_nop 0
	v_add_f32_e32 v12, v26, v18
	v_add_f32_e32 v13, v27, v19
	v_med3_f32 v3, v3, s73, v198
	v_rcp_f32_e32 v12, v12
	v_rcp_f32_e32 v13, v13
	s_nop 0
	v_mul_f32_e32 v4, v4, v12
	v_mul_f32_e32 v5, v5, v13
	v_mov_b32_e32 v13, 0
	v_mul_f32_e32 v0, v0, v4
	v_mul_f32_e32 v1, v1, v5
	v_fma_f32 v4, v74, v16, v6
	v_fma_f32 v5, v75, v17, v7
	v_mov_b32_e32 v12, 0
	v_med3_f32 v4, v4, s72, v198
	v_med3_f32 v5, v5, s72, v198
	v_mul_f32_e32 v6, v4, v22
	v_mul_f32_e32 v7, v5, v23
	v_cvt_pk_fp8_f32 v13, v0, v1
	v_cvt_pk_fp8_f32 v12, v8, v9
	v_exp_f32_e32 v6, v6
	v_exp_f32_e32 v7, v7
	s_nop 0
	v_add_f32_e32 v6, v6, v18
	v_add_f32_e32 v7, v7, v19
	v_addc_co_u32_e32 v29, vcc, 0, v25, vcc
	v_rcp_f32_e32 v6, v6
	v_rcp_f32_e32 v7, v7
	s_nop 0
	v_mul_f32_e32 v0, v4, v6
	v_mul_f32_e32 v1, v5, v7
	v_fma_f32 v2, v2, v20, v20
	v_fma_f32 v3, v3, v21, v21
	v_cvt_pk_fp8_f32 v12, v10, v11 op_sel:[0,0,1]
	v_mul_f32_e32 v0, v2, v0
	v_mul_f32_e32 v1, v3, v1
	s_mov_b64 s[6:7], -1
	v_cvt_pk_fp8_f32 v13, v0, v1 op_sel:[0,0,1]
	v_add_co_u32_e32 v0, vcc, 0x58000, v24
	global_store_dwordx2 v[28:29], v[32:33], off
	s_nop 0
	v_addc_co_u32_e32 v1, vcc, 0, v25, vcc
	s_andn2_b64 vcc, exec, s[34:35]
	global_store_dwordx2 v[0:1], v[12:13], off
	s_cbranch_vccnz .LBB0_2452
	s_andn2_b64 vcc, exec, s[20:21]
	s_cbranch_vccnz .LBB0_2451
	s_barrier
	s_branch .LBB0_2451

.LBB0_2576:
	s_lshl_b32 s6, s74, 8
	v_mbcnt_lo_u32_b32 v130, -1, 0
	v_mbcnt_hi_u32_b32 v130, -1, v130
	s_add_i32 s10, s6, s61
	s_lshl_b32 s6, s73, 8
	v_ashrrev_i32_e32 v128, 1, v130
	v_and_b32_e32 v128, -8, v128
	s_or_b32 s6, s6, s62
	s_ashr_i32 s35, s34, 31
	v_add_u32_e32 v150, s6, v128
	s_lshl_b64 s[6:7], s[34:35], 13
	v_and_or_b32 v144, v130, 15, s10
	s_add_u32 s6, s0, s6
	v_or_b32_e32 v154, 16, v144
	v_or_b32_e32 v156, 32, v144
	v_or_b32_e32 v158, 48, v144
	s_addc_u32 s7, s1, s7
	v_ashrrev_i32_e32 v151, 31, v150
	v_ashrrev_i32_e32 v145, 31, v144
	v_ashrrev_i32_e32 v155, 31, v154
	v_ashrrev_i32_e32 v157, 31, v156
	v_ashrrev_i32_e32 v159, 31, v158
	v_lshl_add_u64 v[128:129], v[150:151], 2, s[6:7]
	v_lshl_add_u64 v[130:131], v[144:145], 2, s[14:15]
	v_lshl_add_u64 v[132:133], v[154:155], 2, s[14:15]
	v_lshl_add_u64 v[134:135], v[156:157], 2, s[14:15]
	v_lshl_add_u64 v[136:137], v[158:159], 2, s[14:15]
	global_load_dword v146, v[130:131], off
	global_load_dword v148, v[130:131], off offset:512
	global_load_dword v152, v[130:131], off offset:576
	global_load_dword v167, v[130:131], off offset:640
	global_load_dword v169, v[132:133], off
	global_load_dword v171, v[134:135], off
	global_load_dword v173, v[136:137], off
	global_load_dword v175, v[130:131], off offset:704
	global_load_dwordx4 v[140:143], v[128:129], off
	s_nop 0
	global_load_dwordx4 v[136:139], v[128:129], off offset:16
	global_load_dwordx4 v[132:135], v[128:129], off offset:512
	s_nop 0
	global_load_dwordx4 v[128:131], v[128:129], off offset:528
	v_mov_b32_e32 v163, 0
	v_mov_b32_e32 v160, 0
	v_mov_b32_e32 v161, 0
	v_mov_b32_e32 v164, 0
	v_mov_b32_e32 v165, 0
	v_mov_b32_e32 v162, 0
	v_lshlrev_b64 v[144:145], 11, v[144:145]
	v_lshl_add_u64 v[144:145], s[12:13], 0, v[144:145]
	v_lshl_add_u64 v[144:145], v[144:145], 0, v[150:151]
	v_lshlrev_b64 v[154:155], 11, v[154:155]
	s_mov_b64 s[6:7], -1
	s_waitcnt vmcnt(11)
	v_mul_f32_e32 v166, 0x42000000, v146
	s_waitcnt vmcnt(10)
	v_mul_f32_e32 v168, 0x42000000, v148
	s_waitcnt vmcnt(9)
	v_mul_f32_e32 v152, 0x42000000, v152
	s_waitcnt vmcnt(8)
	v_mul_f32_e32 v148, 0x42000000, v167
	s_waitcnt vmcnt(7)
	v_mul_f32_e32 v170, 0x42000000, v169
	s_waitcnt vmcnt(6)
	v_mul_f32_e32 v172, 0x42000000, v171
	s_waitcnt vmcnt(5)
	v_mul_f32_e32 v174, 0x42000000, v173
	s_waitcnt vmcnt(4)
	v_mul_f32_e32 v146, 0x42000000, v175
	s_waitcnt vmcnt(3)
	v_fma_f32 v124, v124, s18, v140
	v_fma_f32 v125, v125, s18, v141
	s_waitcnt vmcnt(2)
	v_fma_f32 v88, v88, s18, v136
	v_fma_f32 v89, v89, s18, v137
	v_fma_f32 v72, v72, s18, v136
	v_fma_f32 v73, v73, s18, v137
	s_waitcnt vmcnt(0)
	v_fma_f32 v104, v104, s18, v128
	v_fma_f32 v105, v105, s18, v129
	v_fma_f32 v92, v92, s18, v128
	v_fma_f32 v93, v93, s18, v129
	v_mul_f32_e32 v104, v104, v166
	v_mul_f32_e32 v105, v105, v166
	v_mul_f32_e32 v92, v92, v170
	v_mul_f32_e32 v93, v93, v170
	v_cvt_pk_fp8_f32 v163, v104, v105
	v_mov_b32_e32 v105, 0
	v_cvt_pk_fp8_f32 v105, v92, v93
	v_fma_f32 v92, v94, s18, v130
	v_fma_f32 v93, v95, s18, v131
	v_fma_f32 v94, v98, s18, v142
	v_fma_f32 v95, v99, s18, v143
	v_mul_f32_e32 v88, v88, v172
	v_mul_f32_e32 v89, v89, v172
	v_mov_b32_e32 v99, 0
	v_cvt_pk_fp8_f32 v99, v88, v89
	v_fma_f32 v88, v90, s18, v138
	v_fma_f32 v89, v91, s18, v139
	v_fma_f32 v76, v76, s18, v128
	v_fma_f32 v77, v77, s18, v129
	v_mul_f32_e32 v88, v88, v172
	v_mul_f32_e32 v89, v89, v172
	v_mul_f32_e32 v76, v76, v172
	v_mul_f32_e32 v77, v77, v172
	v_cvt_pk_fp8_f32 v99, v88, v89 op_sel:[0,0,1]
	v_mov_b32_e32 v89, 0
	v_cvt_pk_fp8_f32 v89, v76, v77
	v_fma_f32 v76, v78, s18, v130
	v_fma_f32 v77, v79, s18, v131
	v_fma_f32 v78, v82, s18, v142
	v_fma_f32 v79, v83, s18, v143
	v_mul_f32_e32 v72, v72, v174
	v_mul_f32_e32 v73, v73, v174
	v_mov_b32_e32 v83, 0
	v_cvt_pk_fp8_f32 v83, v72, v73
	v_fma_f32 v72, v74, s18, v138
	v_fma_f32 v73, v75, s18, v139
	v_fma_f32 v64, v64, s18, v128
	v_fma_f32 v65, v65, s18, v129
	v_mul_f32_e32 v72, v72, v174
	v_mul_f32_e32 v73, v73, v174
	v_mul_f32_e32 v64, v64, v174
	v_mul_f32_e32 v65, v65, v174
	v_cvt_pk_fp8_f32 v83, v72, v73 op_sel:[0,0,1]
	v_mov_b32_e32 v73, 0
	v_fma_f32 v56, v56, s18, v136
	v_fma_f32 v57, v57, s18, v137
	v_cvt_pk_fp8_f32 v73, v64, v65
	v_fma_f32 v64, v66, s18, v130
	v_fma_f32 v65, v67, s18, v131
	v_mul_f32_e32 v56, v56, v168
	v_mul_f32_e32 v57, v57, v168
	v_mov_b32_e32 v67, 0
	v_cvt_pk_fp8_f32 v67, v56, v57
	v_fma_f32 v56, v58, s18, v138
	v_fma_f32 v57, v59, s18, v139
	v_fma_f32 v44, v44, s18, v128
	v_fma_f32 v45, v45, s18, v129
	v_mul_f32_e32 v56, v56, v168
	v_mul_f32_e32 v57, v57, v168
	v_mul_f32_e32 v44, v44, v168
	v_mul_f32_e32 v45, v45, v168
	v_cvt_pk_fp8_f32 v67, v56, v57 op_sel:[0,0,1]
	v_mov_b32_e32 v57, 0
	v_fma_f32 v40, v40, s18, v136
	v_fma_f32 v41, v41, s18, v137
	v_cvt_pk_fp8_f32 v57, v44, v45
	v_fma_f32 v44, v46, s18, v130
	v_fma_f32 v45, v47, s18, v131
	v_fma_f32 v46, v50, s18, v142
	v_fma_f32 v47, v51, s18, v143
	v_mul_f32_e32 v40, v40, v152
	v_mul_f32_e32 v41, v41, v152
	v_mov_b32_e32 v51, 0
	v_cvt_pk_fp8_f32 v51, v40, v41
	v_fma_f32 v40, v42, s18, v138
	v_fma_f32 v41, v43, s18, v139
	v_fma_f32 v28, v28, s18, v128
	v_fma_f32 v29, v29, s18, v129
	v_mul_f32_e32 v40, v40, v152
	v_mul_f32_e32 v41, v41, v152
	v_mul_f32_e32 v28, v28, v152
	v_mul_f32_e32 v29, v29, v152
	v_cvt_pk_fp8_f32 v51, v40, v41 op_sel:[0,0,1]
	v_mov_b32_e32 v41, 0
	v_fma_f32 v24, v24, s18, v136
	v_fma_f32 v25, v25, s18, v137
	v_cvt_pk_fp8_f32 v41, v28, v29
	v_fma_f32 v28, v30, s18, v130
	v_fma_f32 v29, v31, s18, v131
	v_fma_f32 v30, v34, s18, v142
	v_fma_f32 v31, v35, s18, v143
	v_mul_f32_e32 v24, v24, v148
	v_mul_f32_e32 v25, v25, v148
	v_mov_b32_e32 v35, 0
	v_cvt_pk_fp8_f32 v35, v24, v25
	v_fma_f32 v120, v120, s18, v136
	v_fma_f32 v121, v121, s18, v137
	v_fma_f32 v116, v116, s18, v140
	v_fma_f32 v117, v117, s18, v141
	v_fma_f32 v112, v112, s18, v136
	v_fma_f32 v113, v113, s18, v137
	v_fma_f32 v24, v26, s18, v138
	v_fma_f32 v25, v27, s18, v139
	v_fma_f32 v108, v108, s18, v132
	v_fma_f32 v109, v109, s18, v133
	v_fma_f32 v100, v100, s18, v132
	v_fma_f32 v101, v101, s18, v133
	v_mul_f32_e32 v124, v124, v166
	v_mul_f32_e32 v125, v125, v166
	v_mul_f32_e32 v120, v120, v166
	v_mul_f32_e32 v121, v121, v166
	v_mul_f32_e32 v116, v116, v170
	v_mul_f32_e32 v117, v117, v170
	v_mul_f32_e32 v112, v112, v170
	v_mul_f32_e32 v113, v113, v170
	v_mul_f32_e32 v24, v24, v148
	v_mul_f32_e32 v25, v25, v148
	v_fma_f32 v12, v12, s18, v128
	v_fma_f32 v13, v13, s18, v129
	v_mul_f32_e32 v108, v108, v166
	v_mul_f32_e32 v109, v109, v166
	v_cvt_pk_fp8_f32 v160, v124, v125
	v_cvt_pk_fp8_f32 v161, v120, v121
	v_cvt_pk_fp8_f32 v164, v116, v117
	v_cvt_pk_fp8_f32 v165, v112, v113
	v_mul_f32_e32 v100, v100, v170
	v_mul_f32_e32 v101, v101, v170
	v_mov_b32_e32 v104, 0
	v_cvt_pk_fp8_f32 v35, v24, v25 op_sel:[0,0,1]
	v_mul_f32_e32 v12, v12, v148
	v_mul_f32_e32 v13, v13, v148
	v_mov_b32_e32 v25, 0
	v_fma_f32 v8, v8, s18, v136
	v_fma_f32 v9, v9, s18, v137
	v_cvt_pk_fp8_f32 v162, v108, v109
	v_cvt_pk_fp8_f32 v104, v100, v101
	v_fma_f32 v96, v96, s18, v140
	v_fma_f32 v97, v97, s18, v141
	v_cvt_pk_fp8_f32 v25, v12, v13
	v_fma_f32 v12, v14, s18, v130
	v_fma_f32 v13, v15, s18, v131
	v_fma_f32 v14, v18, s18, v142
	v_fma_f32 v15, v19, s18, v143
	v_mul_f32_e32 v8, v8, v146
	v_mul_f32_e32 v9, v9, v146
	v_mov_b32_e32 v19, 0
	v_fma_f32 v126, v126, s18, v142
	v_fma_f32 v127, v127, s18, v143
	v_fma_f32 v122, v122, s18, v138
	v_fma_f32 v123, v123, s18, v139
	v_fma_f32 v118, v118, s18, v142
	v_fma_f32 v119, v119, s18, v143
	v_fma_f32 v114, v114, s18, v138
	v_fma_f32 v115, v115, s18, v139
	v_mul_f32_e32 v96, v96, v172
	v_mul_f32_e32 v97, v97, v172
	v_mov_b32_e32 v98, 0
	v_fma_f32 v84, v84, s18, v132
	v_fma_f32 v85, v85, s18, v133
	v_cvt_pk_fp8_f32 v19, v8, v9
	v_fma_f32 v110, v110, s18, v134
	v_fma_f32 v111, v111, s18, v135
	v_fma_f32 v106, v106, s18, v130
	v_fma_f32 v107, v107, s18, v131
	v_fma_f32 v102, v102, s18, v134
	v_fma_f32 v103, v103, s18, v135
	v_mul_f32_e32 v126, v126, v166
	v_mul_f32_e32 v127, v127, v166
	v_mul_f32_e32 v122, v122, v166
	v_mul_f32_e32 v123, v123, v166
	v_mul_f32_e32 v118, v118, v170
	v_mul_f32_e32 v119, v119, v170
	v_mul_f32_e32 v114, v114, v170
	v_mul_f32_e32 v115, v115, v170
	v_cvt_pk_fp8_f32 v98, v96, v97
	v_mul_f32_e32 v84, v84, v172
	v_mul_f32_e32 v85, v85, v172
	v_mov_b32_e32 v88, 0
	v_mul_f32_e32 v110, v110, v166
	v_mul_f32_e32 v111, v111, v166
	v_mul_f32_e32 v106, v106, v166
	v_mul_f32_e32 v107, v107, v166
	v_mul_f32_e32 v102, v102, v170
	v_mul_f32_e32 v103, v103, v170
	v_cvt_pk_fp8_f32 v160, v126, v127 op_sel:[0,0,1]
	v_cvt_pk_fp8_f32 v161, v122, v123 op_sel:[0,0,1]
	v_cvt_pk_fp8_f32 v164, v118, v119 op_sel:[0,0,1]
	v_cvt_pk_fp8_f32 v165, v114, v115 op_sel:[0,0,1]
	v_mul_f32_e32 v92, v92, v170
	v_mul_f32_e32 v93, v93, v170
	v_cvt_pk_fp8_f32 v88, v84, v85
	v_fma_f32 v80, v80, s18, v140
	v_fma_f32 v81, v81, s18, v141
	v_fma_f32 v60, v60, s18, v140
	v_fma_f32 v61, v61, s18, v141
	v_mul_f32_e32 v44, v44, v168
	v_mul_f32_e32 v45, v45, v168
	v_fma_f32 v48, v48, s18, v140
	v_fma_f32 v49, v49, s18, v141
	v_fma_f32 v32, v32, s18, v140
	v_fma_f32 v33, v33, s18, v141
	v_fma_f32 v16, v16, s18, v140
	v_fma_f32 v17, v17, s18, v141
	v_fma_f32 v8, v10, s18, v138
	v_fma_f32 v9, v11, s18, v139
	v_cvt_pk_fp8_f32 v162, v110, v111 op_sel:[0,0,1]
	v_cvt_pk_fp8_f32 v163, v106, v107 op_sel:[0,0,1]
	v_cvt_pk_fp8_f32 v104, v102, v103 op_sel:[0,0,1]
	v_cvt_pk_fp8_f32 v105, v92, v93 op_sel:[0,0,1]
	v_mul_f32_e32 v80, v80, v174
	v_mul_f32_e32 v81, v81, v174
	v_mov_b32_e32 v82, 0
	v_fma_f32 v68, v68, s18, v132
	v_fma_f32 v69, v69, s18, v133
	v_mul_f32_e32 v60, v60, v168
	v_mul_f32_e32 v61, v61, v168
	v_mov_b32_e32 v66, 0
	v_fma_f32 v52, v52, s18, v132
	v_fma_f32 v53, v53, s18, v133
	v_cvt_pk_fp8_f32 v57, v44, v45 op_sel:[0,0,1]
	v_add_co_u32_e32 v44, vcc, s50, v144
	v_mul_f32_e32 v48, v48, v152
	v_mul_f32_e32 v49, v49, v152
	v_mov_b32_e32 v50, 0
	v_fma_f32 v36, v36, s18, v132
	v_fma_f32 v37, v37, s18, v133
	v_mul_f32_e32 v32, v32, v148
	v_mul_f32_e32 v33, v33, v148
	v_mov_b32_e32 v34, 0
	v_fma_f32 v20, v20, s18, v132
	v_fma_f32 v21, v21, s18, v133
	v_mul_f32_e32 v16, v16, v146
	v_mul_f32_e32 v17, v17, v146
	v_mov_b32_e32 v18, 0
	v_mul_f32_e32 v8, v8, v146
	v_mul_f32_e32 v9, v9, v146
	v_fma_f32 v4, v4, s18, v132
	v_fma_f32 v5, v5, s18, v133
	v_fma_f32 v0, v0, s18, v128
	v_fma_f32 v1, v1, s18, v129
	v_lshl_add_u64 v[92:93], s[12:13], 0, v[154:155]
	v_mul_f32_e32 v94, v94, v172
	v_mul_f32_e32 v95, v95, v172
	v_fma_f32 v86, v86, s18, v134
	v_fma_f32 v87, v87, s18, v135
	v_cvt_pk_fp8_f32 v82, v80, v81
	v_mul_f32_e32 v68, v68, v174
	v_mul_f32_e32 v69, v69, v174
	v_mov_b32_e32 v72, 0
	v_cvt_pk_fp8_f32 v66, v60, v61
	v_mul_f32_e32 v52, v52, v168
	v_mul_f32_e32 v53, v53, v168
	v_mov_b32_e32 v56, 0
	v_addc_co_u32_e32 v45, vcc, 0, v145, vcc
	v_cvt_pk_fp8_f32 v50, v48, v49
	v_mul_f32_e32 v36, v36, v152
	v_mul_f32_e32 v37, v37, v152
	v_mov_b32_e32 v40, 0
	v_mul_f32_e32 v28, v28, v152
	v_mul_f32_e32 v29, v29, v152
	v_cvt_pk_fp8_f32 v34, v32, v33
	v_mul_f32_e32 v20, v20, v148
	v_mul_f32_e32 v21, v21, v148
	v_mov_b32_e32 v24, 0
	v_cvt_pk_fp8_f32 v18, v16, v17
	v_cvt_pk_fp8_f32 v19, v8, v9 op_sel:[0,0,1]
	v_mul_f32_e32 v4, v4, v146
	v_mul_f32_e32 v5, v5, v146
	v_mul_f32_e32 v0, v0, v146
	v_mul_f32_e32 v1, v1, v146
	v_mov_b32_e32 v8, 0
	v_mov_b32_e32 v9, 0
	v_lshl_add_u64 v[92:93], v[92:93], 0, v[150:151]
	v_cvt_pk_fp8_f32 v98, v94, v95 op_sel:[0,0,1]
	v_mul_f32_e32 v86, v86, v172
	v_mul_f32_e32 v87, v87, v172
	v_mul_f32_e32 v76, v76, v172
	v_mul_f32_e32 v77, v77, v172
	v_cvt_pk_fp8_f32 v72, v68, v69
	v_cvt_pk_fp8_f32 v56, v52, v53
	v_cvt_pk_fp8_f32 v40, v36, v37
	v_cvt_pk_fp8_f32 v41, v28, v29 op_sel:[0,0,1]
	v_add_co_u32_e32 v28, vcc, s67, v144
	v_cvt_pk_fp8_f32 v24, v20, v21
	v_cvt_pk_fp8_f32 v8, v4, v5
	v_cvt_pk_fp8_f32 v9, v0, v1
	global_store_dwordx2 v[144:145], v[160:161], off
	global_store_dwordx2 v[144:145], v[162:163], off offset:128
	global_store_dwordx2 v[92:93], v[164:165], off
	global_store_dwordx2 v[92:93], v[104:105], off offset:128
	v_lshlrev_b64 v[92:93], 11, v[156:157]
	v_cvt_pk_fp8_f32 v88, v86, v87 op_sel:[0,0,1]
	v_cvt_pk_fp8_f32 v89, v76, v77 op_sel:[0,0,1]
	v_fma_f32 v62, v62, s18, v142
	v_fma_f32 v63, v63, s18, v143
	v_addc_co_u32_e32 v29, vcc, 0, v145, vcc
	v_mul_f32_e32 v12, v12, v148
	v_mul_f32_e32 v13, v13, v148
	v_lshl_add_u64 v[76:77], s[12:13], 0, v[92:93]
	v_mul_f32_e32 v78, v78, v174
	v_mul_f32_e32 v79, v79, v174
	v_fma_f32 v70, v70, s18, v134
	v_fma_f32 v71, v71, s18, v135
	v_mul_f32_e32 v62, v62, v168
	v_mul_f32_e32 v63, v63, v168
	v_fma_f32 v54, v54, s18, v134
	v_fma_f32 v55, v55, s18, v135
	v_mul_f32_e32 v46, v46, v152
	v_mul_f32_e32 v47, v47, v152
	v_fma_f32 v38, v38, s18, v134
	v_fma_f32 v39, v39, s18, v135
	v_mul_f32_e32 v30, v30, v148
	v_mul_f32_e32 v31, v31, v148
	v_fma_f32 v22, v22, s18, v134
	v_fma_f32 v23, v23, s18, v135
	v_cvt_pk_fp8_f32 v25, v12, v13 op_sel:[0,0,1]
	v_add_co_u32_e32 v12, vcc, s68, v144
	v_mul_f32_e32 v14, v14, v146
	v_mul_f32_e32 v15, v15, v146
	v_fma_f32 v6, v6, s18, v134
	v_fma_f32 v7, v7, s18, v135
	v_fma_f32 v0, v2, s18, v130
	v_fma_f32 v1, v3, s18, v131
	v_lshl_add_u64 v[76:77], v[76:77], 0, v[150:151]
	v_cvt_pk_fp8_f32 v82, v78, v79 op_sel:[0,0,1]
	v_mul_f32_e32 v70, v70, v174
	v_mul_f32_e32 v71, v71, v174
	v_mul_f32_e32 v64, v64, v174
	v_mul_f32_e32 v65, v65, v174
	v_cvt_pk_fp8_f32 v66, v62, v63 op_sel:[0,0,1]
	v_mul_f32_e32 v54, v54, v168
	v_mul_f32_e32 v55, v55, v168
	v_cvt_pk_fp8_f32 v50, v46, v47 op_sel:[0,0,1]
	v_mul_f32_e32 v38, v38, v152
	v_mul_f32_e32 v39, v39, v152
	v_cvt_pk_fp8_f32 v34, v30, v31 op_sel:[0,0,1]
	v_mul_f32_e32 v22, v22, v148
	v_mul_f32_e32 v23, v23, v148
	v_addc_co_u32_e32 v13, vcc, 0, v145, vcc
	v_cvt_pk_fp8_f32 v18, v14, v15 op_sel:[0,0,1]
	v_mul_f32_e32 v6, v6, v146
	v_mul_f32_e32 v7, v7, v146
	v_mul_f32_e32 v0, v0, v146
	v_mul_f32_e32 v1, v1, v146
	global_store_dwordx2 v[76:77], v[98:99], off
	global_store_dwordx2 v[76:77], v[88:89], off offset:128
	v_lshlrev_b64 v[76:77], 11, v[158:159]
	v_cvt_pk_fp8_f32 v72, v70, v71 op_sel:[0,0,1]
	v_cvt_pk_fp8_f32 v73, v64, v65 op_sel:[0,0,1]
	v_cvt_pk_fp8_f32 v56, v54, v55 op_sel:[0,0,1]
	v_cvt_pk_fp8_f32 v40, v38, v39 op_sel:[0,0,1]
	v_cvt_pk_fp8_f32 v24, v22, v23 op_sel:[0,0,1]
	v_cvt_pk_fp8_f32 v8, v6, v7 op_sel:[0,0,1]
	v_cvt_pk_fp8_f32 v9, v0, v1 op_sel:[0,0,1]
	v_add_co_u32_e32 v0, vcc, s69, v144
	v_lshl_add_u64 v[64:65], s[12:13], 0, v[76:77]
	s_nop 0
	v_addc_co_u32_e32 v1, vcc, 0, v145, vcc
	v_lshl_add_u64 v[64:65], v[64:65], 0, v[150:151]
	s_andn2_b64 vcc, exec, s[28:29]
	global_store_dwordx2 v[64:65], v[82:83], off
	global_store_dwordx2 v[64:65], v[72:73], off offset:128
	v_lshl_add_u64 v[64:65], v[144:145], 0, s[20:21]
	global_store_dwordx2 v[44:45], v[66:67], off
	global_store_dwordx2 v[64:65], v[56:57], off offset:128
	v_lshl_add_u64 v[44:45], v[144:145], 0, s[22:23]
	global_store_dwordx2 v[28:29], v[50:51], off
	global_store_dwordx2 v[44:45], v[40:41], off offset:128
	v_lshl_add_u64 v[28:29], v[144:145], 0, s[24:25]
	global_store_dwordx2 v[12:13], v[34:35], off
	global_store_dwordx2 v[28:29], v[24:25], off offset:128
	v_lshl_add_u64 v[12:13], v[144:145], 0, s[26:27]
	global_store_dwordx2 v[0:1], v[18:19], off
	global_store_dwordx2 v[12:13], v[8:9], off offset:128
	s_cbranch_vccnz .LBB0_2566
	s_andn2_b64 vcc, exec, s[2:3]
	s_cbranch_vccnz .LBB0_2565
	s_barrier
	s_branch .LBB0_2565

.LBB0_2639:
	v_cvt_f32_fp8_e32 v144, v89
	v_cvt_f32_fp8_sdwa v145, v89 src0_sel:BYTE_1
	v_cvt_f32_fp8_e32 v164, v101
	v_cvt_f32_fp8_sdwa v165, v101 src0_sel:BYTE_1
	v_cvt_f32_fp8_e32 v188, v95
	v_cvt_f32_fp8_sdwa v189, v95 src0_sel:BYTE_1
	v_cvt_f32_fp8_sdwa v166, v101 src0_sel:BYTE_2
	v_cvt_f32_fp8_sdwa v167, v101 src0_sel:BYTE_3
	v_cvt_f32_fp8_e32 v168, v100
	v_cvt_f32_fp8_sdwa v169, v100 src0_sel:BYTE_1
	v_cvt_f32_fp8_sdwa v170, v100 src0_sel:BYTE_2
	v_cvt_f32_fp8_sdwa v171, v100 src0_sel:BYTE_3
	v_cvt_f32_fp8_sdwa v190, v95 src0_sel:BYTE_2
	v_cvt_f32_fp8_sdwa v191, v95 src0_sel:BYTE_3
	v_cvt_f32_fp8_e32 v192, v94
	v_cvt_f32_fp8_sdwa v193, v94 src0_sel:BYTE_1
	v_cvt_f32_fp8_sdwa v194, v94 src0_sel:BYTE_2
	v_cvt_f32_fp8_sdwa v195, v94 src0_sel:BYTE_3
	v_cvt_f32_fp8_e32 v212, v71
	v_cvt_f32_fp8_sdwa v213, v71 src0_sel:BYTE_1
	v_cvt_f32_fp8_sdwa v214, v71 src0_sel:BYTE_2
	v_cvt_f32_fp8_sdwa v215, v71 src0_sel:BYTE_3
	v_cvt_f32_fp8_e32 v100, v70
	v_cvt_f32_fp8_sdwa v101, v70 src0_sel:BYTE_1
	v_cvt_f32_fp8_sdwa v94, v70 src0_sel:BYTE_2
	v_cvt_f32_fp8_sdwa v95, v70 src0_sel:BYTE_3
	v_cvt_f32_fp8_e32 v70, v72
	v_cvt_f32_fp8_sdwa v71, v72 src0_sel:BYTE_1
	v_lshlrev_b32_e32 v216, 16, v68
	v_and_b32_e32 v217, 0xffff0000, v68
	v_cvt_f32_fp8_sdwa v146, v89 src0_sel:BYTE_2
	v_cvt_f32_fp8_sdwa v147, v89 src0_sel:BYTE_3
	v_fma_f32 v144, v144, s8, v216
	v_fma_f32 v145, v145, s8, v217
	v_lshlrev_b32_e32 v68, 16, v69
	v_fma_f32 v144, v164, s8, v144
	v_fma_f32 v145, v165, s8, v145
	v_and_b32_e32 v69, 0xffff0000, v69
	v_fma_f32 v144, v188, s8, v144
	v_fma_f32 v145, v189, s8, v145
	v_cvt_f32_fp8_e32 v148, v88
	v_fma_f32 v70, v70, s8, v144
	v_fma_f32 v71, v71, s8, v145
	v_cvt_f32_fp8_sdwa v144, v72 src0_sel:BYTE_2
	v_cvt_f32_fp8_sdwa v145, v72 src0_sel:BYTE_3
	v_cvt_f32_fp8_sdwa v149, v88 src0_sel:BYTE_1
	v_fma_f32 v68, v146, s8, v68
	v_fma_f32 v69, v147, s8, v69
	v_cvt_f32_fp8_e32 v208, v73
	v_fma_f32 v68, v166, s8, v68
	v_fma_f32 v69, v167, s8, v69
	v_cvt_f32_fp8_sdwa v209, v73 src0_sel:BYTE_1
	v_fma_f32 v68, v190, s8, v68
	v_fma_f32 v69, v191, s8, v69
	v_cvt_f32_fp8_sdwa v210, v73 src0_sel:BYTE_2
	v_cvt_f32_fp8_sdwa v211, v73 src0_sel:BYTE_3
	v_fma_f32 v68, v144, s8, v68
	v_fma_f32 v69, v145, s8, v69
	v_cvt_f32_fp8_e32 v72, v74
	v_cvt_f32_fp8_sdwa v73, v74 src0_sel:BYTE_1
	v_lshlrev_b32_e32 v144, 16, v66
	v_and_b32_e32 v145, 0xffff0000, v66
	v_cvt_f32_fp8_sdwa v150, v88 src0_sel:BYTE_2
	v_cvt_f32_fp8_sdwa v151, v88 src0_sel:BYTE_3
	v_fma_f32 v144, v148, s8, v144
	v_fma_f32 v145, v149, s8, v145
	v_lshlrev_b32_e32 v66, 16, v67
	v_fma_f32 v144, v168, s8, v144
	v_fma_f32 v145, v169, s8, v145
	v_and_b32_e32 v67, 0xffff0000, v67
	v_fma_f32 v144, v192, s8, v144
	v_fma_f32 v145, v193, s8, v145
	v_cvt_f32_fp8_e32 v152, v87
	v_fma_f32 v72, v72, s8, v144
	v_fma_f32 v73, v73, s8, v145
	v_cvt_f32_fp8_sdwa v144, v74 src0_sel:BYTE_2
	v_cvt_f32_fp8_sdwa v145, v74 src0_sel:BYTE_3
	v_cvt_f32_fp8_sdwa v153, v87 src0_sel:BYTE_1
	v_fma_f32 v66, v150, s8, v66
	v_fma_f32 v67, v151, s8, v67
	v_cvt_f32_fp8_e32 v172, v97
	v_cvt_f32_fp8_sdwa v173, v97 src0_sel:BYTE_1
	v_fma_f32 v66, v170, s8, v66
	v_fma_f32 v67, v171, s8, v67
	v_cvt_f32_fp8_e32 v196, v81
	v_cvt_f32_fp8_sdwa v197, v81 src0_sel:BYTE_1
	v_fma_f32 v66, v194, s8, v66
	v_fma_f32 v67, v195, s8, v67
	v_cvt_f32_fp8_e32 v204, v75
	v_cvt_f32_fp8_sdwa v205, v75 src0_sel:BYTE_1
	v_cvt_f32_fp8_sdwa v206, v75 src0_sel:BYTE_2
	v_cvt_f32_fp8_sdwa v207, v75 src0_sel:BYTE_3
	v_fma_f32 v66, v144, s8, v66
	v_fma_f32 v67, v145, s8, v67
	v_cvt_f32_fp8_e32 v74, v76
	v_cvt_f32_fp8_sdwa v75, v76 src0_sel:BYTE_1
	v_lshlrev_b32_e32 v144, 16, v64
	v_and_b32_e32 v145, 0xffff0000, v64
	v_cvt_f32_fp8_sdwa v154, v87 src0_sel:BYTE_2
	v_cvt_f32_fp8_sdwa v155, v87 src0_sel:BYTE_3
	v_fma_f32 v144, v152, s8, v144
	v_fma_f32 v145, v153, s8, v145
	v_cvt_f32_fp8_sdwa v174, v97 src0_sel:BYTE_2
	v_cvt_f32_fp8_sdwa v175, v97 src0_sel:BYTE_3
	v_fma_f32 v144, v172, s8, v144
	v_fma_f32 v145, v173, s8, v145
	v_cvt_f32_fp8_sdwa v198, v81 src0_sel:BYTE_2
	v_cvt_f32_fp8_sdwa v199, v81 src0_sel:BYTE_3
	v_fma_f32 v144, v196, s8, v144
	v_fma_f32 v145, v197, s8, v145
	v_lshlrev_b32_e32 v64, 16, v65
	v_fma_f32 v74, v74, s8, v144
	v_fma_f32 v75, v75, s8, v145
	v_cvt_f32_fp8_sdwa v144, v76 src0_sel:BYTE_2
	v_cvt_f32_fp8_sdwa v145, v76 src0_sel:BYTE_3
	v_and_b32_e32 v65, 0xffff0000, v65
	v_cvt_f32_fp8_e32 v156, v86
	v_cvt_f32_fp8_sdwa v157, v86 src0_sel:BYTE_1
	v_fma_f32 v64, v154, s8, v64
	v_fma_f32 v65, v155, s8, v65
	v_cvt_f32_fp8_e32 v176, v96
	v_cvt_f32_fp8_sdwa v177, v96 src0_sel:BYTE_1
	v_fma_f32 v64, v174, s8, v64
	v_fma_f32 v65, v175, s8, v65
	v_cvt_f32_fp8_e32 v200, v77
	v_cvt_f32_fp8_sdwa v201, v77 src0_sel:BYTE_1
	v_fma_f32 v64, v198, s8, v64
	v_fma_f32 v65, v199, s8, v65
	v_cvt_f32_fp8_sdwa v202, v77 src0_sel:BYTE_2
	v_cvt_f32_fp8_sdwa v203, v77 src0_sel:BYTE_3
	v_fma_f32 v64, v144, s8, v64
	v_fma_f32 v65, v145, s8, v65
	v_cvt_f32_fp8_e32 v76, v80
	v_cvt_f32_fp8_sdwa v77, v80 src0_sel:BYTE_1
	v_lshlrev_b32_e32 v144, 16, v62
	v_and_b32_e32 v145, 0xffff0000, v62
	v_cvt_f32_fp8_sdwa v158, v86 src0_sel:BYTE_2
	v_cvt_f32_fp8_sdwa v159, v86 src0_sel:BYTE_3
	v_fma_f32 v144, v156, s8, v144
	v_fma_f32 v145, v157, s8, v145
	v_cvt_f32_fp8_sdwa v178, v96 src0_sel:BYTE_2
	v_cvt_f32_fp8_sdwa v179, v96 src0_sel:BYTE_3
	v_fma_f32 v144, v176, s8, v144
	v_fma_f32 v145, v177, s8, v145
	v_lshlrev_b32_e32 v62, 16, v63
	v_fma_f32 v144, v200, s8, v144
	v_fma_f32 v145, v201, s8, v145
	v_and_b32_e32 v63, 0xffff0000, v63
	v_fma_f32 v76, v76, s8, v144
	v_fma_f32 v77, v77, s8, v145
	v_cvt_f32_fp8_sdwa v144, v80 src0_sel:BYTE_2
	v_cvt_f32_fp8_sdwa v145, v80 src0_sel:BYTE_3
	v_cvt_f32_fp8_e32 v160, v83
	v_cvt_f32_fp8_sdwa v161, v83 src0_sel:BYTE_1
	v_fma_f32 v62, v158, s8, v62
	v_fma_f32 v63, v159, s8, v63
	v_cvt_f32_fp8_e32 v180, v91
	v_cvt_f32_fp8_sdwa v181, v91 src0_sel:BYTE_1
	v_fma_f32 v62, v178, s8, v62
	v_fma_f32 v63, v179, s8, v63
	v_cvt_f32_fp8_e32 v80, v143
	v_fma_f32 v62, v202, s8, v62
	v_fma_f32 v63, v203, s8, v63
	v_cvt_f32_fp8_sdwa v81, v143 src0_sel:BYTE_1
	v_fma_f32 v62, v144, s8, v62
	v_fma_f32 v63, v145, s8, v63
	v_lshlrev_b32_e32 v144, 16, v60
	v_and_b32_e32 v145, 0xffff0000, v60
	v_cvt_f32_fp8_sdwa v162, v83 src0_sel:BYTE_2
	v_cvt_f32_fp8_sdwa v163, v83 src0_sel:BYTE_3
	v_fma_f32 v144, v160, s8, v144
	v_fma_f32 v145, v161, s8, v145
	v_cvt_f32_fp8_sdwa v182, v91 src0_sel:BYTE_2
	v_cvt_f32_fp8_sdwa v183, v91 src0_sel:BYTE_3
	v_fma_f32 v144, v180, s8, v144
	v_fma_f32 v145, v181, s8, v145
	v_lshlrev_b32_e32 v60, 16, v61
	v_fma_f32 v144, v204, s8, v144
	v_fma_f32 v145, v205, s8, v145
	v_and_b32_e32 v61, 0xffff0000, v61
	v_fma_f32 v80, v80, s8, v144
	v_fma_f32 v81, v81, s8, v145
	v_cvt_f32_fp8_sdwa v144, v143 src0_sel:BYTE_2
	v_cvt_f32_fp8_sdwa v145, v143 src0_sel:BYTE_3
	v_cvt_f32_fp8_e32 v88, v82
	v_cvt_f32_fp8_sdwa v89, v82 src0_sel:BYTE_1
	v_fma_f32 v60, v162, s8, v60
	v_fma_f32 v61, v163, s8, v61
	v_cvt_f32_fp8_e32 v184, v90
	v_cvt_f32_fp8_sdwa v185, v90 src0_sel:BYTE_1
	v_fma_f32 v60, v182, s8, v60
	v_fma_f32 v61, v183, s8, v61
	v_lshlrev_b32_e32 v146, 16, v58
	v_fma_f32 v60, v206, s8, v60
	v_fma_f32 v61, v207, s8, v61
	v_and_b32_e32 v147, 0xffff0000, v58
	v_fma_f32 v60, v144, s8, v60
	v_fma_f32 v61, v145, s8, v61
	v_cvt_f32_fp8_e32 v144, v142
	v_cvt_f32_fp8_sdwa v145, v142 src0_sel:BYTE_1
	v_cvt_f32_fp8_sdwa v86, v78 src0_sel:BYTE_2
	v_cvt_f32_fp8_sdwa v87, v78 src0_sel:BYTE_3
	v_fma_f32 v88, v88, s8, v146
	v_fma_f32 v89, v89, s8, v147
	v_cvt_f32_fp8_sdwa v98, v82 src0_sel:BYTE_2
	v_cvt_f32_fp8_sdwa v99, v82 src0_sel:BYTE_3
	v_cvt_f32_fp8_sdwa v96, v84 src0_sel:BYTE_2
	v_cvt_f32_fp8_sdwa v97, v84 src0_sel:BYTE_3
	v_fma_f32 v88, v184, s8, v88
	v_fma_f32 v89, v185, s8, v89
	v_cvt_f32_fp8_e32 v92, v78
	v_cvt_f32_fp8_sdwa v93, v78 src0_sel:BYTE_1
	v_cvt_f32_fp8_e32 v82, v79
	v_cvt_f32_fp8_sdwa v83, v79 src0_sel:BYTE_1
	v_fma_f32 v88, v208, s8, v88
	v_fma_f32 v89, v209, s8, v89
	v_cvt_f32_fp8_sdwa v186, v90 src0_sel:BYTE_2
	v_cvt_f32_fp8_sdwa v187, v90 src0_sel:BYTE_3
	v_cvt_f32_fp8_e32 v102, v84
	v_cvt_f32_fp8_sdwa v103, v84 src0_sel:BYTE_1
	v_cvt_f32_fp8_e32 v90, v85
	v_cvt_f32_fp8_sdwa v91, v85 src0_sel:BYTE_1
	v_fma_f32 v88, v144, s8, v88
	v_fma_f32 v89, v145, s8, v89
	v_cvt_f32_fp8_sdwa v144, v142 src0_sel:BYTE_2
	v_cvt_f32_fp8_sdwa v145, v142 src0_sel:BYTE_3
	v_lshlrev_b32_e32 v142, 16, v56
	v_and_b32_e32 v143, 0xffff0000, v56
	v_lshlrev_b32_e32 v56, 16, v57
	v_and_b32_e32 v57, 0xffff0000, v57
	v_lshlrev_b32_e32 v58, 16, v59
	v_and_b32_e32 v59, 0xffff0000, v59
	v_fma_f32 v56, v86, s8, v56
	v_fma_f32 v57, v87, s8, v57
	v_fma_f32 v58, v98, s8, v58
	v_fma_f32 v59, v99, s8, v59
	v_cvt_f32_fp8_e32 v98, v141
	v_cvt_f32_fp8_sdwa v99, v141 src0_sel:BYTE_1
	v_fma_f32 v56, v96, s8, v56
	v_fma_f32 v57, v97, s8, v57
	v_cvt_f32_fp8_e32 v86, v140
	v_cvt_f32_fp8_sdwa v87, v140 src0_sel:BYTE_1
	v_lshlrev_b32_e32 v96, 16, v54
	v_and_b32_e32 v97, 0xffff0000, v54
	v_cvt_f32_fp8_sdwa v78, v79 src0_sel:BYTE_2
	v_cvt_f32_fp8_sdwa v79, v79 src0_sel:BYTE_3
	v_fma_f32 v92, v92, s8, v142
	v_fma_f32 v93, v93, s8, v143
	v_fma_f32 v82, v82, s8, v96
	v_fma_f32 v83, v83, s8, v97
	v_cvt_f32_fp8_sdwa v84, v85 src0_sel:BYTE_2
	v_cvt_f32_fp8_sdwa v85, v85 src0_sel:BYTE_3
	v_fma_f32 v92, v102, s8, v92
	v_fma_f32 v93, v103, s8, v93
	v_fma_f32 v82, v90, s8, v82
	v_fma_f32 v83, v91, s8, v83
	v_fma_f32 v92, v212, s8, v92
	v_fma_f32 v93, v213, s8, v93
	v_fma_f32 v82, v100, s8, v82
	v_fma_f32 v83, v101, s8, v83
	v_fma_f32 v92, v98, s8, v92
	v_fma_f32 v93, v99, s8, v93
	v_cvt_f32_fp8_sdwa v98, v141 src0_sel:BYTE_2
	v_cvt_f32_fp8_sdwa v99, v141 src0_sel:BYTE_3
	v_fma_f32 v82, v86, s8, v82
	v_fma_f32 v83, v87, s8, v83
	v_cvt_f32_fp8_sdwa v86, v140 src0_sel:BYTE_2
	v_cvt_f32_fp8_sdwa v87, v140 src0_sel:BYTE_3
	v_lshlrev_b32_e32 v54, 16, v55
	v_and_b32_e32 v55, 0xffff0000, v55
	v_fma_f32 v54, v78, s8, v54
	v_fma_f32 v55, v79, s8, v55
	v_fma_f32 v58, v186, s8, v58
	v_fma_f32 v59, v187, s8, v59
	v_fma_f32 v54, v84, s8, v54
	v_fma_f32 v55, v85, s8, v55
	v_fma_f32 v58, v210, s8, v58
	v_fma_f32 v59, v211, s8, v59
	v_fma_f32 v56, v214, s8, v56
	v_fma_f32 v57, v215, s8, v57
	v_fma_f32 v54, v94, s8, v54
	v_fma_f32 v55, v95, s8, v55
	v_fma_f32 v58, v144, s8, v58
	v_fma_f32 v59, v145, s8, v59
	v_fma_f32 v56, v98, s8, v56
	v_fma_f32 v57, v99, s8, v57
	v_fma_f32 v54, v86, s8, v54
	v_fma_f32 v55, v87, s8, v55
	s_andn2_b64 vcc, exec, s[0:1]
	v_mov_b32_e32 v78, 0x7fc00000
	s_cbranch_vccz .LBB0_2643
.LBB0_2640:
	v_mul_f32_e32 v84, v70, v78
	v_mul_f32_e32 v85, v71, v78
	v_mul_f32_e32 v68, v68, v78
	v_mul_f32_e32 v69, v69, v78
	v_mul_f32_e32 v66, v66, v78
	v_mul_f32_e32 v67, v67, v78
	s_waitcnt vmcnt(4)
	v_mul_f32_e32 v70, v14, v68
	v_mul_f32_e32 v71, v15, v69
	v_mul_f32_e32 v68, v12, v84
	v_mul_f32_e32 v69, v13, v85
	global_store_dwordx4 v[34:35], v[68:71], off offset:-4096
	v_mul_f32_e32 v64, v64, v78
	v_mul_f32_e32 v65, v65, v78
	v_mul_f32_e32 v62, v62, v78
	v_mul_f32_e32 v63, v63, v78
	v_mul_f32_e32 v70, v72, v78
	v_mul_f32_e32 v71, v73, v78
	v_mul_f32_e32 v68, v10, v66
	v_mul_f32_e32 v69, v11, v67
	v_mul_f32_e32 v66, v8, v70
	v_mul_f32_e32 v67, v9, v71
	global_store_dwordx4 v[34:35], v[66:69], off offset:-3072
	v_mul_f32_e32 v60, v60, v78
	v_mul_f32_e32 v61, v61, v78
	v_mul_f32_e32 v58, v58, v78
	v_mul_f32_e32 v59, v59, v78
	v_mul_f32_e32 v68, v74, v78
	v_mul_f32_e32 v69, v75, v78
	v_mul_f32_e32 v66, v6, v64
	v_mul_f32_e32 v67, v7, v65
	v_mul_f32_e32 v64, v4, v68
	v_mul_f32_e32 v65, v5, v69
	global_store_dwordx4 v[34:35], v[64:67], off offset:-2048
	v_mul_f32_e32 v56, v56, v78
	v_mul_f32_e32 v57, v57, v78
	v_mul_f32_e32 v54, v54, v78
	v_mul_f32_e32 v55, v55, v78
	v_mul_f32_e32 v66, v76, v78
	v_mul_f32_e32 v67, v77, v78
	v_mul_f32_e32 v64, v2, v62
	v_mul_f32_e32 v65, v3, v63
	v_mul_f32_e32 v62, v0, v66
	v_mul_f32_e32 v63, v1, v67
	global_store_dwordx4 v[34:35], v[62:65], off offset:-1024
	s_add_i32 s12, s12, s5
	v_lshl_add_u64 v[36:37], v[36:37], 0, s[14:15]
	v_mul_f32_e32 v64, v80, v78
	v_mul_f32_e32 v65, v81, v78
	s_waitcnt vmcnt(4)
	v_mul_f32_e32 v62, v30, v60
	v_mul_f32_e32 v63, v31, v61
	v_mul_f32_e32 v60, v28, v64
	v_mul_f32_e32 v61, v29, v65
	global_store_dwordx4 v[34:35], v[60:63], off
	s_andn2_b64 vcc, exec, s[16:17]
	v_mov_b64_e32 v[64:65], v[48:49]
	v_mul_f32_e32 v62, v88, v78
	v_mul_f32_e32 v63, v89, v78
	v_mul_f32_e32 v60, v26, v58
	v_mul_f32_e32 v61, v27, v59
	v_mul_f32_e32 v58, v24, v62
	v_mul_f32_e32 v59, v25, v63
	global_store_dwordx4 v[34:35], v[58:61], off offset:1024
	v_mov_b64_e32 v[62:63], v[46:47]
	v_mov_b64_e32 v[66:67], v[50:51]
	v_mul_f32_e32 v60, v92, v78
	v_mul_f32_e32 v61, v93, v78
	v_mul_f32_e32 v58, v22, v56
	v_mul_f32_e32 v59, v23, v57
	v_mul_f32_e32 v56, v20, v60
	v_mul_f32_e32 v57, v21, v61
	global_store_dwordx4 v[34:35], v[56:59], off offset:2048
	v_mov_b64_e32 v[60:61], v[44:45]
	v_mov_b64_e32 v[68:69], v[52:53]
	v_mul_f32_e32 v58, v82, v78
	v_mul_f32_e32 v59, v83, v78
	v_mul_f32_e32 v56, v18, v54
	v_mul_f32_e32 v57, v19, v55
	v_mul_f32_e32 v54, v16, v58
	v_mul_f32_e32 v55, v17, v59
	global_store_dwordx4 v[34:35], v[54:57], off offset:3072
	v_lshl_add_u64 v[34:35], v[34:35], 0, s[10:11]
	v_mov_b64_e32 v[58:59], v[42:43]
	v_mov_b64_e32 v[54:55], v[38:39]
	v_mov_b64_e32 v[56:57], v[40:41]
	v_mov_b32_e32 v140, v124
	v_mov_b32_e32 v141, v125
	v_mov_b32_e32 v142, v126
	v_mov_b32_e32 v143, v127
	v_mov_b32_e32 v80, v128
	v_mov_b32_e32 v76, v129
	v_mov_b32_e32 v74, v130
	v_mov_b32_e32 v72, v131
	v_mov_b32_e32 v70, v132
	v_mov_b32_e32 v71, v133
	v_mov_b32_e32 v73, v134
	v_mov_b32_e32 v75, v135
	v_mov_b32_e32 v77, v136
	v_mov_b32_e32 v81, v137
	v_mov_b32_e32 v94, v138
	v_mov_b32_e32 v95, v139
	v_mov_b32_e32 v85, v122
	v_mov_b32_e32 v84, v123
	v_mov_b32_e32 v90, v108
	v_mov_b32_e32 v91, v109
	v_mov_b32_e32 v96, v110
	v_mov_b32_e32 v97, v111
	v_mov_b32_e32 v100, v112
	v_mov_b32_e32 v101, v113
	v_mov_b32_e32 v79, v114
	v_mov_b32_e32 v78, v115
	v_mov_b32_e32 v82, v116
	v_mov_b32_e32 v83, v117
	v_mov_b32_e32 v86, v118
	v_mov_b32_e32 v87, v119
	v_mov_b32_e32 v88, v120
	v_mov_b32_e32 v89, v121
	s_cbranch_vccz .LBB0_2644

.LBB0_2643:
	v_mov_b32_e32 v84, v71
	v_mov_b32_e32 v85, v69
	v_mov_b32_e32 v78, v70
	v_mov_b32_e32 v79, v68
	v_mul_f32_e32 v84, v84, v84
	v_mul_f32_e32 v85, v85, v85
	v_mov_b32_e32 v86, v73
	v_mov_b32_e32 v87, v67
	v_fma_f32 v78, v78, v78, v84
	v_fma_f32 v79, v79, v79, v85
	v_mov_b32_e32 v84, v72
	v_mov_b32_e32 v85, v66
	v_mul_f32_e32 v86, v86, v86
	v_mul_f32_e32 v87, v87, v87
	v_mul_f32_e32 v90, v65, v65
	v_fma_f32 v84, v84, v84, v86
	v_fma_f32 v85, v85, v85, v87
	v_mul_f32_e32 v86, v75, v75
	v_pk_add_f32 v[78:79], v[78:79], v[78:79] op_sel:[0,1] op_sel_hi:[1,0]
	v_pk_add_f32 v[84:85], v[84:85], v[84:85] op_sel:[0,1] op_sel_hi:[1,0]
	v_fma_f32 v87, v75, v75, v86
	v_fma_f32 v86, v74, v74, v86
	v_fma_f32 v91, v65, v65, v90
	v_fma_f32 v90, v64, v64, v90
	v_mul_f32_e32 v94, v76, v76
	v_mul_f32_e32 v95, v77, v77
	v_mul_f32_e32 v96, v62, v62
	v_mul_f32_e32 v97, v63, v63
	v_mov_b32_e32 v79, v94
	v_mov_b32_e32 v85, v95
	v_mov_b32_e32 v87, v96
	v_mov_b32_e32 v91, v97
	v_add_f32_e32 v78, v78, v84
	v_add_f32_e32 v79, v79, v85
	v_add_f32_e32 v84, v86, v90
	v_add_f32_e32 v85, v87, v91
	v_mov_b32_e32 v86, v81
	v_mov_b32_e32 v87, v61
	v_add_f32_e32 v78, v78, v84
	v_add_f32_e32 v79, v79, v85
	v_mov_b32_e32 v84, v80
	v_mov_b32_e32 v85, v60
	v_mul_f32_e32 v86, v86, v86
	v_mul_f32_e32 v87, v87, v87
	v_mov_b32_e32 v90, v89
	v_mov_b32_e32 v91, v59
	v_fma_f32 v84, v84, v84, v86
	v_fma_f32 v85, v85, v85, v87
	v_mov_b32_e32 v86, v88
	v_mov_b32_e32 v87, v58
	v_mul_f32_e32 v90, v90, v90
	v_mul_f32_e32 v91, v91, v91
	v_pk_add_f32 v[78:79], v[78:79], v[78:79] op_sel:[0,1] op_sel_hi:[1,0]
	v_pk_add_f32 v[84:85], v[84:85], v[84:85] op_sel:[0,1] op_sel_hi:[1,0]
	v_fma_f32 v86, v86, v86, v90
	v_fma_f32 v87, v87, v87, v91
	v_mul_f32_e32 v90, v93, v93
	v_mul_f32_e32 v94, v57, v57
	v_pk_add_f32 v[86:87], v[86:87], v[86:87] op_sel:[0,1] op_sel_hi:[1,0]
	v_fma_f32 v91, v93, v93, v90
	v_fma_f32 v90, v92, v92, v90
	v_fma_f32 v95, v57, v57, v94
	v_fma_f32 v94, v56, v56, v94
	v_mul_f32_e32 v96, v82, v82
	v_mul_f32_e32 v97, v83, v83
	v_mul_f32_e32 v98, v54, v54
	v_mul_f32_e32 v99, v55, v55
	v_add_f32_e32 v78, v78, v84
	v_add_f32_e32 v79, v79, v85
	v_mov_b32_e32 v87, v97
	v_mov_b32_e32 v79, v96
	v_mov_b32_e32 v91, v98
	v_mov_b32_e32 v95, v99
	v_add_f32_e32 v78, v78, v86
	v_add_f32_e32 v79, v79, v87
	v_add_f32_e32 v84, v90, v94
	v_add_f32_e32 v85, v91, v95
	s_nop 0
	v_add_f32_e32 v78, v78, v84
	v_add_f32_e32 v79, v79, v85
	v_xor_b32_e32 v84, 1, v107
	v_add_f32_e32 v78, v78, v79
	v_and_b32_e32 v79, 64, v107
	v_add_u32_e32 v79, 64, v79
	v_cmp_lt_i32_e32 vcc, v84, v79
	s_nop 1
	v_cndmask_b32_e32 v84, v107, v84, vcc
	v_lshlrev_b32_e32 v84, 2, v84
	ds_bpermute_b32 v84, v84, v78
	s_waitcnt lgkmcnt(0)
	v_add_f32_e32 v78, v78, v84
	v_xor_b32_e32 v84, 2, v107
	v_cmp_lt_i32_e32 vcc, v84, v79
	s_nop 1
	v_cndmask_b32_e32 v84, v107, v84, vcc
	v_lshlrev_b32_e32 v84, 2, v84
	ds_bpermute_b32 v84, v84, v78
	s_waitcnt lgkmcnt(0)
	v_add_f32_e32 v78, v78, v84
	v_xor_b32_e32 v84, 4, v107
	v_cmp_lt_i32_e32 vcc, v84, v79
	s_nop 1
	v_cndmask_b32_e32 v84, v107, v84, vcc
	v_lshlrev_b32_e32 v84, 2, v84
	ds_bpermute_b32 v84, v84, v78
	s_waitcnt lgkmcnt(0)
	v_add_f32_e32 v78, v78, v84
	v_xor_b32_e32 v84, 8, v107
	v_cmp_lt_i32_e32 vcc, v84, v79
	s_nop 1
	v_cndmask_b32_e32 v84, v107, v84, vcc
	v_lshlrev_b32_e32 v84, 2, v84
	ds_bpermute_b32 v84, v84, v78
	s_waitcnt lgkmcnt(0)
	v_add_f32_e32 v78, v78, v84
	v_xor_b32_e32 v84, 16, v107
	v_cmp_lt_i32_e32 vcc, v84, v79
	s_nop 1
	v_cndmask_b32_e32 v84, v107, v84, vcc
	v_lshlrev_b32_e32 v84, 2, v84
	ds_bpermute_b32 v84, v84, v78
	s_waitcnt lgkmcnt(0)
	v_add_f32_e32 v78, v78, v84
	v_xor_b32_e32 v84, 32, v107
	v_cmp_lt_i32_e32 vcc, v84, v79
	s_nop 1
	v_cndmask_b32_e32 v79, v107, v84, vcc
	v_lshlrev_b32_e32 v79, 2, v79
	ds_bpermute_b32 v79, v79, v78
	s_waitcnt lgkmcnt(0)
	v_add_f32_e32 v78, v78, v79
	v_fmamk_f32 v78, v78, 0x3a000000, v105
	v_mul_f32_e32 v79, 0x4f800000, v78
	v_cmp_gt_f32_e32 vcc, s19, v78
	s_nop 1
	v_cndmask_b32_e32 v78, v78, v79, vcc
	v_sqrt_f32_e32 v79, v78
	s_nop 0
	v_add_u32_e32 v84, -1, v79
	v_fma_f32 v85, -v84, v79, v78
	v_cmp_ge_f32_e64 s[2:3], 0, v85
	v_add_u32_e32 v85, 1, v79
	s_nop 0
	v_cndmask_b32_e64 v84, v79, v84, s[2:3]
	v_fma_f32 v79, -v85, v79, v78
	v_cmp_lt_f32_e64 s[2:3], 0, v79
	s_nop 1
	v_cndmask_b32_e64 v79, v84, v85, s[2:3]
	v_mul_f32_e32 v84, 0x37800000, v79
	v_cndmask_b32_e32 v79, v79, v84, vcc
	v_cmp_class_f32_e32 vcc, v78, v106
	s_nop 1
	v_cndmask_b32_e32 v78, v79, v78, vcc
	v_div_scale_f32 v79, s[2:3], v78, v78, 1.0
	v_rcp_f32_e32 v84, v79
	s_nop 0
	v_fma_f32 v85, -v79, v84, 1.0
	v_fmac_f32_e32 v84, v85, v84
	v_div_scale_f32 v85, vcc, 1.0, v78, 1.0
	v_mul_f32_e32 v86, v85, v84
	v_fma_f32 v87, -v79, v86, v85
	v_fmac_f32_e32 v86, v87, v84
	v_fma_f32 v79, -v79, v86, v85
	v_div_fmas_f32 v79, v79, v84, v86
	v_div_fixup_f32 v78, v79, v78, 1.0
	s_branch .LBB0_2640
